# dead zero-initialisations in front of paired fp8 packs removed kernel-wide (277 VALU ops)
# speedup vs baseline: 1.0140x; 1.0039x over previous
; #define LAS __attribute__((address_space(3)))
; __device__ __forceinline__ void transpose_item_fp8(const float* W, int K, int N, unsigned char* WT, float q, LAS float* scr, int item, int lane) {
;     const int nblk = N / 32, kb = item / nblk, nb = item % nblk, k0 = 64 * kb, n0 = 32 * nb;
; #pragma unroll 8
;     for (int i = 0; i < 32; ++i) { const int kk = 2 * i + (lane >> 5); scr[kk * 33 + (lane & 31)] = W[(size_t)(k0 + kk) * N + n0 + (lane & 31)]; }
;     asm volatile("s_waitcnt lgkmcnt(0)" ::: "memory");
.LBB0_72:
	s_lshl_b32 s67, s7, 1
	s_lshl_b32 s70, s4, 1
	v_add_u32_e32 v18, s67, v2
	v_add_u32_e32 v20, s70, v3
	v_add_u32_e32 v22, s67, v4
	v_add_u32_e32 v24, s70, v5
	v_add_u32_e32 v26, s67, v6
	v_add_u32_e32 v28, s70, v7
	v_add_u32_e32 v30, s67, v8
	v_add_u32_e32 v32, s70, v9
	v_add_u32_e32 v34, s67, v10
	v_add_u32_e32 v36, s70, v11
	v_add_u32_e32 v38, s67, v12
	v_add_u32_e32 v40, s70, v13
	v_add_u32_e32 v42, s67, v14
	v_add_u32_e32 v44, s70, v15
	v_add_u32_e32 v46, s67, v16
	v_add_u32_e32 v48, s70, v17
	v_mad_i64_i32 v[18:19], s[68:69], v18, s65, v[0:1]
	v_mad_i64_i32 v[20:21], s[68:69], v20, s65, v[0:1]
	v_mad_i64_i32 v[22:23], s[68:69], v22, s65, v[0:1]
	v_mad_i64_i32 v[24:25], s[68:69], v24, s65, v[0:1]
	v_mad_i64_i32 v[26:27], s[68:69], v26, s65, v[0:1]
	v_mad_i64_i32 v[28:29], s[68:69], v28, s65, v[0:1]
	v_mad_i64_i32 v[30:31], s[68:69], v30, s65, v[0:1]
	v_mad_i64_i32 v[32:33], s[68:69], v32, s65, v[0:1]
	v_mad_i64_i32 v[34:35], s[68:69], v34, s65, v[0:1]
	v_mad_i64_i32 v[36:37], s[68:69], v36, s65, v[0:1]
	v_mad_i64_i32 v[38:39], s[68:69], v38, s65, v[0:1]
	v_mad_i64_i32 v[40:41], s[68:69], v40, s65, v[0:1]
	v_mad_i64_i32 v[42:43], s[68:69], v42, s65, v[0:1]
	v_mad_i64_i32 v[44:45], s[68:69], v44, s65, v[0:1]
	v_mad_i64_i32 v[46:47], s[68:69], v46, s65, v[0:1]
	v_mad_i64_i32 v[48:49], s[68:69], v48, s65, v[0:1]
	global_load_dword v50, v[18:19], off nt
	global_load_dword v51, v[20:21], off nt
	global_load_dword v52, v[22:23], off nt
	global_load_dword v53, v[24:25], off nt
	global_load_dword v54, v[26:27], off nt
	global_load_dword v55, v[28:29], off nt
	global_load_dword v56, v[30:31], off nt
	global_load_dword v57, v[32:33], off nt
	global_load_dword v58, v[34:35], off nt
	global_load_dword v59, v[36:37], off nt
	global_load_dword v60, v[38:39], off nt
	global_load_dword v61, v[40:41], off nt
	global_load_dword v62, v[42:43], off nt
	global_load_dword v63, v[44:45], off nt
	global_load_dword v64, v[46:47], off nt
	global_load_dword v65, v[48:49], off nt
	s_add_i32 s7, s7, 16
	s_add_i32 s4, s4, 16
	s_add_i32 s9, s9, -16
	v_add_u32_e32 v18, s67, v146
	v_add_u32_e32 v20, s70, v141
	v_add_u32_e32 v22, s67, v166
	v_add_u32_e32 v24, s70, v147
	v_add_u32_e32 v26, s67, v168
	v_add_u32_e32 v28, s70, v151
	v_add_u32_e32 v30, s67, v170
	v_add_u32_e32 v32, s70, v167
	v_add_u32_e32 v34, s67, v172
	v_add_u32_e32 v36, s70, v169
	v_add_u32_e32 v38, s67, v174
	v_add_u32_e32 v40, s70, v171
	v_add_u32_e32 v42, s67, v176
	v_add_u32_e32 v44, s70, v173
	v_add_u32_e32 v46, s67, v178
	v_add_u32_e32 v48, s70, v175
	s_cmp_lg_u32 s9, 0
	v_mad_u64_u32 v[18:19], s[68:69], v18, s13, v[150:151]
	v_mad_u64_u32 v[20:21], s[68:69], v20, s13, v[150:151]
	v_mad_u64_u32 v[22:23], s[68:69], v22, s13, v[150:151]
	v_mad_u64_u32 v[24:25], s[68:69], v24, s13, v[150:151]
	v_mad_u64_u32 v[26:27], s[68:69], v26, s13, v[150:151]
	v_mad_u64_u32 v[28:29], s[68:69], v28, s13, v[150:151]
	v_mad_u64_u32 v[30:31], s[68:69], v30, s13, v[150:151]
	v_mad_u64_u32 v[32:33], s[68:69], v32, s13, v[150:151]
	v_mad_u64_u32 v[34:35], s[68:69], v34, s13, v[150:151]
	v_mad_u64_u32 v[36:37], s[68:69], v36, s13, v[150:151]
	v_mad_u64_u32 v[38:39], s[68:69], v38, s13, v[150:151]
	v_mad_u64_u32 v[40:41], s[68:69], v40, s13, v[150:151]
	v_mad_u64_u32 v[42:43], s[68:69], v42, s13, v[150:151]
	v_mad_u64_u32 v[44:45], s[68:69], v44, s13, v[150:151]
	v_mad_u64_u32 v[46:47], s[68:69], v46, s13, v[150:151]
	v_mad_u64_u32 v[48:49], s[68:69], v48, s13, v[150:151]
	s_waitcnt vmcnt(15)
	ds_write_b32 v18, v50
	s_waitcnt vmcnt(14)
	ds_write_b32 v20, v51
	s_waitcnt vmcnt(13)
	ds_write_b32 v22, v52
	s_waitcnt vmcnt(12)
	ds_write_b32 v24, v53
	s_waitcnt vmcnt(11)
	ds_write_b32 v26, v54
	s_waitcnt vmcnt(10)
	ds_write_b32 v28, v55
	s_waitcnt vmcnt(9)
	ds_write_b32 v30, v56
	s_waitcnt vmcnt(8)
	ds_write_b32 v32, v57
	s_waitcnt vmcnt(7)
	ds_write_b32 v34, v58
	s_waitcnt vmcnt(6)
	ds_write_b32 v36, v59
	s_waitcnt vmcnt(5)
	ds_write_b32 v38, v60
	s_waitcnt vmcnt(4)
	ds_write_b32 v40, v61
	s_waitcnt vmcnt(3)
	ds_write_b32 v42, v62
	s_waitcnt vmcnt(2)
	ds_write_b32 v44, v63
	s_waitcnt vmcnt(1)
	ds_write_b32 v46, v64
	s_waitcnt vmcnt(0)
	ds_write_b32 v48, v65
	s_cbranch_scc1 .LBB0_72
; #define LAS __attribute__((address_space(3)))
; __device__ __forceinline__ unsigned pk4_fp8(float x0, float x1, float x2, float x3) { int w = 0; w = __builtin_amdgcn_cvt_pk_fp8_f32(x0, x1, w, false); w = __builtin_amdgcn_cvt_pk_fp8_f32(x2, x3, w, true); return (unsigned)w; }
; __device__ __forceinline__ void transpose_item_fp8(const float* W, int K, int N, unsigned char* WT, float q, LAS float* scr, int item, int lane) {
;     ...
;     const int c = lane & 7;
; #pragma unroll
;     for (int j = 0; j < 4; ++j) { const int n = (lane >> 3) + 8 * j; const LAS float* s = scr + (8 * c) * 33 + n;
;         u32x2 o; o.x = pk4_fp8(s[0 * 33] * q, s[1 * 33] * q, s[2 * 33] * q, s[3 * 33] * q); o.y = pk4_fp8(s[4 * 33] * q, s[5 * 33] * q, s[6 * 33] * q, s[7 * 33] * q);
;         *(u32x2*)(WT + (size_t)(n0 + n) * K + k0 + 8 * c) = o; }
;     asm volatile("s_waitcnt lgkmcnt(0)" ::: "memory");
; }
	s_waitcnt lgkmcnt(0)
	ds_read2_b32 v[0:1], v190 offset1:8
	ds_read2_b32 v[2:3], v190 offset0:33 offset1:41
	ds_read2_b32 v[4:5], v190 offset0:66 offset1:74
	ds_read2_b32 v[8:9], v190 offset0:99 offset1:107
	ds_read2_b32 v[10:11], v190 offset0:132 offset1:140
	ds_read2_b32 v[12:13], v190 offset0:165 offset1:173
	s_waitcnt lgkmcnt(5)
	v_mul_f32_e32 v0, 0x43000000, v0
	s_waitcnt lgkmcnt(4)
	v_mul_f32_e32 v2, 0x43000000, v2
	ds_read2_b32 v[16:17], v190 offset0:198 offset1:206
	ds_read2_b32 v[18:19], v190 offset0:231 offset1:239
	v_cvt_pk_fp8_f32 v14, v0, v2
	s_waitcnt lgkmcnt(3)
	v_mul_f32_e32 v0, 0x43000000, v10
	s_waitcnt lgkmcnt(2)
	v_mul_f32_e32 v2, 0x43000000, v12
	v_cvt_pk_fp8_f32 v15, v0, v2
	s_waitcnt lgkmcnt(1)
	v_mul_f32_e32 v0, 0x43000000, v16
	s_waitcnt lgkmcnt(0)
	v_mul_f32_e32 v2, 0x43000000, v18
	v_mul_f32_e32 v1, 0x43000000, v1
	v_cvt_pk_fp8_f32 v15, v0, v2 op_sel:[0,0,1]
	v_mul_f32_e32 v2, 0x43000000, v3
	v_mul_f32_e32 v3, 0x43000000, v5
	v_cvt_pk_fp8_f32 v0, v1, v2
	v_mul_f32_e32 v2, 0x43000000, v11
	v_mul_f32_e32 v5, 0x43000000, v13
	v_cvt_pk_fp8_f32 v1, v2, v5
	v_mul_f32_e32 v4, 0x43000000, v4
	v_mul_f32_e32 v8, 0x43000000, v8
	v_cvt_pk_fp8_f32 v14, v4, v8 op_sel:[0,0,1]
	v_mul_f32_e32 v4, 0x43000000, v9
	v_add_u32_e32 v20, s6, v189
	v_cvt_pk_fp8_f32 v0, v3, v4 op_sel:[0,0,1]
	v_mul_f32_e32 v2, 0x43000000, v17
	v_mul_f32_e32 v3, 0x43000000, v19
	s_ashr_i32 s9, s8, 31
	v_ashrrev_i32_e32 v21, 31, v20
	v_cvt_pk_fp8_f32 v1, v2, v3 op_sel:[0,0,1]
	v_add_u32_e32 v2, s6, v191
	v_lshl_add_u64 v[6:7], v[164:165], 0, s[8:9]
	v_lshlrev_b64 v[20:21], 10, v[20:21]
	v_ashrrev_i32_e32 v3, 31, v2
	v_lshl_add_u64 v[20:21], v[6:7], 0, v[20:21]
	v_lshlrev_b64 v[2:3], 10, v[2:3]
	global_store_dwordx2 v[20:21], v[14:15], off nt
	v_lshl_add_u64 v[2:3], v[6:7], 0, v[2:3]
	ds_read2_b32 v[4:5], v190 offset0:16 offset1:24
	ds_read2_b32 v[8:9], v190 offset0:49 offset1:57
	ds_read2_b32 v[10:11], v190 offset0:82 offset1:90
	global_store_dwordx2 v[2:3], v[0:1], off nt
	ds_read2_b32 v[0:1], v190 offset0:115 offset1:123
	ds_read2_b32 v[2:3], v190 offset0:148 offset1:156
	ds_read2_b32 v[12:13], v190 offset0:181 offset1:189
	s_waitcnt lgkmcnt(5)
	v_mul_f32_e32 v4, 0x43000000, v4
	s_waitcnt lgkmcnt(4)
	v_mul_f32_e32 v8, 0x43000000, v8
	ds_read2_b32 v[16:17], v190 offset0:214 offset1:222
	ds_read2_b32 v[18:19], v190 offset0:247 offset1:255
	v_cvt_pk_fp8_f32 v14, v4, v8
	s_waitcnt lgkmcnt(3)
	v_mul_f32_e32 v2, 0x43000000, v2
	s_waitcnt lgkmcnt(2)
	v_mul_f32_e32 v4, 0x43000000, v12
	v_cvt_pk_fp8_f32 v15, v2, v4
	v_mul_f32_e32 v10, 0x43000000, v10
	v_mul_f32_e32 v0, 0x43000000, v0
	v_cvt_pk_fp8_f32 v14, v10, v0 op_sel:[0,0,1]
	s_waitcnt lgkmcnt(1)
	v_mul_f32_e32 v0, 0x43000000, v16
	s_waitcnt lgkmcnt(0)
	v_mul_f32_e32 v2, 0x43000000, v18
	v_cvt_pk_fp8_f32 v15, v0, v2 op_sel:[0,0,1]
	v_mul_f32_e32 v2, 0x43000000, v5
	v_mul_f32_e32 v4, 0x43000000, v9
	v_mul_f32_e32 v8, 0x43000000, v1
	v_cvt_pk_fp8_f32 v0, v2, v4
	v_mul_f32_e32 v2, 0x43000000, v3
	v_mul_f32_e32 v3, 0x43000000, v13
	v_cvt_pk_fp8_f32 v1, v2, v3
	v_mul_f32_e32 v5, 0x43000000, v11
	v_mul_f32_e32 v2, 0x43000000, v17
	v_mul_f32_e32 v3, 0x43000000, v19
	v_add_u32_e32 v20, s6, v192
	v_cvt_pk_fp8_f32 v0, v5, v8 op_sel:[0,0,1]
	v_cvt_pk_fp8_f32 v1, v2, v3 op_sel:[0,0,1]
	v_add_u32_e32 v2, s6, v193
	v_ashrrev_i32_e32 v21, 31, v20
	v_ashrrev_i32_e32 v3, 31, v2
	v_lshlrev_b64 v[20:21], 10, v[20:21]
	v_lshlrev_b64 v[2:3], 10, v[2:3]
	v_lshl_add_u64 v[20:21], v[6:7], 0, v[20:21]
	v_lshl_add_u64 v[2:3], v[6:7], 0, v[2:3]
	global_store_dwordx2 v[20:21], v[14:15], off nt
	global_store_dwordx2 v[2:3], v[0:1], off nt
	s_waitcnt lgkmcnt(0)
	s_branch .LBB0_37

; __device__ __forceinline__ unsigned pk4_fp8(float x0, float x1, float x2, float x3) { int w = 0; w = __builtin_amdgcn_cvt_pk_fp8_f32(x0, x1, w, false); w = __builtin_amdgcn_cvt_pk_fp8_f32(x2, x3, w, true); return (unsigned)w; }
; __device__ __forceinline__ int modset(int n) { return (n < NCTX) ? 4 : ((n - NCTX) >> 13); }
; __global__ void __launch_bounds__(512, 2) mega(Args a) {
;     ...
;             for (int t = 0; t < 2; ++t) { const float* md = MOD + (size_t)modset(nn[t]) * 6144; const f32x4* xr = (const f32x4*)XROW0(nn[t]) + lane;
; #pragma unroll
;                 for (int j = 0; j < 4; ++j) { xv_[t][j] = xr[64 * j]; sh_[t][j] = *((const f32x4*)(md) + lane + 64 * j); sc_[t][j] = *((const f32x4*)(md + 1024) + lane + 64 * j); } }
; #pragma unroll
;             for (int t = 0; t < 2; ++t) { unsigned* o8 = (unsigned*)(XHF + (size_t)nn[t] * DM) + lane;
; #pragma unroll
;                 for (int j = 0; j < 4; ++j) { const f32x4 v = xv_[t][j], sh = sh_[t][j], scl = sc_[t][j];
;                     o8[64 * j] = pk4_fp8((v.x * (1.f + scl.x) + sh.x) * ACT_Q, (v.y * (1.f + scl.y) + sh.y) * ACT_Q, (v.z * (1.f + scl.z) + sh.z) * ACT_Q, (v.w * (1.f + scl.w) + sh.w) * ACT_Q); } }
;         }
.LBB0_131:
	s_lshr_b32 s18, s18, 13
	s_and_b64 s[24:25], exec, s[24:25]
	s_cselect_b32 s18, 4, s18
	s_mul_hi_u32 s25, s18, 0x6000
	s_mulk_i32 s18, 0x6000
	s_add_u32 s24, s72, s18
	s_addc_u32 s25, s73, s25
	v_lshl_add_u64 v[94:95], s[24:25], 0, v[52:53]
	v_add_co_u32_e32 v58, vcc, s13, v94
	v_lshl_add_u64 v[86:87], s[26:27], 0, v[52:53]
	s_nop 0
	v_addc_co_u32_e32 v59, vcc, 0, v95, vcc
	global_load_dwordx4 v[54:57], v[86:87], off
	s_nop 0
	global_load_dwordx4 v[58:61], v[58:59], off
	s_nop 0
	global_load_dwordx4 v[62:65], v[94:95], off
	v_lshl_add_u64 v[98:99], v[94:95], 0, s[20:21]
	global_load_dwordx4 v[66:69], v[86:87], off offset:1024
	global_load_dwordx4 v[70:73], v[94:95], off offset:1024
	global_load_dwordx4 v[74:77], v[98:99], off offset:1024
	global_load_dwordx4 v[78:81], v[98:99], off offset:2048
	global_load_dwordx4 v[82:85], v[86:87], off offset:2048
	s_nop 0
	global_load_dwordx4 v[86:89], v[86:87], off offset:3072
	s_nop 0
	global_load_dwordx4 v[90:93], v[94:95], off offset:2048
	s_nop 0
	global_load_dwordx4 v[94:97], v[94:95], off offset:3072
	s_nop 0
	global_load_dwordx4 v[98:101], v[98:99], off offset:3072
	s_waitcnt vmcnt(13)
	v_add_f32_e32 v44, 1.0, v44
	s_waitcnt vmcnt(12)
	v_add_f32_e32 v8, 1.0, v8
	v_fma_f32 v36, v36, v44, v40
	v_add_f32_e32 v40, 1.0, v45
	v_add_f32_e32 v32, 1.0, v32
	v_fma_f32 v0, v0, v8, v4
	v_add_f32_e32 v4, 1.0, v9
	v_fma_f32 v37, v37, v40, v41
	v_add_f32_e32 v40, 1.0, v46
	v_fma_f32 v24, v24, v32, v28
	v_add_f32_e32 v28, 1.0, v33
	v_add_f32_e32 v16, 1.0, v16
	v_fma_f32 v1, v1, v4, v5
	v_add_f32_e32 v4, 1.0, v10
	v_mul_f32_e32 v36, 4.0, v36
	v_mul_f32_e32 v37, 4.0, v37
	v_fma_f32 v38, v38, v40, v42
	v_fma_f32 v25, v25, v28, v29
	v_add_f32_e32 v28, 1.0, v34
	v_fma_f32 v12, v12, v16, v20
	v_add_f32_e32 v16, 1.0, v17
	v_mul_f32_e32 v0, 4.0, v0
	v_mul_f32_e32 v1, 4.0, v1
	v_fma_f32 v2, v2, v4, v6
	v_cvt_pk_fp8_f32 v40, v36, v37
	v_mul_f32_e32 v24, 4.0, v24
	v_mul_f32_e32 v25, 4.0, v25
	v_fma_f32 v26, v26, v28, v30
	v_fma_f32 v13, v13, v16, v21
	v_add_f32_e32 v16, 1.0, v18
	v_cvt_pk_fp8_f32 v4, v0, v1
	v_add_f32_e32 v36, 1.0, v47
	v_cvt_pk_fp8_f32 v28, v24, v25
	v_mul_f32_e32 v12, 4.0, v12
	v_mul_f32_e32 v13, 4.0, v13
	v_fma_f32 v14, v14, v16, v22
	v_add_f32_e32 v0, 1.0, v11
	v_fmac_f32_e32 v43, v39, v36
	v_add_f32_e32 v24, 1.0, v35
	v_cvt_pk_fp8_f32 v16, v12, v13
	v_fmac_f32_e32 v7, v3, v0
	v_mul_f32_e32 v38, 4.0, v38
	v_mul_f32_e32 v36, 4.0, v43
	v_fmac_f32_e32 v31, v27, v24
	v_add_f32_e32 v12, 1.0, v19
	v_mul_f32_e32 v2, 4.0, v2
	v_mul_f32_e32 v0, 4.0, v7
	v_cvt_pk_fp8_f32 v40, v38, v36 op_sel:[0,0,1]
	v_mul_f32_e32 v26, 4.0, v26
	v_mul_f32_e32 v24, 4.0, v31
	v_fmac_f32_e32 v23, v15, v12
	v_cvt_pk_fp8_f32 v4, v2, v0 op_sel:[0,0,1]
	v_cvt_pk_fp8_f32 v28, v26, v24 op_sel:[0,0,1]
	v_mul_f32_e32 v14, 4.0, v14
	v_mul_f32_e32 v12, 4.0, v23
	v_cvt_pk_fp8_f32 v16, v14, v12 op_sel:[0,0,1]
	global_store_dword v[50:51], v40, off offset:-768
	global_store_dword v[50:51], v28, off offset:-512
	global_store_dword v[50:51], v16, off offset:-256
	global_store_dword v[50:51], v4, off
	s_lshl_b64 s[22:23], s[22:23], 10
	s_add_i32 s30, s30, s8
	s_add_u32 s16, s16, s8
	s_addc_u32 s17, s17, s9
	v_lshl_add_u64 v[0:1], v[48:49], 0, s[22:23]
	s_cmp_lt_i32 s30, 0x8400
	v_lshl_add_u64 v[50:51], v[50:51], 0, s[10:11]
	s_waitcnt vmcnt(14)
	v_add_f32_e32 v2, 1.0, v58
	v_add_f32_e32 v3, 1.0, v59
	s_waitcnt vmcnt(13)
	v_fma_f32 v2, v54, v2, v62
	v_fma_f32 v3, v55, v3, v63
	v_mul_f32_e32 v2, 4.0, v2
	v_mul_f32_e32 v3, 4.0, v3
	v_cvt_pk_fp8_f32 v5, v2, v3
	v_add_f32_e32 v4, 1.0, v60
	v_add_f32_e32 v2, 1.0, v61
	v_fma_f32 v4, v56, v4, v64
	v_fmac_f32_e32 v65, v57, v2
	v_mul_f32_e32 v4, 4.0, v4
	v_mul_f32_e32 v2, 4.0, v65
	v_cvt_pk_fp8_f32 v5, v4, v2 op_sel:[0,0,1]
	s_waitcnt vmcnt(10)
	v_add_f32_e32 v2, 1.0, v74
	v_add_f32_e32 v3, 1.0, v75
	v_fma_f32 v2, v66, v2, v70
	v_fma_f32 v3, v67, v3, v71
	v_mul_f32_e32 v2, 4.0, v2
	v_mul_f32_e32 v3, 4.0, v3
	v_cvt_pk_fp8_f32 v6, v2, v3
	v_add_f32_e32 v4, 1.0, v76
	v_add_f32_e32 v2, 1.0, v77
	v_fma_f32 v4, v68, v4, v72
	v_fmac_f32_e32 v73, v69, v2
	v_mul_f32_e32 v4, 4.0, v4
	v_mul_f32_e32 v2, 4.0, v73
	v_cvt_pk_fp8_f32 v6, v4, v2 op_sel:[0,0,1]
	s_waitcnt vmcnt(9)
	v_add_f32_e32 v2, 1.0, v78
	v_add_f32_e32 v3, 1.0, v79
	s_waitcnt vmcnt(6)
	v_fma_f32 v2, v82, v2, v90
	v_fma_f32 v3, v83, v3, v91
	v_mul_f32_e32 v2, 4.0, v2
	v_mul_f32_e32 v3, 4.0, v3
	v_cvt_pk_fp8_f32 v7, v2, v3
	v_add_f32_e32 v4, 1.0, v80
	v_add_f32_e32 v2, 1.0, v81
	v_fma_f32 v4, v84, v4, v92
	v_fmac_f32_e32 v93, v85, v2
	v_mul_f32_e32 v4, 4.0, v4
	v_mul_f32_e32 v2, 4.0, v93
	v_cvt_pk_fp8_f32 v7, v4, v2 op_sel:[0,0,1]
	s_waitcnt vmcnt(4)
	v_add_f32_e32 v2, 1.0, v98
	v_add_f32_e32 v3, 1.0, v99
	v_fma_f32 v2, v86, v2, v94
	v_fma_f32 v3, v87, v3, v95
	v_mul_f32_e32 v2, 4.0, v2
	v_mul_f32_e32 v3, 4.0, v3
	v_cvt_pk_fp8_f32 v8, v2, v3
	v_add_f32_e32 v4, 1.0, v100
	v_add_f32_e32 v2, 1.0, v101
	v_fma_f32 v4, v88, v4, v96
	v_fmac_f32_e32 v97, v89, v2
	v_mul_f32_e32 v4, 4.0, v4
	v_mul_f32_e32 v2, 4.0, v97
	v_cvt_pk_fp8_f32 v8, v4, v2 op_sel:[0,0,1]
	global_store_dword v[0:1], v5, off
	global_store_dword v[0:1], v6, off offset:256
	global_store_dword v[0:1], v7, off offset:512
	global_store_dword v[0:1], v8, off offset:768
	s_cbranch_scc0 .LBB0_136

; #define LAS __attribute__((address_space(3)))
; __device__ __forceinline__ unsigned pk4_fp8(float x0, float x1, float x2, float x3) { int w = 0; w = __builtin_amdgcn_cvt_pk_fp8_f32(x0, x1, w, false); w = __builtin_amdgcn_cvt_pk_fp8_f32(x2, x3, w, true); return (unsigned)w; }
; __device__ __forceinline__ void transpose_item_fp8w(const float* W, int K, int N, unsigned char* WT, float q, LAS unsigned char* scr, int item, int lane) {
;     const int nblk = N / 128, kb = item / nblk, nb = item % nblk, k0 = 64 * kb, n0 = 128 * nb;
;     const int l5 = lane & 31, h = lane >> 5;
;     const float* src = W + (size_t)(k0 + 16 * h) * N + n0 + 4 * l5;
; #pragma unroll
;     for (int b = 0; b < 2; ++b) {
;         f32x4 x[16];
; #pragma unroll
;         for (int s_ = 0; s_ < 16; ++s_) x[s_] = *(const f32x4*)(src + (size_t)(32 * b + s_) * N);
; #pragma unroll
;         for (int i = 0; i < 4; ++i) {
;             u32x4 o;
;             o.x = pk4_fp8(x[0][i] * q, x[1][i] * q, x[2][i] * q, x[3][i] * q); o.y = pk4_fp8(x[4][i] * q, x[5][i] * q, x[6][i] * q, x[7][i] * q);
;             o.z = pk4_fp8(x[8][i] * q, x[9][i] * q, x[10][i] * q, x[11][i] * q); o.w = pk4_fp8(x[12][i] * q, x[13][i] * q, x[14][i] * q, x[15][i] * q);
;             *(LAS u32x4*)(scr + (l5 + 32 * i) * 80 + (2 * b + h) * 16) = o; }
;     }
;     asm volatile("s_waitcnt lgkmcnt(0)" ::: "memory");
.LBB0_331:
	s_cmpk_gt_i32 s5, 0x3df
	s_mov_b64 s[0:1], -1
	s_cbranch_scc0 .LBB0_359
	s_cmpk_gt_u32 s5, 0x46f
	s_cbranch_scc0 .LBB0_346
	s_cmpk_gt_u32 s5, 0x4ef
	s_cbranch_scc0 .LBB0_341
	s_cmpk_gt_u32 s5, 0x6ef
	s_cbranch_scc0 .LBB0_336
	s_add_i32 s2, s5, 0xfffff910
	v_readlane_b32 s8, v253, 32
	s_lshr_b32 s0, s2, 8
	v_readlane_b32 s9, v253, 33
	s_mov_b32 s13, s9
	s_add_i32 s12, s0, s21
	v_readlane_b32 s40, v253, 58
	s_lshl_b64 s[0:1], s[12:13], 23
	v_readlane_b32 s50, v254, 4
	v_readlane_b32 s51, v254, 5
	s_add_u32 s10, s50, s0
	s_addc_u32 s11, s51, s1
	s_lshl_b64 s[8:9], s[12:13], 21
	v_readlane_b32 s0, v246, 15
	s_add_u32 s1, s0, s8
	v_readlane_b32 s0, v246, 16
	s_addc_u32 s8, s0, s9
	s_lshl_b32 s0, s2, 6
	s_and_b32 s9, s0, 0x3c0
	v_add_u32_e32 v0, s9, v101
	s_lshl_b32 s0, s2, 3
	v_ashrrev_i32_e32 v1, 31, v0
	s_and_b32 s0, s0, 0x780
	v_lshlrev_b64 v[0:1], 13, v[0:1]
	v_lshl_add_u64 v[0:1], s[10:11], 0, v[0:1]
	s_lshl_b32 s12, s0, 2
	s_mov_b32 s3, s13
	v_readlane_b32 s41, v253, 59
	v_readlane_b32 s42, v253, 60
	v_readlane_b32 s43, v253, 61
	v_readlane_b32 s44, v253, 62
	v_readlane_b32 s45, v253, 63
	v_writelane_b32 v253, s2, 32
	v_lshl_add_u64 v[0:1], v[0:1], 0, s[12:13]
	v_lshl_add_u64 v[60:61], v[0:1], 0, v[152:153]
	v_writelane_b32 v253, s3, 33
	s_movk_i32 s2, 0x2000
	v_add_co_u32_e32 v4, vcc, s2, v60
	s_movk_i32 s2, 0x4000
	s_nop 0
	v_addc_co_u32_e32 v5, vcc, 0, v61, vcc
	v_add_co_u32_e32 v8, vcc, s2, v60
	s_movk_i32 s2, 0x6000
	s_nop 0
	v_addc_co_u32_e32 v9, vcc, 0, v61, vcc
	v_add_co_u32_e32 v12, vcc, s2, v60
	s_mov_b32 s2, 0x8000
	s_nop 0
	v_addc_co_u32_e32 v13, vcc, 0, v61, vcc
	v_add_co_u32_e32 v16, vcc, s2, v60
	s_mov_b32 s2, 0xa000
	s_nop 0
	v_addc_co_u32_e32 v17, vcc, 0, v61, vcc
	v_add_co_u32_e32 v20, vcc, s2, v60
	s_mov_b32 s2, 0xc000
	s_nop 0
	v_addc_co_u32_e32 v21, vcc, 0, v61, vcc
	v_add_co_u32_e32 v24, vcc, s2, v60
	s_mov_b32 s2, 0xe000
	s_nop 0
	v_addc_co_u32_e32 v25, vcc, 0, v61, vcc
	v_add_co_u32_e32 v28, vcc, s2, v60
	s_mov_b32 s2, 0x10000
	s_nop 0
	v_addc_co_u32_e32 v29, vcc, 0, v61, vcc
	v_add_co_u32_e32 v32, vcc, s2, v60
	s_mov_b32 s2, 0x12000
	s_nop 0
	v_addc_co_u32_e32 v33, vcc, 0, v61, vcc
	v_add_co_u32_e32 v36, vcc, s2, v60
	s_mov_b32 s2, 0x14000
	s_nop 0
	v_addc_co_u32_e32 v37, vcc, 0, v61, vcc
	v_add_co_u32_e32 v40, vcc, s2, v60
	s_mov_b32 s2, 0x16000
	s_nop 0
	v_addc_co_u32_e32 v41, vcc, 0, v61, vcc
	v_add_co_u32_e32 v44, vcc, s2, v60
	s_mov_b32 s2, 0x18000
	s_nop 0
	v_addc_co_u32_e32 v45, vcc, 0, v61, vcc
	v_add_co_u32_e32 v48, vcc, s2, v60
	global_load_dwordx4 v[0:3], v[60:61], off nt
	s_nop 0
	v_addc_co_u32_e32 v49, vcc, 0, v61, vcc
	global_load_dwordx4 v[4:7], v[4:5], off nt
	s_mov_b32 s2, 0x1a000
	global_load_dwordx4 v[12:15], v[12:13], off nt
	v_add_co_u32_e32 v52, vcc, s2, v60
	global_load_dwordx4 v[16:19], v[16:17], off nt
	s_nop 0
	v_addc_co_u32_e32 v53, vcc, 0, v61, vcc
	global_load_dwordx4 v[20:23], v[20:21], off nt
	s_mov_b32 s2, 0x1c000
	global_load_dwordx4 v[28:31], v[28:29], off nt
	v_add_co_u32_e32 v56, vcc, s2, v60
	global_load_dwordx4 v[32:35], v[32:33], off nt
	s_nop 0
	v_addc_co_u32_e32 v57, vcc, 0, v61, vcc
	global_load_dwordx4 v[36:39], v[36:37], off nt
	s_mov_b32 s2, 0x1e000
	global_load_dwordx4 v[44:47], v[44:45], off nt
	v_add_co_u32_e32 v62, vcc, s2, v60
	global_load_dwordx4 v[48:51], v[48:49], off nt
	s_nop 0
	v_addc_co_u32_e32 v63, vcc, 0, v61, vcc
	global_load_dwordx4 v[52:55], v[52:53], off nt
	global_load_dwordx4 v[8:11], v[8:9], off nt
	global_load_dwordx4 v[24:27], v[24:25], off nt
	global_load_dwordx4 v[40:43], v[40:41], off nt
	global_load_dwordx4 v[56:59], v[56:57], off nt
	s_mov_b32 s2, 0x40000
	global_load_dwordx4 v[116:119], v[62:63], off nt
	s_add_u32 s10, s1, s9
	s_addc_u32 s11, s8, 0
	v_readlane_b32 s46, v254, 0
	v_readlane_b32 s47, v254, 1
	v_readlane_b32 s48, v254, 2
	v_readlane_b32 s49, v254, 3
	v_readlane_b32 s52, v254, 6
	v_readlane_b32 s53, v254, 7
	v_readlane_b32 s54, v254, 8
	v_readlane_b32 s55, v254, 9
	s_waitcnt vmcnt(0)
	v_mul_f32_e32 v0, 0x43000000, v0
	s_waitcnt vmcnt(14)
	v_mul_f32_e32 v4, 0x43000000, v4
	v_cvt_pk_fp8_f32 v120, v0, v4
	s_waitcnt vmcnt(13)
	v_mul_f32_e32 v12, 0x43000000, v12
	s_waitcnt vmcnt(12)
	v_mul_f32_e32 v0, 0x43000000, v16
	s_waitcnt vmcnt(11)
	v_mul_f32_e32 v4, 0x43000000, v20
	v_cvt_pk_fp8_f32 v121, v0, v4
	s_waitcnt vmcnt(9)
	v_mul_f32_e32 v0, 0x43000000, v32
	s_waitcnt vmcnt(8)
	v_mul_f32_e32 v4, 0x43000000, v36
	v_cvt_pk_fp8_f32 v122, v0, v4
	s_waitcnt vmcnt(6)
	v_mul_f32_e32 v0, 0x43000000, v48
	s_waitcnt vmcnt(5)
	v_mul_f32_e32 v4, 0x43000000, v52
	v_cvt_pk_fp8_f32 v123, v0, v4
	s_waitcnt vmcnt(4)
	v_mul_f32_e32 v8, 0x43000000, v8
	v_cvt_pk_fp8_f32 v120, v8, v12 op_sel:[0,0,1]
	s_waitcnt vmcnt(3)
	v_mul_f32_e32 v8, 0x43000000, v24
	v_mul_f32_e32 v12, 0x43000000, v28
	v_cvt_pk_fp8_f32 v121, v8, v12 op_sel:[0,0,1]
	s_waitcnt vmcnt(2)
	v_mul_f32_e32 v8, 0x43000000, v40
	v_mul_f32_e32 v12, 0x43000000, v44
	v_cvt_pk_fp8_f32 v122, v8, v12 op_sel:[0,0,1]
	s_waitcnt vmcnt(1)
	v_mul_f32_e32 v8, 0x43000000, v56
	s_waitcnt vmcnt(0)
; #define LAS __attribute__((address_space(3)))
; __device__ __forceinline__ unsigned pk4_fp8(float x0, float x1, float x2, float x3) { int w = 0; w = __builtin_amdgcn_cvt_pk_fp8_f32(x0, x1, w, false); w = __builtin_amdgcn_cvt_pk_fp8_f32(x2, x3, w, true); return (unsigned)w; }
; __device__ __forceinline__ void transpose_item_fp8w(const float* W, int K, int N, unsigned char* WT, float q, LAS unsigned char* scr, int item, int lane) {
;     ...
;     for (int b = 0; b < 2; ++b) {
;         f32x4 x[16];
; #pragma unroll
;         for (int s_ = 0; s_ < 16; ++s_) x[s_] = *(const f32x4*)(src + (size_t)(32 * b + s_) * N);
; #pragma unroll
;         for (int i = 0; i < 4; ++i) {
;             u32x4 o;
;             o.x = pk4_fp8(x[0][i] * q, x[1][i] * q, x[2][i] * q, x[3][i] * q); o.y = pk4_fp8(x[4][i] * q, x[5][i] * q, x[6][i] * q, x[7][i] * q);
;             o.z = pk4_fp8(x[8][i] * q, x[9][i] * q, x[10][i] * q, x[11][i] * q); o.w = pk4_fp8(x[12][i] * q, x[13][i] * q, x[14][i] * q, x[15][i] * q);
;             *(LAS u32x4*)(scr + (l5 + 32 * i) * 80 + (2 * b + h) * 16) = o; }
;     }
;     asm volatile("s_waitcnt lgkmcnt(0)" ::: "memory");
	v_mul_f32_e32 v12, 0x43000000, v116
	v_cvt_pk_fp8_f32 v123, v8, v12 op_sel:[0,0,1]
	v_mul_f32_e32 v0, 0x43000000, v1
	v_mul_f32_e32 v1, 0x43000000, v5
	v_mul_f32_e32 v4, 0x43000000, v9
	ds_write_b128 v98, v[120:123]
	v_cvt_pk_fp8_f32 v120, v0, v1
	v_mul_f32_e32 v0, 0x43000000, v17
	v_mul_f32_e32 v1, 0x43000000, v21
	v_cvt_pk_fp8_f32 v121, v0, v1
	v_mul_f32_e32 v0, 0x43000000, v33
	v_mul_f32_e32 v1, 0x43000000, v37
	v_cvt_pk_fp8_f32 v122, v0, v1
	v_mul_f32_e32 v0, 0x43000000, v49
	v_mul_f32_e32 v1, 0x43000000, v53
	v_mul_f32_e32 v5, 0x43000000, v13
	v_cvt_pk_fp8_f32 v123, v0, v1
	v_cvt_pk_fp8_f32 v120, v4, v5 op_sel:[0,0,1]
	v_mul_f32_e32 v4, 0x43000000, v25
	v_mul_f32_e32 v5, 0x43000000, v29
	v_cvt_pk_fp8_f32 v121, v4, v5 op_sel:[0,0,1]
	v_mul_f32_e32 v4, 0x43000000, v41
	v_mul_f32_e32 v5, 0x43000000, v45
	v_cvt_pk_fp8_f32 v122, v4, v5 op_sel:[0,0,1]
	v_mul_f32_e32 v4, 0x43000000, v57
	v_mul_f32_e32 v5, 0x43000000, v117
	v_cvt_pk_fp8_f32 v123, v4, v5 op_sel:[0,0,1]
	v_mul_f32_e32 v0, 0x43000000, v2
	v_mul_f32_e32 v1, 0x43000000, v6
	v_mul_f32_e32 v2, 0x43000000, v10
	ds_write_b128 v98, v[120:123] offset:2560
	v_cvt_pk_fp8_f32 v120, v0, v1
	v_mul_f32_e32 v0, 0x43000000, v18
	v_mul_f32_e32 v1, 0x43000000, v22
	v_cvt_pk_fp8_f32 v121, v0, v1
	v_mul_f32_e32 v0, 0x43000000, v34
	v_mul_f32_e32 v1, 0x43000000, v38
	v_cvt_pk_fp8_f32 v122, v0, v1
	v_mul_f32_e32 v0, 0x43000000, v50
	v_mul_f32_e32 v1, 0x43000000, v54
	v_mul_f32_e32 v4, 0x43000000, v14
	v_cvt_pk_fp8_f32 v123, v0, v1
	v_cvt_pk_fp8_f32 v120, v2, v4 op_sel:[0,0,1]
	v_mul_f32_e32 v2, 0x43000000, v26
	v_mul_f32_e32 v4, 0x43000000, v30
	v_cvt_pk_fp8_f32 v121, v2, v4 op_sel:[0,0,1]
	v_mul_f32_e32 v2, 0x43000000, v42
	v_mul_f32_e32 v4, 0x43000000, v46
	v_cvt_pk_fp8_f32 v122, v2, v4 op_sel:[0,0,1]
	v_mul_f32_e32 v2, 0x43000000, v58
	v_mul_f32_e32 v4, 0x43000000, v118
	v_cvt_pk_fp8_f32 v123, v2, v4 op_sel:[0,0,1]
	v_mul_f32_e32 v1, 0x43000000, v3
	v_mul_f32_e32 v2, 0x43000000, v7
	v_cvt_pk_fp8_f32 v0, v1, v2
	v_mul_f32_e32 v3, 0x43000000, v11
	v_mul_f32_e32 v4, 0x43000000, v15
	v_mul_f32_e32 v2, 0x43000000, v19
	v_cvt_pk_fp8_f32 v0, v3, v4 op_sel:[0,0,1]
	v_mul_f32_e32 v3, 0x43000000, v23
	v_cvt_pk_fp8_f32 v1, v2, v3
	v_mul_f32_e32 v4, 0x43000000, v27
	v_mul_f32_e32 v5, 0x43000000, v31
	v_mul_f32_e32 v3, 0x43000000, v35
	v_cvt_pk_fp8_f32 v1, v4, v5 op_sel:[0,0,1]
	v_mul_f32_e32 v4, 0x43000000, v39
	v_cvt_pk_fp8_f32 v2, v3, v4
	v_mul_f32_e32 v5, 0x43000000, v43
	v_mul_f32_e32 v6, 0x43000000, v47
	v_mul_f32_e32 v4, 0x43000000, v51
	v_cvt_pk_fp8_f32 v2, v5, v6 op_sel:[0,0,1]
	v_mul_f32_e32 v5, 0x43000000, v55
	v_cvt_pk_fp8_f32 v3, v4, v5
	v_mul_f32_e32 v6, 0x43000000, v59
	v_mul_f32_e32 v7, 0x43000000, v119
	v_mov_b32_e32 v116, v153
	v_cvt_pk_fp8_f32 v3, v6, v7 op_sel:[0,0,1]
	v_mov_b32_e32 v117, v153
	v_mov_b32_e32 v118, v153
	v_mov_b32_e32 v119, v153
	ds_write_b128 v98, v[0:3] offset:7680
	v_add_co_u32_e32 v0, vcc, s2, v60
	s_mov_b32 s2, 0x42000
	s_nop 0
	v_addc_co_u32_e32 v1, vcc, 0, v61, vcc
	v_add_co_u32_e32 v4, vcc, s2, v60
	s_mov_b32 s2, 0x44000
	s_nop 0
	v_addc_co_u32_e32 v5, vcc, 0, v61, vcc
	v_add_co_u32_e32 v8, vcc, s2, v60
	s_mov_b32 s2, 0x46000
	s_nop 0
	v_addc_co_u32_e32 v9, vcc, 0, v61, vcc
	v_add_co_u32_e32 v12, vcc, s2, v60
	s_mov_b32 s2, 0x48000
	s_nop 0
	v_addc_co_u32_e32 v13, vcc, 0, v61, vcc
	global_load_dwordx4 v[8:11], v[8:9], off nt
	ds_write_b128 v98, v[120:123] offset:5120
	global_load_dwordx4 v[16:19], v[12:13], off nt
	v_add_co_u32_e32 v12, vcc, s2, v60
	s_mov_b32 s2, 0x4a000
	s_nop 0
	v_addc_co_u32_e32 v13, vcc, 0, v61, vcc
	v_add_co_u32_e32 v20, vcc, s2, v60
	s_mov_b32 s2, 0x4c000
	s_nop 0
	v_addc_co_u32_e32 v21, vcc, 0, v61, vcc
	global_load_dwordx4 v[12:15], v[12:13], off nt
	s_waitcnt vmcnt(0)
	v_mul_f32_e32 v8, 0x43000000, v8
	global_load_dwordx4 v[24:27], v[20:21], off nt
	v_add_co_u32_e32 v20, vcc, s2, v60
	s_mov_b32 s2, 0x4e000
	s_nop 0
	v_addc_co_u32_e32 v21, vcc, 0, v61, vcc
	global_load_dwordx4 v[28:31], v[20:21], off nt
	v_add_co_u32_e32 v20, vcc, s2, v60
	s_mov_b32 s2, 0x50000
	s_nop 0
	v_addc_co_u32_e32 v21, vcc, 0, v61, vcc
	global_load_dwordx4 v[40:43], v[20:21], off nt
	v_add_co_u32_e32 v20, vcc, s2, v60
	s_mov_b32 s2, 0x52000
	s_nop 0
	v_addc_co_u32_e32 v21, vcc, 0, v61, vcc
	v_add_co_u32_e32 v32, vcc, s2, v60
	s_mov_b32 s2, 0x54000
	s_nop 0
	v_addc_co_u32_e32 v33, vcc, 0, v61, vcc
	v_add_co_u32_e32 v36, vcc, s2, v60
	s_mov_b32 s2, 0x56000
	s_nop 0
	v_addc_co_u32_e32 v37, vcc, 0, v61, vcc
	v_add_co_u32_e32 v44, vcc, s2, v60
	s_mov_b32 s2, 0x58000
	s_nop 0
	v_addc_co_u32_e32 v45, vcc, 0, v61, vcc
	global_load_dwordx4 v[36:39], v[36:37], off nt
	s_waitcnt vmcnt(5)
	v_mul_f32_e32 v16, 0x43000000, v16
	global_load_dwordx4 v[48:51], v[44:45], off nt
	v_add_co_u32_e32 v44, vcc, s2, v60
	global_load_dwordx4 v[0:3], v[0:1], off nt
	s_nop 0
	v_addc_co_u32_e32 v45, vcc, 0, v61, vcc
	global_load_dwordx4 v[4:7], v[4:5], off nt
	s_mov_b32 s2, 0x5a000
	v_add_co_u32_e32 v52, vcc, s2, v60
	global_load_dwordx4 v[20:23], v[20:21], off nt
	s_nop 0
	v_addc_co_u32_e32 v53, vcc, 0, v61, vcc
	global_load_dwordx4 v[32:35], v[32:33], off nt
	s_mov_b32 s2, 0x5c000
	global_load_dwordx4 v[44:47], v[44:45], off nt
	v_add_co_u32_e32 v56, vcc, s2, v60
	global_load_dwordx4 v[52:55], v[52:53], off nt
	s_nop 0
	v_addc_co_u32_e32 v57, vcc, 0, v61, vcc
	s_mov_b32 s2, 0x5e000
	v_add_co_u32_e32 v60, vcc, s2, v60
	global_load_dwordx4 v[56:59], v[56:57], off nt
	s_nop 0
	v_addc_co_u32_e32 v61, vcc, 0, v61, vcc
	global_load_dwordx4 v[60:63], v[60:61], off nt
	s_waitcnt vmcnt(0)
	v_mul_f32_e32 v0, 0x43000000, v0
	s_waitcnt vmcnt(6)
; #define LAS __attribute__((address_space(3)))
; __device__ __forceinline__ unsigned pk4_fp8(float x0, float x1, float x2, float x3) { int w = 0; w = __builtin_amdgcn_cvt_pk_fp8_f32(x0, x1, w, false); w = __builtin_amdgcn_cvt_pk_fp8_f32(x2, x3, w, true); return (unsigned)w; }
; __device__ __forceinline__ void transpose_item_fp8w(const float* W, int K, int N, unsigned char* WT, float q, LAS unsigned char* scr, int item, int lane) {
;     ...
;     for (int b = 0; b < 2; ++b) {
;         f32x4 x[16];
; #pragma unroll
;         for (int s_ = 0; s_ < 16; ++s_) x[s_] = *(const f32x4*)(src + (size_t)(32 * b + s_) * N);
; #pragma unroll
;         for (int i = 0; i < 4; ++i) {
;             u32x4 o;
;             o.x = pk4_fp8(x[0][i] * q, x[1][i] * q, x[2][i] * q, x[3][i] * q); o.y = pk4_fp8(x[4][i] * q, x[5][i] * q, x[6][i] * q, x[7][i] * q);
;             o.z = pk4_fp8(x[8][i] * q, x[9][i] * q, x[10][i] * q, x[11][i] * q); o.w = pk4_fp8(x[12][i] * q, x[13][i] * q, x[14][i] * q, x[15][i] * q);
;             *(LAS u32x4*)(scr + (l5 + 32 * i) * 80 + (2 * b + h) * 16) = o; }
;     }
;     asm volatile("s_waitcnt lgkmcnt(0)" ::: "memory");
; #pragma unroll
;     for (int qd = 0; qd < 8; ++qd) {
;         const int rho = 16 * qd + (lane >> 2), piece = lane & 3;
;         const u32x4 o = *(const LAS u32x4*)(scr + rho * 80 + piece * 16);
;         const int nl = 4 * (rho & 31) + (rho >> 5);
;         *(u32x4*)(WT + (size_t)(n0 + nl) * K + k0 + piece * 16) = o; }
	v_mul_f32_e32 v4, 0x43000000, v4
	v_cvt_pk_fp8_f32 v116, v0, v4
	v_mul_f32_e32 v0, 0x43000000, v12
	v_mul_f32_e32 v4, 0x43000000, v24
	v_cvt_pk_fp8_f32 v117, v0, v4
	s_waitcnt vmcnt(5)
	v_mul_f32_e32 v0, 0x43000000, v20
	v_cvt_pk_fp8_f32 v116, v8, v16 op_sel:[0,0,1]
	s_waitcnt vmcnt(4)
	v_mul_f32_e32 v4, 0x43000000, v32
	v_cvt_pk_fp8_f32 v118, v0, v4
	s_waitcnt vmcnt(3)
	v_mul_f32_e32 v0, 0x43000000, v44
	v_mul_f32_e32 v8, 0x43000000, v28
	v_mul_f32_e32 v12, 0x43000000, v40
	s_waitcnt vmcnt(2)
	v_mul_f32_e32 v4, 0x43000000, v52
	v_cvt_pk_fp8_f32 v119, v0, v4
	v_cvt_pk_fp8_f32 v117, v8, v12 op_sel:[0,0,1]
	v_mul_f32_e32 v8, 0x43000000, v36
	v_mul_f32_e32 v12, 0x43000000, v48
	v_cvt_pk_fp8_f32 v118, v8, v12 op_sel:[0,0,1]
	s_waitcnt vmcnt(1)
	v_mul_f32_e32 v8, 0x43000000, v56
	v_mul_f32_e32 v0, 0x43000000, v1
	v_mul_f32_e32 v1, 0x43000000, v5
	s_waitcnt vmcnt(0)
	v_mul_f32_e32 v12, 0x43000000, v60
	v_cvt_pk_fp8_f32 v119, v8, v12 op_sel:[0,0,1]
	v_mul_f32_e32 v4, 0x43000000, v9
	v_mul_f32_e32 v5, 0x43000000, v17
	ds_write_b128 v98, v[116:119] offset:32
	v_cvt_pk_fp8_f32 v116, v0, v1
	v_mul_f32_e32 v0, 0x43000000, v13
	v_mul_f32_e32 v1, 0x43000000, v25
	v_cvt_pk_fp8_f32 v117, v0, v1
	v_mul_f32_e32 v0, 0x43000000, v21
	v_mul_f32_e32 v1, 0x43000000, v33
	v_cvt_pk_fp8_f32 v118, v0, v1
	v_mul_f32_e32 v0, 0x43000000, v45
	v_mul_f32_e32 v1, 0x43000000, v53
	v_cvt_pk_fp8_f32 v119, v0, v1
	v_cvt_pk_fp8_f32 v116, v4, v5 op_sel:[0,0,1]
	v_mul_f32_e32 v4, 0x43000000, v29
	v_mul_f32_e32 v5, 0x43000000, v41
	v_cvt_pk_fp8_f32 v117, v4, v5 op_sel:[0,0,1]
	v_mul_f32_e32 v4, 0x43000000, v37
	v_mul_f32_e32 v5, 0x43000000, v49
	v_cvt_pk_fp8_f32 v118, v4, v5 op_sel:[0,0,1]
	v_mul_f32_e32 v4, 0x43000000, v57
	v_mul_f32_e32 v5, 0x43000000, v61
	v_cvt_pk_fp8_f32 v119, v4, v5 op_sel:[0,0,1]
	v_mul_f32_e32 v0, 0x43000000, v2
	v_mul_f32_e32 v1, 0x43000000, v6
	v_mul_f32_e32 v2, 0x43000000, v10
	ds_write_b128 v98, v[116:119] offset:2592
	v_cvt_pk_fp8_f32 v116, v0, v1
	v_mul_f32_e32 v0, 0x43000000, v14
	v_mul_f32_e32 v1, 0x43000000, v26
	v_cvt_pk_fp8_f32 v117, v0, v1
	v_mul_f32_e32 v0, 0x43000000, v22
	v_mul_f32_e32 v1, 0x43000000, v34
	v_cvt_pk_fp8_f32 v118, v0, v1
	v_mul_f32_e32 v0, 0x43000000, v46
	v_mul_f32_e32 v1, 0x43000000, v54
	v_mul_f32_e32 v4, 0x43000000, v18
	v_cvt_pk_fp8_f32 v119, v0, v1
	v_cvt_pk_fp8_f32 v116, v2, v4 op_sel:[0,0,1]
	v_mul_f32_e32 v2, 0x43000000, v30
	v_mul_f32_e32 v4, 0x43000000, v42
	v_cvt_pk_fp8_f32 v117, v2, v4 op_sel:[0,0,1]
	v_mul_f32_e32 v2, 0x43000000, v38
	v_mul_f32_e32 v4, 0x43000000, v50
	v_cvt_pk_fp8_f32 v118, v2, v4 op_sel:[0,0,1]
	v_mul_f32_e32 v2, 0x43000000, v58
	v_mul_f32_e32 v4, 0x43000000, v62
	v_cvt_pk_fp8_f32 v119, v2, v4 op_sel:[0,0,1]
	v_mul_f32_e32 v1, 0x43000000, v3
	v_mul_f32_e32 v2, 0x43000000, v7
	v_cvt_pk_fp8_f32 v0, v1, v2
	v_mul_f32_e32 v3, 0x43000000, v11
	v_mul_f32_e32 v4, 0x43000000, v19
	v_mul_f32_e32 v2, 0x43000000, v15
	v_cvt_pk_fp8_f32 v0, v3, v4 op_sel:[0,0,1]
	v_mul_f32_e32 v3, 0x43000000, v27
	v_cvt_pk_fp8_f32 v1, v2, v3
	v_mul_f32_e32 v4, 0x43000000, v31
	v_mul_f32_e32 v5, 0x43000000, v43
	v_mul_f32_e32 v3, 0x43000000, v23
	v_cvt_pk_fp8_f32 v1, v4, v5 op_sel:[0,0,1]
	v_mul_f32_e32 v4, 0x43000000, v35
	v_cvt_pk_fp8_f32 v2, v3, v4
	v_mul_f32_e32 v5, 0x43000000, v39
	v_mul_f32_e32 v6, 0x43000000, v51
	v_mul_f32_e32 v4, 0x43000000, v47
	v_cvt_pk_fp8_f32 v2, v5, v6 op_sel:[0,0,1]
	v_mul_f32_e32 v5, 0x43000000, v55
	v_cvt_pk_fp8_f32 v3, v4, v5
	v_mul_f32_e32 v6, 0x43000000, v59
	v_mul_f32_e32 v7, 0x43000000, v63
	ds_write_b128 v98, v[116:119] offset:5152
	v_cvt_pk_fp8_f32 v3, v6, v7 op_sel:[0,0,1]
	v_add_u32_e32 v6, s0, v102
	v_ashrrev_i32_e32 v7, 31, v6
	v_lshl_add_u64 v[4:5], s[10:11], 0, v[64:65]
	ds_write_b128 v98, v[0:3] offset:7712
	s_waitcnt lgkmcnt(0)
	ds_read_b128 v[0:3], v99
	v_lshlrev_b64 v[6:7], 10, v[6:7]
	v_lshl_add_u64 v[6:7], v[4:5], 0, v[6:7]
	s_waitcnt lgkmcnt(0)
	global_store_dwordx4 v[6:7], v[0:3], off nt
	ds_read_b128 v[0:3], v99 offset:1280
	v_add_u32_e32 v6, s0, v103
	v_ashrrev_i32_e32 v7, 31, v6
	v_lshlrev_b64 v[6:7], 10, v[6:7]
	v_lshl_add_u64 v[6:7], v[4:5], 0, v[6:7]
	s_waitcnt lgkmcnt(0)
	global_store_dwordx4 v[6:7], v[0:3], off nt
	ds_read_b128 v[0:3], v99 offset:2560
	v_add_u32_e32 v6, s0, v104
	v_ashrrev_i32_e32 v7, 31, v6
	v_lshlrev_b64 v[6:7], 10, v[6:7]
	v_lshl_add_u64 v[6:7], v[4:5], 0, v[6:7]
	s_waitcnt lgkmcnt(0)
	global_store_dwordx4 v[6:7], v[0:3], off nt
	ds_read_b128 v[0:3], v99 offset:3840
	v_add_u32_e32 v6, s0, v105
	v_ashrrev_i32_e32 v7, 31, v6
	v_lshlrev_b64 v[6:7], 10, v[6:7]
	v_lshl_add_u64 v[6:7], v[4:5], 0, v[6:7]
	s_waitcnt lgkmcnt(0)
	global_store_dwordx4 v[6:7], v[0:3], off nt
	ds_read_b128 v[0:3], v99 offset:5120
	v_add_u32_e32 v6, s0, v106
	v_ashrrev_i32_e32 v7, 31, v6
	v_lshlrev_b64 v[6:7], 10, v[6:7]
	v_lshl_add_u64 v[6:7], v[4:5], 0, v[6:7]
	s_waitcnt lgkmcnt(0)
	global_store_dwordx4 v[6:7], v[0:3], off nt
	ds_read_b128 v[0:3], v99 offset:6400
	v_add_u32_e32 v6, s0, v107
	v_ashrrev_i32_e32 v7, 31, v6
	v_lshlrev_b64 v[6:7], 10, v[6:7]
	v_lshl_add_u64 v[6:7], v[4:5], 0, v[6:7]
	s_waitcnt lgkmcnt(0)
	global_store_dwordx4 v[6:7], v[0:3], off nt
	ds_read_b128 v[0:3], v99 offset:7680
	v_add_u32_e32 v6, s0, v108
	v_ashrrev_i32_e32 v7, 31, v6
	v_lshlrev_b64 v[6:7], 10, v[6:7]
	v_lshl_add_u64 v[6:7], v[4:5], 0, v[6:7]
	s_waitcnt lgkmcnt(0)
	global_store_dwordx4 v[6:7], v[0:3], off nt
	ds_read_b128 v[0:3], v99 offset:8960
	v_add_u32_e32 v6, s0, v109
	v_ashrrev_i32_e32 v7, 31, v6
	v_lshlrev_b64 v[6:7], 10, v[6:7]
	v_lshl_add_u64 v[4:5], v[4:5], 0, v[6:7]
	s_waitcnt lgkmcnt(0)
	global_store_dwordx4 v[4:5], v[0:3], off nt
	s_waitcnt lgkmcnt(0)
	s_mov_b64 s[0:1], 0

; #define LAS __attribute__((address_space(3)))
; __device__ __forceinline__ void transpose_item_fp8(const float* W, int K, int N, unsigned char* WT, float q, LAS float* scr, int item, int lane) {
;     const int nblk = N / 32, kb = item / nblk, nb = item % nblk, k0 = 64 * kb, n0 = 32 * nb;
; #pragma unroll 8
;     for (int i = 0; i < 32; ++i) { const int kk = 2 * i + (lane >> 5); scr[kk * 33 + (lane & 31)] = W[(size_t)(k0 + kk) * N + n0 + (lane & 31)]; }
;     asm volatile("s_waitcnt lgkmcnt(0)" ::: "memory");
.LBB0_361:
	s_lshl_b32 s11, s1, 1
	s_lshl_b32 s12, s0, 1
	v_add_u32_e32 v18, s11, v2
	v_add_u32_e32 v20, s12, v3
	v_mad_i64_i32 v[18:19], s[14:15], v18, s82, v[0:1]
	v_mad_i64_i32 v[20:21], s[14:15], v20, s82, v[0:1]
	global_load_dword v24, v[18:19], off nt
	global_load_dword v25, v[20:21], off nt
	v_add_u32_e32 v23, s11, v96
	v_add_u32_e32 v22, s12, v69
	v_mad_u64_u32 v[18:19], s[14:15], v23, s83, v[68:69]
	v_mad_u64_u32 v[20:21], s[14:15], v22, s83, v[68:69]
	v_add_u32_e32 v23, s11, v84
	v_add_u32_e32 v22, s12, v85
	s_add_i32 s1, s1, 16
	s_add_i32 s0, s0, 16
	s_add_i32 s9, s9, -16
	s_cmp_lg_u32 s9, 0
	s_waitcnt vmcnt(0)
	ds_write_b32 v18, v24
	s_waitcnt vmcnt(0)
	ds_write_b32 v20, v25
	v_add_u32_e32 v18, s11, v4
	v_add_u32_e32 v20, s12, v5
	v_mad_i64_i32 v[18:19], s[14:15], v18, s82, v[0:1]
	v_mad_i64_i32 v[20:21], s[14:15], v20, s82, v[0:1]
	global_load_dword v24, v[18:19], off nt
	global_load_dword v25, v[20:21], off nt
	v_mad_u64_u32 v[18:19], s[14:15], v23, s83, v[68:69]
	v_mad_u64_u32 v[20:21], s[14:15], v22, s83, v[68:69]
	v_add_u32_e32 v23, s11, v86
	v_add_u32_e32 v22, s12, v87
	s_waitcnt vmcnt(0)
	ds_write_b32 v18, v24
	s_waitcnt vmcnt(0)
	ds_write_b32 v20, v25
	v_add_u32_e32 v18, s11, v6
	v_add_u32_e32 v20, s12, v7
	v_mad_i64_i32 v[18:19], s[14:15], v18, s82, v[0:1]
	v_mad_i64_i32 v[20:21], s[14:15], v20, s82, v[0:1]
	global_load_dword v24, v[18:19], off nt
	global_load_dword v25, v[20:21], off nt
	v_mad_u64_u32 v[18:19], s[14:15], v23, s83, v[68:69]
	v_mad_u64_u32 v[20:21], s[14:15], v22, s83, v[68:69]
	v_add_u32_e32 v23, s11, v88
	v_add_u32_e32 v22, s12, v89
	s_waitcnt vmcnt(0)
	ds_write_b32 v18, v24
	s_waitcnt vmcnt(0)
	ds_write_b32 v20, v25
	v_add_u32_e32 v18, s11, v8
	v_add_u32_e32 v20, s12, v9
	v_mad_i64_i32 v[18:19], s[14:15], v18, s82, v[0:1]
	v_mad_i64_i32 v[20:21], s[14:15], v20, s82, v[0:1]
	global_load_dword v24, v[18:19], off nt
	global_load_dword v25, v[20:21], off nt
	v_mad_u64_u32 v[18:19], s[14:15], v23, s83, v[68:69]
	v_mad_u64_u32 v[20:21], s[14:15], v22, s83, v[68:69]
	v_add_u32_e32 v23, s11, v90
	v_add_u32_e32 v22, s12, v91
	s_waitcnt vmcnt(0)
	ds_write_b32 v18, v24
	s_waitcnt vmcnt(0)
	ds_write_b32 v20, v25
	v_add_u32_e32 v18, s11, v10
	v_add_u32_e32 v20, s12, v11
	v_mad_i64_i32 v[18:19], s[14:15], v18, s82, v[0:1]
	v_mad_i64_i32 v[20:21], s[14:15], v20, s82, v[0:1]
	global_load_dword v24, v[18:19], off nt
	global_load_dword v25, v[20:21], off nt
	v_mad_u64_u32 v[18:19], s[14:15], v23, s83, v[68:69]
	v_mad_u64_u32 v[20:21], s[14:15], v22, s83, v[68:69]
	v_add_u32_e32 v23, s11, v92
	v_add_u32_e32 v22, s12, v93
	s_waitcnt vmcnt(0)
	ds_write_b32 v18, v24
	s_waitcnt vmcnt(0)
	ds_write_b32 v20, v25
	v_add_u32_e32 v18, s11, v12
	v_add_u32_e32 v20, s12, v13
	v_mad_i64_i32 v[18:19], s[14:15], v18, s82, v[0:1]
	v_mad_i64_i32 v[20:21], s[14:15], v20, s82, v[0:1]
	global_load_dword v24, v[18:19], off nt
	global_load_dword v25, v[20:21], off nt
	v_mad_u64_u32 v[18:19], s[14:15], v23, s83, v[68:69]
	v_mad_u64_u32 v[20:21], s[14:15], v22, s83, v[68:69]
	v_add_u32_e32 v23, s11, v94
	v_add_u32_e32 v22, s12, v95
	s_waitcnt vmcnt(0)
	ds_write_b32 v18, v24
	s_waitcnt vmcnt(0)
	ds_write_b32 v20, v25
	v_add_u32_e32 v18, s11, v14
	v_add_u32_e32 v20, s12, v15
	v_mad_i64_i32 v[18:19], s[14:15], v18, s82, v[0:1]
	v_mad_i64_i32 v[20:21], s[14:15], v20, s82, v[0:1]
	global_load_dword v24, v[18:19], off nt
	global_load_dword v25, v[20:21], off nt
	v_mad_u64_u32 v[18:19], s[14:15], v23, s83, v[68:69]
	v_mad_u64_u32 v[20:21], s[14:15], v22, s83, v[68:69]
	v_add_u32_e32 v22, s12, v97
	v_add_u32_e32 v23, s11, v100
	s_waitcnt vmcnt(0)
	ds_write_b32 v18, v24
	s_waitcnt vmcnt(0)
	ds_write_b32 v20, v25
	v_add_u32_e32 v18, s11, v16
	v_add_u32_e32 v20, s12, v17
	v_mad_i64_i32 v[18:19], s[12:13], v18, s82, v[0:1]
	v_mad_i64_i32 v[20:21], s[12:13], v20, s82, v[0:1]
	global_load_dword v24, v[18:19], off nt
	global_load_dword v25, v[20:21], off nt
	v_mad_u64_u32 v[18:19], s[12:13], v23, s83, v[68:69]
	v_mad_u64_u32 v[20:21], s[12:13], v22, s83, v[68:69]
	s_waitcnt vmcnt(0)
	ds_write_b32 v18, v24
	s_waitcnt vmcnt(0)
	ds_write_b32 v20, v25
	s_cbranch_scc1 .LBB0_361
; #define LAS __attribute__((address_space(3)))
; __device__ __forceinline__ unsigned pk4_fp8(float x0, float x1, float x2, float x3) { int w = 0; w = __builtin_amdgcn_cvt_pk_fp8_f32(x0, x1, w, false); w = __builtin_amdgcn_cvt_pk_fp8_f32(x2, x3, w, true); return (unsigned)w; }
; __device__ __forceinline__ void transpose_item_fp8(const float* W, int K, int N, unsigned char* WT, float q, LAS float* scr, int item, int lane) {
;     ...
;     const int c = lane & 7;
; #pragma unroll
;     for (int j = 0; j < 4; ++j) { const int n = (lane >> 3) + 8 * j; const LAS float* s = scr + (8 * c) * 33 + n;
;         u32x2 o; o.x = pk4_fp8(s[0 * 33] * q, s[1 * 33] * q, s[2 * 33] * q, s[3 * 33] * q); o.y = pk4_fp8(s[4 * 33] * q, s[5 * 33] * q, s[6 * 33] * q, s[7 * 33] * q);
;         *(u32x2*)(WT + (size_t)(n0 + n) * K + k0 + 8 * c) = o; }
;     asm volatile("s_waitcnt lgkmcnt(0)" ::: "memory");
; }
	s_waitcnt lgkmcnt(0)
	ds_read2_b32 v[2:3], v111 offset1:8
	ds_read2_b32 v[4:5], v111 offset0:33 offset1:41
	ds_read2_b32 v[12:13], v111 offset0:132 offset1:140
	ds_read2_b32 v[14:15], v111 offset0:165 offset1:173
	ds_read2_b32 v[6:7], v111 offset0:66 offset1:74
	ds_read2_b32 v[8:9], v111 offset0:99 offset1:107
	s_waitcnt lgkmcnt(5)
	v_mul_f32_e32 v2, 0x43000000, v2
	s_waitcnt lgkmcnt(4)
	v_mul_f32_e32 v4, 0x43000000, v4
	ds_read2_b32 v[16:17], v111 offset0:198 offset1:206
	ds_read2_b32 v[18:19], v111 offset0:231 offset1:239
	v_cvt_pk_fp8_f32 v10, v2, v4
	s_waitcnt lgkmcnt(5)
	v_mul_f32_e32 v2, 0x43000000, v12
	s_waitcnt lgkmcnt(4)
	v_mul_f32_e32 v4, 0x43000000, v14
	v_cvt_pk_fp8_f32 v11, v2, v4
	v_mul_f32_e32 v3, 0x43000000, v3
	v_mul_f32_e32 v4, 0x43000000, v5
	v_cvt_pk_fp8_f32 v2, v3, v4
	s_waitcnt lgkmcnt(3)
	v_mul_f32_e32 v6, 0x43000000, v6
	s_waitcnt lgkmcnt(2)
	v_mul_f32_e32 v8, 0x43000000, v8
	v_cvt_pk_fp8_f32 v10, v6, v8 op_sel:[0,0,1]
	s_waitcnt lgkmcnt(1)
	v_mul_f32_e32 v6, 0x43000000, v16
	s_waitcnt lgkmcnt(0)
	v_mul_f32_e32 v8, 0x43000000, v18
	v_cvt_pk_fp8_f32 v11, v6, v8 op_sel:[0,0,1]
	v_mul_f32_e32 v5, 0x43000000, v7
	v_mul_f32_e32 v6, 0x43000000, v9
	v_cvt_pk_fp8_f32 v2, v5, v6 op_sel:[0,0,1]
	v_mul_f32_e32 v4, 0x43000000, v13
	v_mul_f32_e32 v5, 0x43000000, v15
	v_cvt_pk_fp8_f32 v3, v4, v5
	v_mul_f32_e32 v6, 0x43000000, v17
	v_mul_f32_e32 v7, 0x43000000, v19
	v_add_u32_e32 v4, s8, v112
	v_cvt_pk_fp8_f32 v3, v6, v7 op_sel:[0,0,1]
	s_ashr_i32 s11, s10, 31
	v_ashrrev_i32_e32 v5, 31, v4
	v_lshl_add_u64 v[0:1], v[82:83], 0, s[10:11]
	v_lshlrev_b64 v[4:5], 10, v[4:5]
	v_lshl_add_u64 v[4:5], v[0:1], 0, v[4:5]
	global_store_dwordx2 v[4:5], v[2:3], off nt
	ds_read2_b32 v[2:3], v111 offset0:16 offset1:24
	ds_read2_b32 v[4:5], v111 offset0:49 offset1:57
	v_add_u32_e32 v20, s8, v110
	ds_read2_b32 v[12:13], v111 offset0:148 offset1:156
	ds_read2_b32 v[14:15], v111 offset0:181 offset1:189
	v_ashrrev_i32_e32 v21, 31, v20
	v_lshlrev_b64 v[20:21], 10, v[20:21]
	v_lshl_add_u64 v[20:21], v[0:1], 0, v[20:21]
	ds_read2_b32 v[6:7], v111 offset0:82 offset1:90
	ds_read2_b32 v[8:9], v111 offset0:115 offset1:123
	global_store_dwordx2 v[20:21], v[10:11], off nt
	s_waitcnt lgkmcnt(5)
	v_mul_f32_e32 v2, 0x43000000, v2
	s_waitcnt lgkmcnt(4)
	v_mul_f32_e32 v4, 0x43000000, v4
	ds_read2_b32 v[16:17], v111 offset0:214 offset1:222
	ds_read2_b32 v[18:19], v111 offset0:247 offset1:255
	v_cvt_pk_fp8_f32 v10, v2, v4
	s_waitcnt lgkmcnt(5)
	v_mul_f32_e32 v2, 0x43000000, v12
	s_waitcnt lgkmcnt(4)
	v_mul_f32_e32 v4, 0x43000000, v14
	v_cvt_pk_fp8_f32 v11, v2, v4
	v_mul_f32_e32 v3, 0x43000000, v3
	v_mul_f32_e32 v4, 0x43000000, v5
	v_cvt_pk_fp8_f32 v2, v3, v4
	s_waitcnt lgkmcnt(3)
	v_mul_f32_e32 v6, 0x43000000, v6
	s_waitcnt lgkmcnt(2)
	v_mul_f32_e32 v8, 0x43000000, v8
	v_cvt_pk_fp8_f32 v10, v6, v8 op_sel:[0,0,1]
	s_waitcnt lgkmcnt(1)
	v_mul_f32_e32 v6, 0x43000000, v16
	s_waitcnt lgkmcnt(0)
	v_mul_f32_e32 v8, 0x43000000, v18
	v_cvt_pk_fp8_f32 v11, v6, v8 op_sel:[0,0,1]
	v_mul_f32_e32 v5, 0x43000000, v7
	v_mul_f32_e32 v6, 0x43000000, v9
	v_cvt_pk_fp8_f32 v2, v5, v6 op_sel:[0,0,1]
	v_mul_f32_e32 v4, 0x43000000, v13
	v_mul_f32_e32 v5, 0x43000000, v15
	v_cvt_pk_fp8_f32 v3, v4, v5
	v_mul_f32_e32 v6, 0x43000000, v17
	v_mul_f32_e32 v7, 0x43000000, v19
	v_add_u32_e32 v20, s8, v113
	v_cvt_pk_fp8_f32 v3, v6, v7 op_sel:[0,0,1]
	v_add_u32_e32 v4, s8, v114
	v_ashrrev_i32_e32 v21, 31, v20
	v_ashrrev_i32_e32 v5, 31, v4
	v_lshlrev_b64 v[20:21], 10, v[20:21]
	v_lshlrev_b64 v[4:5], 10, v[4:5]
	v_lshl_add_u64 v[20:21], v[0:1], 0, v[20:21]
	v_lshl_add_u64 v[0:1], v[0:1], 0, v[4:5]
	global_store_dwordx2 v[20:21], v[10:11], off nt
	global_store_dwordx2 v[0:1], v[2:3], off nt
	s_waitcnt lgkmcnt(0)
	s_branch .LBB0_330

; __device__ __forceinline__ unsigned pk4_fp8(float x0, float x1, float x2, float x3) { int w = 0; w = __builtin_amdgcn_cvt_pk_fp8_f32(x0, x1, w, false); w = __builtin_amdgcn_cvt_pk_fp8_f32(x2, x3, w, true); return (unsigned)w; }
;     __device__ __forceinline__ void operator()(const f32x4 (&acc)[2][2][4][2], const Unit& u, int wr, int wc, int fr, int fq) const {
;         const int row0 = u.pm * BM + wr * 64 + fr, cw = wc * 32 + 8 * fq;
;         unsigned char* base = KB + (u.pn * 2) * 192 + cw;
; #pragma unroll
;         for (int ai = 0; ai < 2; ++ai)
; #pragma unroll
;             for (int m = 0; m < 4; ++m) { unsigned char* rowp = base + (size_t)(row0 + ai * HALF + m * 16) * 768;
; #pragma unroll
;                 for (int bj = 0; bj < 2; ++bj) { const f32x4 v0 = acc[ai][bj][m][0] * QK_Q, v1 = acc[ai][bj][m][1] * QK_Q;
;                     u32x2 w; w.x = pk4_fp8(v0[0], v0[1], v0[2], v0[3]); w.y = pk4_fp8(v1[0], v1[1], v1[2], v1[3]);
;                     *(u32x2*)(rowp + bj * 192) = w; } }
;     }
.LBB0_456:
	s_mov_b32 s4, 0x41000000
	v_pk_mul_f32 v[124:125], v[124:125], s[4:5] op_sel_hi:[1,0]
	v_cvt_pk_fp8_f32 v146, v124, v125
	v_pk_mul_f32 v[120:121], v[120:121], s[4:5] op_sel_hi:[1,0]
	v_cvt_pk_fp8_f32 v147, v120, v121
	v_pk_mul_f32 v[120:121], v[126:127], s[4:5] op_sel_hi:[1,0]
	v_pk_mul_f32 v[116:117], v[116:117], s[4:5] op_sel_hi:[1,0]
	v_cvt_pk_fp8_f32 v146, v120, v121 op_sel:[0,0,1]
	v_pk_mul_f32 v[108:109], v[108:109], s[4:5] op_sel_hi:[1,0]
	v_cvt_pk_fp8_f32 v120, v116, v117
	v_cvt_pk_fp8_f32 v121, v108, v109
	v_pk_mul_f32 v[122:123], v[122:123], s[4:5] op_sel_hi:[1,0]
	s_mul_i32 s0, s69, 0x180
	v_cvt_pk_fp8_f32 v147, v122, v123 op_sel:[0,0,1]
	v_pk_mul_f32 v[108:109], v[118:119], s[4:5] op_sel_hi:[1,0]
	v_pk_mul_f32 v[110:111], v[110:111], s[4:5] op_sel_hi:[1,0]
	s_ashr_i32 s1, s0, 31
	v_cvt_pk_fp8_f32 v120, v108, v109 op_sel:[0,0,1]
	v_cvt_pk_fp8_f32 v121, v110, v111 op_sel:[0,0,1]
	v_lshl_add_u32 v145, s70, 8, v142
	v_lshl_add_u64 v[140:141], v[138:139], 0, s[0:1]
	s_movk_i32 s2, 0x300
	v_mad_i64_i32 v[108:109], s[0:1], v145, s2, v[140:141]
	global_store_dwordx2 v[108:109], v[146:147], off
	global_store_dwordx2 v[108:109], v[120:121], off offset:192
	v_pk_mul_f32 v[108:109], v[112:113], s[4:5] op_sel_hi:[1,0]
	v_cvt_pk_fp8_f32 v110, v108, v109
	v_pk_mul_f32 v[104:105], v[104:105], s[4:5] op_sel_hi:[1,0]
	v_cvt_pk_fp8_f32 v111, v104, v105
	v_pk_mul_f32 v[104:105], v[114:115], s[4:5] op_sel_hi:[1,0]
	v_pk_mul_f32 v[100:101], v[100:101], s[4:5] op_sel_hi:[1,0]
	v_cvt_pk_fp8_f32 v110, v104, v105 op_sel:[0,0,1]
	v_pk_mul_f32 v[92:93], v[92:93], s[4:5] op_sel_hi:[1,0]
	v_cvt_pk_fp8_f32 v104, v100, v101
	v_cvt_pk_fp8_f32 v105, v92, v93
	v_pk_mul_f32 v[106:107], v[106:107], s[4:5] op_sel_hi:[1,0]
	v_pk_mul_f32 v[92:93], v[102:103], s[4:5] op_sel_hi:[1,0]
	v_cvt_pk_fp8_f32 v111, v106, v107 op_sel:[0,0,1]
	v_pk_mul_f32 v[94:95], v[94:95], s[4:5] op_sel_hi:[1,0]
	v_cvt_pk_fp8_f32 v104, v92, v93 op_sel:[0,0,1]
	v_cvt_pk_fp8_f32 v105, v94, v95 op_sel:[0,0,1]
	v_or_b32_e32 v116, 16, v145
	v_mad_i64_i32 v[92:93], s[0:1], v116, s2, v[140:141]
	global_store_dwordx2 v[92:93], v[110:111], off
	global_store_dwordx2 v[92:93], v[104:105], off offset:192
	v_pk_mul_f32 v[92:93], v[96:97], s[4:5] op_sel_hi:[1,0]
	v_cvt_pk_fp8_f32 v94, v92, v93
	v_pk_mul_f32 v[88:89], v[88:89], s[4:5] op_sel_hi:[1,0]
	v_cvt_pk_fp8_f32 v95, v88, v89
	v_pk_mul_f32 v[88:89], v[98:99], s[4:5] op_sel_hi:[1,0]
	v_pk_mul_f32 v[84:85], v[84:85], s[4:5] op_sel_hi:[1,0]
	v_cvt_pk_fp8_f32 v94, v88, v89 op_sel:[0,0,1]
	v_pk_mul_f32 v[76:77], v[76:77], s[4:5] op_sel_hi:[1,0]
	v_cvt_pk_fp8_f32 v88, v84, v85
	v_cvt_pk_fp8_f32 v89, v76, v77
	v_pk_mul_f32 v[90:91], v[90:91], s[4:5] op_sel_hi:[1,0]
	v_pk_mul_f32 v[76:77], v[86:87], s[4:5] op_sel_hi:[1,0]
	v_cvt_pk_fp8_f32 v95, v90, v91 op_sel:[0,0,1]
	v_pk_mul_f32 v[78:79], v[78:79], s[4:5] op_sel_hi:[1,0]
	v_cvt_pk_fp8_f32 v88, v76, v77 op_sel:[0,0,1]
	v_cvt_pk_fp8_f32 v89, v78, v79 op_sel:[0,0,1]
	v_or_b32_e32 v100, 32, v145
	v_mad_i64_i32 v[76:77], s[0:1], v100, s2, v[140:141]
	global_store_dwordx2 v[76:77], v[94:95], off
	global_store_dwordx2 v[76:77], v[88:89], off offset:192
	v_pk_mul_f32 v[76:77], v[80:81], s[4:5] op_sel_hi:[1,0]
	v_cvt_pk_fp8_f32 v78, v76, v77
	v_pk_mul_f32 v[72:73], v[72:73], s[4:5] op_sel_hi:[1,0]
	v_cvt_pk_fp8_f32 v79, v72, v73
	v_pk_mul_f32 v[72:73], v[82:83], s[4:5] op_sel_hi:[1,0]
	v_pk_mul_f32 v[68:69], v[68:69], s[4:5] op_sel_hi:[1,0]
	v_cvt_pk_fp8_f32 v78, v72, v73 op_sel:[0,0,1]
	v_pk_mul_f32 v[64:65], v[64:65], s[4:5] op_sel_hi:[1,0]
	v_cvt_pk_fp8_f32 v72, v68, v69
	v_cvt_pk_fp8_f32 v73, v64, v65
	v_pk_mul_f32 v[74:75], v[74:75], s[4:5] op_sel_hi:[1,0]
	v_pk_mul_f32 v[64:65], v[70:71], s[4:5] op_sel_hi:[1,0]
	v_cvt_pk_fp8_f32 v79, v74, v75 op_sel:[0,0,1]
	v_pk_mul_f32 v[66:67], v[66:67], s[4:5] op_sel_hi:[1,0]
	v_cvt_pk_fp8_f32 v72, v64, v65 op_sel:[0,0,1]
	v_cvt_pk_fp8_f32 v73, v66, v67 op_sel:[0,0,1]
	v_or_b32_e32 v84, 48, v145
	v_mad_i64_i32 v[64:65], s[0:1], v84, s2, v[140:141]
	global_store_dwordx2 v[64:65], v[78:79], off
	global_store_dwordx2 v[64:65], v[72:73], off offset:192
; #define LAS __attribute__((address_space(3)))
; __device__ __forceinline__ unsigned pk4_fp8(float x0, float x1, float x2, float x3) { int w = 0; w = __builtin_amdgcn_cvt_pk_fp8_f32(x0, x1, w, false); w = __builtin_amdgcn_cvt_pk_fp8_f32(x2, x3, w, true); return (unsigned)w; }
; #define PG8_BAR __builtin_amdgcn_s_barrier()
; #define PG8_SCHED __builtin_amdgcn_sched_barrier(0)
; template <class Epi, class Sched, bool GATHER, bool FP8 = false>
; __device__ __forceinline__ void gemm_phase(LAS unsigned char* lds, const Gemm g, const Sched& S, const Epi& E, const int wave_s) {
;     ...
;         if (wr == 0) PG8_BAR;
;         if constexpr (FP8) { asm volatile("s_nop 15\n\ts_nop 15" ::: "memory"); PG8_SCHED; }
;         if constexpr (Epi::BIAS_LDS) E(acc, cur, wr, wc, fr, fq, (const LAS float*)(lds + Epi::BIAS_OFF + (ui & 1) * 1024)); else E(acc, cur, wr, wc, fr, fq);
;         if (!has_next) break;
;     __device__ __forceinline__ void operator()(const f32x4 (&acc)[2][2][4][2], const Unit& u, int wr, int wc, int fr, int fq) const {
;         const int row0 = u.pm * BM + wr * 64 + fr, cw = wc * 32 + 8 * fq;
;         unsigned char* base = KB + (u.pn * 2) * 192 + cw;
; #pragma unroll
;         for (int ai = 0; ai < 2; ++ai)
; #pragma unroll
;             for (int m = 0; m < 4; ++m) { unsigned char* rowp = base + (size_t)(row0 + ai * HALF + m * 16) * 768;
; #pragma unroll
;                 for (int bj = 0; bj < 2; ++bj) { const f32x4 v0 = acc[ai][bj][m][0] * QK_Q, v1 = acc[ai][bj][m][1] * QK_Q;
;                     u32x2 w; w.x = pk4_fp8(v0[0], v0[1], v0[2], v0[3]); w.y = pk4_fp8(v1[0], v1[1], v1[2], v1[3]);
;                     *(u32x2*)(rowp + bj * 192) = w; } }
;     }
	v_pk_mul_f32 v[60:61], v[60:61], s[4:5] op_sel_hi:[1,0]
	v_cvt_pk_fp8_f32 v64, v60, v61
	v_pk_mul_f32 v[56:57], v[56:57], s[4:5] op_sel_hi:[1,0]
	v_cvt_pk_fp8_f32 v65, v56, v57
	v_pk_mul_f32 v[56:57], v[62:63], s[4:5] op_sel_hi:[1,0]
	v_pk_mul_f32 v[44:45], v[44:45], s[4:5] op_sel_hi:[1,0]
	v_cvt_pk_fp8_f32 v64, v56, v57 op_sel:[0,0,1]
	v_pk_mul_f32 v[36:37], v[36:37], s[4:5] op_sel_hi:[1,0]
	v_cvt_pk_fp8_f32 v56, v44, v45
	v_cvt_pk_fp8_f32 v57, v36, v37
	v_pk_mul_f32 v[58:59], v[58:59], s[4:5] op_sel_hi:[1,0]
	v_pk_mul_f32 v[36:37], v[46:47], s[4:5] op_sel_hi:[1,0]
	v_cvt_pk_fp8_f32 v65, v58, v59 op_sel:[0,0,1]
	v_pk_mul_f32 v[38:39], v[38:39], s[4:5] op_sel_hi:[1,0]
	v_cvt_pk_fp8_f32 v56, v36, v37 op_sel:[0,0,1]
	v_cvt_pk_fp8_f32 v57, v38, v39 op_sel:[0,0,1]
	v_add_u32_e32 v66, 0x80, v145
	v_mad_i64_i32 v[36:37], s[0:1], v66, s2, v[140:141]
	global_store_dwordx2 v[36:37], v[64:65], off
	global_store_dwordx2 v[36:37], v[56:57], off offset:192
	v_pk_mul_f32 v[36:37], v[40:41], s[4:5] op_sel_hi:[1,0]
	v_cvt_pk_fp8_f32 v38, v36, v37
	v_pk_mul_f32 v[32:33], v[32:33], s[4:5] op_sel_hi:[1,0]
	v_cvt_pk_fp8_f32 v39, v32, v33
	v_pk_mul_f32 v[32:33], v[42:43], s[4:5] op_sel_hi:[1,0]
	v_pk_mul_f32 v[20:21], v[20:21], s[4:5] op_sel_hi:[1,0]
	v_cvt_pk_fp8_f32 v38, v32, v33 op_sel:[0,0,1]
	v_pk_mul_f32 v[8:9], v[8:9], s[4:5] op_sel_hi:[1,0]
	v_cvt_pk_fp8_f32 v32, v20, v21
	v_cvt_pk_fp8_f32 v33, v8, v9
	v_pk_mul_f32 v[34:35], v[34:35], s[4:5] op_sel_hi:[1,0]
	v_pk_mul_f32 v[8:9], v[22:23], s[4:5] op_sel_hi:[1,0]
	v_cvt_pk_fp8_f32 v39, v34, v35 op_sel:[0,0,1]
	v_pk_mul_f32 v[10:11], v[10:11], s[4:5] op_sel_hi:[1,0]
	v_cvt_pk_fp8_f32 v32, v8, v9 op_sel:[0,0,1]
	v_cvt_pk_fp8_f32 v33, v10, v11 op_sel:[0,0,1]
	v_add_u32_e32 v44, 0x90, v145
	v_mad_i64_i32 v[8:9], s[0:1], v44, s2, v[140:141]
	global_store_dwordx2 v[8:9], v[38:39], off
	global_store_dwordx2 v[8:9], v[32:33], off offset:192
	v_pk_mul_f32 v[8:9], v[16:17], s[4:5] op_sel_hi:[1,0]
	v_pk_mul_f32 v[10:11], v[12:13], s[4:5] op_sel_hi:[1,0]
	v_cvt_pk_fp8_f32 v12, v8, v9
	v_cvt_pk_fp8_f32 v13, v10, v11
	v_pk_mul_f32 v[8:9], v[18:19], s[4:5] op_sel_hi:[1,0]
	v_pk_mul_f32 v[10:11], v[14:15], s[4:5] op_sel_hi:[1,0]
	v_cvt_pk_fp8_f32 v12, v8, v9 op_sel:[0,0,1]
	v_cvt_pk_fp8_f32 v13, v10, v11 op_sel:[0,0,1]
	v_pk_mul_f32 v[8:9], v[48:49], s[4:5] op_sel_hi:[1,0]
	v_pk_mul_f32 v[10:11], v[52:53], s[4:5] op_sel_hi:[1,0]
	v_cvt_pk_fp8_f32 v14, v8, v9
	v_cvt_pk_fp8_f32 v15, v10, v11
	v_pk_mul_f32 v[8:9], v[50:51], s[4:5] op_sel_hi:[1,0]
	v_pk_mul_f32 v[10:11], v[54:55], s[4:5] op_sel_hi:[1,0]
	v_cvt_pk_fp8_f32 v14, v8, v9 op_sel:[0,0,1]
	v_cvt_pk_fp8_f32 v15, v10, v11 op_sel:[0,0,1]
	v_add_u32_e32 v20, 0xa0, v145
	v_mad_i64_i32 v[8:9], s[0:1], v20, s2, v[140:141]
	global_store_dwordx2 v[8:9], v[12:13], off
	global_store_dwordx2 v[8:9], v[14:15], off offset:192
	v_pk_mul_f32 v[4:5], v[4:5], s[4:5] op_sel_hi:[1,0]
	v_pk_mul_f32 v[0:1], v[0:1], s[4:5] op_sel_hi:[1,0]
	v_cvt_pk_fp8_f32 v8, v4, v5
	v_cvt_pk_fp8_f32 v9, v0, v1
	v_pk_mul_f32 v[0:1], v[6:7], s[4:5] op_sel_hi:[1,0]
	v_pk_mul_f32 v[2:3], v[2:3], s[4:5] op_sel_hi:[1,0]
	v_cvt_pk_fp8_f32 v8, v0, v1 op_sel:[0,0,1]
	v_cvt_pk_fp8_f32 v9, v2, v3 op_sel:[0,0,1]
	v_pk_mul_f32 v[0:1], v[24:25], s[4:5] op_sel_hi:[1,0]
	v_pk_mul_f32 v[2:3], v[28:29], s[4:5] op_sel_hi:[1,0]
	v_cvt_pk_fp8_f32 v4, v0, v1
	v_cvt_pk_fp8_f32 v5, v2, v3
	v_pk_mul_f32 v[0:1], v[26:27], s[4:5] op_sel_hi:[1,0]
	v_pk_mul_f32 v[2:3], v[30:31], s[4:5] op_sel_hi:[1,0]
	v_add_u32_e32 v10, 0xb0, v145
	v_cvt_pk_fp8_f32 v4, v0, v1 op_sel:[0,0,1]
	v_cvt_pk_fp8_f32 v5, v2, v3 op_sel:[0,0,1]
	v_mad_i64_i32 v[0:1], s[0:1], v10, s2, v[140:141]
	v_readlane_b32 s72, v254, 26
	s_andn2_b64 vcc, exec, s[42:43]
	s_mov_b64 s[0:1], -1
	v_readlane_b32 s73, v254, 27
	v_readlane_b32 s74, v254, 28
	v_readlane_b32 s76, v254, 29
	global_store_dwordx2 v[0:1], v[8:9], off
	global_store_dwordx2 v[0:1], v[4:5], off offset:192
	v_readlane_b32 s77, v254, 30
	s_cbranch_vccnz .LBB0_449
	s_andn2_b64 vcc, exec, s[8:9]
	s_cbranch_vccnz .LBB0_448
	s_barrier
	s_branch .LBB0_448

; __device__ __forceinline__ unsigned pk4_fp8(float x0, float x1, float x2, float x3) { int w = 0; w = __builtin_amdgcn_cvt_pk_fp8_f32(x0, x1, w, false); w = __builtin_amdgcn_cvt_pk_fp8_f32(x2, x3, w, true); return (unsigned)w; }
;     __device__ __forceinline__ void operator()(const f32x4 (&acc)[2][2][4][2], const Unit& u, int wr, int wc, int fr, int fq) const {
;         const int row0 = u.pm * BM + wr * 64 + fr, col0 = u.pn * BM + wc * 32 + 8 * fq;
; #pragma unroll
;         for (int bj = 0; bj < 2; ++bj) {
;             const int n = col0 + bj * HALF;
;             const int b = (n < NCTX) ? (n >> 8) : ((n - NCTX) >> 13); const int key = (n < NCTX) ? (n & 255) : CTXL + ((n - NCTX) & 8191);
;             const int tile = key >> 6, kk0 = key & 63; const int boff = (kk0 >> 5) * 16 + 4 * ((kk0 & 31) >> 3);
; #pragma unroll
;             for (int ai = 0; ai < 2; ++ai)
; #pragma unroll
;                 for (int m = 0; m < 4; ++m) { const int vc = row0 + ai * HALF + m * 16; const int hh = vc >> 7, v = vc & 127;
;                     unsigned char* p = VT + ((size_t)((b * 4 + hh) * (KEYS / 64) + tile)) * VT_TILE + v * VT_ROW + boff;
;                     const f32x4 v0 = acc[ai][bj][m][0] * PV_Q, v1 = acc[ai][bj][m][1] * PV_Q;
;                     *(unsigned*)p = pk4_fp8(v0[0], v0[1], v0[2], v0[3]); *(unsigned*)(p + 32) = pk4_fp8(v1[0], v1[1], v1[2], v1[3]); } }
;     }
.LBB0_472:
	s_lshl_b32 s0, s71, 8
	s_add_i32 s1, s0, s66
	s_lshl_b32 s0, s70, 8
	v_or_b32_e32 v145, s0, v143
	v_add_u32_e32 v146, 0x1c00, v145
	s_movk_i32 s2, 0x400
	v_and_b32_e32 v146, 0x1f78, v146
	s_addk_i32 s0, 0xfc00
	v_cmp_gt_i32_e32 vcc, s2, v145
	v_add_u32_e32 v146, 0x100, v146
	s_lshr_b32 s0, s0, 13
	v_cndmask_b32_e32 v149, v146, v143, vcc
	v_mov_b32_e32 v147, s0
	v_mov_b32_e32 v154, s70
	v_lshrrev_b32_e32 v146, 6, v149
	v_lshrrev_b32_e32 v149, 1, v149
	v_cndmask_b32_e32 v148, v147, v154, vcc
	v_and_b32_e32 v152, 28, v149
	s_mov_b32 s4, 0x41000000
	v_lshlrev_b32_e32 v155, 2, v148
	v_lshl_add_u64 v[148:149], s[86:87], 0, v[152:153]
	v_pk_mul_f32 v[124:125], v[124:125], s[4:5] op_sel_hi:[1,0]
	v_cvt_pk_fp8_f32 v152, v124, v125
	v_pk_mul_f32 v[120:121], v[120:121], s[4:5] op_sel_hi:[1,0]
	v_mov_b32_e32 v124, v153
	v_cvt_pk_fp8_f32 v124, v120, v121
	v_pk_mul_f32 v[120:121], v[126:127], s[4:5] op_sel_hi:[1,0]
	v_pk_mul_f32 v[116:117], v[116:117], s[4:5] op_sel_hi:[1,0]
	v_cvt_pk_fp8_f32 v152, v120, v121 op_sel:[0,0,1]
	v_cvt_pk_fp8_f32 v120, v116, v117
	v_pk_mul_f32 v[112:113], v[112:113], s[4:5] op_sel_hi:[1,0]
	v_mov_b32_e32 v116, v153
	v_cvt_pk_fp8_f32 v116, v112, v113
	v_pk_mul_f32 v[112:113], v[118:119], s[4:5] op_sel_hi:[1,0]
	v_pk_mul_f32 v[108:109], v[108:109], s[4:5] op_sel_hi:[1,0]
	v_cvt_pk_fp8_f32 v120, v112, v113 op_sel:[0,0,1]
	v_cvt_pk_fp8_f32 v112, v108, v109
	v_pk_mul_f32 v[104:105], v[104:105], s[4:5] op_sel_hi:[1,0]
	v_mov_b32_e32 v108, v153
	v_cvt_pk_fp8_f32 v108, v104, v105
	v_pk_mul_f32 v[104:105], v[110:111], s[4:5] op_sel_hi:[1,0]
	v_pk_mul_f32 v[100:101], v[100:101], s[4:5] op_sel_hi:[1,0]
	v_cvt_pk_fp8_f32 v112, v104, v105 op_sel:[0,0,1]
	v_mov_b32_e32 v104, v153
	v_pk_mul_f32 v[96:97], v[96:97], s[4:5] op_sel_hi:[1,0]
	v_cvt_pk_fp8_f32 v104, v100, v101
	v_cvt_pk_fp8_f32 v100, v96, v97
	v_pk_mul_f32 v[98:99], v[98:99], s[4:5] op_sel_hi:[1,0]
	v_pk_mul_f32 v[92:93], v[92:93], s[4:5] op_sel_hi:[1,0]
	v_pk_mul_f32 v[88:89], v[88:89], s[4:5] op_sel_hi:[1,0]
	v_cvt_pk_fp8_f32 v100, v98, v99 op_sel:[0,0,1]
	v_cvt_pk_fp8_f32 v98, v92, v93
	v_mov_b32_e32 v92, v153
	v_cvt_pk_fp8_f32 v92, v88, v89
	v_pk_mul_f32 v[88:89], v[94:95], s[4:5] op_sel_hi:[1,0]
	v_pk_mul_f32 v[84:85], v[84:85], s[4:5] op_sel_hi:[1,0]
	v_cvt_pk_fp8_f32 v98, v88, v89 op_sel:[0,0,1]
	v_cvt_pk_fp8_f32 v88, v84, v85
	v_pk_mul_f32 v[80:81], v[80:81], s[4:5] op_sel_hi:[1,0]
	v_mov_b32_e32 v84, v153
	v_cvt_pk_fp8_f32 v84, v80, v81
	v_pk_mul_f32 v[80:81], v[86:87], s[4:5] op_sel_hi:[1,0]
	v_pk_mul_f32 v[76:77], v[76:77], s[4:5] op_sel_hi:[1,0]
	v_cvt_pk_fp8_f32 v88, v80, v81 op_sel:[0,0,1]
	v_cvt_pk_fp8_f32 v80, v76, v77
	v_pk_mul_f32 v[72:73], v[72:73], s[4:5] op_sel_hi:[1,0]
	v_cvt_pk_fp8_f32 v76, v72, v73
	v_pk_mul_f32 v[72:73], v[78:79], s[4:5] op_sel_hi:[1,0]
	v_pk_mul_f32 v[60:61], v[60:61], s[4:5] op_sel_hi:[1,0]
	v_cvt_pk_fp8_f32 v80, v72, v73 op_sel:[0,0,1]
	v_pk_mul_f32 v[56:57], v[56:57], s[4:5] op_sel_hi:[1,0]
	v_cvt_pk_fp8_f32 v72, v60, v61
	v_cvt_pk_fp8_f32 v60, v56, v57
	v_pk_mul_f32 v[56:57], v[62:63], s[4:5] op_sel_hi:[1,0]
	v_pk_mul_f32 v[62:63], v[68:69], s[4:5] op_sel_hi:[1,0]
	v_cvt_pk_fp8_f32 v68, v62, v63
	v_pk_mul_f32 v[62:63], v[70:71], s[4:5] op_sel_hi:[1,0]
	v_pk_mul_f32 v[52:53], v[52:53], s[4:5] op_sel_hi:[1,0]
	v_pk_mul_f32 v[48:49], v[48:49], s[4:5] op_sel_hi:[1,0]
	v_cvt_pk_fp8_f32 v68, v62, v63 op_sel:[0,0,1]
	v_cvt_pk_fp8_f32 v62, v52, v53
	v_mov_b32_e32 v52, v153
	v_cvt_pk_fp8_f32 v52, v48, v49
	v_pk_mul_f32 v[48:49], v[54:55], s[4:5] op_sel_hi:[1,0]
	v_pk_mul_f32 v[44:45], v[44:45], s[4:5] op_sel_hi:[1,0]
	v_cvt_pk_fp8_f32 v62, v48, v49 op_sel:[0,0,1]
	v_cvt_pk_fp8_f32 v48, v44, v45
	v_pk_mul_f32 v[40:41], v[40:41], s[4:5] op_sel_hi:[1,0]
	v_mov_b32_e32 v44, v153
	v_cvt_pk_fp8_f32 v44, v40, v41
	v_pk_mul_f32 v[40:41], v[46:47], s[4:5] op_sel_hi:[1,0]
	v_pk_mul_f32 v[36:37], v[36:37], s[4:5] op_sel_hi:[1,0]
	v_cvt_pk_fp8_f32 v48, v40, v41 op_sel:[0,0,1]
	v_mov_b32_e32 v40, v153
	v_pk_mul_f32 v[32:33], v[32:33], s[4:5] op_sel_hi:[1,0]
	v_cvt_pk_fp8_f32 v40, v36, v37
	v_cvt_pk_fp8_f32 v36, v32, v33
	v_pk_mul_f32 v[34:35], v[34:35], s[4:5] op_sel_hi:[1,0]
	v_pk_mul_f32 v[12:13], v[12:13], s[4:5] op_sel_hi:[1,0]
	s_ashr_i32 s0, s1, 7
	v_cvt_pk_fp8_f32 v36, v34, v35 op_sel:[0,0,1]
	v_cvt_pk_fp8_f32 v34, v12, v13
	s_addk_i32 s1, 0x80
	v_pk_mul_f32 v[58:59], v[58:59], s[4:5] op_sel_hi:[1,0]
	v_pk_mul_f32 v[96:97], v[102:103], s[4:5] op_sel_hi:[1,0]
	s_ashr_i32 s1, s1, 7
	v_cvt_pk_fp8_f32 v72, v56, v57 op_sel:[0,0,1]
	v_cvt_pk_fp8_f32 v60, v58, v59 op_sel:[0,0,1]
	v_or_b32_e32 v56, 0x80, v145
	v_add_u32_e32 v58, 0x1c80, v145
	v_pk_mul_f32 v[8:9], v[8:9], s[4:5] op_sel_hi:[1,0]
	v_add_u32_e32 v150, s0, v155
	v_pk_mul_f32 v[122:123], v[122:123], s[4:5] op_sel_hi:[1,0]
	v_pk_mul_f32 v[106:107], v[106:107], s[4:5] op_sel_hi:[1,0]
	v_cvt_pk_fp8_f32 v104, v96, v97 op_sel:[0,0,1]
	v_add_u32_e32 v96, s1, v155
	v_pk_mul_f32 v[90:91], v[90:91], s[4:5] op_sel_hi:[1,0]
	v_pk_mul_f32 v[74:75], v[74:75], s[4:5] op_sel_hi:[1,0]
	v_cmp_gt_i32_e32 vcc, s2, v56
	v_mov_b32_e32 v56, 0x80
	s_movk_i32 s2, 0xf8
	v_and_b32_e32 v58, 0x1ff8, v58
	v_pk_mul_f32 v[64:65], v[64:65], s[4:5] op_sel_hi:[1,0]
; __device__ __forceinline__ unsigned pk4_fp8(float x0, float x1, float x2, float x3) { int w = 0; w = __builtin_amdgcn_cvt_pk_fp8_f32(x0, x1, w, false); w = __builtin_amdgcn_cvt_pk_fp8_f32(x2, x3, w, true); return (unsigned)w; }
;     __device__ __forceinline__ void operator()(const f32x4 (&acc)[2][2][4][2], const Unit& u, int wr, int wc, int fr, int fq) const {
;         const int row0 = u.pm * BM + wr * 64 + fr, col0 = u.pn * BM + wc * 32 + 8 * fq;
; #pragma unroll
;         for (int bj = 0; bj < 2; ++bj) {
;             const int n = col0 + bj * HALF;
;             const int b = (n < NCTX) ? (n >> 8) : ((n - NCTX) >> 13); const int key = (n < NCTX) ? (n & 255) : CTXL + ((n - NCTX) & 8191);
;             const int tile = key >> 6, kk0 = key & 63; const int boff = (kk0 >> 5) * 16 + 4 * ((kk0 & 31) >> 3);
; #pragma unroll
;             for (int ai = 0; ai < 2; ++ai)
; #pragma unroll
;                 for (int m = 0; m < 4; ++m) { const int vc = row0 + ai * HALF + m * 16; const int hh = vc >> 7, v = vc & 127;
;                     unsigned char* p = VT + ((size_t)((b * 4 + hh) * (KEYS / 64) + tile)) * VT_TILE + v * VT_ROW + boff;
;                     const f32x4 v0 = acc[ai][bj][m][0] * PV_Q, v1 = acc[ai][bj][m][1] * PV_Q;
;                     *(unsigned*)p = pk4_fp8(v0[0], v0[1], v0[2], v0[3]); *(unsigned*)(p + 32) = pk4_fp8(v1[0], v1[1], v1[2], v1[3]); } }
;     }
	v_cvt_pk_fp8_f32 v12, v8, v9
	v_pk_mul_f32 v[8:9], v[14:15], s[4:5] op_sel_hi:[1,0]
	v_mad_u64_u32 v[150:151], s[40:41], v150, s83, v[146:147]
	s_movk_i32 s3, 0x2800
	v_cvt_pk_fp8_f32 v124, v122, v123 op_sel:[0,0,1]
	v_cvt_pk_fp8_f32 v108, v106, v107 op_sel:[0,0,1]
	v_mad_u64_u32 v[96:97], s[40:41], v96, s83, v[146:147]
	v_cvt_pk_fp8_f32 v92, v90, v91 op_sel:[0,0,1]
	v_cvt_pk_fp8_f32 v76, v74, v75 op_sel:[0,0,1]
	v_bitop3_b32 v56, v145, s2, v56 bitop3:0xc8
	v_add_u32_e32 v58, 0x100, v58
	v_cvt_pk_fp8_f32 v69, v64, v65
	v_cvt_pk_fp8_f32 v34, v8, v9 op_sel:[0,0,1]
	v_pk_mul_f32 v[4:5], v[4:5], s[4:5] op_sel_hi:[1,0]
	v_mad_i64_i32 v[150:151], s[40:41], v150, s3, v[148:149]
	v_pk_mul_f32 v[114:115], v[114:115], s[4:5] op_sel_hi:[1,0]
	v_mad_i64_i32 v[96:97], s[40:41], v96, s3, v[148:149]
	v_pk_mul_f32 v[82:83], v[82:83], s[4:5] op_sel_hi:[1,0]
	v_cndmask_b32_e32 v57, v147, v154, vcc
	v_cndmask_b32_e32 v58, v58, v56, vcc
	v_pk_mul_f32 v[0:1], v[0:1], s[4:5] op_sel_hi:[1,0]
	v_cvt_pk_fp8_f32 v8, v4, v5
	v_lshl_add_u64 v[150:151], v[150:151], 0, v[140:141]
	v_cvt_pk_fp8_f32 v116, v114, v115 op_sel:[0,0,1]
	v_lshl_add_u64 v[96:97], v[96:97], 0, v[140:141]
	v_cvt_pk_fp8_f32 v84, v82, v83 op_sel:[0,0,1]
	v_lshrrev_b32_e32 v56, 6, v58
	v_lshrrev_b32_e32 v58, 1, v58
	v_lshlrev_b32_e32 v57, 2, v57
	v_pk_mul_f32 v[32:33], v[38:39], s[4:5] op_sel_hi:[1,0]
	v_cvt_pk_fp8_f32 v4, v0, v1
	global_store_dword v[150:151], v152, off
	global_store_dword v[150:151], v124, off offset:32
	global_store_dword v[150:151], v120, off offset:1280
	global_store_dword v[150:151], v116, off offset:1312
	global_store_dword v[150:151], v112, off offset:2560
	global_store_dword v[150:151], v108, off offset:2592
	global_store_dword v[150:151], v104, off offset:3840
	global_store_dword v[150:151], v100, off offset:3872
	global_store_dword v[96:97], v98, off
	global_store_dword v[96:97], v92, off offset:32
	global_store_dword v[96:97], v88, off offset:1280
	global_store_dword v[96:97], v84, off offset:1312
	global_store_dword v[96:97], v80, off offset:2560
	global_store_dword v[96:97], v76, off offset:2592
	global_store_dword v[96:97], v72, off offset:3840
	global_store_dword v[96:97], v60, off offset:3872
	v_and_b32_e32 v152, 28, v58
	v_add_u32_e32 v60, s0, v57
	v_pk_mul_f32 v[64:65], v[66:67], s[4:5] op_sel_hi:[1,0]
	v_pk_mul_f32 v[42:43], v[42:43], s[4:5] op_sel_hi:[1,0]
	v_cvt_pk_fp8_f32 v40, v32, v33 op_sel:[0,0,1]
	v_add_u32_e32 v32, s1, v57
	v_pk_mul_f32 v[10:11], v[10:11], s[4:5] op_sel_hi:[1,0]
	v_lshl_add_u64 v[58:59], s[86:87], 0, v[152:153]
	v_mad_u64_u32 v[60:61], s[40:41], v60, s83, v[56:57]
	v_cvt_pk_fp8_f32 v69, v64, v65 op_sel:[0,0,1]
	v_cvt_pk_fp8_f32 v44, v42, v43 op_sel:[0,0,1]
	v_mad_u64_u32 v[32:33], s[0:1], v32, s83, v[56:57]
	v_cvt_pk_fp8_f32 v12, v10, v11 op_sel:[0,0,1]
	v_pk_mul_f32 v[0:1], v[6:7], s[4:5] op_sel_hi:[1,0]
	v_mad_i64_i32 v[60:61], s[40:41], v60, s3, v[58:59]
	v_pk_mul_f32 v[50:51], v[50:51], s[4:5] op_sel_hi:[1,0]
	v_mad_i64_i32 v[32:33], s[0:1], v32, s3, v[58:59]
	v_pk_mul_f32 v[2:3], v[2:3], s[4:5] op_sel_hi:[1,0]
	v_cvt_pk_fp8_f32 v8, v0, v1 op_sel:[0,0,1]
	v_lshl_add_u64 v[60:61], v[60:61], 0, v[140:141]
	v_cvt_pk_fp8_f32 v52, v50, v51 op_sel:[0,0,1]
	v_lshl_add_u64 v[32:33], v[32:33], 0, v[140:141]
	v_cvt_pk_fp8_f32 v4, v2, v3 op_sel:[0,0,1]
	global_store_dword v[60:61], v68, off
	global_store_dword v[60:61], v69, off offset:32
	global_store_dword v[60:61], v62, off offset:1280
	global_store_dword v[60:61], v52, off offset:1312
	global_store_dword v[60:61], v48, off offset:2560
	global_store_dword v[60:61], v44, off offset:2592
	global_store_dword v[60:61], v40, off offset:3840
	global_store_dword v[60:61], v36, off offset:3872
	global_store_dword v[32:33], v34, off
	global_store_dword v[32:33], v12, off offset:32
	global_store_dword v[32:33], v8, off offset:1280
	global_store_dword v[32:33], v4, off offset:1312
	v_pk_mul_f32 v[0:1], v[24:25], s[4:5] op_sel_hi:[1,0]
	v_pk_mul_f32 v[2:3], v[28:29], s[4:5] op_sel_hi:[1,0]
	v_cvt_pk_fp8_f32 v4, v0, v1
	v_cvt_pk_fp8_f32 v5, v2, v3
	v_pk_mul_f32 v[0:1], v[26:27], s[4:5] op_sel_hi:[1,0]
	v_pk_mul_f32 v[2:3], v[30:31], s[4:5] op_sel_hi:[1,0]
	v_cvt_pk_fp8_f32 v4, v0, v1 op_sel:[0,0,1]
	v_pk_mul_f32 v[0:1], v[16:17], s[4:5] op_sel_hi:[1,0]
	v_cvt_pk_fp8_f32 v5, v2, v3 op_sel:[0,0,1]
	v_pk_mul_f32 v[2:3], v[20:21], s[4:5] op_sel_hi:[1,0]
	v_cvt_pk_fp8_f32 v6, v0, v1
	v_cvt_pk_fp8_f32 v7, v2, v3
	v_pk_mul_f32 v[0:1], v[18:19], s[4:5] op_sel_hi:[1,0]
	v_pk_mul_f32 v[2:3], v[22:23], s[4:5] op_sel_hi:[1,0]
	v_cvt_pk_fp8_f32 v6, v0, v1 op_sel:[0,0,1]
	v_readlane_b32 s72, v254, 26
	v_cvt_pk_fp8_f32 v7, v2, v3 op_sel:[0,0,1]
	s_andn2_b64 vcc, exec, s[42:43]
	s_mov_b64 s[0:1], -1
	v_readlane_b32 s73, v254, 27
	v_readlane_b32 s74, v254, 28
	v_readlane_b32 s76, v254, 29
	global_store_dword v[32:33], v4, off offset:2560
	global_store_dword v[32:33], v5, off offset:2592
	global_store_dword v[32:33], v6, off offset:3840
	global_store_dword v[32:33], v7, off offset:3872
	v_readlane_b32 s77, v254, 30
	s_cbranch_vccnz .LBB0_465
	s_andn2_b64 vcc, exec, s[8:9]
	s_cbranch_vccnz .LBB0_464
	s_barrier
	s_branch .LBB0_464

; __device__ __forceinline__ unsigned pk4_fp8(float x0, float x1, float x2, float x3) { int w = 0; w = __builtin_amdgcn_cvt_pk_fp8_f32(x0, x1, w, false); w = __builtin_amdgcn_cvt_pk_fp8_f32(x2, x3, w, true); return (unsigned)w; }
; __device__ __forceinline__ void attn_unit(const bf16_t* Qb, const unsigned char* Kh, const unsigned char* Vh, bf16_t* Ob, int seq, int cbase, int lbase, int t0, const f32x2* atab, char* lds, const int wave_s) {
;     ...
;     const bf16_t* Qw = Qb + (long)(wid * QBLK + r32) * LDQ + hi * 32;
; #pragma unroll
;     for (int ks = 0; ks < 3; ++ks) {
;         float x[32];
; #pragma unroll
;         for (int c4 = 0; c4 < 4; ++c4) { const u32x4 w = *reinterpret_cast<const u32x4*>(Qw + ks * 64 + c4 * 8);
;             x[8 * c4 + 0] = bflo(w.x); x[8 * c4 + 1] = bfhi(w.x); x[8 * c4 + 2] = bflo(w.y); x[8 * c4 + 3] = bfhi(w.y); x[8 * c4 + 4] = bflo(w.z); x[8 * c4 + 5] = bfhi(w.z); x[8 * c4 + 6] = bflo(w.w); x[8 * c4 + 7] = bfhi(w.w); }
;         if (ks == 2 && t0 >= 0) { const int t = t0 + wid * QBLK + r32; const int pos = hi ? (t & 63) : (t >> 6); const f32x2* tb = atab + pos * 16;
; #pragma unroll
;             for (int f = 0; f < 16; ++f) { const f32x2 cs = tb[f]; const float a = x[2 * f], b = x[2 * f + 1]; x[2 * f] = a * cs.x - b * cs.y; x[2 * f + 1] = b * cs.x + a * cs.y; } }
;         v8i q;
; #pragma unroll
;         for (int c = 0; c < 8; ++c) q[c] = (int)pk4_fp8(x[4 * c] * QC_Q, x[4 * c + 1] * QC_Q, x[4 * c + 2] * QC_Q, x[4 * c + 3] * QC_Q);
;         qr[ks] = q; }
.LBB0_548:
	v_mul_f32_e32 v38, 0x3fd53b94, v54
	v_mul_f32_e32 v39, 0x3fd53b94, v46
	v_cvt_pk_fp8_f32 v112, v38, v39
	v_mul_f32_e32 v37, 0x3fd53b94, v37
	v_mul_f32_e32 v38, 0x3fd53b94, v63
	v_cvt_pk_fp8_f32 v113, v37, v38
	v_mul_f32_e32 v36, 0x3fd53b94, v36
	v_mul_f32_e32 v46, 0x3fd53b94, v62
	v_cvt_pk_fp8_f32 v112, v36, v46 op_sel:[0,0,1]
	v_mul_f32_e32 v35, 0x3fd53b94, v35
	v_mul_f32_e32 v36, 0x3fd53b94, v61
	v_cvt_pk_fp8_f32 v113, v35, v36 op_sel:[0,0,1]
	v_mul_f32_e32 v34, 0x3fd53b94, v34
	v_mul_f32_e32 v35, 0x3fd53b94, v60
	v_cvt_pk_fp8_f32 v114, v34, v35
	v_mul_f32_e32 v33, 0x3fd53b94, v33
	v_mul_f32_e32 v34, 0x3fd53b94, v59
	v_cvt_pk_fp8_f32 v115, v33, v34
	v_mul_f32_e32 v32, 0x3fd53b94, v32
	v_mul_f32_e32 v36, 0x3fd53b94, v58
	v_cvt_pk_fp8_f32 v114, v32, v36 op_sel:[0,0,1]
	v_mul_f32_e32 v32, 0x3fd53b94, v65
	v_mul_f32_e32 v33, 0x3fd53b94, v57
	v_cvt_pk_fp8_f32 v115, v32, v33 op_sel:[0,0,1]
	v_lshlrev_b32_e32 v32, 16, v28
	v_and_b32_e32 v28, 0xffff0000, v28
	v_lshlrev_b32_e32 v34, 16, v30
	v_and_b32_e32 v30, 0xffff0000, v30
	v_mul_f32_e32 v32, 0x3fd53b94, v32
	v_mul_f32_e32 v28, 0x3fd53b94, v28
	v_cvt_pk_fp8_f32 v120, v32, v28
	v_mul_f32_e32 v28, 0x3fd53b94, v34
	v_mul_f32_e32 v30, 0x3fd53b94, v30
	v_cvt_pk_fp8_f32 v121, v28, v30
	v_lshlrev_b32_e32 v33, 16, v29
	v_and_b32_e32 v29, 0xffff0000, v29
	v_lshlrev_b32_e32 v35, 16, v31
	v_and_b32_e32 v31, 0xffff0000, v31
	v_mul_f32_e32 v33, 0x3fd53b94, v33
	v_mul_f32_e32 v29, 0x3fd53b94, v29
	v_lshlrev_b32_e32 v36, 16, v24
	v_and_b32_e32 v24, 0xffff0000, v24
	v_cvt_pk_fp8_f32 v120, v33, v29 op_sel:[0,0,1]
	v_mul_f32_e32 v28, 0x3fd53b94, v35
	v_mul_f32_e32 v29, 0x3fd53b94, v31
	v_lshlrev_b32_e32 v38, 16, v26
	v_and_b32_e32 v26, 0xffff0000, v26
	v_cvt_pk_fp8_f32 v121, v28, v29 op_sel:[0,0,1]
	v_mul_f32_e32 v28, 0x3fd53b94, v36
	v_mul_f32_e32 v24, 0x3fd53b94, v24
	v_cvt_pk_fp8_f32 v122, v28, v24
	v_mul_f32_e32 v24, 0x3fd53b94, v38
	v_mul_f32_e32 v26, 0x3fd53b94, v26
	v_cvt_pk_fp8_f32 v123, v24, v26
	v_lshlrev_b32_e32 v37, 16, v25
	v_and_b32_e32 v25, 0xffff0000, v25
	v_lshlrev_b32_e32 v39, 16, v27
	v_and_b32_e32 v27, 0xffff0000, v27
	v_mul_f32_e32 v29, 0x3fd53b94, v37
	v_mul_f32_e32 v25, 0x3fd53b94, v25
	v_mul_f32_e32 v54, 0x3fd53b94, v56
	v_lshlrev_b32_e32 v56, 16, v20
	v_and_b32_e32 v20, 0xffff0000, v20
	v_cvt_pk_fp8_f32 v122, v29, v25 op_sel:[0,0,1]
	v_mul_f32_e32 v24, 0x3fd53b94, v39
	v_mul_f32_e32 v25, 0x3fd53b94, v27
	v_lshlrev_b32_e32 v58, 16, v22
	v_and_b32_e32 v22, 0xffff0000, v22
	v_cvt_pk_fp8_f32 v123, v24, v25 op_sel:[0,0,1]
	v_mul_f32_e32 v24, 0x3fd53b94, v56
	v_mul_f32_e32 v20, 0x3fd53b94, v20
	v_cvt_pk_fp8_f32 v124, v24, v20
	v_mul_f32_e32 v20, 0x3fd53b94, v58
	v_mul_f32_e32 v22, 0x3fd53b94, v22
	v_cvt_pk_fp8_f32 v125, v20, v22
	v_lshlrev_b32_e32 v57, 16, v21
	v_and_b32_e32 v21, 0xffff0000, v21
	v_lshlrev_b32_e32 v59, 16, v23
	v_and_b32_e32 v23, 0xffff0000, v23
	v_mul_f32_e32 v25, 0x3fd53b94, v57
	v_mul_f32_e32 v21, 0x3fd53b94, v21
	v_lshlrev_b32_e32 v60, 16, v16
	v_and_b32_e32 v16, 0xffff0000, v16
	v_cvt_pk_fp8_f32 v124, v25, v21 op_sel:[0,0,1]
	v_mul_f32_e32 v20, 0x3fd53b94, v59
	v_mul_f32_e32 v21, 0x3fd53b94, v23
	v_lshlrev_b32_e32 v62, 16, v18
	v_and_b32_e32 v18, 0xffff0000, v18
	v_cvt_pk_fp8_f32 v125, v20, v21 op_sel:[0,0,1]
	v_mul_f32_e32 v20, 0x3fd53b94, v60
	v_mul_f32_e32 v16, 0x3fd53b94, v16
	v_cvt_pk_fp8_f32 v126, v20, v16
	v_mul_f32_e32 v16, 0x3fd53b94, v62
	v_mul_f32_e32 v18, 0x3fd53b94, v18
	v_cvt_pk_fp8_f32 v127, v16, v18
	v_lshlrev_b32_e32 v61, 16, v17
	v_and_b32_e32 v17, 0xffff0000, v17
	v_lshlrev_b32_e32 v63, 16, v19
	v_and_b32_e32 v19, 0xffff0000, v19
	v_mul_f32_e32 v21, 0x3fd53b94, v61
	v_mul_f32_e32 v17, 0x3fd53b94, v17
	v_cvt_pk_fp8_f32 v126, v21, v17 op_sel:[0,0,1]
	v_mul_f32_e32 v16, 0x3fd53b94, v63
	v_mul_f32_e32 v17, 0x3fd53b94, v19
	v_cvt_pk_fp8_f32 v127, v16, v17 op_sel:[0,0,1]
	v_lshlrev_b32_e32 v16, 16, v12
	v_and_b32_e32 v12, 0xffff0000, v12
	v_lshlrev_b32_e32 v18, 16, v14
	v_and_b32_e32 v14, 0xffff0000, v14
	v_lshlrev_b32_e32 v58, 16, v0
	v_and_b32_e32 v59, 0xffff0000, v0
	v_lshlrev_b32_e32 v60, 16, v1
	v_and_b32_e32 v61, 0xffff0000, v1
	v_mul_f32_e32 v0, 0x3fd53b94, v16
	v_mul_f32_e32 v1, 0x3fd53b94, v12
	v_cvt_pk_fp8_f32 v128, v0, v1
	v_mul_f32_e32 v0, 0x3fd53b94, v18
	v_mul_f32_e32 v1, 0x3fd53b94, v14
	v_cvt_pk_fp8_f32 v129, v0, v1
	v_lshlrev_b32_e32 v19, 16, v15
	v_and_b32_e32 v15, 0xffff0000, v15
	v_lshlrev_b32_e32 v20, 16, v8
	v_and_b32_e32 v8, 0xffff0000, v8
	v_mul_f32_e32 v0, 0x3fd53b94, v19
	v_mul_f32_e32 v1, 0x3fd53b94, v15
	v_lshlrev_b32_e32 v22, 16, v10
	v_and_b32_e32 v10, 0xffff0000, v10
	v_cvt_pk_fp8_f32 v129, v0, v1 op_sel:[0,0,1]
	v_mul_f32_e32 v0, 0x3fd53b94, v20
	v_mul_f32_e32 v1, 0x3fd53b94, v8
	v_lshlrev_b32_e32 v17, 16, v13
	v_and_b32_e32 v13, 0xffff0000, v13
	v_cvt_pk_fp8_f32 v130, v0, v1
	v_mul_f32_e32 v0, 0x3fd53b94, v22
	v_mul_f32_e32 v1, 0x3fd53b94, v10
	v_mul_u32_u24_e32 v177, 0xd0, v155
	v_mul_f32_e32 v46, 0x3fd53b94, v64
	v_lshlrev_b32_e32 v21, 16, v9
	v_lshlrev_b32_e32 v23, 16, v11
	v_lshlrev_b32_e32 v62, 16, v2
	v_and_b32_e32 v63, 0xffff0000, v2
	v_lshlrev_b32_e32 v64, 16, v3
	v_and_b32_e32 v65, 0xffff0000, v3
	v_mul_f32_e32 v2, 0x3fd53b94, v17
	v_mul_f32_e32 v3, 0x3fd53b94, v13
	v_cvt_pk_fp8_f32 v131, v0, v1
	v_add3_u32 v178, 0, v177, v161
	v_cvt_pk_fp8_f32 v128, v2, v3 op_sel:[0,0,1]
	v_mul_f32_e32 v2, 0x3fd53b94, v21
	v_mul_f32_e32 v0, 0x3fd53b94, v23
	s_waitcnt vmcnt(0)
	s_waitcnt vmcnt(0) lgkmcnt(0)
	s_barrier
; __device__ __forceinline__ void qkt(f32x16& p0, f32x16& p1, const float m_reg, const char* Ks, const v8i* q8, int r32, int hi) {
;     { const float ini = PSH - m_reg;
; #pragma unroll
;       for (int r = 0; r < 16; ++r) { p0[r] = ini; p1[r] = ini; } }
; #pragma unroll
;     for (int ks = 0; ks < 3; ++ks) { const char* kp = Ks + r32 * KROWB + ks * 64 + hi * 32;
;         const v8i a0 = __builtin_shufflevector(*reinterpret_cast<const v4i*>(kp), *reinterpret_cast<const v4i*>(kp + 16), 0, 1, 2, 3, 4, 5, 6, 7);
;         const v8i a1 = __builtin_shufflevector(*reinterpret_cast<const v4i*>(kp + 32 * KROWB), *reinterpret_cast<const v4i*>(kp + 32 * KROWB + 16), 0, 1, 2, 3, 4, 5, 6, 7);
;         p0 = __builtin_amdgcn_mfma_scale_f32_32x32x64_f8f6f4(a0, q8[ks], p0, 0, 0, 0, QK_E, 0, QC_E);
;         p1 = __builtin_amdgcn_mfma_scale_f32_32x32x64_f8f6f4(a1, q8[ks], p1, 0, 0, 0, QK_E, 0, QC_E); }
; __device__ __forceinline__ void attn_unit(const bf16_t* Qb, const unsigned char* Kh, const unsigned char* Vh, bf16_t* Ob, int seq, int cbase, int lbase, int t0, const f32x2* atab, char* lds, const int wave_s) {
;     ...
;     const bf16_t* Qw = Qb + (long)(wid * QBLK + r32) * LDQ + hi * 32;
; #pragma unroll
;     for (int ks = 0; ks < 3; ++ks) {
;         float x[32];
; #pragma unroll
;         for (int c4 = 0; c4 < 4; ++c4) { const u32x4 w = *reinterpret_cast<const u32x4*>(Qw + ks * 64 + c4 * 8);
;             x[8 * c4 + 0] = bflo(w.x); x[8 * c4 + 1] = bfhi(w.x); x[8 * c4 + 2] = bflo(w.y); x[8 * c4 + 3] = bfhi(w.y); x[8 * c4 + 4] = bflo(w.z); x[8 * c4 + 5] = bfhi(w.z); x[8 * c4 + 6] = bflo(w.w); x[8 * c4 + 7] = bfhi(w.w); }
;         if (ks == 2 && t0 >= 0) { const int t = t0 + wid * QBLK + r32; const int pos = hi ? (t & 63) : (t >> 6); const f32x2* tb = atab + pos * 16;
; #pragma unroll
;             for (int f = 0; f < 16; ++f) { const f32x2 cs = tb[f]; const float a = x[2 * f], b = x[2 * f + 1]; x[2 * f] = a * cs.x - b * cs.y; x[2 * f + 1] = b * cs.x + a * cs.y; } }
;         v8i q;
; #pragma unroll
;         for (int c = 0; c < 8; ++c) q[c] = (int)pk4_fp8(x[4 * c] * QC_Q, x[4 * c + 1] * QC_Q, x[4 * c + 2] * QC_Q, x[4 * c + 3] * QC_Q);
;         qr[ks] = q; }
	ds_read_b128 v[16:19], v178
	ds_read_b128 v[20:23], v178 offset:16
	v_readlane_b32 s8, v254, 10
	v_and_b32_e32 v9, 0xffff0000, v9
	v_and_b32_e32 v11, 0xffff0000, v11
	v_readlane_b32 s9, v254, 11
	v_readlane_b32 s10, v254, 12
	v_readlane_b32 s11, v254, 13
	v_readlane_b32 s12, v254, 14
	v_readlane_b32 s13, v254, 15
	v_readlane_b32 s14, v254, 16
	v_readlane_b32 s15, v254, 17
	v_lshlrev_b32_e32 v24, 16, v4
	v_and_b32_e32 v4, 0xffff0000, v4
	v_lshlrev_b32_e32 v25, 16, v5
	v_and_b32_e32 v5, 0xffff0000, v5
	v_mul_f32_e32 v3, 0x3fd53b94, v9
	v_mul_f32_e32 v1, 0x3fd53b94, v11
	v_readlane_b32 s16, v254, 18
	v_readlane_b32 s17, v254, 19
	v_readlane_b32 s18, v254, 20
	v_readlane_b32 s19, v254, 21
	v_readlane_b32 s20, v254, 22
	v_readlane_b32 s21, v254, 23
	v_readlane_b32 s22, v254, 24
	v_readlane_b32 s23, v254, 25
	s_mov_b32 s9, s8
	s_mov_b32 s10, s8
	s_mov_b32 s11, s8
	s_mov_b32 s12, s8
	s_mov_b32 s13, s8
	s_mov_b32 s14, s8
	s_mov_b32 s15, s8
	s_mov_b32 s0, s8
	v_lshlrev_b32_e32 v32, 16, v6
	v_and_b32_e32 v33, 0xffff0000, v6
	v_lshlrev_b32_e32 v56, 16, v7
	v_and_b32_e32 v57, 0xffff0000, v7
	v_cvt_pk_fp8_f32 v130, v2, v3 op_sel:[0,0,1]
	v_cvt_pk_fp8_f32 v131, v0, v1 op_sel:[0,0,1]
	v_mul_f32_e32 v35, 0x3fd53b94, v4
	v_mul_f32_e32 v67, 0x3fd53b94, v5
	s_mov_b32 s16, s8
	s_mov_b32 s17, s8
	s_mov_b32 s18, s8
	s_mov_b32 s19, s8
	s_mov_b32 s20, s8
	s_mov_b32 s21, s8
	s_mov_b32 s22, s8
	s_mov_b32 s23, s8
	v_writelane_b32 v254, s0, 10
	v_mul_f32_e32 v34, 0x3fd53b94, v24
	v_mul_f32_e32 v66, 0x3fd53b94, v25
	v_mov_b64_e32 v[0:1], s[8:9]
	v_mov_b64_e32 v[2:3], s[10:11]
	v_mov_b64_e32 v[4:5], s[12:13]
	v_mov_b64_e32 v[6:7], s[14:15]
	v_mov_b64_e32 v[8:9], s[16:17]
	v_mov_b64_e32 v[10:11], s[18:19]
	v_mov_b64_e32 v[12:13], s[20:21]
	v_mov_b64_e32 v[14:15], s[22:23]
	v_mul_f32_e32 v32, 0x3fd53b94, v32
	s_waitcnt lgkmcnt(0)
	v_mfma_scale_f32_32x32x64_f8f6f4 v[16:31], v[16:23], v[120:127], v[0:15], v201, v200 op_sel_hi:[0,0,0]
	v_mul_f32_e32 v33, 0x3fd53b94, v33
	v_cvt_pk_fp8_f32 v132, v34, v35
	v_cvt_pk_fp8_f32 v133, v32, v33
	ds_read_b128 v[32:35], v178 offset:6656
	ds_read_b128 v[36:39], v178 offset:6672
	v_mul_f32_e32 v56, 0x3fd53b94, v56
	v_mul_f32_e32 v57, 0x3fd53b94, v57
	v_cvt_pk_fp8_f32 v133, v56, v57 op_sel:[0,0,1]
	v_mul_f32_e32 v56, 0x3fd53b94, v58
	v_mul_f32_e32 v57, 0x3fd53b94, v59
	v_cvt_pk_fp8_f32 v134, v56, v57
	v_mul_f32_e32 v56, 0x3fd53b94, v62
	v_mul_f32_e32 v57, 0x3fd53b94, v63
	s_waitcnt lgkmcnt(0)
	v_mfma_scale_f32_32x32x64_f8f6f4 v[0:15], v[32:39], v[120:127], v[0:15], v201, v200 op_sel_hi:[0,0,0]
	v_cvt_pk_fp8_f32 v135, v56, v57
	v_mul_f32_e32 v58, 0x3fd53b94, v60
	v_mul_f32_e32 v59, 0x3fd53b94, v61
	ds_read_b128 v[32:35], v178 offset:64
	ds_read_b128 v[36:39], v178 offset:80
	v_mul_f32_e32 v56, 0x3fd53b94, v64
	v_mul_f32_e32 v57, 0x3fd53b94, v65
	v_cvt_pk_fp8_f32 v132, v66, v67 op_sel:[0,0,1]
	v_cvt_pk_fp8_f32 v134, v58, v59 op_sel:[0,0,1]
	v_cvt_pk_fp8_f32 v135, v56, v57 op_sel:[0,0,1]
	v_mul_f32_e32 v41, 0x3fd53b94, v41
	v_cvt_pk_fp8_f32 v116, v46, v54
	s_waitcnt lgkmcnt(0)
	v_mfma_scale_f32_32x32x64_f8f6f4 v[16:31], v[32:39], v[128:135], v[16:31], v201, v200 op_sel_hi:[0,0,0]
	v_mul_f32_e32 v32, 0x3fd53b94, v52
	v_mul_f32_e32 v33, 0x3fd53b94, v40
	v_cvt_pk_fp8_f32 v117, v32, v33
	ds_read_b128 v[32:35], v178 offset:6720
	ds_read_b128 v[36:39], v178 offset:6736
	v_mul_f32_e32 v40, 0x3fd53b94, v53
	v_mul_f32_e32 v55, 0x3fd53b94, v55
	v_cvt_pk_fp8_f32 v117, v40, v41 op_sel:[0,0,1]
	v_mul_f32_e32 v40, 0x3fd53b94, v50
	v_mul_f32_e32 v41, 0x3fd53b94, v42
	v_cvt_pk_fp8_f32 v118, v40, v41
	v_mul_f32_e32 v40, 0x3fd53b94, v44
	v_mul_f32_e32 v41, 0x3fd53b94, v48
	v_cvt_pk_fp8_f32 v119, v40, v41
	v_mul_f32_e32 v47, 0x3fd53b94, v47
	v_mul_f32_e32 v42, 0x3fd53b94, v51
	s_waitcnt lgkmcnt(0)
	v_mfma_scale_f32_32x32x64_f8f6f4 v[0:15], v[32:39], v[128:135], v[0:15], v201, v200 op_sel_hi:[0,0,0]
	v_mul_f32_e32 v43, 0x3fd53b94, v43
	ds_read_b128 v[32:35], v178 offset:128
	ds_read_b128 v[36:39], v178 offset:144
	v_mul_f32_e32 v40, 0x3fd53b94, v45
	v_mul_f32_e32 v41, 0x3fd53b94, v49
	v_cvt_pk_fp8_f32 v116, v55, v47 op_sel:[0,0,1]
	v_cvt_pk_fp8_f32 v118, v42, v43 op_sel:[0,0,1]
	v_cvt_pk_fp8_f32 v119, v40, v41 op_sel:[0,0,1]
	v_writelane_b32 v254, s1, 11
	v_writelane_b32 v254, s2, 12
	v_writelane_b32 v254, s3, 13
	v_writelane_b32 v254, s4, 14
	v_writelane_b32 v254, s5, 15
	v_writelane_b32 v254, s6, 16
	v_writelane_b32 v254, s7, 17
	v_writelane_b32 v254, s8, 18
	s_waitcnt lgkmcnt(0)
; __device__ __forceinline__ float max3f(float a, float b, float c) { return fmaxf(fmaxf(a, b), c); }
; __device__ __forceinline__ void partialSM(f32x16& p0, f32x16& p1, float& m_reg, float& alpha, const bool first) {
;     float ma = max3f(p0[0], p0[1], p0[2]), mb = max3f(p0[3], p0[4], p0[5]), mc = max3f(p0[6], p0[7], p0[8]), md = max3f(p0[9], p0[10], p0[11]);
;     ma = max3f(ma, p0[12], p0[13]); mb = max3f(mb, p0[14], p0[15]); mc = max3f(mc, p1[0], p1[1]); md = max3f(md, p1[2], p1[3]);
;     ma = max3f(ma, p1[4], p1[5]); mb = max3f(mb, p1[6], p1[7]); mc = max3f(mc, p1[8], p1[9]); md = max3f(md, p1[10], p1[11]);
;     ma = max3f(ma, p1[12], p1[13]); mb = max3f(mb, p1[14], p1[15]);
;     float pmax = fmaxf(max3f(ma, mb, mc), md);
;     { auto rr = __builtin_amdgcn_permlane32_swap(__float_as_uint(pmax), __float_as_uint(pmax), false, false);
;       pmax = fmaxf(__uint_as_float(rr[0]), __uint_as_float(rr[1])); }
;     const float u = pmax - PSH;
;     if (__builtin_expect(!first && __all(u <= THR2), 1)) { alpha = 1.f; }
;     else { const float dl = first ? u : fmaxf(u, 0.f); alpha = __builtin_amdgcn_exp2f(-dl); m_reg += dl;
; #pragma unroll
;         for (int r = 0; r < 16; ++r) { p0[r] -= dl; p1[r] -= dl; } }
; #pragma unroll
;     for (int r = 0; r < 16; ++r) p0[r] = __builtin_amdgcn_exp2f(p0[r]);
; }
; __device__ __forceinline__ void attn_unit(const bf16_t* Qb, const unsigned char* Kh, const unsigned char* Vh, bf16_t* Ob, int seq, int cbase, int lbase, int t0, const f32x2* atab, char* lds, const int wave_s) {
;     ...
;     float m_reg = 0.f, l_reg = 0; f32x16 o[4] = {}; v8i qr[3];
;     const bf16_t* Qw = Qb + (long)(wid * QBLK + r32) * LDQ + hi * 32;
	v_mfma_scale_f32_32x32x64_f8f6f4 v[16:31], v[32:39], v[112:119], v[16:31], v201, v200 op_sel_hi:[0,0,0]
	ds_read_b128 v[32:35], v178 offset:6784
	ds_read_b128 v[36:39], v178 offset:6800
	v_writelane_b32 v254, s9, 19
	v_writelane_b32 v254, s10, 20
	v_writelane_b32 v254, s11, 21
	v_writelane_b32 v254, s12, 22
	v_writelane_b32 v254, s13, 23
	v_writelane_b32 v254, s14, 24
	v_writelane_b32 v254, s15, 25
	v_readlane_b32 s0, v253, 34
	v_readlane_b32 s1, v253, 35
	s_ashr_i32 s1, s0, 31
	v_writelane_b32 v253, s0, 34
	s_add_i32 s7, s57, 0x80
	v_lshrrev_b32_e32 v172, 5, v72
	v_writelane_b32 v253, s1, 35
	s_waitcnt lgkmcnt(0)
	v_mfma_scale_f32_32x32x64_f8f6f4 v[0:15], v[32:39], v[112:119], v[0:15], v201, v200 op_sel_hi:[0,0,0]
	s_nop 1
	v_max_f32_e32 v32, v17, v17
	v_max_f32_e32 v33, v16, v16
	v_max_f32_e32 v32, v33, v32
	v_max3_f32 v33, v19, v20, v21
	v_max3_f32 v32, v32, v18, v28
	v_max3_f32 v33, v33, v30, v31
	v_max3_f32 v34, v22, v23, v24
	v_max3_f32 v35, v25, v26, v27
	v_readlane_b32 s1, v255, 19
	s_ashr_i32 s0, s1, 31
	s_lshr_b32 s0, s0, 26
	s_add_i32 s0, s1, s0
	s_ashr_i32 s6, s0, 6
	v_readlane_b32 s0, v255, 17
	s_lshl_b32 s2, s0, 13
	s_nop 2
	v_max3_f32 v32, v32, v29, v4
	v_max3_f32 v33, v33, v6, v7
	v_max3_f32 v34, v34, v0, v1
	v_max3_f32 v35, v35, v2, v3
	v_max3_f32 v32, v32, v5, v12
	v_max3_f32 v33, v33, v14, v15
	v_max3_f32 v34, v34, v8, v9
	v_max3_f32 v35, v35, v10, v11
	v_max3_f32 v32, v32, v13, v33
	v_max3_f32 v32, v32, v34, v35
	v_mov_b32_e32 v33, v32
	s_nop 1
	v_permlane32_swap_b32_e32 v32, v33
	v_max_f32_e32 v33, v33, v33
	v_max_f32_e32 v32, v32, v32
	v_max_f32_e32 v32, v32, v33
	v_add_f32_e32 v180, 0xc0400000, v32
	v_sub_f32_e32 v16, v16, v180
	v_exp_f32_e32 v215, v16
	v_sub_f32_e32 v16, v17, v180
	v_exp_f32_e32 v216, v16
	v_sub_f32_e32 v16, v18, v180
	v_exp_f32_e32 v190, v16
	v_sub_f32_e32 v16, v19, v180
	v_exp_f32_e32 v192, v16
	v_sub_f32_e32 v16, v20, v180
	v_exp_f32_e32 v213, v16
	v_sub_f32_e32 v16, v21, v180
	v_exp_f32_e32 v214, v16
	v_sub_f32_e32 v16, v22, v180
	v_exp_f32_e32 v195, v16
	v_sub_f32_e32 v16, v23, v180
	v_exp_f32_e32 v212, v16
	v_sub_f32_e32 v16, v24, v180
	v_exp_f32_e32 v194, v16
	v_sub_f32_e32 v16, v25, v180
	v_exp_f32_e32 v211, v16
	v_sub_f32_e32 v16, v26, v180
	v_exp_f32_e32 v186, v16
	v_sub_f32_e32 v16, v27, v180
	v_exp_f32_e32 v187, v16
	v_sub_f32_e32 v16, v28, v180
	v_exp_f32_e32 v191, v16
	v_sub_f32_e32 v16, v29, v180
	v_exp_f32_e32 v193, v16
	v_sub_f32_e32 v16, v30, v180
	v_readlane_b32 s0, v248, 27
	v_exp_f32_e32 v188, v16
	v_sub_f32_e32 v16, v31, v180
	v_sub_f32_e32 v64, v0, v180
	v_add_u32_e32 v0, s0, v80
	v_readlane_b32 s0, v252, 1
	v_exp_f32_e32 v189, v16
	v_exp_f32_e64 v181, -v180
	s_add_u32 s0, s0, s58
	v_readlane_b32 s1, v252, 2
	v_sub_f32_e32 v79, v15, v180
	v_sub_f32_e32 v78, v14, v180
	v_sub_f32_e32 v65, v1, v180
	v_mov_b32_e32 v1, v153
	s_addc_u32 s1, s1, s59
	v_mov_b32_e32 v14, v153
	v_mov_b32_e32 v15, v153
	v_sub_f32_e32 v77, v13, v180
	v_sub_f32_e32 v76, v12, v180
	v_sub_f32_e32 v75, v11, v180
	v_sub_f32_e32 v74, v10, v180
	v_sub_f32_e32 v73, v9, v180
	v_sub_f32_e32 v72, v8, v180
	v_sub_f32_e32 v71, v7, v180
	v_sub_f32_e32 v70, v6, v180
	v_sub_f32_e32 v69, v5, v180
	v_sub_f32_e32 v68, v4, v180
	v_sub_f32_e32 v67, v3, v180
	v_sub_f32_e32 v66, v2, v180
	v_lshl_add_u64 v[158:159], s[0:1], 0, v[0:1]
	v_mov_b32_e32 v0, v153
	v_mov_b32_e32 v2, v153
	v_mov_b32_e32 v3, v153
	v_mov_b32_e32 v4, v153
	v_mov_b32_e32 v5, v153
	v_mov_b32_e32 v6, v153
	v_mov_b32_e32 v7, v153
	v_mov_b32_e32 v8, v153
	v_mov_b32_e32 v9, v153
	v_mov_b32_e32 v10, v153
	v_mov_b32_e32 v11, v153
	v_mov_b32_e32 v12, v153
	v_mov_b32_e32 v13, v153
	v_mov_b64_e32 v[62:63], v[14:15]
	v_mov_b64_e32 v[46:47], v[14:15]
	v_mov_b64_e32 v[30:31], v[14:15]
	v_mul_u32_u24_e32 v179, 0x50, v155
	v_lshl_add_u32 v174, v155, 2, s31
	v_lshlrev_b32_e32 v173, 4, v172
	v_mov_b32_e32 v157, v153
	s_or_b32 s8, s2, 0x3c0
	s_mov_b32 s9, 0
	v_mov_b32_e32 v175, 0
	s_mov_b32 s11, 1
	v_mov_b64_e32 v[60:61], v[12:13]
	v_mov_b64_e32 v[58:59], v[10:11]
	v_mov_b64_e32 v[56:57], v[8:9]
	v_mov_b64_e32 v[54:55], v[6:7]
	v_mov_b64_e32 v[52:53], v[4:5]
	v_mov_b64_e32 v[50:51], v[2:3]
	v_mov_b64_e32 v[48:49], v[0:1]
	v_mov_b64_e32 v[44:45], v[12:13]
	v_mov_b64_e32 v[42:43], v[10:11]
	v_mov_b64_e32 v[40:41], v[8:9]
	v_mov_b64_e32 v[38:39], v[6:7]
	v_mov_b64_e32 v[36:37], v[4:5]
	v_mov_b64_e32 v[34:35], v[2:3]
	v_mov_b64_e32 v[32:33], v[0:1]
	v_mov_b64_e32 v[28:29], v[12:13]
	v_mov_b64_e32 v[26:27], v[10:11]
	v_mov_b64_e32 v[24:25], v[8:9]
	v_mov_b64_e32 v[22:23], v[6:7]
	v_mov_b64_e32 v[20:21], v[4:5]
	v_mov_b64_e32 v[18:19], v[2:3]
	v_mov_b64_e32 v[16:17], v[0:1]
	s_mov_b32 s13, 1
	s_mov_b32 s20, s3
	v_readlane_b32 s23, v255, 15

; __device__ __forceinline__ unsigned pk4_fp8(float x0, float x1, float x2, float x3) { int w = 0; w = __builtin_amdgcn_cvt_pk_fp8_f32(x0, x1, w, false); w = __builtin_amdgcn_cvt_pk_fp8_f32(x2, x3, w, true); return (unsigned)w; }
; #define SBAR() __builtin_amdgcn_sched_barrier(0)
; #define RESC(a) do { if (__any((a) < 1.f)) { if (hi == 0) al_l[r32] = (a); asm volatile("s_waitcnt lgkmcnt(0)" ::: "memory"); \
;     _Pragma("unroll") for (int d = 0; d < 4; ++d) _Pragma("unroll") for (int r = 0; r < 16; ++r) o[d][r] *= al_l[crow(r, hi)]; } } while (0)
; __device__ __forceinline__ void finishSM(f32x16& p0, f32x16& p1, float alpha, float& l_reg, v8i& pa) {
; #pragma unroll
;     for (int r = 0; r < 16; ++r) p1[r] = __builtin_amdgcn_exp2f(p1[r]);
;     float sa = p0[0] + p0[1], sb = p0[2] + p0[3], sc = p0[4] + p0[5], sd = p0[6] + p0[7];
;     sa += p0[8]; sb += p0[9]; sc += p0[10]; sd += p0[11]; sa += p0[12]; sb += p0[13]; sc += p0[14]; sd += p0[15];
; #pragma unroll
;     for (int r = 0; r < 16; r += 4) { sa += p1[r]; sb += p1[r + 1]; sc += p1[r + 2]; sd += p1[r + 3]; }
;     float ps = (sa + sb) + (sc + sd);
;     { auto rr = __builtin_amdgcn_permlane32_swap(__float_as_uint(ps), __float_as_uint(ps), false, false);
;       ps = __uint_as_float(rr[0]) + __uint_as_float(rr[1]); }
;     l_reg = l_reg * alpha + ps;
; #pragma unroll
;     for (int c = 0; c < 4; ++c) { pa[c] = (int)pk4_fp8(p0[4 * c], p0[4 * c + 1], p0[4 * c + 2], p0[4 * c + 3]);
;         pa[4 + c] = (int)pk4_fp8(p1[4 * c], p1[4 * c + 1], p1[4 * c + 2], p1[4 * c + 3]); }
; }
; __device__ __forceinline__ void attn_unit(const bf16_t* Qb, const unsigned char* Kh, const unsigned char* Vh, bf16_t* Ob, int seq, int cbase, int lbase, int t0, const f32x2* atab, char* lds, const int wave_s) {
;     ...
;     SBAR(); qkt(pB0, pB1, m_reg, KBUF(bj), qr, r32, hi);
;     finishSM(pA0, pA1, alA, l_reg, pa); SBAR();
;     pv_d0(o, VBASE(bprev), pa, r32, hi); partialSM(pB0, pB1, m_reg, alB, false);
;     RESC(alB);
;     finishSM(pB0, pB1, alB, l_reg, pa); SBAR();
;     pv_d0(o, VBASE(bj), pa, r32, hi);
;     if (hi == 0) li_l[r32] = l_reg; asm volatile("s_waitcnt lgkmcnt(0)" ::: "memory");
.LBB0_573:
	v_cvt_pk_fp8_f32 v218, v215, v216
	v_cvt_pk_fp8_f32 v222, v143, v145
	v_cvt_pk_fp8_f32 v219, v213, v214
	v_cvt_pk_fp8_f32 v223, v144, v146
	v_cvt_pk_fp8_f32 v220, v194, v211
	v_cvt_pk_fp8_f32 v224, v139, v140
	v_cvt_pk_fp8_f32 v221, v191, v193
	v_cvt_pk_fp8_f32 v225, v135, v136
	v_cvt_pk_fp8_f32 v218, v190, v192 op_sel:[0,0,1]
	v_cvt_pk_fp8_f32 v222, v137, v138 op_sel:[0,0,1]
	v_cvt_pk_fp8_f32 v219, v195, v212 op_sel:[0,0,1]
	v_cvt_pk_fp8_f32 v223, v141, v142 op_sel:[0,0,1]
	v_cvt_pk_fp8_f32 v220, v186, v187 op_sel:[0,0,1]
	v_cvt_pk_fp8_f32 v224, v131, v132 op_sel:[0,0,1]
	v_cvt_pk_fp8_f32 v221, v188, v189 op_sel:[0,0,1]
	v_cvt_pk_fp8_f32 v225, v133, v134 op_sel:[0,0,1]
	v_cmp_gt_f32_e32 vcc, 1.0, v130
	s_waitcnt lgkmcnt(6)
	v_mfma_scale_f32_32x32x64_f8f6f4 v[0:15], v[218:225], v[120:127], v[0:15], v201, v201 op_sel_hi:[0,0,0]
	s_waitcnt lgkmcnt(4)
	v_mfma_scale_f32_32x32x64_f8f6f4 v[48:63], v[218:225], v[112:119], v[48:63], v201, v201 op_sel_hi:[0,0,0]
	s_waitcnt lgkmcnt(2)
	v_mfma_scale_f32_32x32x64_f8f6f4 v[32:47], v[218:225], v[72:79], v[32:47], v201, v201 op_sel_hi:[0,0,0]
	s_waitcnt lgkmcnt(0)
	v_mfma_scale_f32_32x32x64_f8f6f4 v[16:31], v[218:225], v[64:71], v[16:31], v201, v201 op_sel_hi:[0,0,0]
	s_cbranch_vccz .LBB0_577
	s_and_saveexec_b64 s[0:1], s[44:45]
	ds_write_b32 v174, v130 offset:128
	s_or_b64 exec, exec, s[0:1]
	s_waitcnt lgkmcnt(0)
	v_add_u32_e32 v76, s31, v173
	ds_read_b128 v[64:67], v76 offset:224
	ds_read_b128 v[68:71], v76 offset:192
	ds_read_b128 v[72:75], v76 offset:160
	ds_read_b128 v[76:79], v76 offset:128
	s_waitcnt lgkmcnt(3)
	s_nop 3
	v_pk_mul_f32 v[12:13], v[12:13], v[64:65]
	s_waitcnt lgkmcnt(2)
	v_pk_mul_f32 v[8:9], v[8:9], v[68:69]
	s_waitcnt lgkmcnt(1)
	v_pk_mul_f32 v[4:5], v[4:5], v[72:73]
	v_pk_mul_f32 v[14:15], v[14:15], v[66:67]
	v_pk_mul_f32 v[10:11], v[10:11], v[70:71]
	v_pk_mul_f32 v[6:7], v[6:7], v[74:75]
	s_waitcnt lgkmcnt(0)
	v_pk_mul_f32 v[2:3], v[2:3], v[78:79]
	v_pk_mul_f32 v[0:1], v[0:1], v[76:77]
	v_pk_mul_f32 v[60:61], v[60:61], v[64:65]
	v_pk_mul_f32 v[56:57], v[56:57], v[68:69]
	v_pk_mul_f32 v[52:53], v[52:53], v[72:73]
	v_pk_mul_f32 v[62:63], v[62:63], v[66:67]
	v_pk_mul_f32 v[58:59], v[58:59], v[70:71]
	v_pk_mul_f32 v[54:55], v[54:55], v[74:75]
	v_pk_mul_f32 v[50:51], v[50:51], v[78:79]
	v_pk_mul_f32 v[48:49], v[48:49], v[76:77]
	v_pk_mul_f32 v[44:45], v[44:45], v[64:65]
	v_pk_mul_f32 v[40:41], v[40:41], v[68:69]
	v_pk_mul_f32 v[36:37], v[36:37], v[72:73]
	v_pk_mul_f32 v[46:47], v[46:47], v[66:67]
	v_pk_mul_f32 v[42:43], v[42:43], v[70:71]
	v_pk_mul_f32 v[38:39], v[38:39], v[74:75]
	v_pk_mul_f32 v[34:35], v[34:35], v[78:79]
	v_pk_mul_f32 v[32:33], v[32:33], v[76:77]
	v_pk_mul_f32 v[28:29], v[28:29], v[64:65]
	v_pk_mul_f32 v[24:25], v[24:25], v[68:69]
	v_pk_mul_f32 v[20:21], v[20:21], v[72:73]
	v_pk_mul_f32 v[30:31], v[30:31], v[66:67]
	v_pk_mul_f32 v[26:27], v[26:27], v[70:71]
	v_pk_mul_f32 v[22:23], v[22:23], v[74:75]
	v_pk_mul_f32 v[18:19], v[18:19], v[78:79]
	v_pk_mul_f32 v[16:17], v[16:17], v[76:77]
.LBB0_577:
	v_exp_f32_e32 v118, v96
	v_exp_f32_e32 v119, v97
	v_exp_f32_e32 v112, v98
	v_exp_f32_e32 v113, v99
	v_exp_f32_e32 v116, v100
	v_exp_f32_e32 v117, v101
	v_exp_f32_e32 v114, v102
	v_exp_f32_e32 v115, v103
	v_exp_f32_e32 v102, v104
	v_exp_f32_e32 v103, v105
	v_exp_f32_e32 v96, v106
	v_exp_f32_e32 v97, v107
	v_exp_f32_e32 v100, v108
	v_exp_f32_e32 v101, v109
	v_exp_f32_e32 v98, v110
	v_exp_f32_e32 v99, v111
	v_exp_f32_e32 v126, v80
	v_exp_f32_e32 v127, v81
	v_exp_f32_e32 v120, v82
	v_exp_f32_e32 v121, v83
	v_exp_f32_e32 v124, v84
	v_exp_f32_e32 v125, v85
	v_exp_f32_e32 v122, v86
	v_exp_f32_e32 v123, v87
	v_add_f32_e32 v64, v119, v118
	v_add_f32_e32 v65, v113, v112
	v_add_f32_e32 v66, v117, v116
	v_add_f32_e32 v67, v115, v114
	v_exp_f32_e32 v110, v88
	v_exp_f32_e32 v111, v89
	v_exp_f32_e32 v104, v90
	v_exp_f32_e32 v105, v91
	v_add_f32_e32 v64, v102, v64
	v_add_f32_e32 v65, v103, v65
	v_add_f32_e32 v66, v96, v66
	v_add_f32_e32 v67, v97, v67
	v_exp_f32_e32 v108, v92
	v_exp_f32_e32 v109, v93
	v_exp_f32_e32 v106, v94
	v_exp_f32_e32 v107, v95
	v_add_f32_e32 v64, v100, v64
	v_add_f32_e32 v65, v101, v65
	v_add_f32_e32 v66, v98, v66
	v_add_f32_e32 v67, v99, v67
	v_add_f32_e32 v64, v126, v64
	v_add_f32_e32 v65, v65, v127
	v_add_f32_e32 v66, v66, v120
	v_add_f32_e32 v67, v67, v121
	v_add_f32_e32 v64, v124, v64
	v_add_f32_e32 v65, v125, v65
	v_add_f32_e32 v66, v122, v66
	v_add_f32_e32 v67, v123, v67
	v_add_f32_e32 v64, v110, v64
	v_add_f32_e32 v65, v111, v65
	v_add_f32_e32 v66, v104, v66
	v_add_f32_e32 v67, v105, v67
	v_add_f32_e32 v64, v108, v64
	v_add_f32_e32 v65, v109, v65
	v_add_f32_e32 v66, v106, v66
	v_add_f32_e32 v67, v107, v67
	v_add_f32_e32 v64, v65, v64
	v_add_f32_e32 v65, v66, v67
	v_add_f32_e32 v131, v65, v64
	v_mov_b32_e32 v132, v131
	s_nop 1
	v_permlane32_swap_b32_e32 v131, v132
	ds_read_b128 v[88:91], v176 offset:13312
	ds_read_b128 v[92:95], v176 offset:13328
	ds_read_b128 v[80:83], v176 offset:15872
	ds_read_b128 v[84:87], v176 offset:15888
	ds_read_b128 v[72:75], v176 offset:18432
	ds_read_b128 v[76:79], v176 offset:18448
	ds_read_b128 v[64:67], v176 offset:20992
	ds_read_b128 v[68:71], v176 offset:21008
	s_and_saveexec_b64 s[0:1], s[44:45]
	v_add_f32_e32 v128, v128, v129
	v_fmac_f32_e32 v128, v175, v184
	v_add_f32_e32 v129, v131, v132
	v_fmac_f32_e32 v129, v128, v130
	ds_write_b32 v174, v129
	s_or_b64 exec, exec, s[0:1]
	v_cvt_pk_fp8_f32 v128, v118, v119
	v_cvt_pk_fp8_f32 v132, v126, v127
	v_cvt_pk_fp8_f32 v129, v116, v117
	v_cvt_pk_fp8_f32 v133, v124, v125
	v_cvt_pk_fp8_f32 v130, v102, v103
	v_cvt_pk_fp8_f32 v134, v110, v111
	v_cvt_pk_fp8_f32 v131, v100, v101
	v_cvt_pk_fp8_f32 v135, v108, v109
	v_cvt_pk_fp8_f32 v128, v112, v113 op_sel:[0,0,1]
	v_cvt_pk_fp8_f32 v132, v120, v121 op_sel:[0,0,1]
	v_cvt_pk_fp8_f32 v129, v114, v115 op_sel:[0,0,1]
	v_cvt_pk_fp8_f32 v133, v122, v123 op_sel:[0,0,1]
	v_cvt_pk_fp8_f32 v130, v96, v97 op_sel:[0,0,1]
	v_cvt_pk_fp8_f32 v134, v104, v105 op_sel:[0,0,1]
	v_cvt_pk_fp8_f32 v131, v98, v99 op_sel:[0,0,1]
	v_cvt_pk_fp8_f32 v135, v106, v107 op_sel:[0,0,1]
	s_waitcnt lgkmcnt(0)
; __device__ __forceinline__ unsigned f2bf(float f) { return pk2(f, 0.f) & 0xffffu; }
; __device__ __forceinline__ int crow(int r, int hi) { return (r & 3) + 8 * (r >> 2) + 4 * hi; }
; __device__ __forceinline__ void attn_unit(const bf16_t* Qb, const unsigned char* Kh, const unsigned char* Vh, bf16_t* Ob, int seq, int cbase, int lbase, int t0, const f32x2* atab, char* lds, const int wave_s) {
;     ...
;     pv_d0(o, VBASE(bj), pa, r32, hi);
;     if (hi == 0) li_l[r32] = l_reg; asm volatile("s_waitcnt lgkmcnt(0)" ::: "memory");
;     float rli[16];
; #pragma unroll
;     for (int r = 0; r < 16; ++r) rli[r] = 8.f * __builtin_amdgcn_rcpf(li_l[crow(r, hi)]);
;     bf16_t* Ow = Ob + (long)(wid * QBLK) * LDO;
; #pragma unroll
;     for (int r = 0; r < 16; ++r) { const int orow = crow(r, hi);
; #pragma unroll
;         for (int d0 = 0; d0 < 4; ++d0) Ow[(long)orow * LDO + d0 * 32 + r32] = (bf16_t)f2bf(o[d0][r] * rli[r]); }
	v_readlane_b32 s0, v255, 18
	v_readlane_b32 s2, v253, 34
	s_waitcnt lgkmcnt(6)
	v_mfma_scale_f32_32x32x64_f8f6f4 v[0:15], v[128:135], v[88:95], v[0:15], v201, v201 op_sel_hi:[0,0,0]
	v_add_u32_e32 v88, s31, v173
	s_lshl_b32 s0, s0, 7
	v_readlane_b32 s3, v253, 35
	s_ashr_i32 s1, s0, 31
	s_lshl_b64 s[6:7], s[2:3], 11
	v_readlane_b32 s2, v248, 53
	v_readlane_b32 s3, v248, 54
	s_add_u32 s2, s2, s6
	s_addc_u32 s3, s3, s7
	s_lshl_b64 s[0:1], s[0:1], 1
	s_add_u32 s0, s2, s0
	s_addc_u32 s1, s3, s1
	v_readlane_b32 s2, v248, 32
	v_readlane_b32 s3, v248, 33
	s_add_u32 s0, s0, s2
	s_waitcnt lgkmcnt(4)
	v_mfma_scale_f32_32x32x64_f8f6f4 v[48:63], v[128:135], v[80:87], v[48:63], v201, v201 op_sel_hi:[0,0,0]
	ds_read_b128 v[80:83], v88
	ds_read_b128 v[84:87], v88 offset:32
	s_addc_u32 s1, s1, s3
	v_lshlrev_b32_e32 v152, 1, v155
	s_waitcnt lgkmcnt(1)
	v_rcp_f32_e32 v80, v80
	v_rcp_f32_e32 v81, v81
	v_rcp_f32_e32 v82, v82
	v_rcp_f32_e32 v83, v83
	v_mul_f32_e32 v80, 0x41000000, v80
	v_mul_f32_e32 v0, v0, v80
	v_cvt_pk_bf16_f32 v0, v0, v153
	v_mul_f32_e32 v81, 0x41000000, v81
	v_mul_f32_e32 v82, 0x41000000, v82
	v_mul_f32_e32 v83, 0x41000000, v83
	v_mfma_scale_f32_32x32x64_f8f6f4 v[32:47], v[128:135], v[72:79], v[32:47], v201, v201 op_sel_hi:[0,0,0]
	ds_read_b128 v[72:75], v88 offset:64
	ds_read_b128 v[76:79], v88 offset:96
	s_waitcnt lgkmcnt(2)
	v_rcp_f32_e32 v84, v84
	v_rcp_f32_e32 v85, v85
	v_rcp_f32_e32 v86, v86
	s_waitcnt lgkmcnt(1)
	v_rcp_f32_e32 v73, v73
	v_rcp_f32_e32 v74, v74
	v_rcp_f32_e32 v75, v75
	v_mul_f32_e32 v84, 0x41000000, v84
	v_mul_f32_e32 v85, 0x41000000, v85
	v_mul_f32_e32 v86, 0x41000000, v86
	v_rcp_f32_e32 v87, v87
	v_rcp_f32_e32 v72, v72
	v_mul_f32_e32 v87, 0x41000000, v87
	v_mfma_scale_f32_32x32x64_f8f6f4 v[16:31], v[128:135], v[64:71], v[16:31], v201, v201 op_sel_hi:[0,0,0]
	s_waitcnt lgkmcnt(0)
	v_rcp_f32_e32 v64, v76
	v_rcp_f32_e32 v65, v77
	v_rcp_f32_e32 v66, v78
	v_rcp_f32_e32 v67, v79
	v_mul_f32_e32 v68, 0x41000000, v73
	v_mul_f32_e32 v69, 0x41000000, v74
	v_mul_f32_e32 v70, 0x41000000, v75
	v_mul_f32_e32 v71, 0x41000000, v64
	v_mul_f32_e32 v73, 0x41000000, v65
	v_mul_f32_e32 v74, 0x41000000, v66
	v_mul_f32_e32 v75, 0x41000000, v67
	v_lshlrev_b32_e32 v64, 13, v172
	v_lshl_add_u64 v[66:67], s[0:1], 0, v[152:153]
	v_mov_b32_e32 v65, v153
	v_lshl_add_u64 v[64:65], v[66:67], 0, v[64:65]
	global_store_short v[64:65], v0, off
	v_mul_f32_e32 v0, v48, v80
	v_cvt_pk_bf16_f32 v0, v0, v153
	global_store_short v[64:65], v0, off offset:64
	v_mul_f32_e32 v0, v32, v80
	v_cvt_pk_bf16_f32 v0, v0, v153
	global_store_short v[64:65], v0, off offset:128
	v_mul_f32_e32 v0, v16, v80
	v_cvt_pk_bf16_f32 v0, v0, v153
	global_store_short v[64:65], v0, off offset:192
	v_mul_f32_e32 v0, v1, v81
	v_cvt_pk_bf16_f32 v0, v0, v153
	global_store_short v[64:65], v0, off offset:2048
	v_mul_f32_e32 v0, v49, v81
	v_cvt_pk_bf16_f32 v0, v0, v153
	global_store_short v[64:65], v0, off offset:2112
	v_mul_f32_e32 v0, v33, v81
	v_cvt_pk_bf16_f32 v0, v0, v153
	global_store_short v[64:65], v0, off offset:2176
	v_mul_f32_e32 v0, v17, v81
	v_cvt_pk_bf16_f32 v0, v0, v153
	global_store_short v[64:65], v0, off offset:2240
	v_mul_f32_e32 v0, v2, v82
	s_movk_i32 s0, 0x1000
	v_cvt_pk_bf16_f32 v2, v0, v153
	v_add_co_u32_e32 v0, vcc, s0, v64
	s_movk_i32 s0, 0x4000
	s_nop 0
	v_addc_co_u32_e32 v1, vcc, 0, v65, vcc
	global_store_short v[0:1], v2, off
	v_mul_f32_e32 v2, v50, v82
	v_cvt_pk_bf16_f32 v2, v2, v153
	global_store_short v[0:1], v2, off offset:64
	v_mul_f32_e32 v2, v34, v82
	v_cvt_pk_bf16_f32 v2, v2, v153
	global_store_short v[0:1], v2, off offset:128
	v_mul_f32_e32 v2, v18, v82
	v_cvt_pk_bf16_f32 v2, v2, v153
	global_store_short v[0:1], v2, off offset:192
	v_mul_f32_e32 v2, v3, v83
	v_cvt_pk_bf16_f32 v2, v2, v153
	global_store_short v[0:1], v2, off offset:2048
	v_mul_f32_e32 v2, v51, v83
	v_cvt_pk_bf16_f32 v2, v2, v153
	global_store_short v[0:1], v2, off offset:2112
	v_mul_f32_e32 v2, v35, v83
	v_cvt_pk_bf16_f32 v2, v2, v153
	global_store_short v[0:1], v2, off offset:2176
	v_mul_f32_e32 v2, v19, v83
	v_cvt_pk_bf16_f32 v2, v2, v153
	global_store_short v[0:1], v2, off offset:2240
	v_mul_f32_e32 v0, v4, v84
	v_cvt_pk_bf16_f32 v4, v0, v153
	v_add_co_u32_e32 v0, vcc, s0, v64
	s_movk_i32 s0, 0x5000
	s_nop 0
	v_addc_co_u32_e32 v1, vcc, 0, v65, vcc
	v_add_co_u32_e32 v2, vcc, s0, v64
	v_mul_f32_e32 v72, 0x41000000, v72
	s_nop 0
	v_addc_co_u32_e32 v3, vcc, 0, v65, vcc
	global_store_short v[2:3], v4, off offset:-4096
	v_mul_f32_e32 v4, v52, v84
	v_cvt_pk_bf16_f32 v4, v4, v153
	global_store_short v[0:1], v4, off offset:64
	v_mul_f32_e32 v4, v36, v84
	v_cvt_pk_bf16_f32 v4, v4, v153
	global_store_short v[0:1], v4, off offset:128
	v_mul_f32_e32 v4, v20, v84
	v_cvt_pk_bf16_f32 v4, v4, v153
	global_store_short v[0:1], v4, off offset:192
	v_mul_f32_e32 v4, v5, v85
	v_cvt_pk_bf16_f32 v4, v4, v153
	global_store_short v[0:1], v4, off offset:2048
	v_mul_f32_e32 v4, v53, v85
	v_cvt_pk_bf16_f32 v4, v4, v153
	global_store_short v[0:1], v4, off offset:2112
	v_mul_f32_e32 v4, v37, v85
	v_cvt_pk_bf16_f32 v4, v4, v153
	global_store_short v[0:1], v4, off offset:2176
	v_mul_f32_e32 v4, v21, v85
	v_cvt_pk_bf16_f32 v4, v4, v153
	global_store_short v[0:1], v4, off offset:2240
; __device__ __forceinline__ unsigned f2bf(float f) { return pk2(f, 0.f) & 0xffffu; }
; __device__ __forceinline__ int crow(int r, int hi) { return (r & 3) + 8 * (r >> 2) + 4 * hi; }
; #define ECTX_PUBLISH(rt_) do { asm volatile("s_waitcnt vmcnt(0)" ::: "memory"); __syncthreads(); \
;         if (tid == 0) { __builtin_amdgcn_fence(__ATOMIC_RELEASE, "agent"); asm volatile("s_waitcnt vmcnt(0)" ::: "memory"); __hip_atomic_fetch_add(ctl + CW_ECTX + (l * 4 + (rt_)) * 64, 1u, RLX_AGENT); } } while (0)
; __device__ __forceinline__ void attn_unit(const bf16_t* Qb, const unsigned char* Kh, const unsigned char* Vh, bf16_t* Ob, int seq, int cbase, int lbase, int t0, const f32x2* atab, char* lds, const int wave_s) {
;     ...
;     for (int r = 0; r < 16; ++r) { const int orow = crow(r, hi);
; #pragma unroll
;         for (int d0 = 0; d0 < 4; ++d0) Ow[(long)orow * LDO + d0 * 32 + r32] = (bf16_t)f2bf(o[d0][r] * rli[r]); }
;     __syncthreads();
; __global__ void __launch_bounds__(512, 2) mega(Args a) {
;     ...
;                 if (rnd == 2) ECTX_PUBLISH(b);
	v_mul_f32_e32 v0, v6, v86
	v_cvt_pk_bf16_f32 v0, v0, v153
	global_store_short v[2:3], v0, off
	v_mul_f32_e32 v0, v54, v86
	v_cvt_pk_bf16_f32 v0, v0, v153
	global_store_short v[2:3], v0, off offset:64
	v_mul_f32_e32 v0, v38, v86
	v_cvt_pk_bf16_f32 v0, v0, v153
	global_store_short v[2:3], v0, off offset:128
	v_mul_f32_e32 v0, v22, v86
	v_cvt_pk_bf16_f32 v0, v0, v153
	global_store_short v[2:3], v0, off offset:192
	v_mul_f32_e32 v0, v7, v87
	v_cvt_pk_bf16_f32 v0, v0, v153
	global_store_short v[2:3], v0, off offset:2048
	v_mul_f32_e32 v0, v55, v87
	v_cvt_pk_bf16_f32 v0, v0, v153
	global_store_short v[2:3], v0, off offset:2112
	v_mul_f32_e32 v0, v39, v87
	v_cvt_pk_bf16_f32 v0, v0, v153
	global_store_short v[2:3], v0, off offset:2176
	v_mul_f32_e32 v0, v23, v87
	v_cvt_pk_bf16_f32 v0, v0, v153
	global_store_short v[2:3], v0, off offset:2240
	v_mul_f32_e32 v0, v8, v72
	s_mov_b32 s0, 0x8000
	v_cvt_pk_bf16_f32 v4, v0, v153
	v_add_co_u32_e32 v0, vcc, s0, v64
	s_mov_b32 s0, 0x9000
	s_nop 0
	v_addc_co_u32_e32 v1, vcc, 0, v65, vcc
	v_add_co_u32_e32 v2, vcc, s0, v64
	s_mov_b32 s0, 0xc000
	s_nop 0
	v_addc_co_u32_e32 v3, vcc, 0, v65, vcc
	global_store_short v[2:3], v4, off offset:-4096
	v_mul_f32_e32 v4, v56, v72
	v_cvt_pk_bf16_f32 v4, v4, v153
	global_store_short v[0:1], v4, off offset:64
	v_mul_f32_e32 v4, v40, v72
	v_cvt_pk_bf16_f32 v4, v4, v153
	global_store_short v[0:1], v4, off offset:128
	v_mul_f32_e32 v4, v24, v72
	v_cvt_pk_bf16_f32 v4, v4, v153
	global_store_short v[0:1], v4, off offset:192
	v_mul_f32_e32 v4, v9, v68
	v_cvt_pk_bf16_f32 v4, v4, v153
	global_store_short v[0:1], v4, off offset:2048
	v_mul_f32_e32 v4, v57, v68
	v_cvt_pk_bf16_f32 v4, v4, v153
	global_store_short v[0:1], v4, off offset:2112
	v_mul_f32_e32 v4, v41, v68
	v_cvt_pk_bf16_f32 v4, v4, v153
	global_store_short v[0:1], v4, off offset:2176
	v_mul_f32_e32 v4, v25, v68
	v_cvt_pk_bf16_f32 v4, v4, v153
	global_store_short v[0:1], v4, off offset:2240
	v_mul_f32_e32 v0, v10, v69
	v_cvt_pk_bf16_f32 v0, v0, v153
	global_store_short v[2:3], v0, off
	v_mul_f32_e32 v0, v58, v69
	v_cvt_pk_bf16_f32 v0, v0, v153
	global_store_short v[2:3], v0, off offset:64
	v_mul_f32_e32 v0, v42, v69
	v_cvt_pk_bf16_f32 v0, v0, v153
	global_store_short v[2:3], v0, off offset:128
	v_mul_f32_e32 v0, v26, v69
	v_cvt_pk_bf16_f32 v0, v0, v153
	global_store_short v[2:3], v0, off offset:192
	v_mul_f32_e32 v0, v11, v70
	v_cvt_pk_bf16_f32 v0, v0, v153
	global_store_short v[2:3], v0, off offset:2048
	v_mul_f32_e32 v0, v59, v70
	v_cvt_pk_bf16_f32 v0, v0, v153
	global_store_short v[2:3], v0, off offset:2112
	v_mul_f32_e32 v0, v43, v70
	v_cvt_pk_bf16_f32 v0, v0, v153
	global_store_short v[2:3], v0, off offset:2176
	v_mul_f32_e32 v0, v27, v70
	v_cvt_pk_bf16_f32 v0, v0, v153
	global_store_short v[2:3], v0, off offset:2240
	v_mul_f32_e32 v0, v12, v71
	v_cvt_pk_bf16_f32 v4, v0, v153
	v_add_co_u32_e32 v0, vcc, s0, v64
	s_mov_b32 s0, 0xd000
	s_nop 0
	v_addc_co_u32_e32 v1, vcc, 0, v65, vcc
	v_add_co_u32_e32 v2, vcc, s0, v64
	s_nop 1
	v_addc_co_u32_e32 v3, vcc, 0, v65, vcc
	global_store_short v[2:3], v4, off offset:-4096
	v_mul_f32_e32 v4, v60, v71
	v_cvt_pk_bf16_f32 v4, v4, v153
	global_store_short v[0:1], v4, off offset:64
	v_mul_f32_e32 v4, v44, v71
	v_cvt_pk_bf16_f32 v4, v4, v153
	global_store_short v[0:1], v4, off offset:128
	v_mul_f32_e32 v4, v28, v71
	v_cvt_pk_bf16_f32 v4, v4, v153
	global_store_short v[0:1], v4, off offset:192
	v_mul_f32_e32 v4, v13, v73
	v_cvt_pk_bf16_f32 v4, v4, v153
	global_store_short v[0:1], v4, off offset:2048
	v_mul_f32_e32 v4, v61, v73
	v_cvt_pk_bf16_f32 v4, v4, v153
	global_store_short v[0:1], v4, off offset:2112
	v_mul_f32_e32 v4, v45, v73
	v_cvt_pk_bf16_f32 v4, v4, v153
	global_store_short v[0:1], v4, off offset:2176
	v_mul_f32_e32 v4, v29, v73
	v_cvt_pk_bf16_f32 v4, v4, v153
	global_store_short v[0:1], v4, off offset:2240
	v_mul_f32_e32 v0, v14, v74
	v_cvt_pk_bf16_f32 v0, v0, v153
	global_store_short v[2:3], v0, off
	v_mul_f32_e32 v0, v62, v74
	v_cvt_pk_bf16_f32 v0, v0, v153
	global_store_short v[2:3], v0, off offset:64
	v_mul_f32_e32 v0, v46, v74
	v_cvt_pk_bf16_f32 v0, v0, v153
	global_store_short v[2:3], v0, off offset:128
	v_mul_f32_e32 v0, v30, v74
	v_cvt_pk_bf16_f32 v0, v0, v153
	global_store_short v[2:3], v0, off offset:192
	v_mul_f32_e32 v0, v15, v75
	v_cvt_pk_bf16_f32 v0, v0, v153
	global_store_short v[2:3], v0, off offset:2048
	v_mul_f32_e32 v0, v63, v75
	v_cvt_pk_bf16_f32 v0, v0, v153
	global_store_short v[2:3], v0, off offset:2112
	v_mul_f32_e32 v0, v47, v75
	v_cvt_pk_bf16_f32 v0, v0, v153
	global_store_short v[2:3], v0, off offset:2176
	v_mul_f32_e32 v0, v31, v75
	s_andn2_b64 vcc, exec, s[52:53]
	v_cvt_pk_bf16_f32 v0, v0, v153
	global_store_short v[2:3], v0, off offset:2240
	s_waitcnt vmcnt(63) expcnt(7) lgkmcnt(15)
	s_barrier
	s_cbranch_vccnz .LBB0_583
	s_waitcnt vmcnt(0)
	s_barrier
	s_and_saveexec_b64 s[0:1], s[40:41]
	s_cbranch_execz .LBB0_582
	v_readlane_b32 s2, v255, 17
	s_lshl_b32 s2, s2, 6
	s_add_i32 s6, s2, s62
	s_ashr_i32 s7, s6, 31
	s_lshl_b64 s[6:7], s[6:7], 2
	v_readlane_b32 s2, v248, 34
	s_add_u32 s6, s2, s6
	v_readlane_b32 s2, v248, 35
	s_addc_u32 s7, s2, s7
	buffer_wbl2 sc1
	s_waitcnt vmcnt(0)
	s_waitcnt vmcnt(0)
	global_atomic_add v153, v197, s[6:7]

; #define LAS __attribute__((address_space(3)))
; __device__ __forceinline__ unsigned pk4_fp8(float x0, float x1, float x2, float x3) { int w = 0; w = __builtin_amdgcn_cvt_pk_fp8_f32(x0, x1, w, false); w = __builtin_amdgcn_cvt_pk_fp8_f32(x2, x3, w, true); return (unsigned)w; }
; __device__ __forceinline__ void transpose_item_fp8w(const float* W, int K, int N, unsigned char* WT, float q, LAS unsigned char* scr, int item, int lane) {
;     const int nblk = N / 128, kb = item / nblk, nb = item % nblk, k0 = 64 * kb, n0 = 128 * nb;
;     const int l5 = lane & 31, h = lane >> 5;
;     const float* src = W + (size_t)(k0 + 16 * h) * N + n0 + 4 * l5;
; #pragma unroll
;     for (int b = 0; b < 2; ++b) {
;         f32x4 x[16];
; #pragma unroll
;         for (int s_ = 0; s_ < 16; ++s_) x[s_] = *(const f32x4*)(src + (size_t)(32 * b + s_) * N);
; #pragma unroll
;         for (int i = 0; i < 4; ++i) {
;             u32x4 o;
;             o.x = pk4_fp8(x[0][i] * q, x[1][i] * q, x[2][i] * q, x[3][i] * q); o.y = pk4_fp8(x[4][i] * q, x[5][i] * q, x[6][i] * q, x[7][i] * q);
;             o.z = pk4_fp8(x[8][i] * q, x[9][i] * q, x[10][i] * q, x[11][i] * q); o.w = pk4_fp8(x[12][i] * q, x[13][i] * q, x[14][i] * q, x[15][i] * q);
;             *(LAS u32x4*)(scr + (l5 + 32 * i) * 80 + (2 * b + h) * 16) = o; }
;     }
;     asm volatile("s_waitcnt lgkmcnt(0)" ::: "memory");
; #pragma unroll
;     for (int qd = 0; qd < 8; ++qd) {
;         const int rho = 16 * qd + (lane >> 2), piece = lane & 3;
;         const u32x4 o = *(const LAS u32x4*)(scr + rho * 80 + piece * 16);
;         const int nl = 4 * (rho & 31) + (rho >> 5);
;         *(u32x4*)(WT + (size_t)(n0 + nl) * K + k0 + piece * 16) = o; }
;     asm volatile("s_waitcnt lgkmcnt(0)" ::: "memory");
; }
.LBB0_662:
	s_cmpk_gt_i32 s5, 0x3df
	s_mov_b64 s[0:1], -1
	s_cbranch_scc0 .LBB0_694
	s_cmpk_gt_u32 s5, 0x46f
	s_cbranch_scc0 .LBB0_681
	s_cmpk_gt_u32 s5, 0x4ef
	s_cbranch_scc0 .LBB0_676
	s_cmpk_gt_u32 s5, 0x6ef
	s_cbranch_scc0 .LBB0_671
	s_cmpk_gt_u32 s5, 0x26ef
	v_lshlrev_b32_e32 v152, 2, v64
	v_add_u32_e32 v118, v102, v103
	s_cbranch_scc0 .LBB0_668
	s_add_i32 s4, s5, 0xffffd910
	v_readlane_b32 s2, v253, 32
	s_lshr_b32 s0, s4, 7
	v_readlane_b32 s3, v253, 33
	s_mov_b32 s11, s3
	s_add_i32 s10, s0, s56
	v_readlane_b32 s40, v253, 58
	s_lshl_b64 s[2:3], s[10:11], 20
	s_lshl_b64 s[0:1], s[10:11], 22
	v_readlane_b32 s54, v254, 8
	v_readlane_b32 s55, v254, 9
	s_add_u32 s8, s54, s0
	s_addc_u32 s9, s55, s1
	v_readlane_b32 s0, v246, 17
	s_add_u32 s1, s0, s2
	v_readlane_b32 s0, v246, 18
	s_addc_u32 s6, s0, s3
	s_lshl_b32 s0, s4, 6
	s_and_b32 s7, s0, 0x3c0
	v_add_u32_e32 v0, s7, v99
	s_lshl_b32 s0, s4, 3
	v_ashrrev_i32_e32 v1, 31, v0
	s_and_b32 s0, s0, 0x380
	v_lshlrev_b64 v[0:1], 12, v[0:1]
	v_lshl_add_u64 v[0:1], s[8:9], 0, v[0:1]
	s_lshl_b32 s10, s0, 2
	s_mov_b32 s3, s11
	v_readlane_b32 s41, v253, 59
	v_readlane_b32 s42, v253, 60
	v_readlane_b32 s43, v253, 61
	v_readlane_b32 s44, v253, 62
	v_readlane_b32 s45, v253, 63
	v_writelane_b32 v253, s2, 32
	v_lshl_add_u64 v[0:1], v[0:1], 0, s[10:11]
	v_lshl_add_u64 v[100:101], v[0:1], 0, v[152:153]
	v_writelane_b32 v253, s3, 33
	s_movk_i32 s2, 0x2000
	v_add_co_u32_e32 v8, vcc, s2, v100
	s_movk_i32 s2, 0x4000
	s_nop 0
	v_addc_co_u32_e32 v9, vcc, 0, v101, vcc
	v_add_co_u32_e32 v12, vcc, s2, v100
	s_movk_i32 s2, 0x6000
	s_nop 0
	v_addc_co_u32_e32 v13, vcc, 0, v101, vcc
	v_add_co_u32_e32 v24, vcc, s2, v100
	s_mov_b32 s2, 0x8000
	s_nop 0
	v_addc_co_u32_e32 v25, vcc, 0, v101, vcc
	v_add_co_u32_e32 v28, vcc, s2, v100
	s_mov_b32 s2, 0xa000
	s_nop 0
	v_addc_co_u32_e32 v29, vcc, 0, v101, vcc
	v_add_co_u32_e32 v40, vcc, s2, v100
	s_mov_b32 s2, 0xc000
	s_nop 0
	v_addc_co_u32_e32 v41, vcc, 0, v101, vcc
	global_load_dwordx4 v[0:3], v[100:101], off nt
	v_add_co_u32_e32 v44, vcc, s2, v100
	global_load_dwordx4 v[4:7], v[8:9], off offset:-4096 nt
	s_nop 0
	global_load_dwordx4 v[8:11], v[8:9], off nt
	s_nop 0
	global_load_dwordx4 v[16:19], v[12:13], off offset:-4096 nt
	s_nop 0
	global_load_dwordx4 v[12:15], v[12:13], off nt
	v_addc_co_u32_e32 v45, vcc, 0, v101, vcc
	s_mov_b32 s2, 0xe000
	global_load_dwordx4 v[20:23], v[24:25], off offset:-4096 nt
	s_nop 0
	global_load_dwordx4 v[24:27], v[24:25], off nt
	s_nop 0
	global_load_dwordx4 v[32:35], v[28:29], off offset:-4096 nt
	s_nop 0
	global_load_dwordx4 v[28:31], v[28:29], off nt
	v_add_co_u32_e32 v56, vcc, s2, v100
	global_load_dwordx4 v[36:39], v[40:41], off offset:-4096 nt
	s_nop 0
	global_load_dwordx4 v[40:43], v[40:41], off nt
	s_nop 0
	global_load_dwordx4 v[48:51], v[44:45], off offset:-4096 nt
	s_nop 0
	global_load_dwordx4 v[44:47], v[44:45], off nt
	v_addc_co_u32_e32 v57, vcc, 0, v101, vcc
	global_load_dwordx4 v[52:55], v[56:57], off offset:-4096 nt
	s_nop 0
	global_load_dwordx4 v[56:59], v[56:57], off nt
	s_mov_b32 s2, 0xf000
	v_add_co_u32_e32 v60, vcc, s2, v100
	s_nop 0
	v_addc_co_u32_e32 v61, vcc, 0, v101, vcc
	global_load_dwordx4 v[60:63], v[60:61], off nt
	s_mov_b32 s2, 0x21000
	v_readlane_b32 s46, v254, 0
	v_readlane_b32 s47, v254, 1
	v_readlane_b32 s48, v254, 2
	v_readlane_b32 s49, v254, 3
	v_readlane_b32 s50, v254, 4
	v_readlane_b32 s51, v254, 5
	v_readlane_b32 s52, v254, 6
	v_readlane_b32 s53, v254, 7
	s_waitcnt vmcnt(0)
	v_mul_f32_e32 v0, 0x43800000, v0
	v_mul_f32_e32 v4, 0x43800000, v4
	v_cvt_pk_fp8_f32 v120, v0, v4
	v_mul_f32_e32 v0, 0x43800000, v12
	v_mul_f32_e32 v8, 0x43800000, v8
	v_mul_f32_e32 v16, 0x43800000, v16
	v_mul_f32_e32 v4, 0x43800000, v20
	v_cvt_pk_fp8_f32 v121, v0, v4
	v_mul_f32_e32 v0, 0x43800000, v28
	v_cvt_pk_fp8_f32 v120, v8, v16 op_sel:[0,0,1]
	v_mul_f32_e32 v4, 0x43800000, v36
	v_cvt_pk_fp8_f32 v122, v0, v4
	v_mul_f32_e32 v0, 0x43800000, v44
	v_mul_f32_e32 v8, 0x43800000, v24
	v_mul_f32_e32 v4, 0x43800000, v52
	v_cvt_pk_fp8_f32 v123, v0, v4
	v_mul_f32_e32 v12, 0x43800000, v32
	v_cvt_pk_fp8_f32 v121, v8, v12 op_sel:[0,0,1]
	v_mul_f32_e32 v8, 0x43800000, v40
	v_mul_f32_e32 v12, 0x43800000, v48
	v_cvt_pk_fp8_f32 v122, v8, v12 op_sel:[0,0,1]
	v_mul_f32_e32 v8, 0x43800000, v56
	v_mul_f32_e32 v12, 0x43800000, v60
	v_cvt_pk_fp8_f32 v123, v8, v12 op_sel:[0,0,1]
	v_mul_f32_e32 v0, 0x43800000, v1
	v_mul_f32_e32 v1, 0x43800000, v5
	v_mul_f32_e32 v4, 0x43800000, v9
	ds_write_b128 v117, v[120:123]
	v_cvt_pk_fp8_f32 v120, v0, v1
	v_mul_f32_e32 v0, 0x43800000, v13
	v_mul_f32_e32 v1, 0x43800000, v21
	v_cvt_pk_fp8_f32 v121, v0, v1
	v_mul_f32_e32 v0, 0x43800000, v29
	v_mul_f32_e32 v1, 0x43800000, v37
	v_cvt_pk_fp8_f32 v122, v0, v1
	v_mul_f32_e32 v0, 0x43800000, v45
	v_mul_f32_e32 v1, 0x43800000, v53
	v_mul_f32_e32 v5, 0x43800000, v17
	v_cvt_pk_fp8_f32 v123, v0, v1
	v_cvt_pk_fp8_f32 v120, v4, v5 op_sel:[0,0,1]
	v_mul_f32_e32 v4, 0x43800000, v25
	v_mul_f32_e32 v5, 0x43800000, v33
	v_cvt_pk_fp8_f32 v121, v4, v5 op_sel:[0,0,1]
	v_mul_f32_e32 v4, 0x43800000, v41
	v_mul_f32_e32 v5, 0x43800000, v49
	v_cvt_pk_fp8_f32 v122, v4, v5 op_sel:[0,0,1]
	v_mul_f32_e32 v4, 0x43800000, v57
	v_mul_f32_e32 v5, 0x43800000, v61
	v_cvt_pk_fp8_f32 v123, v4, v5 op_sel:[0,0,1]
	v_mul_f32_e32 v0, 0x43800000, v2
	v_mul_f32_e32 v1, 0x43800000, v6
	v_mul_f32_e32 v2, 0x43800000, v10
	ds_write_b128 v117, v[120:123] offset:2560
	v_cvt_pk_fp8_f32 v120, v0, v1
	v_mul_f32_e32 v0, 0x43800000, v14
	v_mul_f32_e32 v1, 0x43800000, v22
	v_cvt_pk_fp8_f32 v121, v0, v1
	v_mul_f32_e32 v0, 0x43800000, v30
	v_mul_f32_e32 v1, 0x43800000, v38
	v_cvt_pk_fp8_f32 v122, v0, v1
	v_mul_f32_e32 v0, 0x43800000, v46
; #define LAS __attribute__((address_space(3)))
; __device__ __forceinline__ unsigned pk4_fp8(float x0, float x1, float x2, float x3) { int w = 0; w = __builtin_amdgcn_cvt_pk_fp8_f32(x0, x1, w, false); w = __builtin_amdgcn_cvt_pk_fp8_f32(x2, x3, w, true); return (unsigned)w; }
; __device__ __forceinline__ void transpose_item_fp8w(const float* W, int K, int N, unsigned char* WT, float q, LAS unsigned char* scr, int item, int lane) {
;     ...
;     for (int b = 0; b < 2; ++b) {
;         f32x4 x[16];
; #pragma unroll
;         for (int s_ = 0; s_ < 16; ++s_) x[s_] = *(const f32x4*)(src + (size_t)(32 * b + s_) * N);
; #pragma unroll
;         for (int i = 0; i < 4; ++i) {
;             u32x4 o;
;             o.x = pk4_fp8(x[0][i] * q, x[1][i] * q, x[2][i] * q, x[3][i] * q); o.y = pk4_fp8(x[4][i] * q, x[5][i] * q, x[6][i] * q, x[7][i] * q);
;             o.z = pk4_fp8(x[8][i] * q, x[9][i] * q, x[10][i] * q, x[11][i] * q); o.w = pk4_fp8(x[12][i] * q, x[13][i] * q, x[14][i] * q, x[15][i] * q);
;             *(LAS u32x4*)(scr + (l5 + 32 * i) * 80 + (2 * b + h) * 16) = o; }
	v_mul_f32_e32 v1, 0x43800000, v54
	v_mul_f32_e32 v4, 0x43800000, v18
	v_cvt_pk_fp8_f32 v123, v0, v1
	v_cvt_pk_fp8_f32 v120, v2, v4 op_sel:[0,0,1]
	v_mul_f32_e32 v2, 0x43800000, v26
	v_mul_f32_e32 v4, 0x43800000, v34
	v_cvt_pk_fp8_f32 v121, v2, v4 op_sel:[0,0,1]
	v_mul_f32_e32 v2, 0x43800000, v42
	v_mul_f32_e32 v4, 0x43800000, v50
	v_cvt_pk_fp8_f32 v122, v2, v4 op_sel:[0,0,1]
	v_mul_f32_e32 v2, 0x43800000, v58
	v_mul_f32_e32 v4, 0x43800000, v62
	v_cvt_pk_fp8_f32 v123, v2, v4 op_sel:[0,0,1]
	v_mul_f32_e32 v1, 0x43800000, v3
	v_mul_f32_e32 v2, 0x43800000, v7
	v_cvt_pk_fp8_f32 v0, v1, v2
	v_mul_f32_e32 v3, 0x43800000, v11
	v_mul_f32_e32 v4, 0x43800000, v19
	v_mul_f32_e32 v2, 0x43800000, v15
	v_cvt_pk_fp8_f32 v0, v3, v4 op_sel:[0,0,1]
	v_mul_f32_e32 v3, 0x43800000, v23
	v_cvt_pk_fp8_f32 v1, v2, v3
	v_mul_f32_e32 v4, 0x43800000, v27
	v_mul_f32_e32 v5, 0x43800000, v35
	v_mul_f32_e32 v3, 0x43800000, v31
	v_cvt_pk_fp8_f32 v1, v4, v5 op_sel:[0,0,1]
	v_mul_f32_e32 v4, 0x43800000, v39
	v_cvt_pk_fp8_f32 v2, v3, v4
	v_mul_f32_e32 v5, 0x43800000, v43
	v_mul_f32_e32 v6, 0x43800000, v51
	v_mul_f32_e32 v4, 0x43800000, v47
	v_cvt_pk_fp8_f32 v2, v5, v6 op_sel:[0,0,1]
	v_mul_f32_e32 v5, 0x43800000, v55
	v_cvt_pk_fp8_f32 v3, v4, v5
	v_mul_f32_e32 v6, 0x43800000, v59
	v_mul_f32_e32 v7, 0x43800000, v63
	ds_write_b128 v117, v[120:123] offset:5120
	v_cvt_pk_fp8_f32 v3, v6, v7 op_sel:[0,0,1]
	v_mov_b32_e32 v122, v153
	v_mov_b32_e32 v121, v153
	ds_write_b128 v117, v[0:3] offset:7680
	v_add_co_u32_e32 v0, vcc, s2, v100
	s_mov_b32 s2, 0x23000
	s_nop 0
	v_addc_co_u32_e32 v1, vcc, 0, v101, vcc
	global_load_dwordx4 v[32:35], v[0:1], off offset:-4096 nt
	global_load_dwordx4 v[36:39], v[0:1], off nt
	v_add_co_u32_e32 v0, vcc, s2, v100
	s_mov_b32 s2, 0x25000
	s_nop 0
	v_addc_co_u32_e32 v1, vcc, 0, v101, vcc
	global_load_dwordx4 v[48:51], v[0:1], off offset:-4096 nt
	global_load_dwordx4 v[52:55], v[0:1], off nt
	v_add_co_u32_e32 v0, vcc, s2, v100
	s_mov_b32 s2, 0x27000
	s_nop 0
	v_addc_co_u32_e32 v1, vcc, 0, v101, vcc
	global_load_dwordx4 v[40:43], v[0:1], off offset:-4096 nt
	global_load_dwordx4 v[44:47], v[0:1], off nt
	v_add_co_u32_e32 v0, vcc, s2, v100
	s_mov_b32 s2, 0x29000
	s_nop 0
	v_addc_co_u32_e32 v1, vcc, 0, v101, vcc
	v_add_co_u32_e32 v4, vcc, s2, v100
	s_mov_b32 s2, 0x2b000
	s_nop 0
	v_addc_co_u32_e32 v5, vcc, 0, v101, vcc
	v_add_co_u32_e32 v8, vcc, s2, v100
	s_mov_b32 s2, 0x2d000
	s_nop 0
	v_addc_co_u32_e32 v9, vcc, 0, v101, vcc
	v_add_co_u32_e32 v12, vcc, s2, v100
	global_load_dwordx4 v[56:59], v[0:1], off offset:-4096 nt
	global_load_dwordx4 v[60:63], v[0:1], off nt
	s_nop 0
	global_load_dwordx4 v[0:3], v[4:5], off offset:-4096 nt
	s_nop 0
	global_load_dwordx4 v[4:7], v[4:5], off nt
	v_addc_co_u32_e32 v13, vcc, 0, v101, vcc
	global_load_dwordx4 v[16:19], v[8:9], off offset:-4096 nt
	global_load_dwordx4 v[20:23], v[8:9], off nt
	s_nop 0
	global_load_dwordx4 v[8:11], v[12:13], off offset:-4096 nt
	s_nop 0
	global_load_dwordx4 v[12:15], v[12:13], off nt
	s_mov_b32 s2, 0x2f000
	v_add_co_u32_e32 v28, vcc, s2, v100
	s_nop 0
	v_addc_co_u32_e32 v29, vcc, 0, v101, vcc
	global_load_dwordx4 v[24:27], v[28:29], off offset:-4096 nt
	s_nop 0
	global_load_dwordx4 v[28:31], v[28:29], off nt
	s_add_u32 s2, s1, s7
	s_addc_u32 s3, s6, 0
	s_waitcnt vmcnt(0)
	v_mul_f32_e32 v32, 0x43800000, v32
	s_waitcnt vmcnt(14)
	v_mul_f32_e32 v36, 0x43800000, v36
	v_cvt_pk_fp8_f32 v120, v32, v36
	s_waitcnt vmcnt(13)
	v_mul_f32_e32 v48, 0x43800000, v48
	s_waitcnt vmcnt(12)
	v_mul_f32_e32 v52, 0x43800000, v52
	v_cvt_pk_fp8_f32 v120, v48, v52 op_sel:[0,0,1]
	s_waitcnt vmcnt(11)
	v_mul_f32_e32 v32, 0x43800000, v40
	s_waitcnt vmcnt(10)
	v_mul_f32_e32 v36, 0x43800000, v44
	v_cvt_pk_fp8_f32 v121, v32, v36
	s_waitcnt vmcnt(9)
	v_mul_f32_e32 v40, 0x43800000, v56
	s_waitcnt vmcnt(7)
	v_mul_f32_e32 v0, 0x43800000, v0
	s_waitcnt vmcnt(6)
	v_mul_f32_e32 v4, 0x43800000, v4
	v_cvt_pk_fp8_f32 v122, v0, v4
	v_mul_f32_e32 v44, 0x43800000, v60
	s_waitcnt vmcnt(3)
	v_mul_f32_e32 v0, 0x43800000, v8
	s_waitcnt vmcnt(2)
	v_mul_f32_e32 v4, 0x43800000, v12
	v_cvt_pk_fp8_f32 v123, v0, v4
	v_mul_f32_e32 v16, 0x43800000, v16
	v_mul_f32_e32 v20, 0x43800000, v20
	v_cvt_pk_fp8_f32 v121, v40, v44 op_sel:[0,0,1]
	v_cvt_pk_fp8_f32 v122, v16, v20 op_sel:[0,0,1]
	s_waitcnt vmcnt(1)
	v_mul_f32_e32 v8, 0x43800000, v24
	s_waitcnt vmcnt(0)
; #define LAS __attribute__((address_space(3)))
; __device__ __forceinline__ unsigned pk4_fp8(float x0, float x1, float x2, float x3) { int w = 0; w = __builtin_amdgcn_cvt_pk_fp8_f32(x0, x1, w, false); w = __builtin_amdgcn_cvt_pk_fp8_f32(x2, x3, w, true); return (unsigned)w; }
; __device__ __forceinline__ void transpose_item_fp8w(const float* W, int K, int N, unsigned char* WT, float q, LAS unsigned char* scr, int item, int lane) {
;     ...
; #pragma unroll
;         for (int s_ = 0; s_ < 16; ++s_) x[s_] = *(const f32x4*)(src + (size_t)(32 * b + s_) * N);
; #pragma unroll
;         for (int i = 0; i < 4; ++i) {
;             u32x4 o;
;             o.x = pk4_fp8(x[0][i] * q, x[1][i] * q, x[2][i] * q, x[3][i] * q); o.y = pk4_fp8(x[4][i] * q, x[5][i] * q, x[6][i] * q, x[7][i] * q);
;             o.z = pk4_fp8(x[8][i] * q, x[9][i] * q, x[10][i] * q, x[11][i] * q); o.w = pk4_fp8(x[12][i] * q, x[13][i] * q, x[14][i] * q, x[15][i] * q);
;             *(LAS u32x4*)(scr + (l5 + 32 * i) * 80 + (2 * b + h) * 16) = o; }
;     }
;     asm volatile("s_waitcnt lgkmcnt(0)" ::: "memory");
; #pragma unroll
;     for (int qd = 0; qd < 8; ++qd) {
;         const int rho = 16 * qd + (lane >> 2), piece = lane & 3;
;         const u32x4 o = *(const LAS u32x4*)(scr + rho * 80 + piece * 16);
;         const int nl = 4 * (rho & 31) + (rho >> 5);
;         *(u32x4*)(WT + (size_t)(n0 + nl) * K + k0 + piece * 16) = o; }
;     asm volatile("s_waitcnt lgkmcnt(0)" ::: "memory");
	v_mul_f32_e32 v12, 0x43800000, v28
	v_cvt_pk_fp8_f32 v123, v8, v12 op_sel:[0,0,1]
	v_mul_f32_e32 v0, 0x43800000, v33
	v_mul_f32_e32 v4, 0x43800000, v37
	v_mul_f32_e32 v8, 0x43800000, v49
	ds_write_b128 v117, v[120:123] offset:32
	v_cvt_pk_fp8_f32 v120, v0, v4
	v_mul_f32_e32 v0, 0x43800000, v41
	v_mul_f32_e32 v4, 0x43800000, v45
	v_cvt_pk_fp8_f32 v121, v0, v4
	v_mul_f32_e32 v0, 0x43800000, v1
	v_mul_f32_e32 v1, 0x43800000, v5
	v_cvt_pk_fp8_f32 v122, v0, v1
	v_mul_f32_e32 v0, 0x43800000, v9
	v_mul_f32_e32 v1, 0x43800000, v13
	v_cvt_pk_fp8_f32 v123, v0, v1
	v_mul_f32_e32 v12, 0x43800000, v53
	v_mul_f32_e32 v4, 0x43800000, v17
	v_mul_f32_e32 v5, 0x43800000, v21
	v_cvt_pk_fp8_f32 v120, v8, v12 op_sel:[0,0,1]
	v_mul_f32_e32 v8, 0x43800000, v57
	v_mul_f32_e32 v12, 0x43800000, v61
	v_cvt_pk_fp8_f32 v122, v4, v5 op_sel:[0,0,1]
	v_mul_f32_e32 v4, 0x43800000, v25
	v_mul_f32_e32 v5, 0x43800000, v29
	v_cvt_pk_fp8_f32 v121, v8, v12 op_sel:[0,0,1]
	v_cvt_pk_fp8_f32 v123, v4, v5 op_sel:[0,0,1]
	v_mul_f32_e32 v0, 0x43800000, v34
	v_mul_f32_e32 v1, 0x43800000, v38
	v_mul_f32_e32 v4, 0x43800000, v50
	ds_write_b128 v117, v[120:123] offset:2592
	v_cvt_pk_fp8_f32 v120, v0, v1
	v_mul_f32_e32 v0, 0x43800000, v42
	v_mul_f32_e32 v1, 0x43800000, v46
	v_cvt_pk_fp8_f32 v121, v0, v1
	v_mul_f32_e32 v0, 0x43800000, v2
	v_mul_f32_e32 v1, 0x43800000, v6
	v_cvt_pk_fp8_f32 v122, v0, v1
	v_mul_f32_e32 v0, 0x43800000, v10
	v_mul_f32_e32 v1, 0x43800000, v14
	v_mul_f32_e32 v5, 0x43800000, v54
	v_cvt_pk_fp8_f32 v123, v0, v1
	v_cvt_pk_fp8_f32 v120, v4, v5 op_sel:[0,0,1]
	v_mul_f32_e32 v4, 0x43800000, v58
	v_mul_f32_e32 v5, 0x43800000, v62
	v_cvt_pk_fp8_f32 v121, v4, v5 op_sel:[0,0,1]
	v_mul_f32_e32 v2, 0x43800000, v18
	v_mul_f32_e32 v4, 0x43800000, v22
	v_cvt_pk_fp8_f32 v122, v2, v4 op_sel:[0,0,1]
	v_mul_f32_e32 v2, 0x43800000, v26
	v_mul_f32_e32 v4, 0x43800000, v30
	v_cvt_pk_fp8_f32 v123, v2, v4 op_sel:[0,0,1]
	v_mul_f32_e32 v1, 0x43800000, v35
	v_mul_f32_e32 v2, 0x43800000, v39
	v_cvt_pk_fp8_f32 v0, v1, v2
	v_mul_f32_e32 v4, 0x43800000, v51
	v_mul_f32_e32 v5, 0x43800000, v55
	v_mul_f32_e32 v2, 0x43800000, v43
	v_cvt_pk_fp8_f32 v0, v4, v5 op_sel:[0,0,1]
	v_mul_f32_e32 v4, 0x43800000, v47
	v_cvt_pk_fp8_f32 v1, v2, v4
	v_mul_f32_e32 v3, 0x43800000, v3
	v_mul_f32_e32 v4, 0x43800000, v7
	v_cvt_pk_fp8_f32 v2, v3, v4
	v_mul_f32_e32 v5, 0x43800000, v59
	v_mul_f32_e32 v6, 0x43800000, v63
	v_cvt_pk_fp8_f32 v1, v5, v6 op_sel:[0,0,1]
	v_mul_f32_e32 v5, 0x43800000, v19
	v_mul_f32_e32 v6, 0x43800000, v23
	v_cvt_pk_fp8_f32 v2, v5, v6 op_sel:[0,0,1]
	v_mul_f32_e32 v4, 0x43800000, v11
	v_mul_f32_e32 v5, 0x43800000, v15
	v_cvt_pk_fp8_f32 v3, v4, v5
	v_mul_f32_e32 v6, 0x43800000, v27
	v_mul_f32_e32 v7, 0x43800000, v31
	ds_write_b128 v117, v[120:123] offset:5152
	v_cvt_pk_fp8_f32 v3, v6, v7 op_sel:[0,0,1]
	v_add_u32_e32 v6, s0, v104
	v_ashrrev_i32_e32 v7, 31, v6
	v_lshl_add_u64 v[4:5], s[2:3], 0, v[66:67]
	ds_write_b128 v117, v[0:3] offset:7712
	s_waitcnt lgkmcnt(0)
	ds_read_b128 v[0:3], v118
	v_lshlrev_b64 v[6:7], 10, v[6:7]
	v_lshl_add_u64 v[6:7], v[4:5], 0, v[6:7]
	s_waitcnt lgkmcnt(0)
	global_store_dwordx4 v[6:7], v[0:3], off nt
	ds_read_b128 v[0:3], v118 offset:1280
	v_add_u32_e32 v6, s0, v105
	v_ashrrev_i32_e32 v7, 31, v6
	v_lshlrev_b64 v[6:7], 10, v[6:7]
	v_lshl_add_u64 v[6:7], v[4:5], 0, v[6:7]
	s_waitcnt lgkmcnt(0)
	global_store_dwordx4 v[6:7], v[0:3], off nt
	ds_read_b128 v[0:3], v118 offset:2560
	v_add_u32_e32 v6, s0, v106
	v_ashrrev_i32_e32 v7, 31, v6
	v_lshlrev_b64 v[6:7], 10, v[6:7]
	v_lshl_add_u64 v[6:7], v[4:5], 0, v[6:7]
	s_waitcnt lgkmcnt(0)
	global_store_dwordx4 v[6:7], v[0:3], off nt
	ds_read_b128 v[0:3], v118 offset:3840
	v_add_u32_e32 v6, s0, v107
	v_ashrrev_i32_e32 v7, 31, v6
	v_lshlrev_b64 v[6:7], 10, v[6:7]
	v_lshl_add_u64 v[6:7], v[4:5], 0, v[6:7]
	s_waitcnt lgkmcnt(0)
	global_store_dwordx4 v[6:7], v[0:3], off nt
	ds_read_b128 v[0:3], v118 offset:5120
	v_add_u32_e32 v6, s0, v108
	v_ashrrev_i32_e32 v7, 31, v6
	v_lshlrev_b64 v[6:7], 10, v[6:7]
	v_lshl_add_u64 v[6:7], v[4:5], 0, v[6:7]
	s_waitcnt lgkmcnt(0)
	global_store_dwordx4 v[6:7], v[0:3], off nt
	ds_read_b128 v[0:3], v118 offset:6400
	v_add_u32_e32 v6, s0, v109
	v_ashrrev_i32_e32 v7, 31, v6
	v_lshlrev_b64 v[6:7], 10, v[6:7]
	v_lshl_add_u64 v[6:7], v[4:5], 0, v[6:7]
	s_waitcnt lgkmcnt(0)
	global_store_dwordx4 v[6:7], v[0:3], off nt
	ds_read_b128 v[0:3], v118 offset:7680
	v_add_u32_e32 v6, s0, v110
	v_ashrrev_i32_e32 v7, 31, v6
	v_lshlrev_b64 v[6:7], 10, v[6:7]
	v_lshl_add_u64 v[6:7], v[4:5], 0, v[6:7]
	s_waitcnt lgkmcnt(0)
	global_store_dwordx4 v[6:7], v[0:3], off nt
	ds_read_b128 v[0:3], v118 offset:8960
	v_add_u32_e32 v6, s0, v111
	v_ashrrev_i32_e32 v7, 31, v6
	v_lshlrev_b64 v[6:7], 10, v[6:7]
	v_lshl_add_u64 v[4:5], v[4:5], 0, v[6:7]
	s_waitcnt lgkmcnt(0)
	global_store_dwordx4 v[4:5], v[0:3], off nt
	s_waitcnt lgkmcnt(0)
	s_mov_b64 s[0:1], 0
; #define LAS __attribute__((address_space(3)))
; __device__ __forceinline__ unsigned pk4_fp8(float x0, float x1, float x2, float x3) { int w = 0; w = __builtin_amdgcn_cvt_pk_fp8_f32(x0, x1, w, false); w = __builtin_amdgcn_cvt_pk_fp8_f32(x2, x3, w, true); return (unsigned)w; }
; __device__ __forceinline__ void transpose_item_fp8w(const float* W, int K, int N, unsigned char* WT, float q, LAS unsigned char* scr, int item, int lane) {
;     const int nblk = N / 128, kb = item / nblk, nb = item % nblk, k0 = 64 * kb, n0 = 128 * nb;
;     const int l5 = lane & 31, h = lane >> 5;
;     const float* src = W + (size_t)(k0 + 16 * h) * N + n0 + 4 * l5;
; #pragma unroll
;     for (int b = 0; b < 2; ++b) {
;         f32x4 x[16];
; #pragma unroll
;         for (int s_ = 0; s_ < 16; ++s_) x[s_] = *(const f32x4*)(src + (size_t)(32 * b + s_) * N);
; #pragma unroll
;         for (int i = 0; i < 4; ++i) {
;             u32x4 o;
;             o.x = pk4_fp8(x[0][i] * q, x[1][i] * q, x[2][i] * q, x[3][i] * q); o.y = pk4_fp8(x[4][i] * q, x[5][i] * q, x[6][i] * q, x[7][i] * q);
;             o.z = pk4_fp8(x[8][i] * q, x[9][i] * q, x[10][i] * q, x[11][i] * q); o.w = pk4_fp8(x[12][i] * q, x[13][i] * q, x[14][i] * q, x[15][i] * q);
;             *(LAS u32x4*)(scr + (l5 + 32 * i) * 80 + (2 * b + h) * 16) = o; }
;     }
;     asm volatile("s_waitcnt lgkmcnt(0)" ::: "memory");
; #pragma unroll
;     for (int qd = 0; qd < 8; ++qd) {
;         const int rho = 16 * qd + (lane >> 2), piece = lane & 3;
;         const u32x4 o = *(const LAS u32x4*)(scr + rho * 80 + piece * 16);
;         const int nl = 4 * (rho & 31) + (rho >> 5);
;         *(u32x4*)(WT + (size_t)(n0 + nl) * K + k0 + piece * 16) = o; }
;     asm volatile("s_waitcnt lgkmcnt(0)" ::: "memory");
; }
.LBB0_668:
	s_andn2_b64 vcc, exec, s[0:1]
	s_cbranch_vccnz .LBB0_670
	s_add_i32 s4, s5, 0xfffff910
	v_readlane_b32 s2, v253, 32
	s_lshr_b32 s0, s4, 8
	v_readlane_b32 s3, v253, 33
	s_mov_b32 s9, s3
	s_add_i32 s8, s0, s56
	v_readlane_b32 s40, v253, 58
	s_lshl_b64 s[0:1], s[8:9], 23
	v_readlane_b32 s50, v254, 4
	v_readlane_b32 s51, v254, 5
	s_add_u32 s2, s50, s0
	s_addc_u32 s3, s51, s1
	s_lshl_b64 s[6:7], s[8:9], 21
	v_readlane_b32 s0, v246, 15
	s_add_u32 s1, s0, s6
	v_readlane_b32 s0, v246, 16
	s_addc_u32 s6, s0, s7
	s_lshl_b32 s0, s4, 6
	s_and_b32 s7, s0, 0x3c0
	v_add_u32_e32 v0, s7, v99
	s_lshl_b32 s0, s4, 3
	v_ashrrev_i32_e32 v1, 31, v0
	s_and_b32 s0, s0, 0x780
	v_lshlrev_b64 v[0:1], 13, v[0:1]
	v_lshl_add_u64 v[0:1], s[2:3], 0, v[0:1]
	s_lshl_b32 s8, s0, 2
	s_mov_b32 s3, s9
	v_readlane_b32 s41, v253, 59
	v_readlane_b32 s42, v253, 60
	v_readlane_b32 s43, v253, 61
	v_readlane_b32 s44, v253, 62
	v_readlane_b32 s45, v253, 63
	v_writelane_b32 v253, s2, 32
	v_lshl_add_u64 v[0:1], v[0:1], 0, s[8:9]
	v_lshl_add_u64 v[60:61], v[0:1], 0, v[152:153]
	v_writelane_b32 v253, s3, 33
	s_movk_i32 s2, 0x2000
	v_add_co_u32_e32 v4, vcc, s2, v60
	s_movk_i32 s2, 0x4000
	s_nop 0
	v_addc_co_u32_e32 v5, vcc, 0, v61, vcc
	v_add_co_u32_e32 v8, vcc, s2, v60
	s_movk_i32 s2, 0x6000
	s_nop 0
	v_addc_co_u32_e32 v9, vcc, 0, v61, vcc
	v_add_co_u32_e32 v12, vcc, s2, v60
	s_mov_b32 s2, 0x8000
	s_nop 0
	v_addc_co_u32_e32 v13, vcc, 0, v61, vcc
	v_add_co_u32_e32 v16, vcc, s2, v60
	s_mov_b32 s2, 0xa000
	s_nop 0
	v_addc_co_u32_e32 v17, vcc, 0, v61, vcc
	v_add_co_u32_e32 v20, vcc, s2, v60
	s_mov_b32 s2, 0xc000
	s_nop 0
	v_addc_co_u32_e32 v21, vcc, 0, v61, vcc
	v_add_co_u32_e32 v24, vcc, s2, v60
	s_mov_b32 s2, 0xe000
	s_nop 0
	v_addc_co_u32_e32 v25, vcc, 0, v61, vcc
	v_add_co_u32_e32 v28, vcc, s2, v60
	s_mov_b32 s2, 0x10000
	s_nop 0
	v_addc_co_u32_e32 v29, vcc, 0, v61, vcc
	v_add_co_u32_e32 v32, vcc, s2, v60
	s_mov_b32 s2, 0x12000
	s_nop 0
	v_addc_co_u32_e32 v33, vcc, 0, v61, vcc
	v_add_co_u32_e32 v36, vcc, s2, v60
	s_mov_b32 s2, 0x14000
	s_nop 0
	v_addc_co_u32_e32 v37, vcc, 0, v61, vcc
	v_add_co_u32_e32 v40, vcc, s2, v60
	s_mov_b32 s2, 0x16000
	s_nop 0
	v_addc_co_u32_e32 v41, vcc, 0, v61, vcc
	v_add_co_u32_e32 v44, vcc, s2, v60
	s_mov_b32 s2, 0x18000
	s_nop 0
	v_addc_co_u32_e32 v45, vcc, 0, v61, vcc
	v_add_co_u32_e32 v48, vcc, s2, v60
	global_load_dwordx4 v[0:3], v[60:61], off nt
	s_nop 0
	v_addc_co_u32_e32 v49, vcc, 0, v61, vcc
	global_load_dwordx4 v[4:7], v[4:5], off nt
	s_mov_b32 s2, 0x1a000
	global_load_dwordx4 v[12:15], v[12:13], off nt
	v_add_co_u32_e32 v52, vcc, s2, v60
	global_load_dwordx4 v[16:19], v[16:17], off nt
	s_nop 0
	v_addc_co_u32_e32 v53, vcc, 0, v61, vcc
	global_load_dwordx4 v[20:23], v[20:21], off nt
	s_mov_b32 s2, 0x1c000
	global_load_dwordx4 v[28:31], v[28:29], off nt
	v_add_co_u32_e32 v56, vcc, s2, v60
	global_load_dwordx4 v[32:35], v[32:33], off nt
	s_nop 0
	v_addc_co_u32_e32 v57, vcc, 0, v61, vcc
	global_load_dwordx4 v[36:39], v[36:37], off nt
	s_mov_b32 s2, 0x1e000
	global_load_dwordx4 v[44:47], v[44:45], off nt
	v_add_co_u32_e32 v62, vcc, s2, v60
	global_load_dwordx4 v[48:51], v[48:49], off nt
	s_nop 0
	v_addc_co_u32_e32 v63, vcc, 0, v61, vcc
	global_load_dwordx4 v[52:55], v[52:53], off nt
	global_load_dwordx4 v[8:11], v[8:9], off nt
	global_load_dwordx4 v[24:27], v[24:25], off nt
	global_load_dwordx4 v[40:43], v[40:41], off nt
	global_load_dwordx4 v[56:59], v[56:57], off nt
	s_mov_b32 s2, 0x40000
	global_load_dwordx4 v[120:123], v[62:63], off nt
	v_readlane_b32 s46, v254, 0
	v_readlane_b32 s47, v254, 1
	v_readlane_b32 s48, v254, 2
	v_readlane_b32 s49, v254, 3
	v_readlane_b32 s52, v254, 6
	v_readlane_b32 s53, v254, 7
	v_readlane_b32 s54, v254, 8
	v_readlane_b32 s55, v254, 9
	s_waitcnt vmcnt(0)
	v_mul_f32_e32 v0, 0x43000000, v0
	v_mul_f32_e32 v4, 0x43000000, v4
	v_cvt_pk_fp8_f32 v124, v0, v4
	v_mul_f32_e32 v12, 0x43000000, v12
	v_mul_f32_e32 v0, 0x43000000, v16
	v_mul_f32_e32 v4, 0x43000000, v20
	v_cvt_pk_fp8_f32 v125, v0, v4
	v_mul_f32_e32 v0, 0x43000000, v32
	v_mul_f32_e32 v4, 0x43000000, v36
	v_cvt_pk_fp8_f32 v126, v0, v4
	v_mul_f32_e32 v0, 0x43000000, v48
	v_mul_f32_e32 v4, 0x43000000, v52
	v_cvt_pk_fp8_f32 v127, v0, v4
	v_mul_f32_e32 v8, 0x43000000, v8
	v_cvt_pk_fp8_f32 v124, v8, v12 op_sel:[0,0,1]
	v_mul_f32_e32 v8, 0x43000000, v24
	v_mul_f32_e32 v12, 0x43000000, v28
	v_cvt_pk_fp8_f32 v125, v8, v12 op_sel:[0,0,1]
	v_mul_f32_e32 v8, 0x43000000, v40
	v_mul_f32_e32 v12, 0x43000000, v44
	v_cvt_pk_fp8_f32 v126, v8, v12 op_sel:[0,0,1]
	v_mul_f32_e32 v8, 0x43000000, v56
	v_mul_f32_e32 v12, 0x43000000, v120
	v_cvt_pk_fp8_f32 v127, v8, v12 op_sel:[0,0,1]
	v_mul_f32_e32 v0, 0x43000000, v1
	v_mul_f32_e32 v1, 0x43000000, v5
	v_mul_f32_e32 v4, 0x43000000, v9
	ds_write_b128 v117, v[124:127]
	v_cvt_pk_fp8_f32 v124, v0, v1
	v_mul_f32_e32 v0, 0x43000000, v17
	v_mul_f32_e32 v1, 0x43000000, v21
	v_cvt_pk_fp8_f32 v125, v0, v1
	v_mul_f32_e32 v0, 0x43000000, v33
	v_mul_f32_e32 v1, 0x43000000, v37
	v_cvt_pk_fp8_f32 v126, v0, v1
	v_mul_f32_e32 v0, 0x43000000, v49
	v_mul_f32_e32 v1, 0x43000000, v53
	v_mul_f32_e32 v5, 0x43000000, v13
	v_cvt_pk_fp8_f32 v127, v0, v1
	v_cvt_pk_fp8_f32 v124, v4, v5 op_sel:[0,0,1]
	v_mul_f32_e32 v4, 0x43000000, v25
	v_mul_f32_e32 v5, 0x43000000, v29
	v_cvt_pk_fp8_f32 v125, v4, v5 op_sel:[0,0,1]
	v_mul_f32_e32 v4, 0x43000000, v41
	v_mul_f32_e32 v5, 0x43000000, v45
	v_cvt_pk_fp8_f32 v126, v4, v5 op_sel:[0,0,1]
	v_mul_f32_e32 v4, 0x43000000, v57
	v_mul_f32_e32 v5, 0x43000000, v121
	v_cvt_pk_fp8_f32 v127, v4, v5 op_sel:[0,0,1]
	v_mul_f32_e32 v0, 0x43000000, v2
	v_mul_f32_e32 v1, 0x43000000, v6
	v_mul_f32_e32 v2, 0x43000000, v10
; #define LAS __attribute__((address_space(3)))
; __device__ __forceinline__ unsigned pk4_fp8(float x0, float x1, float x2, float x3) { int w = 0; w = __builtin_amdgcn_cvt_pk_fp8_f32(x0, x1, w, false); w = __builtin_amdgcn_cvt_pk_fp8_f32(x2, x3, w, true); return (unsigned)w; }
; __device__ __forceinline__ void transpose_item_fp8w(const float* W, int K, int N, unsigned char* WT, float q, LAS unsigned char* scr, int item, int lane) {
;     ...
; #pragma unroll
;         for (int s_ = 0; s_ < 16; ++s_) x[s_] = *(const f32x4*)(src + (size_t)(32 * b + s_) * N);
; #pragma unroll
;         for (int i = 0; i < 4; ++i) {
;             u32x4 o;
;             o.x = pk4_fp8(x[0][i] * q, x[1][i] * q, x[2][i] * q, x[3][i] * q); o.y = pk4_fp8(x[4][i] * q, x[5][i] * q, x[6][i] * q, x[7][i] * q);
;             o.z = pk4_fp8(x[8][i] * q, x[9][i] * q, x[10][i] * q, x[11][i] * q); o.w = pk4_fp8(x[12][i] * q, x[13][i] * q, x[14][i] * q, x[15][i] * q);
;             *(LAS u32x4*)(scr + (l5 + 32 * i) * 80 + (2 * b + h) * 16) = o; }
	ds_write_b128 v117, v[124:127] offset:2560
	v_cvt_pk_fp8_f32 v124, v0, v1
	v_mul_f32_e32 v0, 0x43000000, v18
	v_mul_f32_e32 v1, 0x43000000, v22
	v_cvt_pk_fp8_f32 v125, v0, v1
	v_mul_f32_e32 v0, 0x43000000, v34
	v_mul_f32_e32 v1, 0x43000000, v38
	v_cvt_pk_fp8_f32 v126, v0, v1
	v_mul_f32_e32 v0, 0x43000000, v50
	v_mul_f32_e32 v1, 0x43000000, v54
	v_mul_f32_e32 v4, 0x43000000, v14
	v_cvt_pk_fp8_f32 v127, v0, v1
	v_cvt_pk_fp8_f32 v124, v2, v4 op_sel:[0,0,1]
	v_mul_f32_e32 v2, 0x43000000, v26
	v_mul_f32_e32 v4, 0x43000000, v30
	v_cvt_pk_fp8_f32 v125, v2, v4 op_sel:[0,0,1]
	v_mul_f32_e32 v2, 0x43000000, v42
	v_mul_f32_e32 v4, 0x43000000, v46
	v_cvt_pk_fp8_f32 v126, v2, v4 op_sel:[0,0,1]
	v_mul_f32_e32 v2, 0x43000000, v58
	v_mul_f32_e32 v4, 0x43000000, v122
	v_cvt_pk_fp8_f32 v127, v2, v4 op_sel:[0,0,1]
	v_mul_f32_e32 v1, 0x43000000, v3
	v_mul_f32_e32 v2, 0x43000000, v7
	v_cvt_pk_fp8_f32 v0, v1, v2
	v_mul_f32_e32 v3, 0x43000000, v11
	v_mul_f32_e32 v4, 0x43000000, v15
	v_mul_f32_e32 v2, 0x43000000, v19
	v_cvt_pk_fp8_f32 v0, v3, v4 op_sel:[0,0,1]
	v_mul_f32_e32 v3, 0x43000000, v23
	v_cvt_pk_fp8_f32 v1, v2, v3
	v_mul_f32_e32 v4, 0x43000000, v27
	v_mul_f32_e32 v5, 0x43000000, v31
	v_mul_f32_e32 v3, 0x43000000, v35
	v_cvt_pk_fp8_f32 v1, v4, v5 op_sel:[0,0,1]
	v_mul_f32_e32 v4, 0x43000000, v39
	v_cvt_pk_fp8_f32 v2, v3, v4
	v_mul_f32_e32 v5, 0x43000000, v43
	v_mul_f32_e32 v6, 0x43000000, v47
	v_mul_f32_e32 v4, 0x43000000, v51
	v_cvt_pk_fp8_f32 v2, v5, v6 op_sel:[0,0,1]
	v_mul_f32_e32 v5, 0x43000000, v55
	v_cvt_pk_fp8_f32 v3, v4, v5
	v_mul_f32_e32 v6, 0x43000000, v59
	v_mul_f32_e32 v7, 0x43000000, v123
	v_mov_b32_e32 v120, v153
	v_cvt_pk_fp8_f32 v3, v6, v7 op_sel:[0,0,1]
	v_mov_b32_e32 v121, v153
	v_mov_b32_e32 v122, v153
	v_mov_b32_e32 v123, v153
	ds_write_b128 v117, v[0:3] offset:7680
	v_add_co_u32_e32 v0, vcc, s2, v60
	s_mov_b32 s2, 0x42000
	s_nop 0
	v_addc_co_u32_e32 v1, vcc, 0, v61, vcc
	v_add_co_u32_e32 v4, vcc, s2, v60
	s_mov_b32 s2, 0x44000
	s_nop 0
	v_addc_co_u32_e32 v5, vcc, 0, v61, vcc
	v_add_co_u32_e32 v8, vcc, s2, v60
	s_mov_b32 s2, 0x46000
	s_nop 0
	v_addc_co_u32_e32 v9, vcc, 0, v61, vcc
	v_add_co_u32_e32 v12, vcc, s2, v60
	s_mov_b32 s2, 0x48000
	s_nop 0
	v_addc_co_u32_e32 v13, vcc, 0, v61, vcc
	global_load_dwordx4 v[8:11], v[8:9], off nt
	ds_write_b128 v117, v[124:127] offset:5120
	global_load_dwordx4 v[16:19], v[12:13], off nt
	v_add_co_u32_e32 v12, vcc, s2, v60
	s_mov_b32 s2, 0x4a000
	s_nop 0
	v_addc_co_u32_e32 v13, vcc, 0, v61, vcc
	v_add_co_u32_e32 v20, vcc, s2, v60
	s_mov_b32 s2, 0x4c000
	s_nop 0
	v_addc_co_u32_e32 v21, vcc, 0, v61, vcc
	global_load_dwordx4 v[12:15], v[12:13], off nt
	s_waitcnt vmcnt(0)
	v_mul_f32_e32 v8, 0x43000000, v8
	global_load_dwordx4 v[24:27], v[20:21], off nt
	v_add_co_u32_e32 v20, vcc, s2, v60
	s_mov_b32 s2, 0x4e000
	s_nop 0
	v_addc_co_u32_e32 v21, vcc, 0, v61, vcc
	global_load_dwordx4 v[28:31], v[20:21], off nt
	v_add_co_u32_e32 v20, vcc, s2, v60
	s_mov_b32 s2, 0x50000
	s_nop 0
	v_addc_co_u32_e32 v21, vcc, 0, v61, vcc
	global_load_dwordx4 v[40:43], v[20:21], off nt
	v_add_co_u32_e32 v20, vcc, s2, v60
	s_mov_b32 s2, 0x52000
	s_nop 0
	v_addc_co_u32_e32 v21, vcc, 0, v61, vcc
	v_add_co_u32_e32 v32, vcc, s2, v60
	s_mov_b32 s2, 0x54000
	s_nop 0
	v_addc_co_u32_e32 v33, vcc, 0, v61, vcc
	v_add_co_u32_e32 v36, vcc, s2, v60
	s_mov_b32 s2, 0x56000
	s_nop 0
	v_addc_co_u32_e32 v37, vcc, 0, v61, vcc
	v_add_co_u32_e32 v44, vcc, s2, v60
	s_mov_b32 s2, 0x58000
	s_nop 0
	v_addc_co_u32_e32 v45, vcc, 0, v61, vcc
	global_load_dwordx4 v[36:39], v[36:37], off nt
	s_waitcnt vmcnt(5)
	v_mul_f32_e32 v16, 0x43000000, v16
	global_load_dwordx4 v[48:51], v[44:45], off nt
	v_add_co_u32_e32 v44, vcc, s2, v60
	global_load_dwordx4 v[0:3], v[0:1], off nt
	s_nop 0
	v_addc_co_u32_e32 v45, vcc, 0, v61, vcc
	global_load_dwordx4 v[4:7], v[4:5], off nt
	s_mov_b32 s2, 0x5a000
	v_add_co_u32_e32 v52, vcc, s2, v60
	global_load_dwordx4 v[20:23], v[20:21], off nt
	s_nop 0
	v_addc_co_u32_e32 v53, vcc, 0, v61, vcc
	global_load_dwordx4 v[32:35], v[32:33], off nt
	s_mov_b32 s2, 0x5c000
	global_load_dwordx4 v[44:47], v[44:45], off nt
	v_add_co_u32_e32 v56, vcc, s2, v60
	global_load_dwordx4 v[52:55], v[52:53], off nt
	s_nop 0
	v_addc_co_u32_e32 v57, vcc, 0, v61, vcc
	s_mov_b32 s2, 0x5e000
	v_add_co_u32_e32 v60, vcc, s2, v60
	global_load_dwordx4 v[56:59], v[56:57], off nt
	s_nop 0
	v_addc_co_u32_e32 v61, vcc, 0, v61, vcc
	global_load_dwordx4 v[60:63], v[60:61], off nt
	s_add_u32 s2, s1, s7
	s_addc_u32 s3, s6, 0
	s_waitcnt vmcnt(0)
	v_mul_f32_e32 v0, 0x43000000, v0
	s_waitcnt vmcnt(6)
	v_mul_f32_e32 v4, 0x43000000, v4
	v_cvt_pk_fp8_f32 v120, v0, v4
	v_mul_f32_e32 v0, 0x43000000, v12
	v_mul_f32_e32 v4, 0x43000000, v24
	v_cvt_pk_fp8_f32 v121, v0, v4
	s_waitcnt vmcnt(5)
	v_mul_f32_e32 v0, 0x43000000, v20
	v_cvt_pk_fp8_f32 v120, v8, v16 op_sel:[0,0,1]
	s_waitcnt vmcnt(4)
	v_mul_f32_e32 v4, 0x43000000, v32
	v_cvt_pk_fp8_f32 v122, v0, v4
	s_waitcnt vmcnt(3)
	v_mul_f32_e32 v0, 0x43000000, v44
	v_mul_f32_e32 v8, 0x43000000, v28
	v_mul_f32_e32 v12, 0x43000000, v40
	s_waitcnt vmcnt(2)
; #define LAS __attribute__((address_space(3)))
; __device__ __forceinline__ unsigned pk4_fp8(float x0, float x1, float x2, float x3) { int w = 0; w = __builtin_amdgcn_cvt_pk_fp8_f32(x0, x1, w, false); w = __builtin_amdgcn_cvt_pk_fp8_f32(x2, x3, w, true); return (unsigned)w; }
; __device__ __forceinline__ void transpose_item_fp8w(const float* W, int K, int N, unsigned char* WT, float q, LAS unsigned char* scr, int item, int lane) {
;     ...
; #pragma unroll
;         for (int s_ = 0; s_ < 16; ++s_) x[s_] = *(const f32x4*)(src + (size_t)(32 * b + s_) * N);
; #pragma unroll
;         for (int i = 0; i < 4; ++i) {
;             u32x4 o;
;             o.x = pk4_fp8(x[0][i] * q, x[1][i] * q, x[2][i] * q, x[3][i] * q); o.y = pk4_fp8(x[4][i] * q, x[5][i] * q, x[6][i] * q, x[7][i] * q);
;             o.z = pk4_fp8(x[8][i] * q, x[9][i] * q, x[10][i] * q, x[11][i] * q); o.w = pk4_fp8(x[12][i] * q, x[13][i] * q, x[14][i] * q, x[15][i] * q);
;             *(LAS u32x4*)(scr + (l5 + 32 * i) * 80 + (2 * b + h) * 16) = o; }
;     }
;     asm volatile("s_waitcnt lgkmcnt(0)" ::: "memory");
; #pragma unroll
;     for (int qd = 0; qd < 8; ++qd) {
;         const int rho = 16 * qd + (lane >> 2), piece = lane & 3;
;         const u32x4 o = *(const LAS u32x4*)(scr + rho * 80 + piece * 16);
;         const int nl = 4 * (rho & 31) + (rho >> 5);
;         *(u32x4*)(WT + (size_t)(n0 + nl) * K + k0 + piece * 16) = o; }
;     asm volatile("s_waitcnt lgkmcnt(0)" ::: "memory");
	v_mul_f32_e32 v4, 0x43000000, v52
	v_cvt_pk_fp8_f32 v123, v0, v4
	v_cvt_pk_fp8_f32 v121, v8, v12 op_sel:[0,0,1]
	v_mul_f32_e32 v8, 0x43000000, v36
	v_mul_f32_e32 v12, 0x43000000, v48
	v_cvt_pk_fp8_f32 v122, v8, v12 op_sel:[0,0,1]
	s_waitcnt vmcnt(1)
	v_mul_f32_e32 v8, 0x43000000, v56
	v_mul_f32_e32 v0, 0x43000000, v1
	v_mul_f32_e32 v1, 0x43000000, v5
	s_waitcnt vmcnt(0)
	v_mul_f32_e32 v12, 0x43000000, v60
	v_cvt_pk_fp8_f32 v123, v8, v12 op_sel:[0,0,1]
	v_mul_f32_e32 v4, 0x43000000, v9
	v_mul_f32_e32 v5, 0x43000000, v17
	ds_write_b128 v117, v[120:123] offset:32
	v_cvt_pk_fp8_f32 v120, v0, v1
	v_mul_f32_e32 v0, 0x43000000, v13
	v_mul_f32_e32 v1, 0x43000000, v25
	v_cvt_pk_fp8_f32 v121, v0, v1
	v_mul_f32_e32 v0, 0x43000000, v21
	v_mul_f32_e32 v1, 0x43000000, v33
	v_cvt_pk_fp8_f32 v122, v0, v1
	v_mul_f32_e32 v0, 0x43000000, v45
	v_mul_f32_e32 v1, 0x43000000, v53
	v_cvt_pk_fp8_f32 v123, v0, v1
	v_cvt_pk_fp8_f32 v120, v4, v5 op_sel:[0,0,1]
	v_mul_f32_e32 v4, 0x43000000, v29
	v_mul_f32_e32 v5, 0x43000000, v41
	v_cvt_pk_fp8_f32 v121, v4, v5 op_sel:[0,0,1]
	v_mul_f32_e32 v4, 0x43000000, v37
	v_mul_f32_e32 v5, 0x43000000, v49
	v_cvt_pk_fp8_f32 v122, v4, v5 op_sel:[0,0,1]
	v_mul_f32_e32 v4, 0x43000000, v57
	v_mul_f32_e32 v5, 0x43000000, v61
	v_cvt_pk_fp8_f32 v123, v4, v5 op_sel:[0,0,1]
	v_mul_f32_e32 v0, 0x43000000, v2
	v_mul_f32_e32 v1, 0x43000000, v6
	v_mul_f32_e32 v2, 0x43000000, v10
	ds_write_b128 v117, v[120:123] offset:2592
	v_cvt_pk_fp8_f32 v120, v0, v1
	v_mul_f32_e32 v0, 0x43000000, v14
	v_mul_f32_e32 v1, 0x43000000, v26
	v_cvt_pk_fp8_f32 v121, v0, v1
	v_mul_f32_e32 v0, 0x43000000, v22
	v_mul_f32_e32 v1, 0x43000000, v34
	v_cvt_pk_fp8_f32 v122, v0, v1
	v_mul_f32_e32 v0, 0x43000000, v46
	v_mul_f32_e32 v1, 0x43000000, v54
	v_mul_f32_e32 v4, 0x43000000, v18
	v_cvt_pk_fp8_f32 v123, v0, v1
	v_cvt_pk_fp8_f32 v120, v2, v4 op_sel:[0,0,1]
	v_mul_f32_e32 v2, 0x43000000, v30
	v_mul_f32_e32 v4, 0x43000000, v42
	v_cvt_pk_fp8_f32 v121, v2, v4 op_sel:[0,0,1]
	v_mul_f32_e32 v2, 0x43000000, v38
	v_mul_f32_e32 v4, 0x43000000, v50
	v_cvt_pk_fp8_f32 v122, v2, v4 op_sel:[0,0,1]
	v_mul_f32_e32 v2, 0x43000000, v58
	v_mul_f32_e32 v4, 0x43000000, v62
	v_cvt_pk_fp8_f32 v123, v2, v4 op_sel:[0,0,1]
	v_mul_f32_e32 v1, 0x43000000, v3
	v_mul_f32_e32 v2, 0x43000000, v7
	v_cvt_pk_fp8_f32 v0, v1, v2
	v_mul_f32_e32 v3, 0x43000000, v11
	v_mul_f32_e32 v4, 0x43000000, v19
	v_mul_f32_e32 v2, 0x43000000, v15
	v_cvt_pk_fp8_f32 v0, v3, v4 op_sel:[0,0,1]
	v_mul_f32_e32 v3, 0x43000000, v27
	v_cvt_pk_fp8_f32 v1, v2, v3
	v_mul_f32_e32 v4, 0x43000000, v31
	v_mul_f32_e32 v5, 0x43000000, v43
	v_mul_f32_e32 v3, 0x43000000, v23
	v_cvt_pk_fp8_f32 v1, v4, v5 op_sel:[0,0,1]
	v_mul_f32_e32 v4, 0x43000000, v35
	v_cvt_pk_fp8_f32 v2, v3, v4
	v_mul_f32_e32 v5, 0x43000000, v39
	v_mul_f32_e32 v6, 0x43000000, v51
	v_mul_f32_e32 v4, 0x43000000, v47
	v_cvt_pk_fp8_f32 v2, v5, v6 op_sel:[0,0,1]
	v_mul_f32_e32 v5, 0x43000000, v55
	v_cvt_pk_fp8_f32 v3, v4, v5
	v_mul_f32_e32 v6, 0x43000000, v59
	v_mul_f32_e32 v7, 0x43000000, v63
	ds_write_b128 v117, v[120:123] offset:5152
	v_cvt_pk_fp8_f32 v3, v6, v7 op_sel:[0,0,1]
	v_add_u32_e32 v6, s0, v104
	v_ashrrev_i32_e32 v7, 31, v6
	v_lshl_add_u64 v[4:5], s[2:3], 0, v[66:67]
	ds_write_b128 v117, v[0:3] offset:7712
	s_waitcnt lgkmcnt(0)
	ds_read_b128 v[0:3], v118
	v_lshlrev_b64 v[6:7], 10, v[6:7]
	v_lshl_add_u64 v[6:7], v[4:5], 0, v[6:7]
	s_waitcnt lgkmcnt(0)
	global_store_dwordx4 v[6:7], v[0:3], off nt
	ds_read_b128 v[0:3], v118 offset:1280
	v_add_u32_e32 v6, s0, v105
	v_ashrrev_i32_e32 v7, 31, v6
	v_lshlrev_b64 v[6:7], 10, v[6:7]
	v_lshl_add_u64 v[6:7], v[4:5], 0, v[6:7]
	s_waitcnt lgkmcnt(0)
	global_store_dwordx4 v[6:7], v[0:3], off nt
	ds_read_b128 v[0:3], v118 offset:2560
	v_add_u32_e32 v6, s0, v106
	v_ashrrev_i32_e32 v7, 31, v6
	v_lshlrev_b64 v[6:7], 10, v[6:7]
	v_lshl_add_u64 v[6:7], v[4:5], 0, v[6:7]
	s_waitcnt lgkmcnt(0)
	global_store_dwordx4 v[6:7], v[0:3], off nt
	ds_read_b128 v[0:3], v118 offset:3840
	v_add_u32_e32 v6, s0, v107
	v_ashrrev_i32_e32 v7, 31, v6
	v_lshlrev_b64 v[6:7], 10, v[6:7]
	v_lshl_add_u64 v[6:7], v[4:5], 0, v[6:7]
	s_waitcnt lgkmcnt(0)
	global_store_dwordx4 v[6:7], v[0:3], off nt
	ds_read_b128 v[0:3], v118 offset:5120
	v_add_u32_e32 v6, s0, v108
	v_ashrrev_i32_e32 v7, 31, v6
	v_lshlrev_b64 v[6:7], 10, v[6:7]
	v_lshl_add_u64 v[6:7], v[4:5], 0, v[6:7]
	s_waitcnt lgkmcnt(0)
	global_store_dwordx4 v[6:7], v[0:3], off nt
	ds_read_b128 v[0:3], v118 offset:6400
	v_add_u32_e32 v6, s0, v109
	v_ashrrev_i32_e32 v7, 31, v6
	v_lshlrev_b64 v[6:7], 10, v[6:7]
	v_lshl_add_u64 v[6:7], v[4:5], 0, v[6:7]
	s_waitcnt lgkmcnt(0)
	global_store_dwordx4 v[6:7], v[0:3], off nt
	ds_read_b128 v[0:3], v118 offset:7680
	v_add_u32_e32 v6, s0, v110
	v_ashrrev_i32_e32 v7, 31, v6
	v_lshlrev_b64 v[6:7], 10, v[6:7]
	v_lshl_add_u64 v[6:7], v[4:5], 0, v[6:7]
	s_waitcnt lgkmcnt(0)
	global_store_dwordx4 v[6:7], v[0:3], off nt
	ds_read_b128 v[0:3], v118 offset:8960
	v_add_u32_e32 v6, s0, v111
	v_ashrrev_i32_e32 v7, 31, v6
	v_lshlrev_b64 v[6:7], 10, v[6:7]
	v_lshl_add_u64 v[4:5], v[4:5], 0, v[6:7]
	s_waitcnt lgkmcnt(0)
	global_store_dwordx4 v[4:5], v[0:3], off nt
	s_waitcnt lgkmcnt(0)

; #define LAS __attribute__((address_space(3)))
; __device__ __forceinline__ void transpose_item_fp8(const float* W, int K, int N, unsigned char* WT, float q, LAS float* scr, int item, int lane) {
;     const int nblk = N / 32, kb = item / nblk, nb = item % nblk, k0 = 64 * kb, n0 = 32 * nb;
; #pragma unroll 8
;     for (int i = 0; i < 32; ++i) { const int kk = 2 * i + (lane >> 5); scr[kk * 33 + (lane & 31)] = W[(size_t)(k0 + kk) * N + n0 + (lane & 31)]; }
.LBB0_696:
	s_lshl_b32 s9, s1, 1
	s_lshl_b32 s10, s0, 1
	v_add_u32_e32 v18, s9, v2
	v_add_u32_e32 v20, s10, v3
	v_mad_i64_i32 v[18:19], s[2:3], v18, s82, v[0:1]
	v_mad_i64_i32 v[20:21], s[2:3], v20, s82, v[0:1]
	global_load_dword v24, v[18:19], off nt
	global_load_dword v25, v[20:21], off nt
	v_add_u32_e32 v23, s9, v128
	v_add_u32_e32 v22, s10, v65
	v_mad_u64_u32 v[18:19], s[2:3], v23, s83, v[70:71]
	v_mad_u64_u32 v[20:21], s[2:3], v22, s83, v[70:71]
	v_add_u32_e32 v23, s9, v86
	v_add_u32_e32 v22, s10, v71
	s_add_i32 s1, s1, 16
	s_add_i32 s0, s0, 16
	s_add_i32 s7, s7, -16
	s_cmp_lg_u32 s7, 0
	s_waitcnt vmcnt(0)
	ds_write_b32 v18, v24
	ds_write_b32 v20, v25
	v_add_u32_e32 v18, s9, v4
	v_add_u32_e32 v20, s10, v5
	v_mad_i64_i32 v[18:19], s[2:3], v18, s82, v[0:1]
	v_mad_i64_i32 v[20:21], s[2:3], v20, s82, v[0:1]
	global_load_dword v24, v[18:19], off nt
	global_load_dword v25, v[20:21], off nt
	v_mad_u64_u32 v[18:19], s[2:3], v23, s83, v[70:71]
	v_mad_u64_u32 v[20:21], s[2:3], v22, s83, v[70:71]
	v_add_u32_e32 v23, s9, v88
	v_add_u32_e32 v22, s10, v87
	s_waitcnt vmcnt(0)
	ds_write_b32 v18, v24
	s_waitcnt vmcnt(0)
	ds_write_b32 v20, v25
	v_add_u32_e32 v18, s9, v6
	v_add_u32_e32 v20, s10, v7
	v_mad_i64_i32 v[18:19], s[2:3], v18, s82, v[0:1]
	v_mad_i64_i32 v[20:21], s[2:3], v20, s82, v[0:1]
	global_load_dword v24, v[18:19], off nt
	global_load_dword v25, v[20:21], off nt
	v_mad_u64_u32 v[18:19], s[2:3], v23, s83, v[70:71]
	v_mad_u64_u32 v[20:21], s[2:3], v22, s83, v[70:71]
	v_add_u32_e32 v23, s9, v90
	v_add_u32_e32 v22, s10, v89
	s_waitcnt vmcnt(0)
	ds_write_b32 v18, v24
	s_waitcnt vmcnt(0)
	ds_write_b32 v20, v25
	v_add_u32_e32 v18, s9, v8
	v_add_u32_e32 v20, s10, v9
	v_mad_i64_i32 v[18:19], s[2:3], v18, s82, v[0:1]
	v_mad_i64_i32 v[20:21], s[2:3], v20, s82, v[0:1]
	global_load_dword v24, v[18:19], off nt
	global_load_dword v25, v[20:21], off nt
	v_mad_u64_u32 v[18:19], s[2:3], v23, s83, v[70:71]
	v_mad_u64_u32 v[20:21], s[2:3], v22, s83, v[70:71]
	v_add_u32_e32 v23, s9, v92
	v_add_u32_e32 v22, s10, v91
	s_waitcnt vmcnt(0)
	ds_write_b32 v18, v24
	s_waitcnt vmcnt(0)
	ds_write_b32 v20, v25
	v_add_u32_e32 v18, s9, v10
	v_add_u32_e32 v20, s10, v11
	v_mad_i64_i32 v[18:19], s[2:3], v18, s82, v[0:1]
	v_mad_i64_i32 v[20:21], s[2:3], v20, s82, v[0:1]
	global_load_dword v24, v[18:19], off nt
	global_load_dword v25, v[20:21], off nt
	v_mad_u64_u32 v[18:19], s[2:3], v23, s83, v[70:71]
	v_mad_u64_u32 v[20:21], s[2:3], v22, s83, v[70:71]
	v_add_u32_e32 v23, s9, v94
	v_add_u32_e32 v22, s10, v93
	s_waitcnt vmcnt(0)
	ds_write_b32 v18, v24
	s_waitcnt vmcnt(0)
	ds_write_b32 v20, v25
	v_add_u32_e32 v18, s9, v12
	v_add_u32_e32 v20, s10, v13
	v_mad_i64_i32 v[18:19], s[2:3], v18, s82, v[0:1]
	v_mad_i64_i32 v[20:21], s[2:3], v20, s82, v[0:1]
	global_load_dword v24, v[18:19], off nt
	global_load_dword v25, v[20:21], off nt
	v_mad_u64_u32 v[18:19], s[2:3], v23, s83, v[70:71]
	v_mad_u64_u32 v[20:21], s[2:3], v22, s83, v[70:71]
	v_add_u32_e32 v23, s9, v96
	v_add_u32_e32 v22, s10, v95
	s_waitcnt vmcnt(0)
	ds_write_b32 v18, v24
	s_waitcnt vmcnt(0)
	ds_write_b32 v20, v25
	v_add_u32_e32 v18, s9, v14
	v_add_u32_e32 v20, s10, v15
	v_mad_i64_i32 v[18:19], s[2:3], v18, s82, v[0:1]
	v_mad_i64_i32 v[20:21], s[2:3], v20, s82, v[0:1]
	global_load_dword v24, v[18:19], off nt
	global_load_dword v25, v[20:21], off nt
	v_mad_u64_u32 v[18:19], s[2:3], v23, s83, v[70:71]
	v_mad_u64_u32 v[20:21], s[2:3], v22, s83, v[70:71]
	v_add_u32_e32 v23, s9, v98
	v_add_u32_e32 v22, s10, v97
	s_waitcnt vmcnt(0)
	ds_write_b32 v18, v24
	s_waitcnt vmcnt(0)
	ds_write_b32 v20, v25
	v_add_u32_e32 v18, s9, v16
	v_add_u32_e32 v20, s10, v17
	v_mad_i64_i32 v[18:19], s[2:3], v18, s82, v[0:1]
	v_mad_i64_i32 v[20:21], s[2:3], v20, s82, v[0:1]
	global_load_dword v24, v[18:19], off nt
	global_load_dword v25, v[20:21], off nt
	v_mad_u64_u32 v[18:19], s[2:3], v23, s83, v[70:71]
	v_mad_u64_u32 v[20:21], s[2:3], v22, s83, v[70:71]
	s_waitcnt vmcnt(0)
	ds_write_b32 v18, v24
	s_waitcnt vmcnt(0)
	ds_write_b32 v20, v25
	s_cbranch_scc1 .LBB0_696
; #define LAS __attribute__((address_space(3)))
; __device__ __forceinline__ unsigned pk4_fp8(float x0, float x1, float x2, float x3) { int w = 0; w = __builtin_amdgcn_cvt_pk_fp8_f32(x0, x1, w, false); w = __builtin_amdgcn_cvt_pk_fp8_f32(x2, x3, w, true); return (unsigned)w; }
; __device__ __forceinline__ void transpose_item_fp8(const float* W, int K, int N, unsigned char* WT, float q, LAS float* scr, int item, int lane) {
;     ...
;     asm volatile("s_waitcnt lgkmcnt(0)" ::: "memory");
;     const int c = lane & 7;
; #pragma unroll
;     for (int j = 0; j < 4; ++j) { const int n = (lane >> 3) + 8 * j; const LAS float* s = scr + (8 * c) * 33 + n;
;         u32x2 o; o.x = pk4_fp8(s[0 * 33] * q, s[1 * 33] * q, s[2 * 33] * q, s[3 * 33] * q); o.y = pk4_fp8(s[4 * 33] * q, s[5 * 33] * q, s[6 * 33] * q, s[7 * 33] * q);
;         *(u32x2*)(WT + (size_t)(n0 + n) * K + k0 + 8 * c) = o; }
;     asm volatile("s_waitcnt lgkmcnt(0)" ::: "memory");
	s_waitcnt lgkmcnt(0)
	ds_read2_b32 v[2:3], v113 offset1:8
	ds_read2_b32 v[4:5], v113 offset0:33 offset1:41
	ds_read2_b32 v[12:13], v113 offset0:132 offset1:140
	ds_read2_b32 v[14:15], v113 offset0:165 offset1:173
	ds_read2_b32 v[6:7], v113 offset0:66 offset1:74
	ds_read2_b32 v[8:9], v113 offset0:99 offset1:107
	s_waitcnt lgkmcnt(5)
	v_mul_f32_e32 v2, 0x43000000, v2
	s_waitcnt lgkmcnt(4)
	v_mul_f32_e32 v4, 0x43000000, v4
	ds_read2_b32 v[16:17], v113 offset0:198 offset1:206
	ds_read2_b32 v[18:19], v113 offset0:231 offset1:239
	v_cvt_pk_fp8_f32 v10, v2, v4
	s_waitcnt lgkmcnt(5)
	v_mul_f32_e32 v2, 0x43000000, v12
	s_waitcnt lgkmcnt(4)
	v_mul_f32_e32 v4, 0x43000000, v14
	v_cvt_pk_fp8_f32 v11, v2, v4
	v_mul_f32_e32 v3, 0x43000000, v3
	v_mul_f32_e32 v4, 0x43000000, v5
	v_cvt_pk_fp8_f32 v2, v3, v4
	s_waitcnt lgkmcnt(3)
	v_mul_f32_e32 v6, 0x43000000, v6
	s_waitcnt lgkmcnt(2)
	v_mul_f32_e32 v8, 0x43000000, v8
	v_cvt_pk_fp8_f32 v10, v6, v8 op_sel:[0,0,1]
	s_waitcnt lgkmcnt(1)
	v_mul_f32_e32 v6, 0x43000000, v16
	s_waitcnt lgkmcnt(0)
	v_mul_f32_e32 v8, 0x43000000, v18
	v_cvt_pk_fp8_f32 v11, v6, v8 op_sel:[0,0,1]
	v_mul_f32_e32 v5, 0x43000000, v7
	v_mul_f32_e32 v6, 0x43000000, v9
	v_cvt_pk_fp8_f32 v2, v5, v6 op_sel:[0,0,1]
	v_mul_f32_e32 v4, 0x43000000, v13
	v_mul_f32_e32 v5, 0x43000000, v15
	v_cvt_pk_fp8_f32 v3, v4, v5
	v_mul_f32_e32 v6, 0x43000000, v17
	v_mul_f32_e32 v7, 0x43000000, v19
	v_add_u32_e32 v4, s6, v114
	v_cvt_pk_fp8_f32 v3, v6, v7 op_sel:[0,0,1]
	s_ashr_i32 s9, s8, 31
	v_ashrrev_i32_e32 v5, 31, v4
	v_lshl_add_u64 v[0:1], v[84:85], 0, s[8:9]
	v_lshlrev_b64 v[4:5], 10, v[4:5]
	v_lshl_add_u64 v[4:5], v[0:1], 0, v[4:5]
	global_store_dwordx2 v[4:5], v[2:3], off nt
	ds_read2_b32 v[2:3], v113 offset0:16 offset1:24
	ds_read2_b32 v[4:5], v113 offset0:49 offset1:57
	v_add_u32_e32 v20, s6, v112
	ds_read2_b32 v[12:13], v113 offset0:148 offset1:156
	ds_read2_b32 v[14:15], v113 offset0:181 offset1:189
	v_ashrrev_i32_e32 v21, 31, v20
	v_lshlrev_b64 v[20:21], 10, v[20:21]
	v_lshl_add_u64 v[20:21], v[0:1], 0, v[20:21]
	ds_read2_b32 v[6:7], v113 offset0:82 offset1:90
	ds_read2_b32 v[8:9], v113 offset0:115 offset1:123
	global_store_dwordx2 v[20:21], v[10:11], off nt
	s_waitcnt lgkmcnt(5)
	v_mul_f32_e32 v2, 0x43000000, v2
	s_waitcnt lgkmcnt(4)
	v_mul_f32_e32 v4, 0x43000000, v4
	ds_read2_b32 v[16:17], v113 offset0:214 offset1:222
	ds_read2_b32 v[18:19], v113 offset0:247 offset1:255
	v_cvt_pk_fp8_f32 v10, v2, v4
	s_waitcnt lgkmcnt(5)
	v_mul_f32_e32 v2, 0x43000000, v12
	s_waitcnt lgkmcnt(4)
	v_mul_f32_e32 v4, 0x43000000, v14
	v_cvt_pk_fp8_f32 v11, v2, v4
	v_mul_f32_e32 v3, 0x43000000, v3
	v_mul_f32_e32 v4, 0x43000000, v5
	v_cvt_pk_fp8_f32 v2, v3, v4
	s_waitcnt lgkmcnt(3)
	v_mul_f32_e32 v6, 0x43000000, v6
	s_waitcnt lgkmcnt(2)
	v_mul_f32_e32 v8, 0x43000000, v8
	v_cvt_pk_fp8_f32 v10, v6, v8 op_sel:[0,0,1]
	s_waitcnt lgkmcnt(1)
	v_mul_f32_e32 v6, 0x43000000, v16
	s_waitcnt lgkmcnt(0)
	v_mul_f32_e32 v8, 0x43000000, v18
	v_cvt_pk_fp8_f32 v11, v6, v8 op_sel:[0,0,1]
	v_mul_f32_e32 v5, 0x43000000, v7
	v_mul_f32_e32 v6, 0x43000000, v9
	v_cvt_pk_fp8_f32 v2, v5, v6 op_sel:[0,0,1]
	v_mul_f32_e32 v4, 0x43000000, v13
	v_mul_f32_e32 v5, 0x43000000, v15
	v_cvt_pk_fp8_f32 v3, v4, v5
	v_mul_f32_e32 v6, 0x43000000, v17
	v_mul_f32_e32 v7, 0x43000000, v19
	v_add_u32_e32 v20, s6, v115
	v_cvt_pk_fp8_f32 v3, v6, v7 op_sel:[0,0,1]
	v_add_u32_e32 v4, s6, v116
	v_ashrrev_i32_e32 v21, 31, v20
	v_ashrrev_i32_e32 v5, 31, v4
	v_lshlrev_b64 v[20:21], 10, v[20:21]
	v_lshlrev_b64 v[4:5], 10, v[4:5]
	v_lshl_add_u64 v[20:21], v[0:1], 0, v[20:21]
	v_lshl_add_u64 v[0:1], v[0:1], 0, v[4:5]
	global_store_dwordx2 v[20:21], v[10:11], off nt
	global_store_dwordx2 v[0:1], v[2:3], off nt
	s_waitcnt lgkmcnt(0)
	s_branch .LBB0_661

; __device__ __forceinline__ int modset(int n) { return (n < NCTX) ? 4 : ((n - NCTX) >> 13); }
; #define XVAL(src_, l_) (((l_) == 0) ? (src_) : (f32x4){bflo(__float_as_uint((src_).x)), bfhi(__float_as_uint((src_).x)), bflo(__float_as_uint((src_).y)), bfhi(__float_as_uint((src_).y))})
; __global__ void __launch_bounds__(512, 2) mega(Args a) {
;     ...
;             for (int p = wave; p < npair; p += 8) {
;                 const int nb = n0 + 2 * p;
;                 f32x4 v[2][4];
;                 const float* md = MODL + (size_t)modset(nb) * 6144;
;                 float sm[2];
;                 {
;                     f32x4 g1v[4];
; #pragma unroll
;                     for (int j = 0; j < 4; ++j) g1v[j] = *((const f32x4*)(md + 2048) + lane + 64 * j);
; #pragma unroll
;                     for (int t = 0; t < 2; ++t) { float s = 0.f;
; #pragma unroll
;                         for (int j = 0; j < 4; ++j) { const f32x4 yv = (f32x4){bflo(yB[t][j].x), bfhi(yB[t][j].x), bflo(yB[t][j].y), bfhi(yB[t][j].y)}; v[t][j] = XVAL(xB[t][j], l) * DN_ALPHA + g1v[j] * yv; s += (v[t][j].x + v[t][j].y) + (v[t][j].z + v[t][j].w); }
;                         sm[t] = s; }
.LBB0_865:
	s_add_i32 s0, s18, 0xfffffc00
	s_lshr_b32 s0, s0, 13
	s_cmpk_gt_i32 s18, 0x3ff
	s_cselect_b32 s0, s0, 4
	s_mul_hi_u32 s1, s0, 0x6000
	s_mulk_i32 s0, 0x6000
	s_add_u32 s0, s5, s0
	s_addc_u32 s1, s31, s1
	v_lshl_add_u64 v[48:49], v[98:99], 4, s[0:1]
	s_mov_b64 s[0:1], 0x2000
	v_lshl_add_u64 v[32:33], v[48:49], 0, s[0:1]
	s_movk_i32 s0, 0x3000
	v_add_co_u32_e32 v50, vcc, s0, v48
	s_waitcnt vmcnt(3)
	v_lshlrev_b32_e32 v52, 16, v100
	v_addc_co_u32_e32 v51, vcc, 0, v49, vcc
	global_load_dwordx4 v[44:47], v[50:51], off offset:-4096
	global_load_dwordx4 v[40:43], v[32:33], off offset:1024
	global_load_dwordx4 v[36:39], v[32:33], off offset:2048
	s_nop 0
	global_load_dwordx4 v[32:35], v[32:33], off offset:3072
	v_and_b32_e32 v53, 0xffff0000, v100
	v_lshlrev_b32_e32 v54, 16, v101
	v_and_b32_e32 v55, 0xffff0000, v101
	v_lshlrev_b32_e32 v56, 16, v0
	v_and_b32_e32 v57, 0xffff0000, v0
	v_lshlrev_b32_e32 v58, 16, v1
	v_and_b32_e32 v59, 0xffff0000, v1
	v_cndmask_b32_e64 v57, v57, v1, s[42:43]
	v_cndmask_b32_e64 v56, v56, v0, s[42:43]
	v_cndmask_b32_e64 v59, v59, v3, s[42:43]
	v_cndmask_b32_e64 v58, v58, v2, s[42:43]
	s_mov_b32 s0, 0x3fd744fd
	s_waitcnt vmcnt(3)
	v_pk_mul_f32 v[54:55], v[46:47], v[54:55]
	v_pk_mul_f32 v[52:53], v[44:45], v[52:53]
	v_pk_fma_f32 v[92:93], v[58:59], s[0:1], v[54:55] op_sel_hi:[1,0,1]
	v_pk_fma_f32 v[94:95], v[56:57], s[0:1], v[52:53] op_sel_hi:[1,0,1]
	v_add_f32_e32 v53, v92, v93
	v_add_f32_e32 v52, v94, v95
	v_add_f32_e32 v52, v52, v53
	v_add_f32_e32 v60, 0, v52
	v_lshlrev_b32_e32 v52, 16, v102
	v_and_b32_e32 v53, 0xffff0000, v102
	v_lshlrev_b32_e32 v54, 16, v103
	v_and_b32_e32 v55, 0xffff0000, v103
	v_lshlrev_b32_e32 v56, 16, v4
	v_and_b32_e32 v57, 0xffff0000, v4
	v_lshlrev_b32_e32 v58, 16, v5
	v_and_b32_e32 v59, 0xffff0000, v5
	v_cndmask_b32_e64 v57, v57, v5, s[42:43]
	v_cndmask_b32_e64 v56, v56, v4, s[42:43]
	v_cndmask_b32_e64 v59, v59, v7, s[42:43]
	v_cndmask_b32_e64 v58, v58, v6, s[42:43]
	s_waitcnt vmcnt(2)
	v_pk_mul_f32 v[54:55], v[42:43], v[54:55]
	v_pk_mul_f32 v[52:53], v[40:41], v[52:53]
	v_pk_fma_f32 v[130:131], v[58:59], s[0:1], v[54:55] op_sel_hi:[1,0,1]
	v_pk_fma_f32 v[134:135], v[56:57], s[0:1], v[52:53] op_sel_hi:[1,0,1]
	v_add_f32_e32 v53, v130, v131
	v_add_f32_e32 v52, v134, v135
	v_add_f32_e32 v52, v52, v53
	v_add_f32_e32 v60, v60, v52
	v_lshlrev_b32_e32 v52, 16, v106
	v_and_b32_e32 v53, 0xffff0000, v106
	v_lshlrev_b32_e32 v54, 16, v107
	v_and_b32_e32 v55, 0xffff0000, v107
	v_lshlrev_b32_e32 v56, 16, v12
	v_and_b32_e32 v57, 0xffff0000, v12
	v_lshlrev_b32_e32 v58, 16, v13
	v_and_b32_e32 v59, 0xffff0000, v13
	v_cndmask_b32_e64 v57, v57, v13, s[42:43]
	v_cndmask_b32_e64 v56, v56, v12, s[42:43]
	v_cndmask_b32_e64 v59, v59, v15, s[42:43]
	v_cndmask_b32_e64 v58, v58, v14, s[42:43]
	s_waitcnt vmcnt(1)
	v_pk_mul_f32 v[54:55], v[38:39], v[54:55]
	v_pk_mul_f32 v[52:53], v[36:37], v[52:53]
	v_pk_fma_f32 v[128:129], v[58:59], s[0:1], v[54:55] op_sel_hi:[1,0,1]
	v_pk_fma_f32 v[132:133], v[56:57], s[0:1], v[52:53] op_sel_hi:[1,0,1]
	v_add_f32_e32 v53, v128, v129
	v_add_f32_e32 v52, v132, v133
	v_add_f32_e32 v52, v52, v53
	v_add_f32_e32 v60, v60, v52
	v_lshlrev_b32_e32 v52, 16, v110
	v_and_b32_e32 v53, 0xffff0000, v110
	v_lshlrev_b32_e32 v54, 16, v111
	v_and_b32_e32 v55, 0xffff0000, v111
	v_lshlrev_b32_e32 v56, 16, v20
	v_and_b32_e32 v57, 0xffff0000, v20
	v_lshlrev_b32_e32 v58, 16, v21
	v_and_b32_e32 v59, 0xffff0000, v21
	v_cndmask_b32_e64 v57, v57, v21, s[42:43]
	v_cndmask_b32_e64 v56, v56, v20, s[42:43]
	v_cndmask_b32_e64 v59, v59, v23, s[42:43]
	v_cndmask_b32_e64 v58, v58, v22, s[42:43]
	s_waitcnt vmcnt(0)
	v_pk_mul_f32 v[54:55], v[34:35], v[54:55]
	v_pk_mul_f32 v[52:53], v[32:33], v[52:53]
	v_pk_fma_f32 v[136:137], v[58:59], s[0:1], v[54:55] op_sel_hi:[1,0,1]
	v_pk_fma_f32 v[138:139], v[56:57], s[0:1], v[52:53] op_sel_hi:[1,0,1]
	v_add_f32_e32 v53, v136, v137
	v_add_f32_e32 v52, v138, v139
	v_add_f32_e32 v52, v52, v53
	v_add_f32_e32 v152, v60, v52
	v_lshlrev_b32_e32 v52, 16, v104
	v_and_b32_e32 v53, 0xffff0000, v104
	v_lshlrev_b32_e32 v54, 16, v105
	v_and_b32_e32 v55, 0xffff0000, v105
	v_lshlrev_b32_e32 v56, 16, v8
	v_and_b32_e32 v57, 0xffff0000, v8
	v_lshlrev_b32_e32 v58, 16, v9
	v_and_b32_e32 v59, 0xffff0000, v9
	v_cndmask_b32_e64 v57, v57, v9, s[42:43]
	v_cndmask_b32_e64 v56, v56, v8, s[42:43]
	v_cndmask_b32_e64 v59, v59, v11, s[42:43]
	v_cndmask_b32_e64 v58, v58, v10, s[42:43]
	v_pk_mul_f32 v[46:47], v[46:47], v[54:55]
	v_pk_mul_f32 v[44:45], v[44:45], v[52:53]
	v_pk_fma_f32 v[154:155], v[58:59], s[0:1], v[46:47] op_sel_hi:[1,0,1]
	v_pk_fma_f32 v[156:157], v[56:57], s[0:1], v[44:45] op_sel_hi:[1,0,1]
	v_add_f32_e32 v45, v154, v155
	v_add_f32_e32 v44, v156, v157
	v_add_f32_e32 v44, v44, v45
	v_add_f32_e32 v56, 0, v44
	v_lshlrev_b32_e32 v44, 16, v108
	v_and_b32_e32 v45, 0xffff0000, v108
	v_lshlrev_b32_e32 v46, 16, v109
	v_and_b32_e32 v47, 0xffff0000, v109
	v_lshlrev_b32_e32 v52, 16, v16
	v_and_b32_e32 v53, 0xffff0000, v16
	v_lshlrev_b32_e32 v54, 16, v17
	v_and_b32_e32 v55, 0xffff0000, v17
	v_cndmask_b32_e64 v53, v53, v17, s[42:43]
	v_cndmask_b32_e64 v52, v52, v16, s[42:43]
	v_cndmask_b32_e64 v55, v55, v19, s[42:43]
	v_cndmask_b32_e64 v54, v54, v18, s[42:43]
	v_pk_mul_f32 v[42:43], v[42:43], v[46:47]
	v_pk_mul_f32 v[40:41], v[40:41], v[44:45]
	v_pk_fma_f32 v[148:149], v[54:55], s[0:1], v[42:43] op_sel_hi:[1,0,1]
	v_pk_fma_f32 v[150:151], v[52:53], s[0:1], v[40:41] op_sel_hi:[1,0,1]
	v_add_f32_e32 v41, v148, v149
	v_add_f32_e32 v40, v150, v151
	v_add_f32_e32 v40, v40, v41
	v_add_f32_e32 v52, v56, v40
	v_lshlrev_b32_e32 v40, 16, v124
	v_and_b32_e32 v41, 0xffff0000, v124
	v_lshlrev_b32_e32 v42, 16, v125
; __global__ void __launch_bounds__(512, 2) mega(Args a) {
;     ...
;                 f32x4 pg[4], pb_[4], psh[4], psc[4];
; #pragma unroll
;                 for (int j = 0; j < 4; ++j) { pg[j] = *((const f32x4*)ln1g + lane + 64 * j); pb_[j] = *((const f32x4*)ln1b + lane + 64 * j); psh[j] = *((const f32x4*)(md + 3072) + lane + 64 * j); psc[j] = *((const f32x4*)(md + 4096) + lane + 64 * j); }
;                 float rstd[2];
;                 { const float mean0 = wave_sum(sm[0]) * (1.f / DM), mean1 = wave_sum(sm[1]) * (1.f / DM); float q0 = 0.f, q1 = 0.f;
; #pragma unroll
;                   for (int j = 0; j < 4; ++j) { v[0][j] = v[0][j] - mean0; q0 += (v[0][j].x * v[0][j].x + v[0][j].y * v[0][j].y) + (v[0][j].z * v[0][j].z + v[0][j].w * v[0][j].w);
;                       v[1][j] = v[1][j] - mean1; q1 += (v[1][j].x * v[1][j].x + v[1][j].y * v[1][j].y) + (v[1][j].z * v[1][j].z + v[1][j].w * v[1][j].w); }
;                   rstd[0] = rsqrtf(wave_sum(q0) * (1.f / DM) + LN_EPS); rstd[1] = rsqrtf(wave_sum(q1) * (1.f / DM) + LN_EPS); }
	v_and_b32_e32 v43, 0xffff0000, v125
	v_lshlrev_b32_e32 v44, 16, v24
	v_and_b32_e32 v45, 0xffff0000, v24
	v_lshlrev_b32_e32 v46, 16, v25
	v_and_b32_e32 v47, 0xffff0000, v25
	v_cndmask_b32_e64 v45, v45, v25, s[42:43]
	v_cndmask_b32_e64 v44, v44, v24, s[42:43]
	v_cndmask_b32_e64 v47, v47, v27, s[42:43]
	v_cndmask_b32_e64 v46, v46, v26, s[42:43]
	v_pk_mul_f32 v[38:39], v[38:39], v[42:43]
	v_pk_mul_f32 v[36:37], v[36:37], v[40:41]
	v_pk_fma_f32 v[144:145], v[46:47], s[0:1], v[38:39] op_sel_hi:[1,0,1]
	v_pk_fma_f32 v[146:147], v[44:45], s[0:1], v[36:37] op_sel_hi:[1,0,1]
	v_add_f32_e32 v37, v144, v145
	v_add_f32_e32 v36, v146, v147
	v_add_f32_e32 v36, v36, v37
	v_add_f32_e32 v44, v52, v36
	v_lshlrev_b32_e32 v36, 16, v126
	v_and_b32_e32 v37, 0xffff0000, v126
	v_lshlrev_b32_e32 v38, 16, v127
	v_and_b32_e32 v39, 0xffff0000, v127
	v_lshlrev_b32_e32 v40, 16, v28
	v_and_b32_e32 v41, 0xffff0000, v28
	v_lshlrev_b32_e32 v42, 16, v29
	v_and_b32_e32 v43, 0xffff0000, v29
	v_cndmask_b32_e64 v41, v41, v29, s[42:43]
	v_cndmask_b32_e64 v40, v40, v28, s[42:43]
	v_cndmask_b32_e64 v43, v43, v31, s[42:43]
	v_cndmask_b32_e64 v42, v42, v30, s[42:43]
	v_pk_mul_f32 v[34:35], v[34:35], v[38:39]
	v_pk_mul_f32 v[32:33], v[32:33], v[36:37]
	v_pk_fma_f32 v[140:141], v[42:43], s[0:1], v[34:35] op_sel_hi:[1,0,1]
	v_pk_fma_f32 v[142:143], v[40:41], s[0:1], v[32:33] op_sel_hi:[1,0,1]
	v_add_f32_e32 v33, v140, v141
	v_add_f32_e32 v32, v142, v143
	v_add_f32_e32 v32, v32, v33
	v_add_f32_e32 v158, v44, v32
	s_mov_b64 s[0:1], 0x3000
	v_lshl_add_u64 v[32:33], v[48:49], 0, s[0:1]
	s_movk_i32 s0, 0x4000
	v_add_co_u32_e32 v34, vcc, s0, v48
	v_lshl_add_u64 v[44:45], v[48:49], 0, s[10:11]
	s_nop 0
	v_addc_co_u32_e32 v35, vcc, 0, v49, vcc
	global_load_dwordx4 v[80:83], v[50:51], off
	global_load_dwordx4 v[164:167], v[34:35], off
	global_load_dwordx4 v[84:87], v[112:113], off
	global_load_dwordx4 v[68:71], v[112:113], off offset:1024
	global_load_dwordx4 v[88:91], v[114:115], off
	global_load_dwordx4 v[72:75], v[114:115], off offset:1024
	global_load_dwordx4 v[64:67], v[32:33], off offset:1024
	global_load_dwordx4 v[48:51], v[32:33], off offset:2048
	global_load_dwordx4 v[52:55], v[112:113], off offset:2048
	global_load_dwordx4 v[36:39], v[112:113], off offset:3072
	global_load_dwordx4 v[56:59], v[114:115], off offset:2048
	global_load_dwordx4 v[40:43], v[114:115], off offset:3072
	global_load_dwordx4 v[76:79], v[44:45], off offset:1024
	s_nop 0
	global_load_dwordx4 v[32:35], v[32:33], off offset:3072
	s_nop 0
	global_load_dwordx4 v[60:63], v[44:45], off offset:2048
	s_nop 0
	global_load_dwordx4 v[44:47], v[44:45], off offset:3072
	v_add_f32_dpp v152, v152, v152 quad_perm:[1,0,3,2] row_mask:0xf bank_mask:0xf bound_ctrl:1
	v_add_f32_dpp v158, v158, v158 quad_perm:[1,0,3,2] row_mask:0xf bank_mask:0xf bound_ctrl:1
	s_mov_b32 s0, 0x3a800000
	v_add_f32_dpp v152, v152, v152 quad_perm:[2,3,0,1] row_mask:0xf bank_mask:0xf bound_ctrl:1
	v_add_f32_dpp v158, v158, v158 quad_perm:[2,3,0,1] row_mask:0xf bank_mask:0xf bound_ctrl:1
	s_nop 0
	v_add_f32_dpp v152, v152, v152 row_half_mirror row_mask:0xf bank_mask:0xf bound_ctrl:1
	v_add_f32_dpp v158, v158, v158 row_half_mirror row_mask:0xf bank_mask:0xf bound_ctrl:1
	s_nop 0
	v_add_f32_dpp v152, v152, v152 row_mirror row_mask:0xf bank_mask:0xf bound_ctrl:1
	v_mov_b32_e32 v159, v152
	s_nop 1
	v_permlane16_swap_b32_e32 v152, v159
	v_add_f32_e32 v152, v152, v159
	v_mov_b32_e32 v159, v152
	s_nop 1
	v_permlane32_swap_b32_e32 v152, v159
	v_add_f32_dpp v158, v158, v158 row_mirror row_mask:0xf bank_mask:0xf bound_ctrl:1
	v_add_f32_e32 v152, v152, v159
	v_mov_b32_e32 v159, v158
	s_nop 1
	v_permlane16_swap_b32_e32 v158, v159
	v_add_f32_e32 v158, v158, v159
	v_mov_b32_e32 v159, v158
	s_nop 1
	v_permlane32_swap_b32_e32 v158, v159
	v_fmac_f32_e32 v93, 0xba800000, v152
	v_fmac_f32_e32 v95, 0xba800000, v152
	v_add_f32_e32 v158, v158, v159
	v_fmamk_f32 v92, v152, 0xba800000, v92
	v_fmamk_f32 v94, v152, 0xba800000, v94
	v_mul_f32_e32 v159, v95, v95
	v_mul_f32_e32 v160, v93, v93
	v_fmac_f32_e32 v159, v94, v94
	v_fmac_f32_e32 v160, v92, v92
	v_fmac_f32_e32 v155, 0xba800000, v158
	v_fmac_f32_e32 v157, 0xba800000, v158
	v_add_f32_e32 v159, v159, v160
	v_fmamk_f32 v154, v158, 0xba800000, v154
	v_fmamk_f32 v156, v158, 0xba800000, v156
	v_mul_f32_e32 v160, v157, v157
	v_mul_f32_e32 v161, v155, v155
	v_fmac_f32_e32 v160, v156, v156
	v_fmac_f32_e32 v161, v154, v154
	v_fmac_f32_e32 v131, 0xba800000, v152
	v_fmac_f32_e32 v135, 0xba800000, v152
	v_add_f32_e32 v160, v160, v161
	v_fmamk_f32 v130, v152, 0xba800000, v130
	v_fmamk_f32 v134, v152, 0xba800000, v134
	v_mul_f32_e32 v161, v135, v135
	v_mul_f32_e32 v168, v131, v131
	v_fmac_f32_e32 v161, v134, v134
	v_fmac_f32_e32 v168, v130, v130
	v_add_f32_e32 v161, v161, v168
	v_fmac_f32_e32 v149, 0xba800000, v158
	v_fmac_f32_e32 v151, 0xba800000, v158
	v_add_f32_e32 v159, v159, v161
	v_fmamk_f32 v148, v158, 0xba800000, v148
	v_fmamk_f32 v150, v158, 0xba800000, v150
	v_mul_f32_e32 v161, v151, v151
	v_mul_f32_e32 v168, v149, v149
	v_fmac_f32_e32 v161, v150, v150
	v_fmac_f32_e32 v168, v148, v148
	v_add_f32_e32 v161, v161, v168
	v_fmac_f32_e32 v129, 0xba800000, v152
	v_fmac_f32_e32 v133, 0xba800000, v152
	v_add_f32_e32 v160, v160, v161
	v_fmamk_f32 v128, v152, 0xba800000, v128
	v_fmamk_f32 v132, v152, 0xba800000, v132
	v_mul_f32_e32 v161, v133, v133
	v_mul_f32_e32 v168, v129, v129
	v_fmac_f32_e32 v161, v132, v132
	v_fmac_f32_e32 v168, v128, v128
	v_add_f32_e32 v161, v161, v168
	v_fmac_f32_e32 v145, 0xba800000, v158
	v_fmac_f32_e32 v147, 0xba800000, v158
	v_add_f32_e32 v159, v159, v161
	v_fmamk_f32 v144, v158, 0xba800000, v144
; __device__ __forceinline__ unsigned pk2(float lo, float hi) { unsigned r; asm("v_cvt_pk_bf16_f32 %0, %1, %2" : "=v"(r) : "v"(lo), "v"(hi)); return r; }
; __device__ __forceinline__ unsigned pk4_fp8(float x0, float x1, float x2, float x3) { int w = 0; w = __builtin_amdgcn_cvt_pk_fp8_f32(x0, x1, w, false); w = __builtin_amdgcn_cvt_pk_fp8_f32(x2, x3, w, true); return (unsigned)w; }
; __global__ void __launch_bounds__(512, 2) mega(Args a) {
;     ...
;                   rstd[0] = rsqrtf(wave_sum(q0) * (1.f / DM) + LN_EPS); rstd[1] = rsqrtf(wave_sum(q1) * (1.f / DM) + LN_EPS); }
;                 __builtin_amdgcn_sched_barrier(0);
; #pragma unroll
;                 for (int j = 0; j < 4; ++j)
; #pragma unroll
;                     for (int t = 0; t < 2; ++t) { const int n = nb + t;
;                         v[t][j] = v[t][j] * rstd[t] * pg[j] + pb_[j]; { u32x2 xw_; xw_.x = pk2(v[t][j].x, v[t][j].y); xw_.y = pk2(v[t][j].z, v[t][j].w); *((u32x2*)(XRB + (size_t)n * DM) + lane + 64 * j) = xw_; }
;                         v[t][j] = v[t][j] * (psc[j] + 1.f) + psh[j];
;                         *((unsigned*)(XH8 + (size_t)n * DM) + lane + 64 * j) = pk4_fp8(v[t][j].x * ACT_Q, v[t][j].y * ACT_Q, v[t][j].z * ACT_Q, v[t][j].w * ACT_Q); }
	v_fmamk_f32 v146, v158, 0xba800000, v146
	v_mul_f32_e32 v161, v147, v147
	v_mul_f32_e32 v168, v145, v145
	v_fmac_f32_e32 v161, v146, v146
	v_fmac_f32_e32 v168, v144, v144
	v_add_f32_e32 v161, v161, v168
	v_fmac_f32_e32 v137, 0xba800000, v152
	v_fmac_f32_e32 v139, 0xba800000, v152
	v_add_f32_e32 v160, v160, v161
	v_fmamk_f32 v136, v152, 0xba800000, v136
	v_fmamk_f32 v138, v152, 0xba800000, v138
	v_mul_f32_e32 v152, v139, v139
	v_mul_f32_e32 v161, v137, v137
	v_fmac_f32_e32 v152, v138, v138
	v_fmac_f32_e32 v161, v136, v136
	v_add_f32_e32 v152, v152, v161
	v_add_f32_e32 v152, v159, v152
	v_fmac_f32_e32 v141, 0xba800000, v158
	v_fmac_f32_e32 v143, 0xba800000, v158
	v_add_f32_dpp v152, v152, v152 quad_perm:[1,0,3,2] row_mask:0xf bank_mask:0xf bound_ctrl:1
	v_fmamk_f32 v140, v158, 0xba800000, v140
	v_fmamk_f32 v142, v158, 0xba800000, v142
	v_add_f32_dpp v152, v152, v152 quad_perm:[2,3,0,1] row_mask:0xf bank_mask:0xf bound_ctrl:1
	v_mul_f32_e32 v158, v143, v143
	v_mul_f32_e32 v159, v141, v141
	v_add_f32_dpp v152, v152, v152 row_half_mirror row_mask:0xf bank_mask:0xf bound_ctrl:1
	v_fmac_f32_e32 v158, v142, v142
	v_fmac_f32_e32 v159, v140, v140
	v_add_f32_dpp v152, v152, v152 row_mirror row_mask:0xf bank_mask:0xf bound_ctrl:1
	v_add_f32_e32 v158, v158, v159
	v_mov_b32_e32 v159, v152
	v_add_f32_e32 v158, v160, v158
	s_nop 0
	v_permlane16_swap_b32_e32 v152, v159
	v_add_f32_e32 v159, v152, v159
	s_nop 0
	v_add_f32_dpp v152, v158, v158 quad_perm:[1,0,3,2] row_mask:0xf bank_mask:0xf bound_ctrl:1
	v_mov_b32_e32 v161, v159
	s_nop 1
	v_permlane32_swap_b32_e32 v159, v161
	v_add_f32_dpp v152, v152, v152 quad_perm:[2,3,0,1] row_mask:0xf bank_mask:0xf bound_ctrl:1
	s_nop 1
	v_add_f32_dpp v152, v152, v152 row_half_mirror row_mask:0xf bank_mask:0xf bound_ctrl:1
	s_nop 1
	v_add_f32_dpp v152, v152, v152 row_mirror row_mask:0xf bank_mask:0xf bound_ctrl:1
	v_mov_b32_e32 v158, v152
	s_nop 1
	v_permlane16_swap_b32_e32 v152, v158
	v_add_f32_e32 v158, v152, v158
	v_mov_b32_e32 v160, v158
	s_nop 1
	v_permlane32_swap_b32_e32 v158, v160
	v_pk_add_f32 v[158:159], v[158:159], v[160:161]
	s_nop 0
	v_pk_fma_f32 v[158:159], v[158:159], s[0:1], v[162:163] op_sel_hi:[1,0,0]
	s_nop 0
	v_mul_f32_e32 v152, 0x4b800000, v159
	v_cmp_gt_f32_e32 vcc, s94, v159
	v_cmp_gt_f32_e64 s[60:61], s94, v158
	s_nop 0
	v_cndmask_b32_e32 v152, v159, v152, vcc
	v_mul_f32_e32 v159, 0x4b800000, v158
	v_rsq_f32_e32 v152, v152
	v_cndmask_b32_e64 v158, v158, v159, s[60:61]
	v_rsq_f32_e32 v158, v158
	v_mul_f32_e32 v159, 0x45800000, v152
	v_cndmask_b32_e32 v172, v152, v159, vcc
	v_mul_f32_e32 v152, 0x45800000, v158
	v_cndmask_b32_e64 v152, v158, v152, s[60:61]
	v_pk_mul_f32 v[94:95], v[94:95], v[172:173] op_sel_hi:[1,0]
	v_lshl_add_u64 v[158:159], s[78:79], 0, v[122:123]
	s_brev_b32 s0, 44
	v_pk_mul_f32 v[92:93], v[92:93], v[172:173] op_sel_hi:[1,0]
	s_waitcnt vmcnt(11)
	v_pk_fma_f32 v[94:95], v[84:85], v[94:95], v[88:89]
	v_add_co_u32_e32 v158, vcc, s0, v158
	v_pk_add_f32 v[164:165], v[164:165], 1.0 op_sel_hi:[1,0]
	v_pk_mul_f32 v[156:157], v[156:157], v[152:153] op_sel_hi:[1,0]
	v_pk_fma_f32 v[92:93], v[86:87], v[92:93], v[90:91]
	v_cvt_pk_bf16_f32 v160, v94, v95
	v_addc_co_u32_e32 v159, vcc, 0, v159, vcc
	v_cvt_pk_bf16_f32 v161, v92, v93
	v_pk_fma_f32 v[94:95], v[94:95], v[164:165], v[80:81]
	v_pk_fma_f32 v[88:89], v[84:85], v[156:157], v[88:89]
	global_store_dwordx2 v[158:159], v[160:161], off
	v_mul_f32_e32 v160, 4.0, v94
	v_mul_f32_e32 v161, 4.0, v95
	v_pk_mul_f32 v[154:155], v[154:155], v[152:153] op_sel_hi:[1,0]
	v_pk_fma_f32 v[84:85], v[88:89], v[164:165], v[80:81]
	v_cvt_pk_fp8_f32 v168, v160, v161
	v_pk_fma_f32 v[86:87], v[86:87], v[154:155], v[90:91]
	v_mul_f32_e32 v80, 4.0, v84
	v_mul_f32_e32 v81, 4.0, v85
	v_pk_add_f32 v[166:167], v[166:167], 1.0 op_sel_hi:[1,0]
	v_cvt_pk_fp8_f32 v90, v80, v81
	v_pk_fma_f32 v[92:93], v[92:93], v[166:167], v[82:83]
	v_pk_fma_f32 v[80:81], v[86:87], v[166:167], v[82:83]
	v_mul_f32_e32 v160, 4.0, v92
	v_mul_f32_e32 v161, 4.0, v93
	v_cvt_pk_fp8_f32 v168, v160, v161 op_sel:[0,0,1]
	v_mul_f32_e32 v82, 4.0, v80
	v_mul_f32_e32 v83, 4.0, v81
	v_lshl_add_u64 v[160:161], s[78:79], 0, v[120:121]
	s_mov_b32 s0, 0x72600000
	v_cvt_pk_fp8_f32 v90, v82, v83 op_sel:[0,0,1]
	v_add_co_u32_e32 v160, vcc, s0, v160
	v_cvt_pk_bf16_f32 v82, v88, v89
	v_cvt_pk_bf16_f32 v83, v86, v87
	s_waitcnt vmcnt(4)
; __device__ __forceinline__ unsigned pk2(float lo, float hi) { unsigned r; asm("v_cvt_pk_bf16_f32 %0, %1, %2" : "=v"(r) : "v"(lo), "v"(hi)); return r; }
; __device__ __forceinline__ unsigned pk4_fp8(float x0, float x1, float x2, float x3) { int w = 0; w = __builtin_amdgcn_cvt_pk_fp8_f32(x0, x1, w, false); w = __builtin_amdgcn_cvt_pk_fp8_f32(x2, x3, w, true); return (unsigned)w; }
; #define XLOAD(dst_, l_, n_, j_) do { if ((l_) == 0) dst_ = *((const f32x4*)XROW0(n_) + lane + 64 * (j_)); else { const u32x2 w_ = *((const u32x2*)(XRB + (size_t)(n_) * DM) + lane + 64 * (j_)); dst_ = (f32x4){__uint_as_float(w_.x), __uint_as_float(w_.y), 0.f, 0.f}; } } while (0)
; __global__ void __launch_bounds__(512, 2) mega(Args a) {
;     ...
; #pragma unroll
;                 for (int j = 0; j < 4; ++j)
; #pragma unroll
;                     for (int t = 0; t < 2; ++t) { const int n = nb + t;
;                         v[t][j] = v[t][j] * rstd[t] * pg[j] + pb_[j]; { u32x2 xw_; xw_.x = pk2(v[t][j].x, v[t][j].y); xw_.y = pk2(v[t][j].z, v[t][j].w); *((u32x2*)(XRB + (size_t)n * DM) + lane + 64 * j) = xw_; }
;                         v[t][j] = v[t][j] * (psc[j] + 1.f) + psh[j];
;                         *((unsigned*)(XH8 + (size_t)n * DM) + lane + 64 * j) = pk4_fp8(v[t][j].x * ACT_Q, v[t][j].y * ACT_Q, v[t][j].z * ACT_Q, v[t][j].w * ACT_Q); }
;                 __builtin_amdgcn_sched_barrier(0);
;                 if (p + 8 < npair) {
; #pragma unroll
;                     for (int j = 0; j < 4; ++j) { XLOAD(xB[0][j], l, nb + 16, j); yB[0][j] = *((const u32x2*)(YB + (size_t)(nb + 16) * DM) + lane + 64 * j); } }
	v_pk_add_f32 v[88:89], v[78:79], 1.0 op_sel_hi:[1,0]
	v_addc_co_u32_e32 v161, vcc, 0, v161, vcc
	global_store_dword v[160:161], v168, off
	global_store_dwordx2 v[158:159], v[82:83], off offset:2048
	global_store_dword v[160:161], v90, off offset:1024
	v_pk_mul_f32 v[82:83], v[134:135], v[172:173] op_sel_hi:[1,0]
	v_pk_add_f32 v[90:91], v[76:77], 1.0 op_sel_hi:[1,0]
	v_pk_fma_f32 v[82:83], v[68:69], v[82:83], v[72:73]
	v_pk_mul_f32 v[86:87], v[130:131], v[172:173] op_sel_hi:[1,0]
	v_pk_fma_f32 v[78:79], v[82:83], v[90:91], v[64:65]
	v_mul_f32_e32 v76, 4.0, v78
	v_mul_f32_e32 v77, 4.0, v79
	v_cvt_pk_fp8_f32 v130, v76, v77
	v_pk_fma_f32 v[86:87], v[70:71], v[86:87], v[74:75]
	v_cvt_pk_bf16_f32 v82, v82, v83
	s_nop 0
	v_pk_fma_f32 v[76:77], v[86:87], v[88:89], v[66:67]
	v_cvt_pk_bf16_f32 v83, v86, v87
	v_pk_mul_f32 v[86:87], v[148:149], v[152:153] op_sel_hi:[1,0]
	v_mul_f32_e32 v131, 4.0, v76
	v_mul_f32_e32 v134, 4.0, v77
	v_cvt_pk_fp8_f32 v130, v131, v134 op_sel:[0,0,1]
	global_store_dwordx2 v[158:159], v[82:83], off offset:512
	global_store_dword v[160:161], v130, off offset:256
	v_pk_mul_f32 v[82:83], v[150:151], v[152:153] op_sel_hi:[1,0]
	v_pk_fma_f32 v[70:71], v[70:71], v[86:87], v[74:75]
	v_pk_fma_f32 v[72:73], v[68:69], v[82:83], v[72:73]
	v_pk_fma_f32 v[68:69], v[72:73], v[90:91], v[64:65]
	v_mul_f32_e32 v64, 4.0, v68
	v_mul_f32_e32 v65, 4.0, v69
	v_cvt_pk_fp8_f32 v74, v64, v65
	v_pk_fma_f32 v[64:65], v[70:71], v[88:89], v[66:67]
	s_nop 0
	v_mul_f32_e32 v66, 4.0, v64
	v_mul_f32_e32 v67, 4.0, v65
	v_cvt_pk_fp8_f32 v74, v66, v67 op_sel:[0,0,1]
	v_cvt_pk_bf16_f32 v66, v72, v73
	v_cvt_pk_bf16_f32 v67, v70, v71
	global_store_dwordx2 v[158:159], v[66:67], off offset:2560
	global_store_dword v[160:161], v74, off offset:1280
	v_pk_mul_f32 v[66:67], v[132:133], v[172:173] op_sel_hi:[1,0]
	s_waitcnt vmcnt(9)
	v_pk_add_f32 v[74:75], v[60:61], 1.0 op_sel_hi:[1,0]
	v_pk_fma_f32 v[66:67], v[52:53], v[66:67], v[56:57]
	v_pk_add_f32 v[72:73], v[62:63], 1.0 op_sel_hi:[1,0]
	v_pk_fma_f32 v[62:63], v[66:67], v[74:75], v[48:49]
	v_pk_mul_f32 v[70:71], v[128:129], v[172:173] op_sel_hi:[1,0]
	v_mul_f32_e32 v60, 4.0, v62
	v_mul_f32_e32 v61, 4.0, v63
	v_cvt_pk_fp8_f32 v82, v60, v61
	v_pk_fma_f32 v[70:71], v[54:55], v[70:71], v[58:59]
	v_cvt_pk_bf16_f32 v66, v66, v67
	s_nop 0
	v_pk_fma_f32 v[60:61], v[70:71], v[72:73], v[50:51]
	v_cvt_pk_bf16_f32 v67, v70, v71
	v_pk_mul_f32 v[70:71], v[144:145], v[152:153] op_sel_hi:[1,0]
	v_mul_f32_e32 v83, 4.0, v60
	v_mul_f32_e32 v86, 4.0, v61
	v_cvt_pk_fp8_f32 v82, v83, v86 op_sel:[0,0,1]
	global_store_dwordx2 v[158:159], v[66:67], off offset:1024
	global_store_dword v[160:161], v82, off offset:512
	v_pk_mul_f32 v[66:67], v[146:147], v[152:153] op_sel_hi:[1,0]
	v_pk_fma_f32 v[54:55], v[54:55], v[70:71], v[58:59]
	v_pk_fma_f32 v[56:57], v[52:53], v[66:67], v[56:57]
	v_pk_fma_f32 v[52:53], v[56:57], v[74:75], v[48:49]
	v_mul_f32_e32 v48, 4.0, v52
	v_mul_f32_e32 v49, 4.0, v53
	v_cvt_pk_fp8_f32 v58, v48, v49
	v_pk_fma_f32 v[48:49], v[54:55], v[72:73], v[50:51]
	s_nop 0
	v_mul_f32_e32 v50, 4.0, v48
	v_mul_f32_e32 v51, 4.0, v49
	v_cvt_pk_fp8_f32 v58, v50, v51 op_sel:[0,0,1]
	v_cvt_pk_bf16_f32 v50, v56, v57
	v_cvt_pk_bf16_f32 v51, v54, v55
	global_store_dwordx2 v[158:159], v[50:51], off offset:3072
	global_store_dword v[160:161], v58, off offset:1536
	v_pk_mul_f32 v[50:51], v[138:139], v[172:173] op_sel_hi:[1,0]
	s_waitcnt vmcnt(12)
	v_pk_add_f32 v[58:59], v[44:45], 1.0 op_sel_hi:[1,0]
	v_pk_fma_f32 v[50:51], v[36:37], v[50:51], v[40:41]
	v_pk_add_f32 v[56:57], v[46:47], 1.0 op_sel_hi:[1,0]
	v_pk_fma_f32 v[46:47], v[50:51], v[58:59], v[32:33]
	v_pk_mul_f32 v[54:55], v[136:137], v[172:173] op_sel_hi:[1,0]
	v_mul_f32_e32 v44, 4.0, v46
	v_mul_f32_e32 v45, 4.0, v47
	v_cvt_pk_fp8_f32 v66, v44, v45
	v_pk_fma_f32 v[54:55], v[38:39], v[54:55], v[42:43]
	v_cvt_pk_bf16_f32 v50, v50, v51
	s_nop 0
	v_pk_fma_f32 v[44:45], v[54:55], v[56:57], v[34:35]
	v_cvt_pk_bf16_f32 v51, v54, v55
	v_pk_mul_f32 v[54:55], v[140:141], v[152:153] op_sel_hi:[1,0]
	v_mul_f32_e32 v67, 4.0, v44
	v_mul_f32_e32 v70, 4.0, v45
	v_cvt_pk_fp8_f32 v66, v67, v70 op_sel:[0,0,1]
	global_store_dwordx2 v[158:159], v[50:51], off offset:1536
	global_store_dword v[160:161], v66, off offset:768
	v_pk_mul_f32 v[50:51], v[142:143], v[152:153] op_sel_hi:[1,0]
	v_pk_fma_f32 v[38:39], v[38:39], v[54:55], v[42:43]
	v_pk_fma_f32 v[40:41], v[36:37], v[50:51], v[40:41]
	v_pk_fma_f32 v[36:37], v[40:41], v[58:59], v[32:33]
	s_nop 0
	v_mul_f32_e32 v32, 4.0, v36
	v_mul_f32_e32 v33, 4.0, v37
	v_cvt_pk_fp8_f32 v42, v32, v33
	v_pk_fma_f32 v[32:33], v[38:39], v[56:57], v[34:35]
	s_nop 0
	v_mul_f32_e32 v34, 4.0, v32
	v_mul_f32_e32 v35, 4.0, v33
	v_cvt_pk_fp8_f32 v42, v34, v35 op_sel:[0,0,1]
	v_cvt_pk_bf16_f32 v34, v40, v41
	v_cvt_pk_bf16_f32 v35, v38, v39
	global_store_dwordx2 v[158:159], v[34:35], off offset:3584
	global_store_dword v[160:161], v42, off offset:1792
	s_add_i32 s19, s19, 8
	v_readlane_b32 s0, v251, 30
	s_cmp_lt_i32 s19, s0
	s_cselect_b64 s[10:11], -1, 0
	s_cmp_ge_i32 s19, s0
	s_cselect_b64 s[8:9], -1, 0
	s_and_b64 vcc, exec, s[8:9]
	s_cbranch_vccnz .LBB0_883
	s_add_i32 s2, s18, 16
	s_ashr_i32 s3, s2, 31
	s_lshl_b64 s[12:13], s[2:3], 11
	v_readlane_b32 s14, v253, 32
	s_cmpk_lt_i32 s18, 0x3f0
	v_readlane_b32 s15, v253, 33
	s_cselect_b64 s[0:1], -1, 0
	s_mov_b32 s17, s15
	s_add_i32 s16, s18, 0xfffffc10
	v_writelane_b32 v253, s14, 32
	v_lshl_add_u64 v[34:35], v[116:117], 0, s[12:13]
	s_nop 0
	v_writelane_b32 v253, s15, 33
	s_lshl_b64 s[14:15], s[16:17], 12
	v_readlane_b32 s16, v251, 39
	v_readlane_b32 s17, v251, 40
	s_add_u32 s16, s16, s14
	s_addc_u32 s17, s17, s15
	s_lshl_b64 s[2:3], s[2:3], 12
	v_readlane_b32 s14, v251, 41
	v_readlane_b32 s15, v251, 42
	s_add_u32 s62, s14, s2
	s_addc_u32 s63, s15, s3
	s_mov_b64 s[14:15], -1
	s_and_b64 vcc, exec, s[6:7]
	s_cbranch_vccz .LBB0_868
	global_load_dwordx2 v[150:151], v[34:35], off
	v_mov_b32_e32 v152, v153
	s_mov_b64 s[14:15], 0
	s_waitcnt vmcnt(0)
	v_mov_b64_e32 v[0:1], v[150:151]
	v_mov_b64_e32 v[2:3], v[152:153]

; #define LAS __attribute__((address_space(3)))
; __device__ __forceinline__ unsigned pk4_fp8(float x0, float x1, float x2, float x3) { int w = 0; w = __builtin_amdgcn_cvt_pk_fp8_f32(x0, x1, w, false); w = __builtin_amdgcn_cvt_pk_fp8_f32(x2, x3, w, true); return (unsigned)w; }
; #define PG8_SCHED __builtin_amdgcn_sched_barrier(0)
; template <class Epi, class Sched, bool GATHER, bool FP8 = false>
; __device__ __forceinline__ void gemm_phase(LAS unsigned char* lds, const Gemm g, const Sched& S, const Epi& E, const int wave_s) {
;     ...
;         if constexpr (FP8) { asm volatile("s_nop 15\n\ts_nop 15" ::: "memory"); PG8_SCHED; }
;     __device__ __forceinline__ void operator()(const f32x4 (&acc)[2][2][4][2], const Unit& u, int wr, int wc, int fr, int fq, const LAS float* bl) const {
;         const int pnl = u.pn & 7;
;         const int row0 = u.pm * BM + wr * 64 + fr, cl = wc * 32 + 8 * fq, col0 = pnl * BM + cl;
; #pragma unroll
;         for (int ai = 0; ai < 2; ++ai)
; #pragma unroll
;             for (int m = 0; m < 4; ++m) { unsigned char* rowp = ACT + (size_t)(row0 + ai * HALF + m * 16) * 1024 + (col0 >> 1);
; #pragma unroll
;                 for (int bj = 0; bj < 2; ++bj) { const f32x4 v0 = acc[ai][bj][m][0] + *(const LAS f32x4*)(bl + cl + bj * HALF), v1 = acc[ai][bj][m][1] + *(const LAS f32x4*)(bl + cl + bj * HALF + 4);
;                     float o[4];
; #pragma unroll
;                     for (int i = 0; i < 4; ++i) { const float hg = (i < 2) ? v0[2 * i] : v1[2 * i - 4], hl = (i < 2) ? v0[2 * i + 1] : v1[2 * i - 3];
;                         const float glu = fminf(hg, 7.f), lin4 = fminf(fmaxf(hl, -7.f), 7.f) * ACT_Q + ACT_Q;
;                         const float sg = __builtin_amdgcn_rcpf(1.f + __builtin_amdgcn_exp2f(glu * (-1.702f * 1.4426950408889634f)));
;                         o[i] = glu * sg * lin4; }
;                     *(unsigned*)(rowp + bj * (HALF / 2)) = pk4_fp8(o[0], o[1], o[2], o[3]); } }
.LBB0_1474:
	s_nop 15
	s_nop 15
	s_lshl_b32 s0, s65, 10
	s_and_b32 s0, s0, 0x400
	v_add_u32_e32 v16, s0, v179
	ds_read_b128 v[8:11], v16
	ds_read_b128 v[4:7], v16 offset:16
	s_lshl_b32 s1, s44, 8
	s_and_b32 s1, s1, 0x700
	v_or_b32_e32 v0, s1, v177
	s_waitcnt lgkmcnt(0)
	v_pk_add_f32 v[2:3], v[158:159], v[8:9]
	v_lshrrev_b32_e32 v152, 1, v0
	v_min_f32_e32 v2, 0x40e00000, v2
	v_mul_f32_e32 v12, 0xc01d265f, v2
	v_exp_f32_e32 v17, v12
	v_pk_add_f32 v[0:1], v[160:161], v[10:11]
	v_readlane_b32 s0, v246, 45
	v_min_f32_e32 v0, 0x40e00000, v0
	v_add_f32_e32 v17, 1.0, v17
	v_rcp_f32_e32 v17, v17
	v_mul_f32_e32 v22, 0xc01d265f, v0
	v_readlane_b32 s1, v246, 46
	v_exp_f32_e32 v22, v22
	v_pk_add_f32 v[14:15], v[154:155], v[4:5]
	v_lshl_add_u64 v[18:19], s[0:1], 0, v[152:153]
	s_mov_b32 s1, 0xc0e00000
	v_med3_f32 v3, v3, s1, v210
	v_fma_f32 v3, v3, 4.0, 4.0
	v_mul_f32_e32 v2, v2, v17
	v_min_f32_e32 v14, 0x40e00000, v14
	v_mul_f32_e32 v2, v3, v2
	v_add_f32_e32 v3, 1.0, v22
	v_mul_f32_e32 v17, 0xc01d265f, v14
	v_rcp_f32_e32 v3, v3
	v_exp_f32_e32 v17, v17
	v_pk_add_f32 v[12:13], v[156:157], v[6:7]
	v_med3_f32 v1, v1, s1, v210
	v_mul_f32_e32 v0, v0, v3
	v_add_f32_e32 v3, 1.0, v17
	v_rcp_f32_e32 v3, v3
	v_min_f32_e32 v12, 0x40e00000, v12
	v_fma_f32 v1, v1, 4.0, 4.0
	v_mul_f32_e32 v0, v1, v0
	v_mul_f32_e32 v3, v14, v3
	v_mul_f32_e32 v14, 0xc01d265f, v12
	v_exp_f32_e32 v14, v14
	v_med3_f32 v1, v15, s1, v210
	v_fma_f32 v1, v1, 4.0, 4.0
	v_mul_f32_e32 v15, v1, v3
	v_med3_f32 v1, v13, s1, v210
	v_fma_f32 v13, v1, 4.0, 4.0
	v_add_f32_e32 v1, 1.0, v14
	v_rcp_f32_e32 v14, v1
	v_cvt_pk_fp8_f32 v28, v2, v0
	ds_read_b128 v[0:3], v16 offset:512
	v_mul_f32_e32 v12, v12, v14
	v_mul_f32_e32 v12, v13, v12
	v_cvt_pk_fp8_f32 v28, v15, v12 op_sel:[0,0,1]
	ds_read_b128 v[12:15], v16 offset:528
	s_waitcnt lgkmcnt(0)
	v_pk_add_f32 v[16:17], v[148:149], v[0:1]
	v_lshl_add_u32 v20, s64, 8, v215
	v_min_f32_e32 v16, 0x40e00000, v16
	v_mul_f32_e32 v22, 0xc01d265f, v16
	v_exp_f32_e32 v29, v22
	v_pk_add_f32 v[22:23], v[150:151], v[2:3]
	v_med3_f32 v17, v17, s1, v210
	v_min_f32_e32 v22, 0x40e00000, v22
	v_add_f32_e32 v29, 1.0, v29
	v_rcp_f32_e32 v29, v29
	v_mul_f32_e32 v30, 0xc01d265f, v22
	v_exp_f32_e32 v30, v30
	v_pk_add_f32 v[26:27], v[144:145], v[12:13]
	v_fma_f32 v17, v17, 4.0, 4.0
	v_mul_f32_e32 v16, v16, v29
	v_mul_f32_e32 v16, v17, v16
	v_med3_f32 v17, v23, s1, v210
	v_min_f32_e32 v23, 0x40e00000, v26
	v_add_f32_e32 v29, 1.0, v30
	v_mul_f32_e32 v26, 0xc01d265f, v23
	v_rcp_f32_e32 v29, v29
	v_exp_f32_e32 v26, v26
	v_pk_add_f32 v[24:25], v[146:147], v[14:15]
	v_fma_f32 v17, v17, 4.0, 4.0
	v_mul_f32_e32 v22, v22, v29
	v_add_f32_e32 v26, 1.0, v26
	v_min_f32_e32 v24, 0x40e00000, v24
	v_mul_f32_e32 v17, v17, v22
	v_med3_f32 v22, v27, s1, v210
	v_rcp_f32_e32 v26, v26
	v_mul_f32_e32 v27, 0xc01d265f, v24
	v_exp_f32_e32 v27, v27
	v_fma_f32 v22, v22, 4.0, 4.0
	v_mul_f32_e32 v23, v23, v26
	v_mul_f32_e32 v22, v22, v23
	v_med3_f32 v23, v25, s1, v210
	v_add_f32_e32 v25, 1.0, v27
	v_rcp_f32_e32 v25, v25
	v_cvt_pk_fp8_f32 v26, v16, v17
	v_fma_f32 v16, v23, 4.0, 4.0
	v_mul_f32_e32 v17, v24, v25
	v_ashrrev_i32_e32 v21, 31, v20
	v_mul_f32_e32 v16, v16, v17
	v_pk_add_f32 v[24:25], v[140:141], v[8:9]
	v_cvt_pk_fp8_f32 v26, v22, v16 op_sel:[0,0,1]
	v_lshlrev_b64 v[16:17], 10, v[20:21]
	v_min_f32_e32 v21, 0x40e00000, v24
	v_mul_f32_e32 v24, 0xc01d265f, v21
	v_exp_f32_e32 v24, v24
	v_lshl_add_u64 v[16:17], v[18:19], 0, v[16:17]
	global_store_dword v[16:17], v28, off
	global_store_dword v[16:17], v26, off offset:64
	v_pk_add_f32 v[26:27], v[142:143], v[10:11]
	v_pk_add_f32 v[30:31], v[136:137], v[4:5]
	v_min_f32_e32 v26, 0x40e00000, v26
	v_add_f32_e32 v24, 1.0, v24
	v_mul_f32_e32 v136, 0xc01d265f, v26
	v_rcp_f32_e32 v24, v24
	v_exp_f32_e32 v136, v136
	v_med3_f32 v25, v25, s1, v210
	v_fma_f32 v25, v25, 4.0, 4.0
	v_mul_f32_e32 v21, v21, v24
	v_add_f32_e32 v24, 1.0, v136
	v_rcp_f32_e32 v24, v24
	v_mul_f32_e32 v21, v25, v21
	v_med3_f32 v25, v27, s1, v210
	v_pk_add_f32 v[28:29], v[138:139], v[6:7]
	v_mul_f32_e32 v24, v26, v24
	v_min_f32_e32 v26, 0x40e00000, v30
	v_mul_f32_e32 v27, 0xc01d265f, v26
	v_exp_f32_e32 v27, v27
	v_min_f32_e32 v28, 0x40e00000, v28
	v_mul_f32_e32 v30, 0xc01d265f, v28
	v_exp_f32_e32 v30, v30
	v_add_f32_e32 v27, 1.0, v27
	v_rcp_f32_e32 v27, v27
	v_fma_f32 v25, v25, 4.0, 4.0
	v_mul_f32_e32 v24, v25, v24
	v_med3_f32 v25, v31, s1, v210
	v_mul_f32_e32 v26, v26, v27
	v_add_f32_e32 v27, 1.0, v30
	v_rcp_f32_e32 v27, v27
	v_fma_f32 v25, v25, 4.0, 4.0
	v_cvt_pk_fp8_f32 v136, v21, v24
	v_mul_f32_e32 v25, v25, v26
	v_med3_f32 v26, v29, s1, v210
	v_fma_f32 v21, v26, 4.0, 4.0
	v_mul_f32_e32 v24, v28, v27
	v_mul_f32_e32 v21, v21, v24
	v_cvt_pk_fp8_f32 v136, v25, v21 op_sel:[0,0,1]
	v_pk_add_f32 v[24:25], v[132:133], v[0:1]
	v_pk_add_f32 v[26:27], v[134:135], v[2:3]
	v_min_f32_e32 v21, 0x40e00000, v24
	v_mul_f32_e32 v24, 0xc01d265f, v21
	v_exp_f32_e32 v24, v24
	v_min_f32_e32 v26, 0x40e00000, v26
	v_pk_add_f32 v[30:31], v[128:129], v[12:13]
	v_mul_f32_e32 v128, 0xc01d265f, v26
	v_add_f32_e32 v24, 1.0, v24
	v_rcp_f32_e32 v24, v24
	v_exp_f32_e32 v128, v128
	v_med3_f32 v25, v25, s1, v210
	v_fma_f32 v25, v25, 4.0, 4.0
	v_mul_f32_e32 v21, v21, v24
	v_add_f32_e32 v24, 1.0, v128
	v_rcp_f32_e32 v24, v24
	v_mul_f32_e32 v21, v25, v21
	v_med3_f32 v25, v27, s1, v210
	v_pk_add_f32 v[28:29], v[130:131], v[14:15]
	v_mul_f32_e32 v24, v26, v24
	v_min_f32_e32 v26, 0x40e00000, v30
	v_mul_f32_e32 v27, 0xc01d265f, v26
	v_exp_f32_e32 v27, v27
	v_min_f32_e32 v28, 0x40e00000, v28
	v_mul_f32_e32 v30, 0xc01d265f, v28
	v_exp_f32_e32 v30, v30
	v_add_f32_e32 v27, 1.0, v27
	v_rcp_f32_e32 v27, v27
	v_fma_f32 v25, v25, 4.0, 4.0
; #define LAS __attribute__((address_space(3)))
; __device__ __forceinline__ unsigned pk4_fp8(float x0, float x1, float x2, float x3) { int w = 0; w = __builtin_amdgcn_cvt_pk_fp8_f32(x0, x1, w, false); w = __builtin_amdgcn_cvt_pk_fp8_f32(x2, x3, w, true); return (unsigned)w; }
;     __device__ __forceinline__ void operator()(const f32x4 (&acc)[2][2][4][2], const Unit& u, int wr, int wc, int fr, int fq, const LAS float* bl) const {
;     ...
;                 for (int bj = 0; bj < 2; ++bj) { const f32x4 v0 = acc[ai][bj][m][0] + *(const LAS f32x4*)(bl + cl + bj * HALF), v1 = acc[ai][bj][m][1] + *(const LAS f32x4*)(bl + cl + bj * HALF + 4);
;                     float o[4];
; #pragma unroll
;                     for (int i = 0; i < 4; ++i) { const float hg = (i < 2) ? v0[2 * i] : v1[2 * i - 4], hl = (i < 2) ? v0[2 * i + 1] : v1[2 * i - 3];
;                         const float glu = fminf(hg, 7.f), lin4 = fminf(fmaxf(hl, -7.f), 7.f) * ACT_Q + ACT_Q;
;                         const float sg = __builtin_amdgcn_rcpf(1.f + __builtin_amdgcn_exp2f(glu * (-1.702f * 1.4426950408889634f)));
;                         o[i] = glu * sg * lin4; }
;                     *(unsigned*)(rowp + bj * (HALF / 2)) = pk4_fp8(o[0], o[1], o[2], o[3]); } }
	v_mul_f32_e32 v24, v25, v24
	v_med3_f32 v25, v31, s1, v210
	v_mul_f32_e32 v26, v26, v27
	v_add_f32_e32 v27, 1.0, v30
	v_fma_f32 v25, v25, 4.0, 4.0
	v_rcp_f32_e32 v27, v27
	v_mul_f32_e32 v25, v25, v26
	v_med3_f32 v26, v29, s1, v210
	v_cvt_pk_fp8_f32 v29, v21, v24
	v_fma_f32 v21, v26, 4.0, 4.0
	v_mul_f32_e32 v24, v28, v27
	v_mul_f32_e32 v21, v21, v24
	v_cvt_pk_fp8_f32 v29, v25, v21 op_sel:[0,0,1]
	v_pk_add_f32 v[24:25], v[124:125], v[8:9]
	v_pk_add_f32 v[26:27], v[126:127], v[10:11]
	v_min_f32_e32 v21, 0x40e00000, v24
	v_mul_f32_e32 v24, 0xc01d265f, v21
	v_exp_f32_e32 v24, v24
	v_min_f32_e32 v26, 0x40e00000, v26
	v_pk_add_f32 v[30:31], v[120:121], v[4:5]
	v_mul_f32_e32 v120, 0xc01d265f, v26
	v_add_f32_e32 v24, 1.0, v24
	v_rcp_f32_e32 v24, v24
	v_exp_f32_e32 v120, v120
	v_med3_f32 v25, v25, s1, v210
	v_or_b32_e32 v22, 16, v20
	v_mul_f32_e32 v21, v21, v24
	v_add_f32_e32 v24, 1.0, v120
	v_rcp_f32_e32 v24, v24
	v_fma_f32 v25, v25, 4.0, 4.0
	v_ashrrev_i32_e32 v23, 31, v22
	v_mul_f32_e32 v21, v25, v21
	v_mul_f32_e32 v24, v26, v24
	v_min_f32_e32 v26, 0x40e00000, v30
	v_med3_f32 v25, v27, s1, v210
	v_mul_f32_e32 v27, 0xc01d265f, v26
	v_lshlrev_b64 v[22:23], 10, v[22:23]
	v_exp_f32_e32 v27, v27
	v_lshl_add_u64 v[22:23], v[18:19], 0, v[22:23]
	global_store_dword v[22:23], v136, off
	global_store_dword v[22:23], v29, off offset:64
	v_pk_add_f32 v[28:29], v[122:123], v[6:7]
	v_add_f32_e32 v27, 1.0, v27
	v_min_f32_e32 v28, 0x40e00000, v28
	v_mul_f32_e32 v30, 0xc01d265f, v28
	v_rcp_f32_e32 v27, v27
	v_exp_f32_e32 v30, v30
	v_fma_f32 v25, v25, 4.0, 4.0
	v_mul_f32_e32 v24, v25, v24
	v_mul_f32_e32 v26, v26, v27
	v_add_f32_e32 v27, 1.0, v30
	v_rcp_f32_e32 v27, v27
	v_med3_f32 v25, v31, s1, v210
	v_fma_f32 v25, v25, 4.0, 4.0
	v_cvt_pk_fp8_f32 v120, v21, v24
	v_mul_f32_e32 v25, v25, v26
	v_med3_f32 v26, v29, s1, v210
	v_fma_f32 v21, v26, 4.0, 4.0
	v_mul_f32_e32 v24, v28, v27
	v_mul_f32_e32 v21, v21, v24
	v_cvt_pk_fp8_f32 v120, v25, v21 op_sel:[0,0,1]
	v_pk_add_f32 v[24:25], v[116:117], v[0:1]
	v_pk_add_f32 v[26:27], v[118:119], v[2:3]
	v_min_f32_e32 v21, 0x40e00000, v24
	v_mul_f32_e32 v24, 0xc01d265f, v21
	v_exp_f32_e32 v24, v24
	v_min_f32_e32 v26, 0x40e00000, v26
	v_pk_add_f32 v[30:31], v[112:113], v[12:13]
	v_mul_f32_e32 v112, 0xc01d265f, v26
	v_add_f32_e32 v24, 1.0, v24
	v_rcp_f32_e32 v24, v24
	v_exp_f32_e32 v112, v112
	v_med3_f32 v25, v25, s1, v210
	v_fma_f32 v25, v25, 4.0, 4.0
	v_mul_f32_e32 v21, v21, v24
	v_add_f32_e32 v24, 1.0, v112
	v_rcp_f32_e32 v24, v24
	v_mul_f32_e32 v21, v25, v21
	v_med3_f32 v25, v27, s1, v210
	v_pk_add_f32 v[28:29], v[114:115], v[14:15]
	v_mul_f32_e32 v24, v26, v24
	v_min_f32_e32 v26, 0x40e00000, v30
	v_mul_f32_e32 v27, 0xc01d265f, v26
	v_exp_f32_e32 v27, v27
	v_min_f32_e32 v28, 0x40e00000, v28
	v_mul_f32_e32 v30, 0xc01d265f, v28
	v_exp_f32_e32 v30, v30
	v_add_f32_e32 v27, 1.0, v27
	v_rcp_f32_e32 v27, v27
	v_fma_f32 v25, v25, 4.0, 4.0
	v_mul_f32_e32 v24, v25, v24
	v_med3_f32 v25, v31, s1, v210
	v_mul_f32_e32 v26, v26, v27
	v_add_f32_e32 v27, 1.0, v30
	v_fma_f32 v25, v25, 4.0, 4.0
	v_rcp_f32_e32 v27, v27
	v_mul_f32_e32 v25, v25, v26
	v_med3_f32 v26, v29, s1, v210
	v_cvt_pk_fp8_f32 v29, v21, v24
	v_fma_f32 v21, v26, 4.0, 4.0
	v_mul_f32_e32 v24, v28, v27
	v_or_b32_e32 v22, 32, v20
	v_mul_f32_e32 v21, v21, v24
	v_ashrrev_i32_e32 v23, 31, v22
	v_cvt_pk_fp8_f32 v29, v25, v21 op_sel:[0,0,1]
	v_lshlrev_b64 v[22:23], 10, v[22:23]
	v_lshl_add_u64 v[22:23], v[18:19], 0, v[22:23]
	global_store_dword v[22:23], v120, off
	global_store_dword v[22:23], v29, off offset:64
	v_pk_add_f32 v[22:23], v[108:109], v[8:9]
	v_pk_add_f32 v[28:29], v[104:105], v[4:5]
	v_min_f32_e32 v22, 0x40e00000, v22
	v_mul_f32_e32 v24, 0xc01d265f, v22
	v_exp_f32_e32 v30, v24
	v_pk_add_f32 v[24:25], v[110:111], v[10:11]
	v_med3_f32 v23, v23, s1, v210
	v_min_f32_e32 v24, 0x40e00000, v24
	v_add_f32_e32 v30, 1.0, v30
	v_rcp_f32_e32 v30, v30
	v_mul_f32_e32 v31, 0xc01d265f, v24
	v_exp_f32_e32 v31, v31
	v_fma_f32 v23, v23, 4.0, 4.0
	v_mul_f32_e32 v22, v22, v30
	v_mul_f32_e32 v22, v23, v22
	v_med3_f32 v23, v25, s1, v210
	v_min_f32_e32 v25, 0x40e00000, v28
	v_add_f32_e32 v30, 1.0, v31
	v_mul_f32_e32 v28, 0xc01d265f, v25
	v_rcp_f32_e32 v30, v30
	v_exp_f32_e32 v28, v28
	v_pk_add_f32 v[26:27], v[106:107], v[6:7]
	v_fma_f32 v23, v23, 4.0, 4.0
	v_mul_f32_e32 v24, v24, v30
	v_add_f32_e32 v28, 1.0, v28
	v_min_f32_e32 v26, 0x40e00000, v26
	v_mul_f32_e32 v23, v23, v24
	v_med3_f32 v24, v29, s1, v210
	v_rcp_f32_e32 v28, v28
	v_mul_f32_e32 v29, 0xc01d265f, v26
	v_exp_f32_e32 v29, v29
	v_fma_f32 v24, v24, 4.0, 4.0
	v_mul_f32_e32 v25, v25, v28
	v_mul_f32_e32 v24, v24, v25
	v_med3_f32 v25, v27, s1, v210
	v_add_f32_e32 v27, 1.0, v29
	v_rcp_f32_e32 v27, v27
	v_cvt_pk_fp8_f32 v30, v22, v23
	v_fma_f32 v22, v25, 4.0, 4.0
	v_mul_f32_e32 v23, v26, v27
	v_mul_f32_e32 v22, v22, v23
	v_cvt_pk_fp8_f32 v30, v24, v22 op_sel:[0,0,1]
	v_pk_add_f32 v[22:23], v[100:101], v[0:1]
	v_pk_add_f32 v[28:29], v[96:97], v[12:13]
	v_min_f32_e32 v22, 0x40e00000, v22
	v_mul_f32_e32 v24, 0xc01d265f, v22
	v_exp_f32_e32 v31, v24
	v_pk_add_f32 v[24:25], v[102:103], v[2:3]
	v_med3_f32 v23, v23, s1, v210
	v_min_f32_e32 v24, 0x40e00000, v24
	v_add_f32_e32 v31, 1.0, v31
	v_rcp_f32_e32 v31, v31
	v_mul_f32_e32 v96, 0xc01d265f, v24
	v_exp_f32_e32 v96, v96
	v_fma_f32 v23, v23, 4.0, 4.0
	v_mul_f32_e32 v22, v22, v31
	v_mul_f32_e32 v22, v23, v22
	v_med3_f32 v23, v25, s1, v210
	v_min_f32_e32 v25, 0x40e00000, v28
	v_add_f32_e32 v31, 1.0, v96
	v_mul_f32_e32 v28, 0xc01d265f, v25
	v_rcp_f32_e32 v31, v31
	v_exp_f32_e32 v28, v28
	v_pk_add_f32 v[26:27], v[98:99], v[14:15]
	v_fma_f32 v23, v23, 4.0, 4.0
	v_mul_f32_e32 v24, v24, v31
; #define LAS __attribute__((address_space(3)))
; __device__ __forceinline__ unsigned pk4_fp8(float x0, float x1, float x2, float x3) { int w = 0; w = __builtin_amdgcn_cvt_pk_fp8_f32(x0, x1, w, false); w = __builtin_amdgcn_cvt_pk_fp8_f32(x2, x3, w, true); return (unsigned)w; }
;     __device__ __forceinline__ void operator()(const f32x4 (&acc)[2][2][4][2], const Unit& u, int wr, int wc, int fr, int fq, const LAS float* bl) const {
;     ...
;                 for (int bj = 0; bj < 2; ++bj) { const f32x4 v0 = acc[ai][bj][m][0] + *(const LAS f32x4*)(bl + cl + bj * HALF), v1 = acc[ai][bj][m][1] + *(const LAS f32x4*)(bl + cl + bj * HALF + 4);
;                     float o[4];
; #pragma unroll
;                     for (int i = 0; i < 4; ++i) { const float hg = (i < 2) ? v0[2 * i] : v1[2 * i - 4], hl = (i < 2) ? v0[2 * i + 1] : v1[2 * i - 3];
;                         const float glu = fminf(hg, 7.f), lin4 = fminf(fmaxf(hl, -7.f), 7.f) * ACT_Q + ACT_Q;
;                         const float sg = __builtin_amdgcn_rcpf(1.f + __builtin_amdgcn_exp2f(glu * (-1.702f * 1.4426950408889634f)));
;                         o[i] = glu * sg * lin4; }
;                     *(unsigned*)(rowp + bj * (HALF / 2)) = pk4_fp8(o[0], o[1], o[2], o[3]); } }
	v_add_f32_e32 v28, 1.0, v28
	v_min_f32_e32 v26, 0x40e00000, v26
	v_mul_f32_e32 v23, v23, v24
	v_med3_f32 v24, v29, s1, v210
	v_rcp_f32_e32 v28, v28
	v_mul_f32_e32 v29, 0xc01d265f, v26
	v_exp_f32_e32 v29, v29
	v_fma_f32 v24, v24, 4.0, 4.0
	v_mul_f32_e32 v25, v25, v28
	v_mul_f32_e32 v24, v24, v25
	v_med3_f32 v25, v27, s1, v210
	v_add_f32_e32 v27, 1.0, v29
	v_rcp_f32_e32 v27, v27
	v_cvt_pk_fp8_f32 v28, v22, v23
	v_or_b32_e32 v20, 48, v20
	v_ashrrev_i32_e32 v21, 31, v20
	v_fma_f32 v22, v25, 4.0, 4.0
	v_mul_f32_e32 v23, v26, v27
	v_mul_f32_e32 v22, v22, v23
	v_lshlrev_b64 v[20:21], 10, v[20:21]
	v_cvt_pk_fp8_f32 v28, v24, v22 op_sel:[0,0,1]
	v_lshl_add_u64 v[18:19], v[18:19], 0, v[20:21]
	v_pk_add_f32 v[20:21], v[92:93], v[8:9]
	global_store_dword v[18:19], v30, off
	global_store_dword v[18:19], v28, off offset:64
	v_min_f32_e32 v20, 0x40e00000, v20
	v_mul_f32_e32 v22, 0xc01d265f, v20
	v_exp_f32_e32 v28, v22
	v_pk_add_f32 v[22:23], v[94:95], v[10:11]
	v_med3_f32 v21, v21, s1, v210
	v_min_f32_e32 v22, 0x40e00000, v22
	v_add_f32_e32 v28, 1.0, v28
	v_rcp_f32_e32 v28, v28
	v_mul_f32_e32 v29, 0xc01d265f, v22
	v_exp_f32_e32 v29, v29
	v_pk_add_f32 v[26:27], v[88:89], v[4:5]
	v_fma_f32 v21, v21, 4.0, 4.0
	v_mul_f32_e32 v20, v20, v28
	v_mul_f32_e32 v20, v21, v20
	v_med3_f32 v21, v23, s1, v210
	v_min_f32_e32 v23, 0x40e00000, v26
	v_add_f32_e32 v28, 1.0, v29
	v_mul_f32_e32 v26, 0xc01d265f, v23
	v_rcp_f32_e32 v28, v28
	v_exp_f32_e32 v26, v26
	v_pk_add_f32 v[24:25], v[90:91], v[6:7]
	v_fma_f32 v21, v21, 4.0, 4.0
	v_mul_f32_e32 v22, v22, v28
	v_add_f32_e32 v26, 1.0, v26
	v_min_f32_e32 v24, 0x40e00000, v24
	v_mul_f32_e32 v21, v21, v22
	v_med3_f32 v22, v27, s1, v210
	v_rcp_f32_e32 v26, v26
	v_mul_f32_e32 v27, 0xc01d265f, v24
	v_exp_f32_e32 v27, v27
	v_fma_f32 v22, v22, 4.0, 4.0
	v_mul_f32_e32 v23, v23, v26
	v_mul_f32_e32 v22, v22, v23
	v_med3_f32 v23, v25, s1, v210
	v_add_f32_e32 v25, 1.0, v27
	v_rcp_f32_e32 v25, v25
	v_cvt_pk_fp8_f32 v28, v20, v21
	v_fma_f32 v20, v23, 4.0, 4.0
	v_mul_f32_e32 v21, v24, v25
	v_mul_f32_e32 v20, v20, v21
	v_cvt_pk_fp8_f32 v28, v22, v20 op_sel:[0,0,1]
	v_pk_add_f32 v[20:21], v[84:85], v[0:1]
	v_pk_add_f32 v[26:27], v[80:81], v[12:13]
	v_min_f32_e32 v20, 0x40e00000, v20
	v_mul_f32_e32 v22, 0xc01d265f, v20
	v_exp_f32_e32 v29, v22
	v_pk_add_f32 v[22:23], v[86:87], v[2:3]
	v_med3_f32 v21, v21, s1, v210
	v_min_f32_e32 v22, 0x40e00000, v22
	v_add_f32_e32 v29, 1.0, v29
	v_rcp_f32_e32 v29, v29
	v_mul_f32_e32 v30, 0xc01d265f, v22
	v_exp_f32_e32 v30, v30
	v_fma_f32 v21, v21, 4.0, 4.0
	v_mul_f32_e32 v20, v20, v29
	v_mul_f32_e32 v20, v21, v20
	v_med3_f32 v21, v23, s1, v210
	v_min_f32_e32 v23, 0x40e00000, v26
	v_add_f32_e32 v29, 1.0, v30
	v_mul_f32_e32 v26, 0xc01d265f, v23
	v_rcp_f32_e32 v29, v29
	v_exp_f32_e32 v26, v26
	v_pk_add_f32 v[24:25], v[82:83], v[14:15]
	v_fma_f32 v21, v21, 4.0, 4.0
	v_mul_f32_e32 v22, v22, v29
	v_add_f32_e32 v26, 1.0, v26
	v_min_f32_e32 v24, 0x40e00000, v24
	v_mul_f32_e32 v21, v21, v22
	v_med3_f32 v22, v27, s1, v210
	v_rcp_f32_e32 v26, v26
	v_mul_f32_e32 v27, 0xc01d265f, v24
	v_exp_f32_e32 v27, v27
	v_fma_f32 v22, v22, 4.0, 4.0
	v_mul_f32_e32 v23, v23, v26
	v_mul_f32_e32 v22, v22, v23
	v_med3_f32 v23, v25, s1, v210
	v_add_f32_e32 v25, 1.0, v27
	v_rcp_f32_e32 v25, v25
	v_cvt_pk_fp8_f32 v26, v20, v21
	v_fma_f32 v20, v23, 4.0, 4.0
	v_mul_f32_e32 v21, v24, v25
	v_mul_f32_e32 v20, v20, v21
	v_cvt_pk_fp8_f32 v26, v22, v20 op_sel:[0,0,1]
	s_mov_b32 s0, 0x20000
	v_add_co_u32_e32 v20, vcc, s0, v16
	s_mov_b64 s[2:3], 0x20000
	s_nop 0
	v_addc_co_u32_e32 v21, vcc, 0, v17, vcc
	v_lshl_add_u64 v[18:19], v[16:17], 0, s[2:3]
	global_store_dword v[20:21], v28, off
	global_store_dword v[18:19], v26, off offset:64
	v_pk_add_f32 v[20:21], v[76:77], v[8:9]
	v_pk_add_f32 v[26:27], v[72:73], v[4:5]
	v_min_f32_e32 v20, 0x40e00000, v20
	v_mul_f32_e32 v22, 0xc01d265f, v20
	v_exp_f32_e32 v28, v22
	v_pk_add_f32 v[22:23], v[78:79], v[10:11]
	v_med3_f32 v21, v21, s1, v210
	v_min_f32_e32 v22, 0x40e00000, v22
	v_add_f32_e32 v28, 1.0, v28
	v_rcp_f32_e32 v28, v28
	v_mul_f32_e32 v29, 0xc01d265f, v22
	v_exp_f32_e32 v29, v29
	v_fma_f32 v21, v21, 4.0, 4.0
	v_mul_f32_e32 v20, v20, v28
	v_mul_f32_e32 v20, v21, v20
	v_med3_f32 v21, v23, s1, v210
	v_min_f32_e32 v23, 0x40e00000, v26
	v_add_f32_e32 v28, 1.0, v29
	v_mul_f32_e32 v26, 0xc01d265f, v23
	v_rcp_f32_e32 v28, v28
	v_exp_f32_e32 v26, v26
	v_pk_add_f32 v[24:25], v[74:75], v[6:7]
	v_fma_f32 v21, v21, 4.0, 4.0
	v_mul_f32_e32 v22, v22, v28
	v_add_f32_e32 v26, 1.0, v26
	v_min_f32_e32 v24, 0x40e00000, v24
	v_mul_f32_e32 v21, v21, v22
	v_med3_f32 v22, v27, s1, v210
	v_rcp_f32_e32 v26, v26
	v_mul_f32_e32 v27, 0xc01d265f, v24
	v_exp_f32_e32 v27, v27
	v_fma_f32 v22, v22, 4.0, 4.0
	v_mul_f32_e32 v23, v23, v26
	v_mul_f32_e32 v22, v22, v23
	v_med3_f32 v23, v25, s1, v210
	v_add_f32_e32 v25, 1.0, v27
	v_rcp_f32_e32 v25, v25
	v_cvt_pk_fp8_f32 v28, v20, v21
	v_fma_f32 v20, v23, 4.0, 4.0
	v_mul_f32_e32 v21, v24, v25
	v_mul_f32_e32 v20, v20, v21
	v_cvt_pk_fp8_f32 v28, v22, v20 op_sel:[0,0,1]
	v_pk_add_f32 v[20:21], v[68:69], v[0:1]
	v_pk_add_f32 v[26:27], v[64:65], v[12:13]
	v_min_f32_e32 v20, 0x40e00000, v20
	v_mul_f32_e32 v22, 0xc01d265f, v20
	v_exp_f32_e32 v29, v22
	v_pk_add_f32 v[22:23], v[70:71], v[2:3]
	v_med3_f32 v21, v21, s1, v210
	v_min_f32_e32 v22, 0x40e00000, v22
	v_add_f32_e32 v29, 1.0, v29
	v_rcp_f32_e32 v29, v29
	v_mul_f32_e32 v30, 0xc01d265f, v22
	v_exp_f32_e32 v30, v30
	v_fma_f32 v21, v21, 4.0, 4.0
	v_mul_f32_e32 v20, v20, v29
	v_mul_f32_e32 v20, v21, v20
	v_med3_f32 v21, v23, s1, v210
	v_min_f32_e32 v23, 0x40e00000, v26
	v_add_f32_e32 v29, 1.0, v30
	v_mul_f32_e32 v26, 0xc01d265f, v23
	v_rcp_f32_e32 v29, v29
; #define LAS __attribute__((address_space(3)))
; __device__ __forceinline__ unsigned pk4_fp8(float x0, float x1, float x2, float x3) { int w = 0; w = __builtin_amdgcn_cvt_pk_fp8_f32(x0, x1, w, false); w = __builtin_amdgcn_cvt_pk_fp8_f32(x2, x3, w, true); return (unsigned)w; }
; template <class Epi, class Sched, bool GATHER, bool FP8 = false>
; __device__ __forceinline__ void gemm_phase(LAS unsigned char* lds, const Gemm g, const Sched& S, const Epi& E, const int wave_s) {
;     ...
;         if (!has_next) break;
;     __device__ __forceinline__ void operator()(const f32x4 (&acc)[2][2][4][2], const Unit& u, int wr, int wc, int fr, int fq, const LAS float* bl) const {
;     ...
;                 for (int bj = 0; bj < 2; ++bj) { const f32x4 v0 = acc[ai][bj][m][0] + *(const LAS f32x4*)(bl + cl + bj * HALF), v1 = acc[ai][bj][m][1] + *(const LAS f32x4*)(bl + cl + bj * HALF + 4);
;                     float o[4];
; #pragma unroll
;                     for (int i = 0; i < 4; ++i) { const float hg = (i < 2) ? v0[2 * i] : v1[2 * i - 4], hl = (i < 2) ? v0[2 * i + 1] : v1[2 * i - 3];
;                         const float glu = fminf(hg, 7.f), lin4 = fminf(fmaxf(hl, -7.f), 7.f) * ACT_Q + ACT_Q;
;                         const float sg = __builtin_amdgcn_rcpf(1.f + __builtin_amdgcn_exp2f(glu * (-1.702f * 1.4426950408889634f)));
;                         o[i] = glu * sg * lin4; }
;                     *(unsigned*)(rowp + bj * (HALF / 2)) = pk4_fp8(o[0], o[1], o[2], o[3]); } }
	v_exp_f32_e32 v26, v26
	v_pk_add_f32 v[24:25], v[66:67], v[14:15]
	v_fma_f32 v21, v21, 4.0, 4.0
	v_mul_f32_e32 v22, v22, v29
	v_add_f32_e32 v26, 1.0, v26
	v_min_f32_e32 v24, 0x40e00000, v24
	v_mul_f32_e32 v21, v21, v22
	v_med3_f32 v22, v27, s1, v210
	v_rcp_f32_e32 v26, v26
	v_mul_f32_e32 v27, 0xc01d265f, v24
	v_exp_f32_e32 v27, v27
	v_fma_f32 v22, v22, 4.0, 4.0
	v_mul_f32_e32 v23, v23, v26
	v_mul_f32_e32 v22, v22, v23
	v_med3_f32 v23, v25, s1, v210
	v_add_f32_e32 v25, 1.0, v27
	v_rcp_f32_e32 v25, v25
	v_cvt_pk_fp8_f32 v26, v20, v21
	v_fma_f32 v20, v23, 4.0, 4.0
	v_mul_f32_e32 v21, v24, v25
	v_mul_f32_e32 v20, v20, v21
	v_cvt_pk_fp8_f32 v26, v22, v20 op_sel:[0,0,1]
	s_mov_b32 s0, 0x24000
	v_add_co_u32_e32 v20, vcc, s0, v16
	s_mov_b64 s[2:3], 0x24000
	s_nop 0
	v_addc_co_u32_e32 v21, vcc, 0, v17, vcc
	v_lshl_add_u64 v[18:19], v[16:17], 0, s[2:3]
	global_store_dword v[20:21], v28, off
	global_store_dword v[18:19], v26, off offset:64
	v_pk_add_f32 v[20:21], v[60:61], v[8:9]
	v_pk_add_f32 v[26:27], v[56:57], v[4:5]
	v_min_f32_e32 v20, 0x40e00000, v20
	v_mul_f32_e32 v22, 0xc01d265f, v20
	v_exp_f32_e32 v28, v22
	v_pk_add_f32 v[22:23], v[62:63], v[10:11]
	v_med3_f32 v21, v21, s1, v210
	v_min_f32_e32 v22, 0x40e00000, v22
	v_add_f32_e32 v28, 1.0, v28
	v_rcp_f32_e32 v28, v28
	v_mul_f32_e32 v29, 0xc01d265f, v22
	v_exp_f32_e32 v29, v29
	v_fma_f32 v21, v21, 4.0, 4.0
	v_mul_f32_e32 v20, v20, v28
	v_mul_f32_e32 v20, v21, v20
	v_med3_f32 v21, v23, s1, v210
	v_min_f32_e32 v23, 0x40e00000, v26
	v_add_f32_e32 v28, 1.0, v29
	v_mul_f32_e32 v26, 0xc01d265f, v23
	v_rcp_f32_e32 v28, v28
	v_exp_f32_e32 v26, v26
	v_pk_add_f32 v[24:25], v[58:59], v[6:7]
	v_fma_f32 v21, v21, 4.0, 4.0
	v_mul_f32_e32 v22, v22, v28
	v_add_f32_e32 v26, 1.0, v26
	v_min_f32_e32 v24, 0x40e00000, v24
	v_mul_f32_e32 v21, v21, v22
	v_med3_f32 v22, v27, s1, v210
	v_rcp_f32_e32 v26, v26
	v_mul_f32_e32 v27, 0xc01d265f, v24
	v_exp_f32_e32 v27, v27
	v_fma_f32 v22, v22, 4.0, 4.0
	v_mul_f32_e32 v23, v23, v26
	v_mul_f32_e32 v22, v22, v23
	v_med3_f32 v23, v25, s1, v210
	v_add_f32_e32 v25, 1.0, v27
	v_rcp_f32_e32 v25, v25
	v_cvt_pk_fp8_f32 v28, v20, v21
	v_fma_f32 v20, v23, 4.0, 4.0
	v_mul_f32_e32 v21, v24, v25
	v_mul_f32_e32 v20, v20, v21
	v_cvt_pk_fp8_f32 v28, v22, v20 op_sel:[0,0,1]
	v_pk_add_f32 v[20:21], v[52:53], v[0:1]
	v_pk_add_f32 v[26:27], v[48:49], v[12:13]
	v_min_f32_e32 v20, 0x40e00000, v20
	v_mul_f32_e32 v22, 0xc01d265f, v20
	v_exp_f32_e32 v29, v22
	v_pk_add_f32 v[22:23], v[54:55], v[2:3]
	v_med3_f32 v21, v21, s1, v210
	v_min_f32_e32 v22, 0x40e00000, v22
	v_add_f32_e32 v29, 1.0, v29
	v_rcp_f32_e32 v29, v29
	v_mul_f32_e32 v30, 0xc01d265f, v22
	v_exp_f32_e32 v30, v30
	v_fma_f32 v21, v21, 4.0, 4.0
	v_mul_f32_e32 v20, v20, v29
	v_mul_f32_e32 v20, v21, v20
	v_med3_f32 v21, v23, s1, v210
	v_min_f32_e32 v23, 0x40e00000, v26
	v_add_f32_e32 v29, 1.0, v30
	v_mul_f32_e32 v26, 0xc01d265f, v23
	v_rcp_f32_e32 v29, v29
	v_exp_f32_e32 v26, v26
	v_pk_add_f32 v[24:25], v[50:51], v[14:15]
	v_fma_f32 v21, v21, 4.0, 4.0
	v_mul_f32_e32 v22, v22, v29
	v_add_f32_e32 v26, 1.0, v26
	v_min_f32_e32 v24, 0x40e00000, v24
	v_mul_f32_e32 v21, v21, v22
	v_med3_f32 v22, v27, s1, v210
	v_rcp_f32_e32 v26, v26
	v_mul_f32_e32 v27, 0xc01d265f, v24
	v_exp_f32_e32 v27, v27
	v_fma_f32 v22, v22, 4.0, 4.0
	v_mul_f32_e32 v23, v23, v26
	v_mul_f32_e32 v22, v22, v23
	v_med3_f32 v23, v25, s1, v210
	v_add_f32_e32 v25, 1.0, v27
	v_rcp_f32_e32 v25, v25
	v_cvt_pk_fp8_f32 v26, v20, v21
	v_fma_f32 v20, v23, 4.0, 4.0
	v_mul_f32_e32 v21, v24, v25
	v_mul_f32_e32 v20, v20, v21
	v_cvt_pk_fp8_f32 v26, v22, v20 op_sel:[0,0,1]
	s_mov_b32 s0, 0x28000
	v_add_co_u32_e32 v20, vcc, s0, v16
	v_pk_add_f32 v[8:9], v[44:45], v[8:9]
	s_mov_b64 s[2:3], 0x28000
	v_addc_co_u32_e32 v21, vcc, 0, v17, vcc
	v_min_f32_e32 v8, 0x40e00000, v8
	v_lshl_add_u64 v[18:19], v[16:17], 0, s[2:3]
	global_store_dword v[20:21], v28, off
	global_store_dword v[18:19], v26, off offset:64
	v_mul_f32_e32 v20, 0xc01d265f, v8
	v_exp_f32_e32 v20, v20
	v_pk_add_f32 v[10:11], v[46:47], v[10:11]
	v_med3_f32 v9, v9, s1, v210
	v_min_f32_e32 v10, 0x40e00000, v10
	v_add_f32_e32 v20, 1.0, v20
	v_rcp_f32_e32 v20, v20
	v_mul_f32_e32 v21, 0xc01d265f, v10
	v_exp_f32_e32 v21, v21
	v_pk_add_f32 v[4:5], v[40:41], v[4:5]
	v_fma_f32 v9, v9, 4.0, 4.0
	v_mul_f32_e32 v8, v8, v20
	v_mul_f32_e32 v8, v9, v8
	v_med3_f32 v9, v11, s1, v210
	v_add_f32_e32 v11, 1.0, v21
	v_min_f32_e32 v4, 0x40e00000, v4
	v_rcp_f32_e32 v11, v11
	v_mul_f32_e32 v20, 0xc01d265f, v4
	v_exp_f32_e32 v20, v20
	v_pk_add_f32 v[6:7], v[42:43], v[6:7]
	v_fma_f32 v9, v9, 4.0, 4.0
	v_mul_f32_e32 v10, v10, v11
	v_min_f32_e32 v6, 0x40e00000, v6
	v_mul_f32_e32 v9, v9, v10
	v_add_f32_e32 v10, 1.0, v20
	v_mul_f32_e32 v11, 0xc01d265f, v6
	v_rcp_f32_e32 v10, v10
	v_exp_f32_e32 v11, v11
	v_med3_f32 v5, v5, s1, v210
	v_fma_f32 v5, v5, 4.0, 4.0
	v_mul_f32_e32 v4, v4, v10
	v_add_f32_e32 v10, 1.0, v11
	v_rcp_f32_e32 v10, v10
	v_mul_f32_e32 v11, v5, v4
	v_med3_f32 v4, v7, s1, v210
	v_fma_f32 v7, v4, 4.0, 4.0
	v_pk_add_f32 v[4:5], v[36:37], v[12:13]
	v_mul_f32_e32 v6, v6, v10
	v_min_f32_e32 v4, 0x40e00000, v4
	v_cvt_pk_fp8_f32 v10, v8, v9
	v_mul_f32_e32 v8, 0xc01d265f, v4
	v_exp_f32_e32 v8, v8
	v_pk_add_f32 v[2:3], v[34:35], v[2:3]
	v_pk_add_f32 v[0:1], v[32:33], v[0:1]
	v_min_f32_e32 v2, 0x40e00000, v2
	v_add_f32_e32 v8, 1.0, v8
	v_mul_f32_e32 v9, 0xc01d265f, v2
	v_rcp_f32_e32 v8, v8
	v_exp_f32_e32 v9, v9
	v_min_f32_e32 v0, 0x40e00000, v0
	v_med3_f32 v5, v5, s1, v210
	v_mul_f32_e32 v4, v4, v8
	v_add_f32_e32 v8, 1.0, v9
	v_mul_f32_e32 v9, 0xc01d265f, v0
	v_exp_f32_e32 v9, v9
	v_rcp_f32_e32 v8, v8
	v_fma_f32 v5, v5, 4.0, 4.0
	v_mul_f32_e32 v4, v5, v4
	v_add_f32_e32 v5, 1.0, v9
	v_rcp_f32_e32 v5, v5
	v_mul_f32_e32 v6, v7, v6
	v_med3_f32 v3, v3, s1, v210
	v_cvt_pk_fp8_f32 v10, v11, v6 op_sel:[0,0,1]
	v_pk_add_f32 v[6:7], v[38:39], v[14:15]
	v_mul_f32_e32 v2, v2, v8
	v_fma_f32 v3, v3, 4.0, 4.0
	v_mul_f32_e32 v2, v3, v2
	v_min_f32_e32 v3, 0x40e00000, v6
	v_mul_f32_e32 v0, v0, v5
	v_mul_f32_e32 v5, 0xc01d265f, v3
	v_exp_f32_e32 v5, v5
	v_med3_f32 v1, v1, s1, v210
	v_fma_f32 v1, v1, 4.0, 4.0
	v_mul_f32_e32 v0, v1, v0
	v_add_f32_e32 v5, 1.0, v5
	v_rcp_f32_e32 v5, v5
	v_cvt_pk_fp8_f32 v6, v0, v2
	v_med3_f32 v1, v7, s1, v210
	v_fma_f32 v0, v1, 4.0, 4.0
	v_mul_f32_e32 v1, v3, v5
	v_mul_f32_e32 v0, v0, v1
	s_mov_b32 s0, 0x2c000
	v_cvt_pk_fp8_f32 v6, v4, v0 op_sel:[0,0,1]
	v_add_co_u32_e32 v0, vcc, s0, v16
	s_mov_b64 s[2:3], 0x2c000
	s_nop 0
	v_addc_co_u32_e32 v1, vcc, 0, v17, vcc
	s_and_b64 vcc, exec, s[40:41]
	s_mov_b64 s[0:1], -1
	v_readlane_b32 s22, v254, 47
	s_mov_b32 s20, s84
	v_lshl_add_u64 v[18:19], v[16:17], 0, s[2:3]
	global_store_dword v[0:1], v10, off
	global_store_dword v[18:19], v6, off offset:64
	v_readlane_b32 s23, v254, 48
	s_cbranch_vccnz .LBB0_1465
; #define LAS __attribute__((address_space(3)))
; __device__ __forceinline__ int lane_id() { int l; asm volatile("v_mbcnt_lo_u32_b32 %0, -1, 0\n\tv_mbcnt_hi_u32_b32 %0, -1, %0" : "=v"(l)); return l; }
; template <class Epi, class Sched, bool GATHER, bool FP8 = false>
; __device__ __forceinline__ void gemm_phase(LAS unsigned char* lds, const Gemm g, const Sched& S, const Epi& E, const int wave_s) {
;     ...
;         cur = nxt; cB = nB; cA = nA; ++ui;
;         if constexpr (Epi::BIAS_LDS) { if (wid == 0) __builtin_amdgcn_global_load_lds((const unsigned*)(E.bias_src(cur) + lane_id() * 4), (LAS unsigned*)(lds + Epi::BIAS_OFF + (ui & 1) * 1024), 16, 0, 0); }
	s_andn2_b64 vcc, exec, s[10:11]
	s_cbranch_vccnz .LBB0_1477
	s_lshl_b32 s0, s16, 8
	s_and_b32 s0, s0, 0xfffff800
	s_ashr_i32 s1, s0, 31
	s_lshl_b64 s[0:1], s[0:1], 2
	s_add_u32 s0, s51, s0
	s_addc_u32 s1, s52, s1
	s_lshl_b32 s2, s16, 10
	s_and_b32 s2, s2, 0x1c00
	v_mbcnt_lo_u32_b32 v0, -1, 0
	v_mbcnt_hi_u32_b32 v0, -1, v0
	s_add_u32 s0, s0, s2
	v_lshlrev_b32_e32 v0, 2, v0
	s_addc_u32 s1, s1, 0
	v_ashrrev_i32_e32 v1, 31, v0
	v_lshl_add_u64 v[0:1], v[0:1], 2, s[0:1]
	s_lshl_b32 s0, s62, 10
	s_and_b32 s0, s0, 0x400
	s_add_i32 s0, s0, 0
	s_add_i32 m0, s0, 0x23000
	s_nop 0
	global_load_lds_dwordx4 v[0:1], off

; #define LAS __attribute__((address_space(3)))
; __device__ __forceinline__ unsigned pk4_fp8(float x0, float x1, float x2, float x3) { int w = 0; w = __builtin_amdgcn_cvt_pk_fp8_f32(x0, x1, w, false); w = __builtin_amdgcn_cvt_pk_fp8_f32(x2, x3, w, true); return (unsigned)w; }
;     __device__ __forceinline__ void operator()(const f32x4 (&acc)[2][2][4][2], const Unit& u, int wr, int wc, int fr, int fq, const LAS float* bl) const {
;         const int pnl = u.pn & 3;
;         const int row0 = u.pm * BM + wr * 64 + fr, cl = wc * 32 + 8 * fq, col0 = pnl * BM + cl;
; #pragma unroll
;         for (int ai = 0; ai < 2; ++ai)
; #pragma unroll
;             for (int m = 0; m < 4; ++m) { unsigned char* rowp = O + (size_t)(row0 + ai * HALF + m * 16) * 1024 + col0;
; #pragma unroll
;                 for (int bj = 0; bj < 2; ++bj) { const f32x4 v0 = (acc[ai][bj][m][0] + *(const LAS f32x4*)(bl + cl + bj * HALF)) * DO_Q, v1 = (acc[ai][bj][m][1] + *(const LAS f32x4*)(bl + cl + bj * HALF + 4)) * DO_Q;
;                     u32x2 w; w.x = pk4_fp8(v0[0], v0[1], v0[2], v0[3]); w.y = pk4_fp8(v1[0], v1[1], v1[2], v1[3]);
;                     *(u32x2*)(rowp + bj * HALF) = w; } }
;     }
.LBB0_1574:
	s_nop 15
	s_nop 15
	s_lshl_b32 s0, s71, 10
	s_and_b32 s0, s0, 0x400
	v_add_u32_e32 v24, s0, v214
	ds_read_b128 v[4:7], v24
	ds_read_b128 v[8:11], v24 offset:16
	s_lshl_b32 s1, s48, 8
	v_lshl_add_u32 v18, s46, 8, v211
	s_and_b32 s1, s1, 0x300
	s_waitcnt lgkmcnt(0)
	v_pk_add_f32 v[2:3], v[158:159], v[4:5]
	s_mov_b32 s2, 0x42800000
	v_or_b32_e32 v152, s1, v213
	v_ashrrev_i32_e32 v19, 31, v18
	v_readlane_b32 s0, v246, 47
	v_pk_mul_f32 v[2:3], v[2:3], s[2:3] op_sel_hi:[1,0]
	v_lshlrev_b64 v[0:1], 10, v[18:19]
	v_readlane_b32 s1, v246, 48
	v_pk_add_f32 v[14:15], v[154:155], v[8:9]
	v_cvt_pk_fp8_f32 v20, v2, v3
	v_lshl_add_u64 v[0:1], s[0:1], 0, v[0:1]
	v_pk_mul_f32 v[14:15], v[14:15], s[2:3] op_sel_hi:[1,0]
	v_lshl_add_u64 v[16:17], v[0:1], 0, v[152:153]
	v_pk_add_f32 v[0:1], v[160:161], v[6:7]
	v_cvt_pk_fp8_f32 v21, v14, v15
	v_pk_mul_f32 v[0:1], v[0:1], s[2:3] op_sel_hi:[1,0]
	v_pk_add_f32 v[12:13], v[156:157], v[10:11]
	v_cvt_pk_fp8_f32 v20, v0, v1 op_sel:[0,0,1]
	ds_read_b128 v[0:3], v24 offset:512
	v_pk_mul_f32 v[12:13], v[12:13], s[2:3] op_sel_hi:[1,0]
	v_cvt_pk_fp8_f32 v21, v12, v13 op_sel:[0,0,1]
	s_waitcnt lgkmcnt(0)
	v_pk_add_f32 v[12:13], v[150:151], v[2:3]
	v_pk_add_f32 v[14:15], v[148:149], v[0:1]
	global_store_dwordx2 v[16:17], v[20:21], off
	v_pk_mul_f32 v[20:21], v[12:13], s[2:3] op_sel_hi:[1,0]
	v_pk_mul_f32 v[22:23], v[14:15], s[2:3] op_sel_hi:[1,0]
	ds_read_b128 v[12:15], v24 offset:528
	v_cvt_pk_fp8_f32 v28, v22, v23
	v_pk_add_f32 v[22:23], v[142:143], v[6:7]
	s_waitcnt lgkmcnt(0)
	v_pk_add_f32 v[26:27], v[144:145], v[12:13]
	v_pk_add_f32 v[24:25], v[146:147], v[14:15]
	v_pk_mul_f32 v[26:27], v[26:27], s[2:3] op_sel_hi:[1,0]
	v_pk_mul_f32 v[24:25], v[24:25], s[2:3] op_sel_hi:[1,0]
	v_cvt_pk_fp8_f32 v29, v26, v27
	v_cvt_pk_fp8_f32 v28, v20, v21 op_sel:[0,0,1]
	v_pk_add_f32 v[26:27], v[138:139], v[10:11]
	v_or_b32_e32 v20, 16, v18
	v_cvt_pk_fp8_f32 v29, v24, v25 op_sel:[0,0,1]
	v_pk_add_f32 v[24:25], v[140:141], v[4:5]
	v_pk_mul_f32 v[22:23], v[22:23], s[2:3] op_sel_hi:[1,0]
	v_pk_mul_f32 v[24:25], v[24:25], s[2:3] op_sel_hi:[1,0]
	global_store_dwordx2 v[16:17], v[28:29], off offset:128
	v_pk_add_f32 v[28:29], v[136:137], v[8:9]
	v_cvt_pk_fp8_f32 v30, v24, v25
	v_pk_mul_f32 v[28:29], v[28:29], s[2:3] op_sel_hi:[1,0]
	v_pk_mul_f32 v[26:27], v[26:27], s[2:3] op_sel_hi:[1,0]
	v_cvt_pk_fp8_f32 v31, v28, v29
	v_ashrrev_i32_e32 v21, 31, v20
	v_cvt_pk_fp8_f32 v30, v22, v23 op_sel:[0,0,1]
	v_lshlrev_b64 v[20:21], 10, v[20:21]
	v_cvt_pk_fp8_f32 v31, v26, v27 op_sel:[0,0,1]
	v_lshl_add_u64 v[20:21], s[0:1], 0, v[20:21]
	v_lshl_add_u64 v[20:21], v[20:21], 0, v[152:153]
	v_pk_add_f32 v[24:25], v[132:133], v[0:1]
	v_pk_add_f32 v[28:29], v[128:129], v[12:13]
	global_store_dwordx2 v[20:21], v[30:31], off
	v_pk_mul_f32 v[24:25], v[24:25], s[2:3] op_sel_hi:[1,0]
	v_pk_mul_f32 v[28:29], v[28:29], s[2:3] op_sel_hi:[1,0]
	v_cvt_pk_fp8_f32 v30, v24, v25
	v_cvt_pk_fp8_f32 v31, v28, v29
	v_pk_add_f32 v[22:23], v[134:135], v[2:3]
	v_pk_add_f32 v[26:27], v[130:131], v[14:15]
	v_pk_mul_f32 v[22:23], v[22:23], s[2:3] op_sel_hi:[1,0]
	v_pk_mul_f32 v[26:27], v[26:27], s[2:3] op_sel_hi:[1,0]
	v_cvt_pk_fp8_f32 v30, v22, v23 op_sel:[0,0,1]
	v_cvt_pk_fp8_f32 v31, v26, v27 op_sel:[0,0,1]
	v_pk_add_f32 v[24:25], v[124:125], v[4:5]
	v_pk_add_f32 v[28:29], v[120:121], v[8:9]
	v_pk_mul_f32 v[24:25], v[24:25], s[2:3] op_sel_hi:[1,0]
	global_store_dwordx2 v[20:21], v[30:31], off offset:128
	v_pk_mul_f32 v[28:29], v[28:29], s[2:3] op_sel_hi:[1,0]
	v_cvt_pk_fp8_f32 v30, v24, v25
	v_cvt_pk_fp8_f32 v31, v28, v29
	v_pk_add_f32 v[22:23], v[126:127], v[6:7]
	v_pk_add_f32 v[26:27], v[122:123], v[10:11]
	v_or_b32_e32 v20, 32, v18
	v_pk_mul_f32 v[22:23], v[22:23], s[2:3] op_sel_hi:[1,0]
	v_pk_mul_f32 v[26:27], v[26:27], s[2:3] op_sel_hi:[1,0]
	v_ashrrev_i32_e32 v21, 31, v20
	v_cvt_pk_fp8_f32 v30, v22, v23 op_sel:[0,0,1]
	v_cvt_pk_fp8_f32 v31, v26, v27 op_sel:[0,0,1]
	v_lshlrev_b64 v[20:21], 10, v[20:21]
	v_lshl_add_u64 v[20:21], s[0:1], 0, v[20:21]
	v_lshl_add_u64 v[20:21], v[20:21], 0, v[152:153]
	v_pk_add_f32 v[24:25], v[116:117], v[0:1]
	v_pk_add_f32 v[28:29], v[112:113], v[12:13]
	global_store_dwordx2 v[20:21], v[30:31], off
	v_pk_mul_f32 v[24:25], v[24:25], s[2:3] op_sel_hi:[1,0]
	v_pk_mul_f32 v[28:29], v[28:29], s[2:3] op_sel_hi:[1,0]
	v_cvt_pk_fp8_f32 v30, v24, v25
	v_cvt_pk_fp8_f32 v31, v28, v29
	v_pk_add_f32 v[22:23], v[118:119], v[2:3]
	v_pk_add_f32 v[26:27], v[114:115], v[14:15]
	v_pk_mul_f32 v[22:23], v[22:23], s[2:3] op_sel_hi:[1,0]
	v_pk_mul_f32 v[26:27], v[26:27], s[2:3] op_sel_hi:[1,0]
	v_cvt_pk_fp8_f32 v30, v22, v23 op_sel:[0,0,1]
	v_cvt_pk_fp8_f32 v31, v26, v27 op_sel:[0,0,1]
	v_pk_add_f32 v[22:23], v[108:109], v[4:5]
	v_pk_add_f32 v[26:27], v[104:105], v[8:9]
	v_pk_mul_f32 v[22:23], v[22:23], s[2:3] op_sel_hi:[1,0]
	v_pk_mul_f32 v[26:27], v[26:27], s[2:3] op_sel_hi:[1,0]
	v_cvt_pk_fp8_f32 v28, v22, v23
	v_cvt_pk_fp8_f32 v29, v26, v27
	global_store_dwordx2 v[20:21], v[30:31], off offset:128
	v_pk_add_f32 v[20:21], v[110:111], v[6:7]
	v_pk_add_f32 v[24:25], v[106:107], v[10:11]
	v_or_b32_e32 v18, 48, v18
	v_pk_mul_f32 v[20:21], v[20:21], s[2:3] op_sel_hi:[1,0]
	v_pk_mul_f32 v[24:25], v[24:25], s[2:3] op_sel_hi:[1,0]
	v_ashrrev_i32_e32 v19, 31, v18
	v_cvt_pk_fp8_f32 v28, v20, v21 op_sel:[0,0,1]
	v_cvt_pk_fp8_f32 v29, v24, v25 op_sel:[0,0,1]
	v_lshlrev_b64 v[18:19], 10, v[18:19]
	v_lshl_add_u64 v[18:19], s[0:1], 0, v[18:19]
	v_lshl_add_u64 v[18:19], v[18:19], 0, v[152:153]
	v_pk_add_f32 v[22:23], v[100:101], v[0:1]
	v_pk_add_f32 v[26:27], v[96:97], v[12:13]
	global_store_dwordx2 v[18:19], v[28:29], off
	v_pk_mul_f32 v[22:23], v[22:23], s[2:3] op_sel_hi:[1,0]
; #define LAS __attribute__((address_space(3)))
; __device__ __forceinline__ unsigned pk4_fp8(float x0, float x1, float x2, float x3) { int w = 0; w = __builtin_amdgcn_cvt_pk_fp8_f32(x0, x1, w, false); w = __builtin_amdgcn_cvt_pk_fp8_f32(x2, x3, w, true); return (unsigned)w; }
; __device__ __forceinline__ int lane_id() { int l; asm volatile("v_mbcnt_lo_u32_b32 %0, -1, 0\n\tv_mbcnt_hi_u32_b32 %0, -1, %0" : "=v"(l)); return l; }
; template <class Epi, class Sched, bool GATHER, bool FP8 = false>
; __device__ __forceinline__ void gemm_phase(LAS unsigned char* lds, const Gemm g, const Sched& S, const Epi& E, const int wave_s) {
;     ...
;         if constexpr (Epi::BIAS_LDS) { if (wid == 0) __builtin_amdgcn_global_load_lds((const unsigned*)(E.bias_src(cur) + lane_id() * 4), (LAS unsigned*)(lds + Epi::BIAS_OFF + (ui & 1) * 1024), 16, 0, 0); }
;     __device__ __forceinline__ void operator()(const f32x4 (&acc)[2][2][4][2], const Unit& u, int wr, int wc, int fr, int fq, const LAS float* bl) const {
;         const int pnl = u.pn & 3;
;         const int row0 = u.pm * BM + wr * 64 + fr, cl = wc * 32 + 8 * fq, col0 = pnl * BM + cl;
; #pragma unroll
;         for (int ai = 0; ai < 2; ++ai)
; #pragma unroll
;             for (int m = 0; m < 4; ++m) { unsigned char* rowp = O + (size_t)(row0 + ai * HALF + m * 16) * 1024 + col0;
; #pragma unroll
;                 for (int bj = 0; bj < 2; ++bj) { const f32x4 v0 = (acc[ai][bj][m][0] + *(const LAS f32x4*)(bl + cl + bj * HALF)) * DO_Q, v1 = (acc[ai][bj][m][1] + *(const LAS f32x4*)(bl + cl + bj * HALF + 4)) * DO_Q;
;                     u32x2 w; w.x = pk4_fp8(v0[0], v0[1], v0[2], v0[3]); w.y = pk4_fp8(v1[0], v1[1], v1[2], v1[3]);
;                     *(u32x2*)(rowp + bj * HALF) = w; } }
;     }
	v_pk_mul_f32 v[26:27], v[26:27], s[2:3] op_sel_hi:[1,0]
	v_cvt_pk_fp8_f32 v28, v22, v23
	v_cvt_pk_fp8_f32 v29, v26, v27
	v_pk_add_f32 v[20:21], v[102:103], v[2:3]
	v_pk_add_f32 v[24:25], v[98:99], v[14:15]
	v_pk_mul_f32 v[20:21], v[20:21], s[2:3] op_sel_hi:[1,0]
	v_pk_mul_f32 v[24:25], v[24:25], s[2:3] op_sel_hi:[1,0]
	v_cvt_pk_fp8_f32 v28, v20, v21 op_sel:[0,0,1]
	v_cvt_pk_fp8_f32 v29, v24, v25 op_sel:[0,0,1]
	v_pk_add_f32 v[22:23], v[92:93], v[4:5]
	v_pk_add_f32 v[26:27], v[88:89], v[8:9]
	v_pk_mul_f32 v[22:23], v[22:23], s[2:3] op_sel_hi:[1,0]
	global_store_dwordx2 v[18:19], v[28:29], off offset:128
	v_pk_mul_f32 v[26:27], v[26:27], s[2:3] op_sel_hi:[1,0]
	v_cvt_pk_fp8_f32 v28, v22, v23
	v_cvt_pk_fp8_f32 v29, v26, v27
	v_pk_add_f32 v[20:21], v[94:95], v[6:7]
	v_pk_add_f32 v[24:25], v[90:91], v[10:11]
	v_pk_mul_f32 v[20:21], v[20:21], s[2:3] op_sel_hi:[1,0]
	v_pk_mul_f32 v[24:25], v[24:25], s[2:3] op_sel_hi:[1,0]
	s_mov_b64 s[0:1], 0x20000
	v_cvt_pk_fp8_f32 v28, v20, v21 op_sel:[0,0,1]
	v_cvt_pk_fp8_f32 v29, v24, v25 op_sel:[0,0,1]
	v_lshl_add_u64 v[18:19], v[16:17], 0, s[0:1]
	s_mov_b32 s0, 0x20000
	v_add_co_u32_e32 v20, vcc, s0, v16
	v_pk_add_f32 v[22:23], v[84:85], v[0:1]
	s_nop 0
	v_addc_co_u32_e32 v21, vcc, 0, v17, vcc
	v_pk_add_f32 v[26:27], v[80:81], v[12:13]
	global_store_dwordx2 v[20:21], v[28:29], off
	v_pk_mul_f32 v[22:23], v[22:23], s[2:3] op_sel_hi:[1,0]
	v_pk_mul_f32 v[26:27], v[26:27], s[2:3] op_sel_hi:[1,0]
	v_cvt_pk_fp8_f32 v28, v22, v23
	v_cvt_pk_fp8_f32 v29, v26, v27
	v_pk_add_f32 v[20:21], v[86:87], v[2:3]
	v_pk_add_f32 v[24:25], v[82:83], v[14:15]
	v_pk_mul_f32 v[20:21], v[20:21], s[2:3] op_sel_hi:[1,0]
	v_pk_mul_f32 v[24:25], v[24:25], s[2:3] op_sel_hi:[1,0]
	v_cvt_pk_fp8_f32 v28, v20, v21 op_sel:[0,0,1]
	v_cvt_pk_fp8_f32 v29, v24, v25 op_sel:[0,0,1]
	v_pk_add_f32 v[22:23], v[76:77], v[4:5]
	v_pk_add_f32 v[26:27], v[72:73], v[8:9]
	v_pk_mul_f32 v[22:23], v[22:23], s[2:3] op_sel_hi:[1,0]
	global_store_dwordx2 v[18:19], v[28:29], off offset:128
	v_pk_mul_f32 v[26:27], v[26:27], s[2:3] op_sel_hi:[1,0]
	v_cvt_pk_fp8_f32 v28, v22, v23
	v_cvt_pk_fp8_f32 v29, v26, v27
	v_pk_add_f32 v[20:21], v[78:79], v[6:7]
	v_pk_add_f32 v[24:25], v[74:75], v[10:11]
	v_pk_mul_f32 v[20:21], v[20:21], s[2:3] op_sel_hi:[1,0]
	v_pk_mul_f32 v[24:25], v[24:25], s[2:3] op_sel_hi:[1,0]
	s_mov_b64 s[0:1], 0x24000
	v_cvt_pk_fp8_f32 v28, v20, v21 op_sel:[0,0,1]
	v_cvt_pk_fp8_f32 v29, v24, v25 op_sel:[0,0,1]
	v_lshl_add_u64 v[18:19], v[16:17], 0, s[0:1]
	s_mov_b32 s0, 0x24000
	v_add_co_u32_e32 v20, vcc, s0, v16
	v_pk_add_f32 v[22:23], v[68:69], v[0:1]
	s_nop 0
	v_addc_co_u32_e32 v21, vcc, 0, v17, vcc
	v_pk_add_f32 v[26:27], v[60:61], v[12:13]
	global_store_dwordx2 v[20:21], v[28:29], off
	v_pk_mul_f32 v[22:23], v[22:23], s[2:3] op_sel_hi:[1,0]
	v_pk_mul_f32 v[26:27], v[26:27], s[2:3] op_sel_hi:[1,0]
	v_cvt_pk_fp8_f32 v28, v22, v23
	v_cvt_pk_fp8_f32 v29, v26, v27
	v_pk_add_f32 v[20:21], v[70:71], v[2:3]
	v_pk_add_f32 v[24:25], v[62:63], v[14:15]
	v_pk_mul_f32 v[20:21], v[20:21], s[2:3] op_sel_hi:[1,0]
	v_pk_mul_f32 v[24:25], v[24:25], s[2:3] op_sel_hi:[1,0]
	v_cvt_pk_fp8_f32 v28, v20, v21 op_sel:[0,0,1]
	v_cvt_pk_fp8_f32 v29, v24, v25 op_sel:[0,0,1]
	v_pk_add_f32 v[22:23], v[52:53], v[4:5]
	v_pk_add_f32 v[26:27], v[48:49], v[8:9]
	v_pk_mul_f32 v[22:23], v[22:23], s[2:3] op_sel_hi:[1,0]
	global_store_dwordx2 v[18:19], v[28:29], off offset:128
	v_pk_mul_f32 v[26:27], v[26:27], s[2:3] op_sel_hi:[1,0]
	v_cvt_pk_fp8_f32 v28, v22, v23
	v_cvt_pk_fp8_f32 v29, v26, v27
	v_pk_add_f32 v[20:21], v[54:55], v[6:7]
	v_pk_add_f32 v[24:25], v[50:51], v[10:11]
	v_pk_mul_f32 v[20:21], v[20:21], s[2:3] op_sel_hi:[1,0]
	v_pk_mul_f32 v[24:25], v[24:25], s[2:3] op_sel_hi:[1,0]
	s_mov_b64 s[0:1], 0x28000
	v_cvt_pk_fp8_f32 v28, v20, v21 op_sel:[0,0,1]
	v_cvt_pk_fp8_f32 v29, v24, v25 op_sel:[0,0,1]
	v_lshl_add_u64 v[18:19], v[16:17], 0, s[0:1]
	s_mov_b32 s0, 0x28000
	v_add_co_u32_e32 v20, vcc, s0, v16
	v_pk_add_f32 v[22:23], v[64:65], v[0:1]
	s_nop 0
	v_addc_co_u32_e32 v21, vcc, 0, v17, vcc
	global_store_dwordx2 v[20:21], v[28:29], off
	v_pk_mul_f32 v[22:23], v[22:23], s[2:3] op_sel_hi:[1,0]
	v_pk_add_f32 v[26:27], v[56:57], v[12:13]
	v_cvt_pk_fp8_f32 v28, v22, v23
	v_pk_mul_f32 v[26:27], v[26:27], s[2:3] op_sel_hi:[1,0]
	v_pk_add_f32 v[20:21], v[66:67], v[2:3]
	v_cvt_pk_fp8_f32 v29, v26, v27
	v_pk_mul_f32 v[20:21], v[20:21], s[2:3] op_sel_hi:[1,0]
	v_pk_add_f32 v[4:5], v[36:37], v[4:5]
	v_pk_add_f32 v[8:9], v[32:33], v[8:9]
	v_pk_add_f32 v[24:25], v[58:59], v[14:15]
	v_cvt_pk_fp8_f32 v28, v20, v21 op_sel:[0,0,1]
	v_pk_mul_f32 v[4:5], v[4:5], s[2:3] op_sel_hi:[1,0]
	v_pk_mul_f32 v[8:9], v[8:9], s[2:3] op_sel_hi:[1,0]
	v_pk_mul_f32 v[24:25], v[24:25], s[2:3] op_sel_hi:[1,0]
	v_cvt_pk_fp8_f32 v20, v4, v5
	v_cvt_pk_fp8_f32 v21, v8, v9
	v_cvt_pk_fp8_f32 v29, v24, v25 op_sel:[0,0,1]
	v_pk_add_f32 v[6:7], v[38:39], v[6:7]
	v_pk_add_f32 v[10:11], v[34:35], v[10:11]
	v_pk_mul_f32 v[6:7], v[6:7], s[2:3] op_sel_hi:[1,0]
	v_pk_mul_f32 v[10:11], v[10:11], s[2:3] op_sel_hi:[1,0]
	s_mov_b64 s[0:1], 0x2c000
	v_cvt_pk_fp8_f32 v20, v6, v7 op_sel:[0,0,1]
	v_cvt_pk_fp8_f32 v21, v10, v11 op_sel:[0,0,1]
	v_pk_add_f32 v[0:1], v[44:45], v[0:1]
	v_pk_add_f32 v[6:7], v[40:41], v[12:13]
	global_store_dwordx2 v[18:19], v[28:29], off offset:128
	v_lshl_add_u64 v[18:19], v[16:17], 0, s[0:1]
	s_mov_b32 s0, 0x2c000
	v_pk_mul_f32 v[0:1], v[0:1], s[2:3] op_sel_hi:[1,0]
	v_pk_mul_f32 v[6:7], v[6:7], s[2:3] op_sel_hi:[1,0]
	v_add_co_u32_e32 v4, vcc, s0, v16
	v_cvt_pk_fp8_f32 v8, v0, v1
	v_cvt_pk_fp8_f32 v9, v6, v7
	v_addc_co_u32_e32 v5, vcc, 0, v17, vcc
	global_store_dwordx2 v[4:5], v[20:21], off
	v_pk_add_f32 v[2:3], v[46:47], v[2:3]
	v_pk_add_f32 v[4:5], v[42:43], v[14:15]
	v_pk_mul_f32 v[2:3], v[2:3], s[2:3] op_sel_hi:[1,0]
	v_pk_mul_f32 v[4:5], v[4:5], s[2:3] op_sel_hi:[1,0]
	v_cvt_pk_fp8_f32 v8, v2, v3 op_sel:[0,0,1]
	v_cvt_pk_fp8_f32 v9, v4, v5 op_sel:[0,0,1]
	v_readlane_b32 s76, v254, 29
	v_readlane_b32 s77, v254, 30
	s_mov_b64 s[0:1], -1
	s_andn2_b64 vcc, exec, s[40:41]
	v_readlane_b32 s74, v254, 28
	v_readlane_b32 s77, v254, 31
	global_store_dwordx2 v[18:19], v[8:9], off offset:128
	s_cbranch_vccnz .LBB0_1563
	s_andn2_b64 vcc, exec, s[10:11]
	s_cbranch_vccnz .LBB0_1577
	s_lshl_b32 s0, s18, 8
	s_and_b32 s0, s0, 0xfffffc00
	s_ashr_i32 s1, s0, 31
	s_lshl_b64 s[0:1], s[0:1], 2
	s_add_u32 s0, s61, s0
	s_addc_u32 s1, s62, s1
	s_lshl_b32 s2, s18, 10
	s_and_b32 s2, s2, 0xc00
	v_mbcnt_lo_u32_b32 v0, -1, 0
	v_mbcnt_hi_u32_b32 v0, -1, v0
	s_add_u32 s0, s0, s2
	v_lshlrev_b32_e32 v0, 2, v0
	s_addc_u32 s1, s1, 0
	v_ashrrev_i32_e32 v1, 31, v0
	v_lshl_add_u64 v[0:1], v[0:1], 2, s[0:1]
	s_lshl_b32 s0, s70, 10
	s_and_b32 s0, s0, 0x400
	s_add_i32 s0, s0, 0
	s_add_i32 m0, s0, 0x23000
	s_nop 0
	global_load_lds_dwordx4 v[0:1], off

; __device__ __forceinline__ unsigned pk2(float lo, float hi) { unsigned r; asm("v_cvt_pk_bf16_f32 %0, %1, %2" : "=v"(r) : "v"(lo), "v"(hi)); return r; }
; __device__ __forceinline__ unsigned pk4_fp8(float x0, float x1, float x2, float x3) { int w = 0; w = __builtin_amdgcn_cvt_pk_fp8_f32(x0, x1, w, false); w = __builtin_amdgcn_cvt_pk_fp8_f32(x2, x3, w, true); return (unsigned)w; }
; __global__ void __launch_bounds__(512, 2) mega(Args a) {
;     ...
;                 float rstd[2];
;                 { const float mean0 = wave_sum(sm[0]) * (1.f / DM), mean1 = wave_sum(sm[1]) * (1.f / DM); float q0 = 0.f, q1 = 0.f;
; #pragma unroll
;                   for (int j = 0; j < 4; ++j) { v[0][j] = v[0][j] - mean0; q0 += (v[0][j].x * v[0][j].x + v[0][j].y * v[0][j].y) + (v[0][j].z * v[0][j].z + v[0][j].w * v[0][j].w);
;                       v[1][j] = v[1][j] - mean1; q1 += (v[1][j].x * v[1][j].x + v[1][j].y * v[1][j].y) + (v[1][j].z * v[1][j].z + v[1][j].w * v[1][j].w); }
;                   rstd[0] = rsqrtf(wave_sum(q0) * (1.f / DM) + LN_EPS); rstd[1] = rsqrtf(wave_sum(q1) * (1.f / DM) + LN_EPS); }
;                 __builtin_amdgcn_sched_barrier(0);
; #pragma unroll
;                 for (int j = 0; j < 4; ++j) { __builtin_amdgcn_sched_barrier(0);
;                     f32x4 psh = (f32x4){0.f, 0.f, 0.f, 0.f}, psc = psh;
;                     if (!lastl) { psh = *((const f32x4*)(mdn) + lane + 64 * j); psc = *((const f32x4*)(mdn + 1024) + lane + 64 * j); }
; #pragma unroll
;                     for (int t = 0; t < 2; ++t) { const int nn = n + t;
;                         v[t][j] = v[t][j] * rstd[t] * pg[j] + pb_[j];
;                         if (lastl) *((f32x4*)(a.out + (size_t)(nn - NCTX) * DM) + lane + 64 * j) = v[t][j];
;                         else { u32x2 xw_; xw_.x = pk2(v[t][j].x, v[t][j].y); xw_.y = pk2(v[t][j].z, v[t][j].w); *((u32x2*)(XRB + (size_t)nn * DM) + lane + 64 * j) = xw_;
;                             const f32x4 hh = (v[t][j] * (psc + 1.f) + psh) * ACT_Q; *((unsigned*)(XHF + (size_t)nn * DM) + lane + 64 * j) = pk4_fp8(hh.x, hh.y, hh.z, hh.w); } } }
.LBB0_1648:
	v_pk_add_f32 v[54:55], v[54:55], v[114:115]
	s_mov_b32 s0, 0x3a800000
	v_pk_fma_f32 v[138:139], v[54:55], s[0:1], v[162:163] op_sel_hi:[1,0,0]
	v_readlane_b32 s2, v254, 58
	v_mul_f32_e32 v54, 0x4b800000, v139
	v_cmp_gt_f32_e32 vcc, s94, v139
	v_readlane_b32 s3, v254, 59
	v_cmp_gt_f32_e64 s[42:43], s94, v138
	v_cndmask_b32_e32 v54, v139, v54, vcc
	v_rsq_f32_e32 v54, v54
	s_mov_b64 s[0:1], -1
	v_lshl_add_u64 v[114:115], s[78:79], 0, v[74:75]
	v_mul_f32_e32 v55, 0x45800000, v54
	v_cndmask_b32_e32 v120, v54, v55, vcc
	v_pk_mul_f32 v[104:105], v[104:105], v[120:121] op_sel_hi:[1,0]
	v_pk_mul_f32 v[52:53], v[52:53], v[120:121] op_sel_hi:[1,0]
	s_and_b64 vcc, exec, s[2:3]
	s_waitcnt vmcnt(0)
	v_pk_fma_f32 v[54:55], v[46:47], v[52:53], v[50:51]
	v_pk_fma_f32 v[52:53], v[44:45], v[104:105], v[48:49]
	v_lshl_add_u64 v[104:105], s[78:79], 0, v[70:71]
	s_cbranch_vccz .LBB0_1650
	v_add_co_u32_e32 v166, vcc, 0x34000000, v114
	v_cvt_pk_bf16_f32 v164, v52, v53
	v_cvt_pk_bf16_f32 v165, v54, v55
	s_nop 0
	v_addc_co_u32_e32 v167, vcc, 0, v115, vcc
	global_store_dwordx2 v[166:167], v[164:165], off
	v_pk_fma_f32 v[166:167], v[134:135], v[52:53], v[40:41]
	v_pk_fma_f32 v[164:165], v[136:137], v[54:55], v[42:43]
	v_pk_mul_f32 v[166:167], v[166:167], 4.0 op_sel_hi:[1,0]
	v_pk_mul_f32 v[164:165], v[164:165], 4.0 op_sel_hi:[1,0]
	v_cvt_pk_fp8_f32 v121, v166, v167
	s_mov_b64 s[0:1], 0
	v_cvt_pk_fp8_f32 v121, v164, v165 op_sel:[0,0,1]
	v_add_co_u32_e32 v164, vcc, 0x3c400000, v104
	s_nop 1
	v_addc_co_u32_e32 v165, vcc, 0, v105, vcc
	global_store_dword v[164:165], v121, off

; __device__ __forceinline__ unsigned pk2(float lo, float hi) { unsigned r; asm("v_cvt_pk_bf16_f32 %0, %1, %2" : "=v"(r) : "v"(lo), "v"(hi)); return r; }
; __device__ __forceinline__ unsigned pk4_fp8(float x0, float x1, float x2, float x3) { int w = 0; w = __builtin_amdgcn_cvt_pk_fp8_f32(x0, x1, w, false); w = __builtin_amdgcn_cvt_pk_fp8_f32(x2, x3, w, true); return (unsigned)w; }
; __global__ void __launch_bounds__(512, 2) mega(Args a) {
;     ...
;                 { const float mean0 = wave_sum(sm[0]) * (1.f / DM), mean1 = wave_sum(sm[1]) * (1.f / DM); float q0 = 0.f, q1 = 0.f;
; #pragma unroll
;                   for (int j = 0; j < 4; ++j) { v[0][j] = v[0][j] - mean0; q0 += (v[0][j].x * v[0][j].x + v[0][j].y * v[0][j].y) + (v[0][j].z * v[0][j].z + v[0][j].w * v[0][j].w);
;                       v[1][j] = v[1][j] - mean1; q1 += (v[1][j].x * v[1][j].x + v[1][j].y * v[1][j].y) + (v[1][j].z * v[1][j].z + v[1][j].w * v[1][j].w); }
;                   rstd[0] = rsqrtf(wave_sum(q0) * (1.f / DM) + LN_EPS); rstd[1] = rsqrtf(wave_sum(q1) * (1.f / DM) + LN_EPS); }
;                 __builtin_amdgcn_sched_barrier(0);
; #pragma unroll
;                 for (int j = 0; j < 4; ++j) { __builtin_amdgcn_sched_barrier(0);
;                     f32x4 psh = (f32x4){0.f, 0.f, 0.f, 0.f}, psc = psh;
;                     if (!lastl) { psh = *((const f32x4*)(mdn) + lane + 64 * j); psc = *((const f32x4*)(mdn + 1024) + lane + 64 * j); }
; #pragma unroll
;                     for (int t = 0; t < 2; ++t) { const int nn = n + t;
;                         v[t][j] = v[t][j] * rstd[t] * pg[j] + pb_[j];
;                         if (lastl) *((f32x4*)(a.out + (size_t)(nn - NCTX) * DM) + lane + 64 * j) = v[t][j];
;                         else { u32x2 xw_; xw_.x = pk2(v[t][j].x, v[t][j].y); xw_.y = pk2(v[t][j].z, v[t][j].w); *((u32x2*)(XRB + (size_t)nn * DM) + lane + 64 * j) = xw_;
;                             const f32x4 hh = (v[t][j] * (psc + 1.f) + psh) * ACT_Q; *((unsigned*)(XHF + (size_t)nn * DM) + lane + 64 * j) = pk4_fp8(hh.x, hh.y, hh.z, hh.w); } } }
.LBB0_1652:
	s_nop 1
	v_mul_f32_e32 v52, 0x4b800000, v138
	v_cndmask_b32_e64 v52, v138, v52, s[42:43]
	v_rsq_f32_e32 v52, v52
	s_and_b64 vcc, exec, s[40:41]
	s_mov_b64 s[0:1], -1
	v_mul_f32_e32 v53, 0x45800000, v52
	v_cndmask_b32_e64 v52, v52, v53, s[42:43]
	v_pk_mul_f32 v[54:55], v[132:133], v[52:53] op_sel_hi:[1,0]
	v_pk_mul_f32 v[130:131], v[130:131], v[52:53] op_sel_hi:[1,0]
	v_pk_fma_f32 v[44:45], v[44:45], v[54:55], v[48:49]
	v_pk_fma_f32 v[46:47], v[46:47], v[130:131], v[50:51]
	s_cbranch_vccnz .LBB0_1654
	v_add_co_u32_e32 v50, vcc, 0x34000000, v114
	v_cvt_pk_bf16_f32 v48, v44, v45
	v_pk_fma_f32 v[40:41], v[134:135], v[44:45], v[40:41]
	s_nop 0
	v_addc_co_u32_e32 v51, vcc, 0, v115, vcc
	v_cvt_pk_bf16_f32 v49, v46, v47
	global_store_dwordx2 v[50:51], v[48:49], off offset:2048
	v_pk_mul_f32 v[40:41], v[40:41], 4.0 op_sel_hi:[1,0]
	v_cvt_pk_fp8_f32 v48, v40, v41
	v_pk_fma_f32 v[42:43], v[136:137], v[46:47], v[42:43]
	v_add_co_u32_e32 v40, vcc, 0x3c400000, v104
	v_pk_mul_f32 v[42:43], v[42:43], 4.0 op_sel_hi:[1,0]
	s_nop 0
	v_addc_co_u32_e32 v41, vcc, 0, v105, vcc
	v_cvt_pk_fp8_f32 v48, v42, v43 op_sel:[0,0,1]
	s_mov_b64 s[0:1], 0
	global_store_dword v[40:41], v48, off offset:1024

; __device__ __forceinline__ unsigned pk2(float lo, float hi) { unsigned r; asm("v_cvt_pk_bf16_f32 %0, %1, %2" : "=v"(r) : "v"(lo), "v"(hi)); return r; }
; __device__ __forceinline__ unsigned pk4_fp8(float x0, float x1, float x2, float x3) { int w = 0; w = __builtin_amdgcn_cvt_pk_fp8_f32(x0, x1, w, false); w = __builtin_amdgcn_cvt_pk_fp8_f32(x2, x3, w, true); return (unsigned)w; }
; __global__ void __launch_bounds__(512, 2) mega(Args a) {
;     ...
; #pragma unroll
;                 for (int j = 0; j < 4; ++j) { __builtin_amdgcn_sched_barrier(0);
;                     f32x4 psh = (f32x4){0.f, 0.f, 0.f, 0.f}, psc = psh;
;                     if (!lastl) { psh = *((const f32x4*)(mdn) + lane + 64 * j); psc = *((const f32x4*)(mdn + 1024) + lane + 64 * j); }
; #pragma unroll
;                     for (int t = 0; t < 2; ++t) { const int nn = n + t;
;                         v[t][j] = v[t][j] * rstd[t] * pg[j] + pb_[j];
;                         if (lastl) *((f32x4*)(a.out + (size_t)(nn - NCTX) * DM) + lane + 64 * j) = v[t][j];
;                         else { u32x2 xw_; xw_.x = pk2(v[t][j].x, v[t][j].y); xw_.y = pk2(v[t][j].z, v[t][j].w); *((u32x2*)(XRB + (size_t)nn * DM) + lane + 64 * j) = xw_;
;                             const f32x4 hh = (v[t][j] * (psc + 1.f) + psh) * ACT_Q; *((unsigned*)(XHF + (size_t)nn * DM) + lane + 64 * j) = pk4_fp8(hh.x, hh.y, hh.z, hh.w); } } }
.LBB0_1659:
	v_mov_b32_e32 v121, v120
	v_mov_b32_e32 v44, v120
	v_mov_b32_e32 v45, v120
	v_pk_mul_f32 v[44:45], v[122:123], v[44:45]
	v_pk_mul_f32 v[54:55], v[124:125], v[120:121]
	v_pk_fma_f32 v[46:47], v[34:35], v[44:45], v[38:39]
	v_pk_fma_f32 v[44:45], v[32:33], v[54:55], v[36:37]
	s_and_b64 vcc, exec, s[40:41]
	s_mov_b64 s[0:1], -1
	s_cbranch_vccnz .LBB0_1661
	v_add_co_u32_e32 v122, vcc, 0x34000000, v114
	v_cvt_pk_bf16_f32 v54, v44, v45
	v_cvt_pk_bf16_f32 v55, v46, v47
	s_nop 0
	v_addc_co_u32_e32 v123, vcc, 0, v115, vcc
	global_store_dwordx2 v[122:123], v[54:55], off offset:512
	v_pk_fma_f32 v[122:123], v[48:49], v[44:45], v[40:41]
	v_pk_fma_f32 v[54:55], v[50:51], v[46:47], v[42:43]
	v_pk_mul_f32 v[122:123], v[122:123], 4.0 op_sel_hi:[1,0]
	v_pk_mul_f32 v[54:55], v[54:55], 4.0 op_sel_hi:[1,0]
	v_cvt_pk_fp8_f32 v53, v122, v123
	s_mov_b64 s[0:1], 0
	v_cvt_pk_fp8_f32 v53, v54, v55 op_sel:[0,0,1]
	v_add_co_u32_e32 v54, vcc, 0x3c400000, v104
	s_nop 1
	v_addc_co_u32_e32 v55, vcc, 0, v105, vcc
	global_store_dword v[54:55], v53, off offset:256

; __device__ __forceinline__ unsigned pk2(float lo, float hi) { unsigned r; asm("v_cvt_pk_bf16_f32 %0, %1, %2" : "=v"(r) : "v"(lo), "v"(hi)); return r; }
; __device__ __forceinline__ unsigned pk4_fp8(float x0, float x1, float x2, float x3) { int w = 0; w = __builtin_amdgcn_cvt_pk_fp8_f32(x0, x1, w, false); w = __builtin_amdgcn_cvt_pk_fp8_f32(x2, x3, w, true); return (unsigned)w; }
; __global__ void __launch_bounds__(512, 2) mega(Args a) {
;     ...
; #pragma unroll
;                 for (int j = 0; j < 4; ++j) { __builtin_amdgcn_sched_barrier(0);
;                     f32x4 psh = (f32x4){0.f, 0.f, 0.f, 0.f}, psc = psh;
;                     if (!lastl) { psh = *((const f32x4*)(mdn) + lane + 64 * j); psc = *((const f32x4*)(mdn + 1024) + lane + 64 * j); }
; #pragma unroll
;                     for (int t = 0; t < 2; ++t) { const int nn = n + t;
;                         v[t][j] = v[t][j] * rstd[t] * pg[j] + pb_[j];
;                         if (lastl) *((f32x4*)(a.out + (size_t)(nn - NCTX) * DM) + lane + 64 * j) = v[t][j];
;                         else { u32x2 xw_; xw_.x = pk2(v[t][j].x, v[t][j].y); xw_.y = pk2(v[t][j].z, v[t][j].w); *((u32x2*)(XRB + (size_t)nn * DM) + lane + 64 * j) = xw_;
;                             const f32x4 hh = (v[t][j] * (psc + 1.f) + psh) * ACT_Q; *((unsigned*)(XHF + (size_t)nn * DM) + lane + 64 * j) = pk4_fp8(hh.x, hh.y, hh.z, hh.w); } } }
.LBB0_1663:
	v_mov_b32_e32 v53, v52
	s_nop 0
	v_mov_b32_e32 v44, v52
	v_mov_b32_e32 v45, v52
	v_pk_mul_f32 v[44:45], v[126:127], v[44:45]
	v_pk_mul_f32 v[46:47], v[128:129], v[52:53]
	v_pk_fma_f32 v[34:35], v[34:35], v[44:45], v[38:39]
	v_pk_fma_f32 v[32:33], v[32:33], v[46:47], v[36:37]
	s_and_b64 vcc, exec, s[40:41]
	s_mov_b64 s[0:1], -1
	s_cbranch_vccnz .LBB0_1665
	v_add_co_u32_e32 v38, vcc, 0x34000000, v114
	v_cvt_pk_bf16_f32 v36, v32, v33
	v_cvt_pk_bf16_f32 v37, v34, v35
	s_mov_b64 s[0:1], 0
	s_nop 0
	v_addc_co_u32_e32 v39, vcc, 0, v115, vcc
	global_store_dwordx2 v[38:39], v[36:37], off offset:2560
	v_pk_fma_f32 v[38:39], v[48:49], v[32:33], v[40:41]
	v_pk_mul_f32 v[38:39], v[38:39], 4.0 op_sel_hi:[1,0]
	v_pk_fma_f32 v[36:37], v[50:51], v[34:35], v[42:43]
	v_cvt_pk_fp8_f32 v40, v38, v39
	v_pk_mul_f32 v[36:37], v[36:37], 4.0 op_sel_hi:[1,0]
	s_nop 0
	v_cvt_pk_fp8_f32 v40, v36, v37 op_sel:[0,0,1]
	v_add_co_u32_e32 v36, vcc, 0x3c400000, v104
	s_nop 1
	v_addc_co_u32_e32 v37, vcc, 0, v105, vcc
	global_store_dword v[36:37], v40, off offset:1280

; __device__ __forceinline__ unsigned pk2(float lo, float hi) { unsigned r; asm("v_cvt_pk_bf16_f32 %0, %1, %2" : "=v"(r) : "v"(lo), "v"(hi)); return r; }
; __device__ __forceinline__ unsigned pk4_fp8(float x0, float x1, float x2, float x3) { int w = 0; w = __builtin_amdgcn_cvt_pk_fp8_f32(x0, x1, w, false); w = __builtin_amdgcn_cvt_pk_fp8_f32(x2, x3, w, true); return (unsigned)w; }
; __global__ void __launch_bounds__(512, 2) mega(Args a) {
;     ...
; #pragma unroll
;                 for (int j = 0; j < 4; ++j) { __builtin_amdgcn_sched_barrier(0);
;                     f32x4 psh = (f32x4){0.f, 0.f, 0.f, 0.f}, psc = psh;
;                     if (!lastl) { psh = *((const f32x4*)(mdn) + lane + 64 * j); psc = *((const f32x4*)(mdn + 1024) + lane + 64 * j); }
; #pragma unroll
;                     for (int t = 0; t < 2; ++t) { const int nn = n + t;
;                         v[t][j] = v[t][j] * rstd[t] * pg[j] + pb_[j];
;                         if (lastl) *((f32x4*)(a.out + (size_t)(nn - NCTX) * DM) + lane + 64 * j) = v[t][j];
;                         else { u32x2 xw_; xw_.x = pk2(v[t][j].x, v[t][j].y); xw_.y = pk2(v[t][j].z, v[t][j].w); *((u32x2*)(XRB + (size_t)nn * DM) + lane + 64 * j) = xw_;
;                             const f32x4 hh = (v[t][j] * (psc + 1.f) + psh) * ACT_Q; *((unsigned*)(XHF + (size_t)nn * DM) + lane + 64 * j) = pk4_fp8(hh.x, hh.y, hh.z, hh.w); } } }
.LBB0_1670:
	v_mov_b32_e32 v36, v120
	v_mov_b32_e32 v37, v120
	v_pk_mul_f32 v[36:37], v[106:107], v[36:37]
	v_pk_mul_f32 v[44:45], v[108:109], v[120:121]
	v_pk_fma_f32 v[38:39], v[26:27], v[36:37], v[30:31]
	v_pk_fma_f32 v[36:37], v[24:25], v[44:45], v[28:29]
	s_and_b64 vcc, exec, s[40:41]
	s_mov_b64 s[0:1], -1
	s_cbranch_vccnz .LBB0_1672
	v_add_co_u32_e32 v46, vcc, 0x34000000, v114
	v_cvt_pk_bf16_f32 v44, v36, v37
	v_cvt_pk_bf16_f32 v45, v38, v39
	s_nop 0
	v_addc_co_u32_e32 v47, vcc, 0, v115, vcc
	global_store_dwordx2 v[46:47], v[44:45], off offset:1024
	v_pk_fma_f32 v[46:47], v[40:41], v[36:37], v[32:33]
	v_pk_fma_f32 v[44:45], v[42:43], v[38:39], v[34:35]
	v_pk_mul_f32 v[46:47], v[46:47], 4.0 op_sel_hi:[1,0]
	v_pk_mul_f32 v[44:45], v[44:45], 4.0 op_sel_hi:[1,0]
	v_cvt_pk_fp8_f32 v48, v46, v47
	s_mov_b64 s[0:1], 0
	v_cvt_pk_fp8_f32 v48, v44, v45 op_sel:[0,0,1]
	v_add_co_u32_e32 v44, vcc, 0x3c400000, v104
	s_nop 1
	v_addc_co_u32_e32 v45, vcc, 0, v105, vcc
	global_store_dword v[44:45], v48, off offset:512

; __device__ __forceinline__ unsigned pk2(float lo, float hi) { unsigned r; asm("v_cvt_pk_bf16_f32 %0, %1, %2" : "=v"(r) : "v"(lo), "v"(hi)); return r; }
; __device__ __forceinline__ unsigned pk4_fp8(float x0, float x1, float x2, float x3) { int w = 0; w = __builtin_amdgcn_cvt_pk_fp8_f32(x0, x1, w, false); w = __builtin_amdgcn_cvt_pk_fp8_f32(x2, x3, w, true); return (unsigned)w; }
; __global__ void __launch_bounds__(512, 2) mega(Args a) {
;     ...
; #pragma unroll
;                 for (int j = 0; j < 4; ++j) { __builtin_amdgcn_sched_barrier(0);
;                     f32x4 psh = (f32x4){0.f, 0.f, 0.f, 0.f}, psc = psh;
;                     if (!lastl) { psh = *((const f32x4*)(mdn) + lane + 64 * j); psc = *((const f32x4*)(mdn + 1024) + lane + 64 * j); }
; #pragma unroll
;                     for (int t = 0; t < 2; ++t) { const int nn = n + t;
;                         v[t][j] = v[t][j] * rstd[t] * pg[j] + pb_[j];
;                         if (lastl) *((f32x4*)(a.out + (size_t)(nn - NCTX) * DM) + lane + 64 * j) = v[t][j];
;                         else { u32x2 xw_; xw_.x = pk2(v[t][j].x, v[t][j].y); xw_.y = pk2(v[t][j].z, v[t][j].w); *((u32x2*)(XRB + (size_t)nn * DM) + lane + 64 * j) = xw_;
;                             const f32x4 hh = (v[t][j] * (psc + 1.f) + psh) * ACT_Q; *((unsigned*)(XHF + (size_t)nn * DM) + lane + 64 * j) = pk4_fp8(hh.x, hh.y, hh.z, hh.w); } } }
.LBB0_1674:
	s_nop 1
	v_mov_b32_e32 v36, v52
	v_mov_b32_e32 v37, v52
	v_pk_mul_f32 v[36:37], v[110:111], v[36:37]
	v_pk_mul_f32 v[38:39], v[112:113], v[52:53]
	v_pk_fma_f32 v[26:27], v[26:27], v[36:37], v[30:31]
	v_pk_fma_f32 v[24:25], v[24:25], v[38:39], v[28:29]
	s_and_b64 vcc, exec, s[40:41]
	s_mov_b64 s[0:1], -1
	s_cbranch_vccnz .LBB0_1676
	v_add_co_u32_e32 v30, vcc, 0x34000000, v114
	v_cvt_pk_bf16_f32 v28, v24, v25
	v_cvt_pk_bf16_f32 v29, v26, v27
	s_mov_b64 s[0:1], 0
	s_nop 0
	v_addc_co_u32_e32 v31, vcc, 0, v115, vcc
	global_store_dwordx2 v[30:31], v[28:29], off offset:3072
	v_pk_fma_f32 v[30:31], v[40:41], v[24:25], v[32:33]
	v_pk_mul_f32 v[30:31], v[30:31], 4.0 op_sel_hi:[1,0]
	v_pk_fma_f32 v[28:29], v[42:43], v[26:27], v[34:35]
	v_cvt_pk_fp8_f32 v32, v30, v31
	v_pk_mul_f32 v[28:29], v[28:29], 4.0 op_sel_hi:[1,0]
	s_nop 0
	v_cvt_pk_fp8_f32 v32, v28, v29 op_sel:[0,0,1]
	v_add_co_u32_e32 v28, vcc, 0x3c400000, v104
	s_nop 1
	v_addc_co_u32_e32 v29, vcc, 0, v105, vcc
	global_store_dword v[28:29], v32, off offset:1536

; __device__ __forceinline__ unsigned pk2(float lo, float hi) { unsigned r; asm("v_cvt_pk_bf16_f32 %0, %1, %2" : "=v"(r) : "v"(lo), "v"(hi)); return r; }
; __device__ __forceinline__ unsigned pk4_fp8(float x0, float x1, float x2, float x3) { int w = 0; w = __builtin_amdgcn_cvt_pk_fp8_f32(x0, x1, w, false); w = __builtin_amdgcn_cvt_pk_fp8_f32(x2, x3, w, true); return (unsigned)w; }
; __global__ void __launch_bounds__(512, 2) mega(Args a) {
;     ...
; #pragma unroll
;                 for (int j = 0; j < 4; ++j) { __builtin_amdgcn_sched_barrier(0);
;                     f32x4 psh = (f32x4){0.f, 0.f, 0.f, 0.f}, psc = psh;
;                     if (!lastl) { psh = *((const f32x4*)(mdn) + lane + 64 * j); psc = *((const f32x4*)(mdn + 1024) + lane + 64 * j); }
; #pragma unroll
;                     for (int t = 0; t < 2; ++t) { const int nn = n + t;
;                         v[t][j] = v[t][j] * rstd[t] * pg[j] + pb_[j];
;                         if (lastl) *((f32x4*)(a.out + (size_t)(nn - NCTX) * DM) + lane + 64 * j) = v[t][j];
;                         else { u32x2 xw_; xw_.x = pk2(v[t][j].x, v[t][j].y); xw_.y = pk2(v[t][j].z, v[t][j].w); *((u32x2*)(XRB + (size_t)nn * DM) + lane + 64 * j) = xw_;
;                             const f32x4 hh = (v[t][j] * (psc + 1.f) + psh) * ACT_Q; *((unsigned*)(XHF + (size_t)nn * DM) + lane + 64 * j) = pk4_fp8(hh.x, hh.y, hh.z, hh.w); } } }
.LBB0_1681:
	v_mov_b32_e32 v28, v120
	v_mov_b32_e32 v29, v120
	v_pk_mul_f32 v[28:29], v[96:97], v[28:29]
	v_pk_mul_f32 v[36:37], v[102:103], v[120:121]
	v_pk_fma_f32 v[30:31], v[18:19], v[28:29], v[22:23]
	v_pk_fma_f32 v[28:29], v[16:17], v[36:37], v[20:21]
	s_and_b64 vcc, exec, s[40:41]
	s_mov_b64 s[0:1], -1
	s_cbranch_vccnz .LBB0_1683
	v_add_co_u32_e32 v38, vcc, 0x34000000, v114
	v_cvt_pk_bf16_f32 v36, v28, v29
	v_cvt_pk_bf16_f32 v37, v30, v31
	s_nop 0
	v_addc_co_u32_e32 v39, vcc, 0, v115, vcc
	global_store_dwordx2 v[38:39], v[36:37], off offset:1536
	v_pk_fma_f32 v[38:39], v[32:33], v[28:29], v[24:25]
	v_pk_fma_f32 v[36:37], v[34:35], v[30:31], v[26:27]
	v_pk_mul_f32 v[38:39], v[38:39], 4.0 op_sel_hi:[1,0]
	v_pk_mul_f32 v[36:37], v[36:37], 4.0 op_sel_hi:[1,0]
	v_cvt_pk_fp8_f32 v40, v38, v39
	s_mov_b64 s[0:1], 0
	v_cvt_pk_fp8_f32 v40, v36, v37 op_sel:[0,0,1]
	v_add_co_u32_e32 v36, vcc, 0x3c400000, v104
	s_nop 1
	v_addc_co_u32_e32 v37, vcc, 0, v105, vcc
	global_store_dword v[36:37], v40, off offset:768

; __device__ __forceinline__ unsigned pk2(float lo, float hi) { unsigned r; asm("v_cvt_pk_bf16_f32 %0, %1, %2" : "=v"(r) : "v"(lo), "v"(hi)); return r; }
; __device__ __forceinline__ unsigned pk4_fp8(float x0, float x1, float x2, float x3) { int w = 0; w = __builtin_amdgcn_cvt_pk_fp8_f32(x0, x1, w, false); w = __builtin_amdgcn_cvt_pk_fp8_f32(x2, x3, w, true); return (unsigned)w; }
; __global__ void __launch_bounds__(512, 2) mega(Args a) {
;     ...
; #pragma unroll
;                 for (int j = 0; j < 4; ++j) { __builtin_amdgcn_sched_barrier(0);
;                     f32x4 psh = (f32x4){0.f, 0.f, 0.f, 0.f}, psc = psh;
;                     if (!lastl) { psh = *((const f32x4*)(mdn) + lane + 64 * j); psc = *((const f32x4*)(mdn + 1024) + lane + 64 * j); }
; #pragma unroll
;                     for (int t = 0; t < 2; ++t) { const int nn = n + t;
;                         v[t][j] = v[t][j] * rstd[t] * pg[j] + pb_[j];
;                         if (lastl) *((f32x4*)(a.out + (size_t)(nn - NCTX) * DM) + lane + 64 * j) = v[t][j];
;                         else { u32x2 xw_; xw_.x = pk2(v[t][j].x, v[t][j].y); xw_.y = pk2(v[t][j].z, v[t][j].w); *((u32x2*)(XRB + (size_t)nn * DM) + lane + 64 * j) = xw_;
;                             const f32x4 hh = (v[t][j] * (psc + 1.f) + psh) * ACT_Q; *((unsigned*)(XHF + (size_t)nn * DM) + lane + 64 * j) = pk4_fp8(hh.x, hh.y, hh.z, hh.w); } } }
.LBB0_1685:
	s_nop 1
	v_mov_b32_e32 v28, v52
	v_mov_b32_e32 v29, v52
	v_pk_mul_f32 v[28:29], v[98:99], v[28:29]
	v_pk_mul_f32 v[30:31], v[100:101], v[52:53]
	v_pk_fma_f32 v[18:19], v[18:19], v[28:29], v[22:23]
	v_pk_fma_f32 v[16:17], v[16:17], v[30:31], v[20:21]
	s_and_b64 vcc, exec, s[40:41]
	s_mov_b64 s[0:1], -1
	s_cbranch_vccnz .LBB0_1687
	v_add_co_u32_e32 v22, vcc, 0x34000000, v114
	v_cvt_pk_bf16_f32 v20, v16, v17
	v_cvt_pk_bf16_f32 v21, v18, v19
	s_mov_b64 s[0:1], 0
	s_nop 0
	v_addc_co_u32_e32 v23, vcc, 0, v115, vcc
	global_store_dwordx2 v[22:23], v[20:21], off offset:3584
	v_pk_fma_f32 v[22:23], v[32:33], v[16:17], v[24:25]
	v_pk_mul_f32 v[22:23], v[22:23], 4.0 op_sel_hi:[1,0]
	v_pk_fma_f32 v[20:21], v[34:35], v[18:19], v[26:27]
	v_cvt_pk_fp8_f32 v24, v22, v23
	v_pk_mul_f32 v[20:21], v[20:21], 4.0 op_sel_hi:[1,0]
	s_nop 0
	v_cvt_pk_fp8_f32 v24, v20, v21 op_sel:[0,0,1]
	v_add_co_u32_e32 v20, vcc, 0x3c400000, v104
	s_nop 1
	v_addc_co_u32_e32 v21, vcc, 0, v105, vcc
	global_store_dword v[20:21], v24, off offset:1792
